# router: x16 tile re-reads as L1-bypassing sc1 loads, L1-invalidate fence dropped
# speedup vs baseline: 1.0471x; 1.0200x over previous
.LBB0_651:
	s_waitcnt vmcnt(0)
	s_barrier
	s_waitcnt vmcnt(0)
	s_waitcnt vmcnt(0)
	v_readlane_b32 s98, v253, 20
	v_mbcnt_lo_u32_b32 v216, -1, 0
	v_mbcnt_hi_u32_b32 v216, -1, v216
	s_lshr_b32 s99, s98, 1
	s_and_b32 s100, s98, 1
	v_lshrrev_b32_e32 v217, 5, v216
	v_and_b32_e32 v216, 31, v216
	s_lshl_b32 s101, s99, 4
	v_add_u32_e32 v218, s101, v217
	v_lshlrev_b32_e32 v219, 7, v218
	v_lshl_add_u32 v219, v216, 2, v219
	v_add_u32_e32 v219, 0xa400, v219
	v_mul_u32_u24_e32 v218, 0x104, v218
	s_lshl_b32 s101, s100, 7
	v_add_u32_e32 v218, s101, v218
	v_lshl_add_u32 v218, v216, 2, v218
	v_add_u32_e32 v218, 0x6000, v218
	v_mov_b32_e32 v221, s98
	v_mbcnt_lo_u32_b32 v220, -1, 0
	v_mbcnt_hi_u32_b32 v220, -1, v220
	v_lshl_add_u32 v220, v221, 6, v220
	v_and_b32_e32 v221, 7, v220
	v_lshrrev_b32_e32 v220, 3, v220
	v_mul_u32_u24_e32 v221, 0x820, v221
	v_lshl_add_u32 v220, v220, 2, v221
	v_add_u32_e32 v220, 0x6000, v220
	v_add_u32_e32 v221, 0x410, v220
	s_lshl_b32 s101, s99, 13
	s_lshl_b32 s100, s100, 12
	s_add_i32 s101, s101, s100
	v_lshlrev_b32_e32 v217, 9, v217
	v_add_u32_e32 v217, s101, v217
	v_lshl_add_u32 v217, v216, 2, v217
	s_and_saveexec_b64 s[16:17], s[4:5]
	ds_write_b32 v103, v45 offset:58624
	s_or_b64 exec, exec, s[16:17]
	v_add_u32_e32 v0, s62, v42
	v_ashrrev_i32_e32 v1, 31, v0
	v_lshlrev_b64 v[0:1], 11, v[0:1]
	v_lshl_add_u64 v[94:95], v[46:47], 0, v[0:1]
	global_load_dwordx4 v[30:33], v[94:95], off sc1
	global_load_dwordx4 v[34:37], v[48:49], off
	global_load_dwordx4 v[20:23], v[52:53], off
	global_load_dwordx4 v[24:27], v[94:95], off offset:128 sc1
	ds_read_b64 v[38:39], v115 offset:20480
	ds_read_b128 v[98:101], v43 offset:12288
	ds_read_b128 v[122:125], v43 offset:12304
	ds_read_b128 v[126:129], v43 offset:16384
	ds_read_b128 v[130:133], v43 offset:16400
	v_add_u32_e32 v96, 0x6000, v105
	v_mov_b32_e32 v4, 0
	s_waitcnt lgkmcnt(4)
	v_mov_b32_e32 v0, v38
	v_mov_b32_e32 v1, v38
	v_mov_b32_e32 v2, v38
	v_mov_b32_e32 v3, v38
	v_mov_b32_e32 v90, v39
	v_mov_b32_e32 v91, v39
	v_mov_b32_e32 v92, v39
	v_mov_b32_e32 v93, v39
	v_add_u32_e32 v44, 0x6400, v105
	s_mov_b32 s16, 0
	v_mov_b32_e32 v28, v112
	v_mov_b32_e32 v5, v4
	v_mov_b32_e32 v6, v4
	v_mov_b32_e32 v7, v4
	v_mov_b32_e32 v8, v4
	v_mov_b32_e32 v9, v4
	v_mov_b32_e32 v10, v4
	v_mov_b32_e32 v11, v4
	v_mov_b32_e32 v12, v4
	v_mov_b32_e32 v13, v4
	v_mov_b32_e32 v14, v4
	v_mov_b32_e32 v15, v4
	v_mov_b32_e32 v16, v4
	v_mov_b32_e32 v17, v4
	v_mov_b32_e32 v18, v4
	s_waitcnt vmcnt(3)
	v_cvt_f32_f16_sdwa v19, v31 dst_sel:DWORD dst_unused:UNUSED_PAD src0_sel:WORD_1
	v_cvt_f32_f16_e32 v29, v31
	v_cvt_f32_f16_sdwa v31, v30 dst_sel:DWORD dst_unused:UNUSED_PAD src0_sel:WORD_1
	v_cvt_f32_f16_e32 v30, v30
	v_cvt_f32_f16_sdwa v97, v33 dst_sel:DWORD dst_unused:UNUSED_PAD src0_sel:WORD_1
	v_cvt_f32_f16_e32 v136, v33
	v_cvt_f32_f16_sdwa v135, v32 dst_sel:DWORD dst_unused:UNUSED_PAD src0_sel:WORD_1
	v_cvt_f32_f16_e32 v134, v32
	v_sub_f32_e32 v30, v30, v38
	v_sub_f32_e32 v31, v31, v38
	v_sub_f32_e32 v32, v29, v38
	v_sub_f32_e32 v33, v19, v38
	v_sub_f32_e32 v134, v134, v38
	v_sub_f32_e32 v135, v135, v38
	v_sub_f32_e32 v136, v136, v38
	v_sub_f32_e32 v137, v97, v38
	v_pk_mul_f32 v[30:31], v[38:39], v[30:31] op_sel:[1,0]
	v_pk_mul_f32 v[32:33], v[38:39], v[32:33] op_sel:[1,0]
	v_pk_mul_f32 v[136:137], v[38:39], v[136:137] op_sel:[1,0]
	v_pk_mul_f32 v[38:39], v[38:39], v[134:135] op_sel:[1,0]
	s_waitcnt lgkmcnt(1)
	v_fma_f32 v19, v98, v30, v126
	v_fma_f32 v30, v99, v31, v127
	s_waitcnt lgkmcnt(0)
	v_fma_f32 v29, v122, v38, v130
	v_fma_f32 v31, v123, v39, v131
	v_fma_f32 v32, v100, v32, v128
	v_fma_f32 v38, v124, v136, v132
	v_fmac_f32_e32 v129, v101, v33
	v_fmac_f32_e32 v133, v125, v137
	ds_write2_b32 v220, v19, v30 offset1:65
	ds_write2_b32 v221, v29, v31 offset1:65
	ds_write2_b32 v220, v32, v129 offset0:130 offset1:195
	ds_write2_b32 v221, v38, v133 offset0:130 offset1:195
	s_waitcnt vmcnt(2)
	ds_write_b128 v104, v[34:37] offset:41984
	v_mov_b32_e32 v19, v4
	s_waitcnt lgkmcnt(0)
	s_barrier
	ds_read_b32 v200, v218
	ds_read_b32 v208, v219
	ds_read_b32 v201, v218 offset:520
	ds_read_b32 v209, v219 offset:256
	ds_read_b32 v202, v218 offset:1040
	ds_read_b32 v210, v219 offset:512
	ds_read_b32 v203, v218 offset:1560
	ds_read_b32 v211, v219 offset:768
	ds_read_b32 v204, v218 offset:2080
	ds_read_b32 v212, v219 offset:1024
	ds_read_b32 v205, v218 offset:2600
	ds_read_b32 v213, v219 offset:1280
	ds_read_b32 v206, v218 offset:3120
	ds_read_b32 v214, v219 offset:1536
	s_waitcnt lgkmcnt(12)
	v_mfma_f32_32x32x2_f32 v[4:19], v200, v208, v[4:19]
	ds_read_b32 v207, v218 offset:3640
	ds_read_b32 v215, v219 offset:1792
	s_waitcnt lgkmcnt(12)
	v_mfma_f32_32x32x2_f32 v[4:19], v201, v209, v[4:19]
	s_waitcnt lgkmcnt(10)
	v_mfma_f32_32x32x2_f32 v[4:19], v202, v210, v[4:19]
	s_waitcnt lgkmcnt(8)
	v_mfma_f32_32x32x2_f32 v[4:19], v203, v211, v[4:19]
	s_waitcnt lgkmcnt(6)
	v_mfma_f32_32x32x2_f32 v[4:19], v204, v212, v[4:19]
	s_waitcnt lgkmcnt(4)
	v_mfma_f32_32x32x2_f32 v[4:19], v205, v213, v[4:19]
	s_waitcnt lgkmcnt(2)
	v_mfma_f32_32x32x2_f32 v[4:19], v206, v214, v[4:19]
	s_waitcnt lgkmcnt(0)
	v_mfma_f32_32x32x2_f32 v[4:19], v207, v215, v[4:19]
	s_barrier
	global_load_dwordx4 v[32:35], v[94:95], off offset:256 sc1
	global_load_dwordx4 v[28:31], v[54:55], off
	s_waitcnt vmcnt(2)
	v_cvt_f32_f16_sdwa v130, v24 dst_sel:DWORD dst_unused:UNUSED_PAD src0_sel:WORD_1
	v_cvt_f32_f16_e32 v24, v24
	v_cvt_f32_f16_e32 v131, v25
	v_cvt_f32_f16_sdwa v132, v26 dst_sel:DWORD dst_unused:UNUSED_PAD src0_sel:WORD_1
	v_cvt_f32_f16_e32 v135, v26
	ds_read_b128 v[36:39], v43 offset:12544
	ds_read_b128 v[98:101], v43 offset:12560
	ds_read_b128 v[122:125], v43 offset:16640
	ds_read_b128 v[126:129], v43 offset:16656
	v_cvt_f32_f16_sdwa v97, v25 dst_sel:DWORD dst_unused:UNUSED_PAD src0_sel:WORD_1
	v_cvt_f32_f16_sdwa v133, v27 dst_sel:DWORD dst_unused:UNUSED_PAD src0_sel:WORD_1
	v_cvt_f32_f16_e32 v134, v27
	v_sub_f32_e32 v24, v24, v0
	v_sub_f32_e32 v25, v130, v1
	v_sub_f32_e32 v26, v131, v2
	v_pk_mul_f32 v[24:25], v[90:91], v[24:25]
	v_sub_f32_e32 v130, v135, v0
	v_sub_f32_e32 v131, v132, v1
	v_sub_f32_e32 v27, v97, v3
	v_sub_f32_e32 v132, v134, v2
	v_sub_f32_e32 v133, v133, v3
	v_pk_mul_f32 v[130:131], v[90:91], v[130:131]
	s_waitcnt lgkmcnt(1)
	v_fma_f32 v24, v36, v24, v122
	v_fma_f32 v25, v37, v25, v123
	v_pk_mul_f32 v[26:27], v[92:93], v[26:27]
	v_pk_mul_f32 v[132:133], v[92:93], v[132:133]
	s_waitcnt lgkmcnt(0)
	v_fma_f32 v36, v98, v130, v126
	ds_write2_b32 v220, v24, v25 offset1:65
	v_fma_f32 v24, v99, v131, v127
	ds_write2_b32 v221, v36, v24 offset1:65
	v_fma_f32 v24, v38, v26, v124
	v_fma_f32 v25, v100, v132, v128
	v_fmac_f32_e32 v125, v39, v27
	v_fmac_f32_e32 v129, v101, v133
	ds_write2_b32 v220, v24, v125 offset0:130 offset1:195
	ds_write2_b32 v221, v25, v129 offset0:130 offset1:195
	ds_write_b128 v104, v[20:23] offset:41984
	s_mov_b32 s16, 0
	v_mov_b32_e32 v20, v112
	s_waitcnt lgkmcnt(0)
	s_barrier
	ds_read_b32 v200, v218
	ds_read_b32 v208, v219
	ds_read_b32 v201, v218 offset:520
	ds_read_b32 v209, v219 offset:256
	ds_read_b32 v202, v218 offset:1040
	ds_read_b32 v210, v219 offset:512
	ds_read_b32 v203, v218 offset:1560
	ds_read_b32 v211, v219 offset:768
	ds_read_b32 v204, v218 offset:2080
	ds_read_b32 v212, v219 offset:1024
	ds_read_b32 v205, v218 offset:2600
	ds_read_b32 v213, v219 offset:1280
	ds_read_b32 v206, v218 offset:3120
	ds_read_b32 v214, v219 offset:1536
	s_waitcnt lgkmcnt(12)
	v_mfma_f32_32x32x2_f32 v[4:19], v200, v208, v[4:19]
	ds_read_b32 v207, v218 offset:3640
	ds_read_b32 v215, v219 offset:1792
	s_waitcnt lgkmcnt(12)
	v_mfma_f32_32x32x2_f32 v[4:19], v201, v209, v[4:19]
	s_waitcnt lgkmcnt(10)
	v_mfma_f32_32x32x2_f32 v[4:19], v202, v210, v[4:19]
	s_waitcnt lgkmcnt(8)
	v_mfma_f32_32x32x2_f32 v[4:19], v203, v211, v[4:19]
	s_waitcnt lgkmcnt(6)
	v_mfma_f32_32x32x2_f32 v[4:19], v204, v212, v[4:19]
	s_waitcnt lgkmcnt(4)
	v_mfma_f32_32x32x2_f32 v[4:19], v205, v213, v[4:19]
	s_waitcnt lgkmcnt(2)
	v_mfma_f32_32x32x2_f32 v[4:19], v206, v214, v[4:19]
	s_waitcnt lgkmcnt(0)
	v_mfma_f32_32x32x2_f32 v[4:19], v207, v215, v[4:19]
	s_barrier
	global_load_dwordx4 v[36:39], v[94:95], off offset:384 sc1
	global_load_dwordx4 v[20:23], v[56:57], off
	s_waitcnt vmcnt(3)
	v_cvt_f32_f16_sdwa v130, v32 dst_sel:DWORD dst_unused:UNUSED_PAD src0_sel:WORD_1
	v_cvt_f32_f16_e32 v32, v32
	v_cvt_f32_f16_e32 v131, v33
	v_cvt_f32_f16_sdwa v132, v34 dst_sel:DWORD dst_unused:UNUSED_PAD src0_sel:WORD_1
	v_cvt_f32_f16_e32 v135, v34
	ds_read_b128 v[24:27], v43 offset:12800
	ds_read_b128 v[98:101], v43 offset:12816
	ds_read_b128 v[122:125], v43 offset:16896
	ds_read_b128 v[126:129], v43 offset:16912
	v_cvt_f32_f16_sdwa v97, v33 dst_sel:DWORD dst_unused:UNUSED_PAD src0_sel:WORD_1
	v_cvt_f32_f16_sdwa v133, v35 dst_sel:DWORD dst_unused:UNUSED_PAD src0_sel:WORD_1
	v_cvt_f32_f16_e32 v134, v35
	v_sub_f32_e32 v32, v32, v0
	v_sub_f32_e32 v33, v130, v1
	v_sub_f32_e32 v34, v131, v2
	v_pk_mul_f32 v[32:33], v[90:91], v[32:33]
	v_sub_f32_e32 v130, v135, v0
	v_sub_f32_e32 v131, v132, v1
	v_sub_f32_e32 v35, v97, v3
	v_pk_mul_f32 v[130:131], v[90:91], v[130:131]
	s_waitcnt lgkmcnt(1)
	v_fma_f32 v24, v24, v32, v122
	v_fma_f32 v25, v25, v33, v123
	v_pk_mul_f32 v[34:35], v[92:93], v[34:35]
	v_sub_f32_e32 v132, v134, v2
	v_sub_f32_e32 v133, v133, v3
	s_waitcnt lgkmcnt(0)
	v_fma_f32 v32, v98, v130, v126
	ds_write2_b32 v220, v24, v25 offset1:65
	v_fma_f32 v24, v99, v131, v127
	v_pk_mul_f32 v[132:133], v[92:93], v[132:133]
	ds_write2_b32 v221, v32, v24 offset1:65
	v_fma_f32 v24, v26, v34, v124
	v_fmac_f32_e32 v125, v27, v35
	v_fma_f32 v25, v100, v132, v128
	ds_write2_b32 v220, v24, v125 offset0:130 offset1:195
	v_fmac_f32_e32 v129, v101, v133
	s_mov_b32 s16, 0
	v_mov_b32_e32 v24, v112
	ds_write2_b32 v221, v25, v129 offset0:130 offset1:195
	s_waitcnt vmcnt(2)
	ds_write_b128 v104, v[28:31] offset:41984
	s_waitcnt lgkmcnt(0)
	s_barrier
	ds_read_b32 v200, v218
	ds_read_b32 v208, v219
	ds_read_b32 v201, v218 offset:520
	ds_read_b32 v209, v219 offset:256
	ds_read_b32 v202, v218 offset:1040
	ds_read_b32 v210, v219 offset:512
	ds_read_b32 v203, v218 offset:1560
	ds_read_b32 v211, v219 offset:768
	ds_read_b32 v204, v218 offset:2080
	ds_read_b32 v212, v219 offset:1024
	ds_read_b32 v205, v218 offset:2600
	ds_read_b32 v213, v219 offset:1280
	ds_read_b32 v206, v218 offset:3120
	ds_read_b32 v214, v219 offset:1536
	s_waitcnt lgkmcnt(12)
	v_mfma_f32_32x32x2_f32 v[4:19], v200, v208, v[4:19]
	ds_read_b32 v207, v218 offset:3640
	ds_read_b32 v215, v219 offset:1792
	s_waitcnt lgkmcnt(12)
	v_mfma_f32_32x32x2_f32 v[4:19], v201, v209, v[4:19]
	s_waitcnt lgkmcnt(10)
	v_mfma_f32_32x32x2_f32 v[4:19], v202, v210, v[4:19]
	s_waitcnt lgkmcnt(8)
	v_mfma_f32_32x32x2_f32 v[4:19], v203, v211, v[4:19]
	s_waitcnt lgkmcnt(6)
	v_mfma_f32_32x32x2_f32 v[4:19], v204, v212, v[4:19]
	s_waitcnt lgkmcnt(4)
	v_mfma_f32_32x32x2_f32 v[4:19], v205, v213, v[4:19]
	s_waitcnt lgkmcnt(2)
	v_mfma_f32_32x32x2_f32 v[4:19], v206, v214, v[4:19]
	s_waitcnt lgkmcnt(0)
	v_mfma_f32_32x32x2_f32 v[4:19], v207, v215, v[4:19]
	s_barrier
	global_load_dwordx4 v[28:31], v[94:95], off offset:512 sc1
	global_load_dwordx4 v[24:27], v[58:59], off
	s_waitcnt vmcnt(3)
	v_cvt_f32_f16_sdwa v130, v36 dst_sel:DWORD dst_unused:UNUSED_PAD src0_sel:WORD_1
	v_cvt_f32_f16_e32 v36, v36
	v_cvt_f32_f16_e32 v131, v37
	v_cvt_f32_f16_sdwa v132, v38 dst_sel:DWORD dst_unused:UNUSED_PAD src0_sel:WORD_1
	v_cvt_f32_f16_e32 v135, v38
	ds_read_b128 v[32:35], v43 offset:13056
	ds_read_b128 v[98:101], v43 offset:13072
	ds_read_b128 v[122:125], v43 offset:17152
	ds_read_b128 v[126:129], v43 offset:17168
	v_cvt_f32_f16_sdwa v97, v37 dst_sel:DWORD dst_unused:UNUSED_PAD src0_sel:WORD_1
	v_cvt_f32_f16_sdwa v133, v39 dst_sel:DWORD dst_unused:UNUSED_PAD src0_sel:WORD_1
	v_cvt_f32_f16_e32 v134, v39
	v_sub_f32_e32 v36, v36, v0
	v_sub_f32_e32 v37, v130, v1
	v_sub_f32_e32 v38, v131, v2
	v_pk_mul_f32 v[36:37], v[90:91], v[36:37]
	v_sub_f32_e32 v130, v135, v0
	v_sub_f32_e32 v131, v132, v1
	v_sub_f32_e32 v39, v97, v3
	v_sub_f32_e32 v132, v134, v2
	v_sub_f32_e32 v133, v133, v3
	v_pk_mul_f32 v[130:131], v[90:91], v[130:131]
	s_waitcnt lgkmcnt(1)
	v_fma_f32 v32, v32, v36, v122
	v_fma_f32 v33, v33, v37, v123
	v_pk_mul_f32 v[38:39], v[92:93], v[38:39]
	v_pk_mul_f32 v[132:133], v[92:93], v[132:133]
	s_waitcnt lgkmcnt(0)
	v_fma_f32 v36, v98, v130, v126
	ds_write2_b32 v220, v32, v33 offset1:65
	v_fma_f32 v32, v99, v131, v127
	ds_write2_b32 v221, v36, v32 offset1:65
	v_fma_f32 v32, v34, v38, v124
	v_fma_f32 v33, v100, v132, v128
	v_fmac_f32_e32 v125, v35, v39
	v_fmac_f32_e32 v129, v101, v133
	ds_write2_b32 v220, v32, v125 offset0:130 offset1:195
	ds_write2_b32 v221, v33, v129 offset0:130 offset1:195
	s_waitcnt vmcnt(2)
	ds_write_b128 v104, v[20:23] offset:41984
	s_mov_b32 s16, 0
	v_mov_b32_e32 v20, v112
	s_waitcnt lgkmcnt(0)
	s_barrier
	ds_read_b32 v200, v218
	ds_read_b32 v208, v219
	ds_read_b32 v201, v218 offset:520
	ds_read_b32 v209, v219 offset:256
	ds_read_b32 v202, v218 offset:1040
	ds_read_b32 v210, v219 offset:512
	ds_read_b32 v203, v218 offset:1560
	ds_read_b32 v211, v219 offset:768
	ds_read_b32 v204, v218 offset:2080
	ds_read_b32 v212, v219 offset:1024
	ds_read_b32 v205, v218 offset:2600
	ds_read_b32 v213, v219 offset:1280
	ds_read_b32 v206, v218 offset:3120
	ds_read_b32 v214, v219 offset:1536
	s_waitcnt lgkmcnt(12)
	v_mfma_f32_32x32x2_f32 v[4:19], v200, v208, v[4:19]
	ds_read_b32 v207, v218 offset:3640
	ds_read_b32 v215, v219 offset:1792
	s_waitcnt lgkmcnt(12)
	v_mfma_f32_32x32x2_f32 v[4:19], v201, v209, v[4:19]
	s_waitcnt lgkmcnt(10)
	v_mfma_f32_32x32x2_f32 v[4:19], v202, v210, v[4:19]
	s_waitcnt lgkmcnt(8)
	v_mfma_f32_32x32x2_f32 v[4:19], v203, v211, v[4:19]
	s_waitcnt lgkmcnt(6)
	v_mfma_f32_32x32x2_f32 v[4:19], v204, v212, v[4:19]
	s_waitcnt lgkmcnt(4)
	v_mfma_f32_32x32x2_f32 v[4:19], v205, v213, v[4:19]
	s_waitcnt lgkmcnt(2)
	v_mfma_f32_32x32x2_f32 v[4:19], v206, v214, v[4:19]
	s_waitcnt lgkmcnt(0)
	v_mfma_f32_32x32x2_f32 v[4:19], v207, v215, v[4:19]
	s_barrier
	global_load_dwordx4 v[32:35], v[94:95], off offset:640 sc1
	global_load_dwordx4 v[20:23], v[60:61], off
	s_waitcnt vmcnt(3)
	v_cvt_f32_f16_sdwa v130, v28 dst_sel:DWORD dst_unused:UNUSED_PAD src0_sel:WORD_1
	v_cvt_f32_f16_e32 v28, v28
	v_cvt_f32_f16_e32 v131, v29
	v_cvt_f32_f16_sdwa v132, v30 dst_sel:DWORD dst_unused:UNUSED_PAD src0_sel:WORD_1
	v_cvt_f32_f16_e32 v135, v30
	ds_read_b128 v[36:39], v43 offset:13312
	ds_read_b128 v[98:101], v43 offset:13328
	ds_read_b128 v[122:125], v43 offset:17408
	ds_read_b128 v[126:129], v43 offset:17424
	v_cvt_f32_f16_sdwa v97, v29 dst_sel:DWORD dst_unused:UNUSED_PAD src0_sel:WORD_1
	v_cvt_f32_f16_sdwa v133, v31 dst_sel:DWORD dst_unused:UNUSED_PAD src0_sel:WORD_1
	v_cvt_f32_f16_e32 v134, v31
	v_sub_f32_e32 v28, v28, v0
	v_sub_f32_e32 v29, v130, v1
	v_sub_f32_e32 v30, v131, v2
	v_pk_mul_f32 v[28:29], v[90:91], v[28:29]
	v_sub_f32_e32 v130, v135, v0
	v_sub_f32_e32 v131, v132, v1
	v_sub_f32_e32 v31, v97, v3
	v_sub_f32_e32 v132, v134, v2
	v_sub_f32_e32 v133, v133, v3
	v_pk_mul_f32 v[130:131], v[90:91], v[130:131]
	s_waitcnt lgkmcnt(1)
	v_fma_f32 v28, v36, v28, v122
	v_fma_f32 v29, v37, v29, v123
	v_pk_mul_f32 v[30:31], v[92:93], v[30:31]
	v_pk_mul_f32 v[132:133], v[92:93], v[132:133]
	s_waitcnt lgkmcnt(0)
	v_fma_f32 v36, v98, v130, v126
	ds_write2_b32 v220, v28, v29 offset1:65
	v_fma_f32 v28, v99, v131, v127
	ds_write2_b32 v221, v36, v28 offset1:65
	v_fma_f32 v28, v38, v30, v124
	v_fma_f32 v29, v100, v132, v128
	v_fmac_f32_e32 v125, v39, v31
	v_fmac_f32_e32 v129, v101, v133
	ds_write2_b32 v220, v28, v125 offset0:130 offset1:195
	ds_write2_b32 v221, v29, v129 offset0:130 offset1:195
	s_waitcnt vmcnt(2)
	ds_write_b128 v104, v[24:27] offset:41984
	s_mov_b32 s16, 0
	v_mov_b32_e32 v24, v112
	s_waitcnt lgkmcnt(0)
	s_barrier
	ds_read_b32 v200, v218
	ds_read_b32 v208, v219
	ds_read_b32 v201, v218 offset:520
	ds_read_b32 v209, v219 offset:256
	ds_read_b32 v202, v218 offset:1040
	ds_read_b32 v210, v219 offset:512
	ds_read_b32 v203, v218 offset:1560
	ds_read_b32 v211, v219 offset:768
	ds_read_b32 v204, v218 offset:2080
	ds_read_b32 v212, v219 offset:1024
	ds_read_b32 v205, v218 offset:2600
	ds_read_b32 v213, v219 offset:1280
	ds_read_b32 v206, v218 offset:3120
	ds_read_b32 v214, v219 offset:1536
	s_waitcnt lgkmcnt(12)
	v_mfma_f32_32x32x2_f32 v[4:19], v200, v208, v[4:19]
	ds_read_b32 v207, v218 offset:3640
	ds_read_b32 v215, v219 offset:1792
	s_waitcnt lgkmcnt(12)
	v_mfma_f32_32x32x2_f32 v[4:19], v201, v209, v[4:19]
	s_waitcnt lgkmcnt(10)
	v_mfma_f32_32x32x2_f32 v[4:19], v202, v210, v[4:19]
	s_waitcnt lgkmcnt(8)
	v_mfma_f32_32x32x2_f32 v[4:19], v203, v211, v[4:19]
	s_waitcnt lgkmcnt(6)
	v_mfma_f32_32x32x2_f32 v[4:19], v204, v212, v[4:19]
	s_waitcnt lgkmcnt(4)
	v_mfma_f32_32x32x2_f32 v[4:19], v205, v213, v[4:19]
	s_waitcnt lgkmcnt(2)
	v_mfma_f32_32x32x2_f32 v[4:19], v206, v214, v[4:19]
	s_waitcnt lgkmcnt(0)
	v_mfma_f32_32x32x2_f32 v[4:19], v207, v215, v[4:19]
	s_barrier
	global_load_dwordx4 v[28:31], v[94:95], off offset:768 sc1
	global_load_dwordx4 v[24:27], v[62:63], off
	s_waitcnt vmcnt(3)
	v_cvt_f32_f16_sdwa v130, v32 dst_sel:DWORD dst_unused:UNUSED_PAD src0_sel:WORD_1
	v_cvt_f32_f16_e32 v32, v32
	v_cvt_f32_f16_e32 v131, v33
	v_cvt_f32_f16_sdwa v132, v34 dst_sel:DWORD dst_unused:UNUSED_PAD src0_sel:WORD_1
	v_cvt_f32_f16_e32 v135, v34
	ds_read_b128 v[36:39], v43 offset:13568
	ds_read_b128 v[98:101], v43 offset:13584
	ds_read_b128 v[122:125], v43 offset:17664
	ds_read_b128 v[126:129], v43 offset:17680
	v_cvt_f32_f16_sdwa v97, v33 dst_sel:DWORD dst_unused:UNUSED_PAD src0_sel:WORD_1
	v_cvt_f32_f16_sdwa v133, v35 dst_sel:DWORD dst_unused:UNUSED_PAD src0_sel:WORD_1
	v_cvt_f32_f16_e32 v134, v35
	v_sub_f32_e32 v32, v32, v0
	v_sub_f32_e32 v33, v130, v1
	v_sub_f32_e32 v34, v131, v2
	v_pk_mul_f32 v[32:33], v[90:91], v[32:33]
	v_sub_f32_e32 v130, v135, v0
	v_sub_f32_e32 v131, v132, v1
	v_sub_f32_e32 v35, v97, v3
	v_sub_f32_e32 v132, v134, v2
	v_sub_f32_e32 v133, v133, v3
	v_pk_mul_f32 v[130:131], v[90:91], v[130:131]
	s_waitcnt lgkmcnt(1)
	v_fma_f32 v32, v36, v32, v122
	v_fma_f32 v33, v37, v33, v123
	v_pk_mul_f32 v[34:35], v[92:93], v[34:35]
	v_pk_mul_f32 v[132:133], v[92:93], v[132:133]
	s_waitcnt lgkmcnt(0)
	v_fma_f32 v36, v98, v130, v126
	ds_write2_b32 v220, v32, v33 offset1:65
	v_fma_f32 v32, v99, v131, v127
	ds_write2_b32 v221, v36, v32 offset1:65
	v_fma_f32 v32, v38, v34, v124
	v_fma_f32 v33, v100, v132, v128
	v_fmac_f32_e32 v125, v39, v35
	v_fmac_f32_e32 v129, v101, v133
	ds_write2_b32 v220, v32, v125 offset0:130 offset1:195
	ds_write2_b32 v221, v33, v129 offset0:130 offset1:195
	s_waitcnt vmcnt(2)
	ds_write_b128 v104, v[20:23] offset:41984
	s_mov_b32 s16, 0
	v_mov_b32_e32 v20, v112
	s_waitcnt lgkmcnt(0)
	s_barrier
	ds_read_b32 v200, v218
	ds_read_b32 v208, v219
	ds_read_b32 v201, v218 offset:520
	ds_read_b32 v209, v219 offset:256
	ds_read_b32 v202, v218 offset:1040
	ds_read_b32 v210, v219 offset:512
	ds_read_b32 v203, v218 offset:1560
	ds_read_b32 v211, v219 offset:768
	ds_read_b32 v204, v218 offset:2080
	ds_read_b32 v212, v219 offset:1024
	ds_read_b32 v205, v218 offset:2600
	ds_read_b32 v213, v219 offset:1280
	ds_read_b32 v206, v218 offset:3120
	ds_read_b32 v214, v219 offset:1536
	s_waitcnt lgkmcnt(12)
	v_mfma_f32_32x32x2_f32 v[4:19], v200, v208, v[4:19]
	ds_read_b32 v207, v218 offset:3640
	ds_read_b32 v215, v219 offset:1792
	s_waitcnt lgkmcnt(12)
	v_mfma_f32_32x32x2_f32 v[4:19], v201, v209, v[4:19]
	s_waitcnt lgkmcnt(10)
	v_mfma_f32_32x32x2_f32 v[4:19], v202, v210, v[4:19]
	s_waitcnt lgkmcnt(8)
	v_mfma_f32_32x32x2_f32 v[4:19], v203, v211, v[4:19]
	s_waitcnt lgkmcnt(6)
	v_mfma_f32_32x32x2_f32 v[4:19], v204, v212, v[4:19]
	s_waitcnt lgkmcnt(4)
	v_mfma_f32_32x32x2_f32 v[4:19], v205, v213, v[4:19]
	s_waitcnt lgkmcnt(2)
	v_mfma_f32_32x32x2_f32 v[4:19], v206, v214, v[4:19]
	s_waitcnt lgkmcnt(0)
	v_mfma_f32_32x32x2_f32 v[4:19], v207, v215, v[4:19]
	s_barrier
	global_load_dwordx4 v[32:35], v[94:95], off offset:896 sc1
	global_load_dwordx4 v[20:23], v[64:65], off
	s_waitcnt vmcnt(3)
	v_cvt_f32_f16_sdwa v130, v28 dst_sel:DWORD dst_unused:UNUSED_PAD src0_sel:WORD_1
	v_cvt_f32_f16_e32 v28, v28
	v_cvt_f32_f16_e32 v131, v29
	v_cvt_f32_f16_sdwa v132, v30 dst_sel:DWORD dst_unused:UNUSED_PAD src0_sel:WORD_1
	v_cvt_f32_f16_e32 v135, v30
	ds_read_b128 v[36:39], v43 offset:13824
	ds_read_b128 v[98:101], v43 offset:13840
	ds_read_b128 v[122:125], v43 offset:17920
	ds_read_b128 v[126:129], v43 offset:17936
	v_cvt_f32_f16_sdwa v97, v29 dst_sel:DWORD dst_unused:UNUSED_PAD src0_sel:WORD_1
	v_cvt_f32_f16_sdwa v133, v31 dst_sel:DWORD dst_unused:UNUSED_PAD src0_sel:WORD_1
	v_cvt_f32_f16_e32 v134, v31
	v_sub_f32_e32 v28, v28, v0
	v_sub_f32_e32 v29, v130, v1
	v_sub_f32_e32 v30, v131, v2
	v_pk_mul_f32 v[28:29], v[90:91], v[28:29]
	v_sub_f32_e32 v130, v135, v0
	v_sub_f32_e32 v131, v132, v1
	v_sub_f32_e32 v31, v97, v3
	v_sub_f32_e32 v132, v134, v2
	v_sub_f32_e32 v133, v133, v3
	v_pk_mul_f32 v[130:131], v[90:91], v[130:131]
	s_waitcnt lgkmcnt(1)
	v_fma_f32 v28, v36, v28, v122
	v_fma_f32 v29, v37, v29, v123
	v_pk_mul_f32 v[30:31], v[92:93], v[30:31]
	v_pk_mul_f32 v[132:133], v[92:93], v[132:133]
	s_waitcnt lgkmcnt(0)
	v_fma_f32 v36, v98, v130, v126
	ds_write2_b32 v220, v28, v29 offset1:65
	v_fma_f32 v28, v99, v131, v127
	ds_write2_b32 v221, v36, v28 offset1:65
	v_fma_f32 v28, v38, v30, v124
	v_fma_f32 v29, v100, v132, v128
	v_fmac_f32_e32 v125, v39, v31
	v_fmac_f32_e32 v129, v101, v133
	ds_write2_b32 v220, v28, v125 offset0:130 offset1:195
	ds_write2_b32 v221, v29, v129 offset0:130 offset1:195
	s_waitcnt vmcnt(2)
	ds_write_b128 v104, v[24:27] offset:41984
	s_mov_b32 s16, 0
	v_mov_b32_e32 v24, v112
	s_waitcnt lgkmcnt(0)
	s_barrier
	ds_read_b32 v200, v218
	ds_read_b32 v208, v219
	ds_read_b32 v201, v218 offset:520
	ds_read_b32 v209, v219 offset:256
	ds_read_b32 v202, v218 offset:1040
	ds_read_b32 v210, v219 offset:512
	ds_read_b32 v203, v218 offset:1560
	ds_read_b32 v211, v219 offset:768
	ds_read_b32 v204, v218 offset:2080
	ds_read_b32 v212, v219 offset:1024
	ds_read_b32 v205, v218 offset:2600
	ds_read_b32 v213, v219 offset:1280
	ds_read_b32 v206, v218 offset:3120
	ds_read_b32 v214, v219 offset:1536
	s_waitcnt lgkmcnt(12)
	v_mfma_f32_32x32x2_f32 v[4:19], v200, v208, v[4:19]
	ds_read_b32 v207, v218 offset:3640
	ds_read_b32 v215, v219 offset:1792
	s_waitcnt lgkmcnt(12)
	v_mfma_f32_32x32x2_f32 v[4:19], v201, v209, v[4:19]
	s_waitcnt lgkmcnt(10)
	v_mfma_f32_32x32x2_f32 v[4:19], v202, v210, v[4:19]
	s_waitcnt lgkmcnt(8)
	v_mfma_f32_32x32x2_f32 v[4:19], v203, v211, v[4:19]
	s_waitcnt lgkmcnt(6)
	v_mfma_f32_32x32x2_f32 v[4:19], v204, v212, v[4:19]
	s_waitcnt lgkmcnt(4)
	v_mfma_f32_32x32x2_f32 v[4:19], v205, v213, v[4:19]
	s_waitcnt lgkmcnt(2)
	v_mfma_f32_32x32x2_f32 v[4:19], v206, v214, v[4:19]
	s_waitcnt lgkmcnt(0)
	v_mfma_f32_32x32x2_f32 v[4:19], v207, v215, v[4:19]
	s_barrier
	global_load_dwordx4 v[28:31], v[94:95], off offset:1024 sc1
	global_load_dwordx4 v[24:27], v[66:67], off
	s_waitcnt vmcnt(3)
	v_cvt_f32_f16_sdwa v130, v32 dst_sel:DWORD dst_unused:UNUSED_PAD src0_sel:WORD_1
	v_cvt_f32_f16_e32 v32, v32
	v_cvt_f32_f16_e32 v131, v33
	v_cvt_f32_f16_sdwa v132, v34 dst_sel:DWORD dst_unused:UNUSED_PAD src0_sel:WORD_1
	v_cvt_f32_f16_e32 v135, v34
	ds_read_b128 v[36:39], v43 offset:14080
	ds_read_b128 v[98:101], v43 offset:14096
	ds_read_b128 v[122:125], v43 offset:18176
	ds_read_b128 v[126:129], v43 offset:18192
	v_cvt_f32_f16_sdwa v97, v33 dst_sel:DWORD dst_unused:UNUSED_PAD src0_sel:WORD_1
	v_cvt_f32_f16_sdwa v133, v35 dst_sel:DWORD dst_unused:UNUSED_PAD src0_sel:WORD_1
	v_cvt_f32_f16_e32 v134, v35
	v_sub_f32_e32 v32, v32, v0
	v_sub_f32_e32 v33, v130, v1
	v_sub_f32_e32 v34, v131, v2
	v_pk_mul_f32 v[32:33], v[90:91], v[32:33]
	v_sub_f32_e32 v130, v135, v0
	v_sub_f32_e32 v131, v132, v1
	v_sub_f32_e32 v35, v97, v3
	v_sub_f32_e32 v132, v134, v2
	v_sub_f32_e32 v133, v133, v3
	v_pk_mul_f32 v[130:131], v[90:91], v[130:131]
	s_waitcnt lgkmcnt(1)
	v_fma_f32 v32, v36, v32, v122
	v_fma_f32 v33, v37, v33, v123
	v_pk_mul_f32 v[34:35], v[92:93], v[34:35]
	v_pk_mul_f32 v[132:133], v[92:93], v[132:133]
	s_waitcnt lgkmcnt(0)
	v_fma_f32 v36, v98, v130, v126
	ds_write2_b32 v220, v32, v33 offset1:65
	v_fma_f32 v32, v99, v131, v127
	ds_write2_b32 v221, v36, v32 offset1:65
	v_fma_f32 v32, v38, v34, v124
	v_fma_f32 v33, v100, v132, v128
	v_fmac_f32_e32 v125, v39, v35
	v_fmac_f32_e32 v129, v101, v133
	ds_write2_b32 v220, v32, v125 offset0:130 offset1:195
	ds_write2_b32 v221, v33, v129 offset0:130 offset1:195
	s_waitcnt vmcnt(2)
	ds_write_b128 v104, v[20:23] offset:41984
	s_mov_b32 s16, 0
	v_mov_b32_e32 v20, v112
	s_waitcnt lgkmcnt(0)
	s_barrier
	ds_read_b32 v200, v218
	ds_read_b32 v208, v219
	ds_read_b32 v201, v218 offset:520
	ds_read_b32 v209, v219 offset:256
	ds_read_b32 v202, v218 offset:1040
	ds_read_b32 v210, v219 offset:512
	ds_read_b32 v203, v218 offset:1560
	ds_read_b32 v211, v219 offset:768
	ds_read_b32 v204, v218 offset:2080
	ds_read_b32 v212, v219 offset:1024
	ds_read_b32 v205, v218 offset:2600
	ds_read_b32 v213, v219 offset:1280
	ds_read_b32 v206, v218 offset:3120
	ds_read_b32 v214, v219 offset:1536
	s_waitcnt lgkmcnt(12)
	v_mfma_f32_32x32x2_f32 v[4:19], v200, v208, v[4:19]
	ds_read_b32 v207, v218 offset:3640
	ds_read_b32 v215, v219 offset:1792
	s_waitcnt lgkmcnt(12)
	v_mfma_f32_32x32x2_f32 v[4:19], v201, v209, v[4:19]
	s_waitcnt lgkmcnt(10)
	v_mfma_f32_32x32x2_f32 v[4:19], v202, v210, v[4:19]
	s_waitcnt lgkmcnt(8)
	v_mfma_f32_32x32x2_f32 v[4:19], v203, v211, v[4:19]
	s_waitcnt lgkmcnt(6)
	v_mfma_f32_32x32x2_f32 v[4:19], v204, v212, v[4:19]
	s_waitcnt lgkmcnt(4)
	v_mfma_f32_32x32x2_f32 v[4:19], v205, v213, v[4:19]
	s_waitcnt lgkmcnt(2)
	v_mfma_f32_32x32x2_f32 v[4:19], v206, v214, v[4:19]
	s_waitcnt lgkmcnt(0)
	v_mfma_f32_32x32x2_f32 v[4:19], v207, v215, v[4:19]
	s_barrier
	global_load_dwordx4 v[32:35], v[94:95], off offset:1152 sc1
	global_load_dwordx4 v[20:23], v[68:69], off
	s_waitcnt vmcnt(3)
	v_cvt_f32_f16_sdwa v130, v28 dst_sel:DWORD dst_unused:UNUSED_PAD src0_sel:WORD_1
	v_cvt_f32_f16_e32 v28, v28
	v_cvt_f32_f16_e32 v131, v29
	v_cvt_f32_f16_sdwa v132, v30 dst_sel:DWORD dst_unused:UNUSED_PAD src0_sel:WORD_1
	v_cvt_f32_f16_e32 v135, v30
	ds_read_b128 v[36:39], v43 offset:14336
	ds_read_b128 v[98:101], v43 offset:14352
	ds_read_b128 v[122:125], v43 offset:18432
	ds_read_b128 v[126:129], v43 offset:18448
	v_cvt_f32_f16_sdwa v97, v29 dst_sel:DWORD dst_unused:UNUSED_PAD src0_sel:WORD_1
	v_cvt_f32_f16_sdwa v133, v31 dst_sel:DWORD dst_unused:UNUSED_PAD src0_sel:WORD_1
	v_cvt_f32_f16_e32 v134, v31
	v_sub_f32_e32 v28, v28, v0
	v_sub_f32_e32 v29, v130, v1
	v_sub_f32_e32 v30, v131, v2
	v_pk_mul_f32 v[28:29], v[90:91], v[28:29]
	v_sub_f32_e32 v130, v135, v0
	v_sub_f32_e32 v131, v132, v1
	v_sub_f32_e32 v31, v97, v3
	v_sub_f32_e32 v132, v134, v2
	v_sub_f32_e32 v133, v133, v3
	v_pk_mul_f32 v[130:131], v[90:91], v[130:131]
	s_waitcnt lgkmcnt(1)
	v_fma_f32 v28, v36, v28, v122
	v_fma_f32 v29, v37, v29, v123
	v_pk_mul_f32 v[30:31], v[92:93], v[30:31]
	v_pk_mul_f32 v[132:133], v[92:93], v[132:133]
	s_waitcnt lgkmcnt(0)
	v_fma_f32 v36, v98, v130, v126
	ds_write2_b32 v220, v28, v29 offset1:65
	v_fma_f32 v28, v99, v131, v127
	ds_write2_b32 v221, v36, v28 offset1:65
	v_fma_f32 v28, v38, v30, v124
	v_fma_f32 v29, v100, v132, v128
	v_fmac_f32_e32 v125, v39, v31
	v_fmac_f32_e32 v129, v101, v133
	ds_write2_b32 v220, v28, v125 offset0:130 offset1:195
	ds_write2_b32 v221, v29, v129 offset0:130 offset1:195
	s_waitcnt vmcnt(2)
	ds_write_b128 v104, v[24:27] offset:41984
	s_mov_b32 s16, 0
	v_mov_b32_e32 v24, v112
	s_waitcnt lgkmcnt(0)
	s_barrier
	ds_read_b32 v200, v218
	ds_read_b32 v208, v219
	ds_read_b32 v201, v218 offset:520
	ds_read_b32 v209, v219 offset:256
	ds_read_b32 v202, v218 offset:1040
	ds_read_b32 v210, v219 offset:512
	ds_read_b32 v203, v218 offset:1560
	ds_read_b32 v211, v219 offset:768
	ds_read_b32 v204, v218 offset:2080
	ds_read_b32 v212, v219 offset:1024
	ds_read_b32 v205, v218 offset:2600
	ds_read_b32 v213, v219 offset:1280
	ds_read_b32 v206, v218 offset:3120
	ds_read_b32 v214, v219 offset:1536
	s_waitcnt lgkmcnt(12)
	v_mfma_f32_32x32x2_f32 v[4:19], v200, v208, v[4:19]
	ds_read_b32 v207, v218 offset:3640
	ds_read_b32 v215, v219 offset:1792
	s_waitcnt lgkmcnt(12)
	v_mfma_f32_32x32x2_f32 v[4:19], v201, v209, v[4:19]
	s_waitcnt lgkmcnt(10)
	v_mfma_f32_32x32x2_f32 v[4:19], v202, v210, v[4:19]
	s_waitcnt lgkmcnt(8)
	v_mfma_f32_32x32x2_f32 v[4:19], v203, v211, v[4:19]
	s_waitcnt lgkmcnt(6)
	v_mfma_f32_32x32x2_f32 v[4:19], v204, v212, v[4:19]
	s_waitcnt lgkmcnt(4)
	v_mfma_f32_32x32x2_f32 v[4:19], v205, v213, v[4:19]
	s_waitcnt lgkmcnt(2)
	v_mfma_f32_32x32x2_f32 v[4:19], v206, v214, v[4:19]
	s_waitcnt lgkmcnt(0)
	v_mfma_f32_32x32x2_f32 v[4:19], v207, v215, v[4:19]
	s_barrier
	global_load_dwordx4 v[28:31], v[94:95], off offset:1280 sc1
	global_load_dwordx4 v[24:27], v[70:71], off
	s_waitcnt vmcnt(3)
	v_cvt_f32_f16_sdwa v130, v32 dst_sel:DWORD dst_unused:UNUSED_PAD src0_sel:WORD_1
	v_cvt_f32_f16_e32 v32, v32
	v_cvt_f32_f16_e32 v131, v33
	v_cvt_f32_f16_sdwa v132, v34 dst_sel:DWORD dst_unused:UNUSED_PAD src0_sel:WORD_1
	v_cvt_f32_f16_e32 v135, v34
	ds_read_b128 v[36:39], v43 offset:14592
	ds_read_b128 v[98:101], v43 offset:14608
	ds_read_b128 v[122:125], v43 offset:18688
	ds_read_b128 v[126:129], v43 offset:18704
	v_cvt_f32_f16_sdwa v97, v33 dst_sel:DWORD dst_unused:UNUSED_PAD src0_sel:WORD_1
	v_cvt_f32_f16_sdwa v133, v35 dst_sel:DWORD dst_unused:UNUSED_PAD src0_sel:WORD_1
	v_cvt_f32_f16_e32 v134, v35
	v_sub_f32_e32 v32, v32, v0
	v_sub_f32_e32 v33, v130, v1
	v_sub_f32_e32 v34, v131, v2
	v_pk_mul_f32 v[32:33], v[90:91], v[32:33]
	v_sub_f32_e32 v130, v135, v0
	v_sub_f32_e32 v131, v132, v1
	v_sub_f32_e32 v35, v97, v3
	v_sub_f32_e32 v132, v134, v2
	v_sub_f32_e32 v133, v133, v3
	v_pk_mul_f32 v[130:131], v[90:91], v[130:131]
	s_waitcnt lgkmcnt(1)
	v_fma_f32 v32, v36, v32, v122
	v_fma_f32 v33, v37, v33, v123
	v_pk_mul_f32 v[34:35], v[92:93], v[34:35]
	v_pk_mul_f32 v[132:133], v[92:93], v[132:133]
	s_waitcnt lgkmcnt(0)
	v_fma_f32 v36, v98, v130, v126
	ds_write2_b32 v220, v32, v33 offset1:65
	v_fma_f32 v32, v99, v131, v127
	ds_write2_b32 v221, v36, v32 offset1:65
	v_fma_f32 v32, v38, v34, v124
	v_fma_f32 v33, v100, v132, v128
	v_fmac_f32_e32 v125, v39, v35
	v_fmac_f32_e32 v129, v101, v133
	ds_write2_b32 v220, v32, v125 offset0:130 offset1:195
	ds_write2_b32 v221, v33, v129 offset0:130 offset1:195
	s_waitcnt vmcnt(2)
	ds_write_b128 v104, v[20:23] offset:41984
	s_mov_b32 s16, 0
	v_mov_b32_e32 v20, v112
	s_waitcnt lgkmcnt(0)
	s_barrier
	ds_read_b32 v200, v218
	ds_read_b32 v208, v219
	ds_read_b32 v201, v218 offset:520
	ds_read_b32 v209, v219 offset:256
	ds_read_b32 v202, v218 offset:1040
	ds_read_b32 v210, v219 offset:512
	ds_read_b32 v203, v218 offset:1560
	ds_read_b32 v211, v219 offset:768
	ds_read_b32 v204, v218 offset:2080
	ds_read_b32 v212, v219 offset:1024
	ds_read_b32 v205, v218 offset:2600
	ds_read_b32 v213, v219 offset:1280
	ds_read_b32 v206, v218 offset:3120
	ds_read_b32 v214, v219 offset:1536
	s_waitcnt lgkmcnt(12)
	v_mfma_f32_32x32x2_f32 v[4:19], v200, v208, v[4:19]
	ds_read_b32 v207, v218 offset:3640
	ds_read_b32 v215, v219 offset:1792
	s_waitcnt lgkmcnt(12)
	v_mfma_f32_32x32x2_f32 v[4:19], v201, v209, v[4:19]
	s_waitcnt lgkmcnt(10)
	v_mfma_f32_32x32x2_f32 v[4:19], v202, v210, v[4:19]
	s_waitcnt lgkmcnt(8)
	v_mfma_f32_32x32x2_f32 v[4:19], v203, v211, v[4:19]
	s_waitcnt lgkmcnt(6)
	v_mfma_f32_32x32x2_f32 v[4:19], v204, v212, v[4:19]
	s_waitcnt lgkmcnt(4)
	v_mfma_f32_32x32x2_f32 v[4:19], v205, v213, v[4:19]
	s_waitcnt lgkmcnt(2)
	v_mfma_f32_32x32x2_f32 v[4:19], v206, v214, v[4:19]
	s_waitcnt lgkmcnt(0)
	v_mfma_f32_32x32x2_f32 v[4:19], v207, v215, v[4:19]
	s_barrier
	global_load_dwordx4 v[32:35], v[94:95], off offset:1408 sc1
	global_load_dwordx4 v[20:23], v[72:73], off
	s_waitcnt vmcnt(3)
	v_cvt_f32_f16_sdwa v130, v28 dst_sel:DWORD dst_unused:UNUSED_PAD src0_sel:WORD_1
	v_cvt_f32_f16_e32 v28, v28
	v_cvt_f32_f16_e32 v131, v29
	v_cvt_f32_f16_sdwa v132, v30 dst_sel:DWORD dst_unused:UNUSED_PAD src0_sel:WORD_1
	v_cvt_f32_f16_e32 v135, v30
	ds_read_b128 v[36:39], v43 offset:14848
	ds_read_b128 v[98:101], v43 offset:14864
	ds_read_b128 v[122:125], v43 offset:18944
	ds_read_b128 v[126:129], v43 offset:18960
	v_cvt_f32_f16_sdwa v97, v29 dst_sel:DWORD dst_unused:UNUSED_PAD src0_sel:WORD_1
	v_cvt_f32_f16_sdwa v133, v31 dst_sel:DWORD dst_unused:UNUSED_PAD src0_sel:WORD_1
	v_cvt_f32_f16_e32 v134, v31
	v_sub_f32_e32 v28, v28, v0
	v_sub_f32_e32 v29, v130, v1
	v_sub_f32_e32 v30, v131, v2
	v_pk_mul_f32 v[28:29], v[90:91], v[28:29]
	v_sub_f32_e32 v130, v135, v0
	v_sub_f32_e32 v131, v132, v1
	v_sub_f32_e32 v31, v97, v3
	v_sub_f32_e32 v132, v134, v2
	v_sub_f32_e32 v133, v133, v3
	v_pk_mul_f32 v[130:131], v[90:91], v[130:131]
	s_waitcnt lgkmcnt(1)
	v_fma_f32 v28, v36, v28, v122
	v_fma_f32 v29, v37, v29, v123
	v_pk_mul_f32 v[30:31], v[92:93], v[30:31]
	v_pk_mul_f32 v[132:133], v[92:93], v[132:133]
	s_waitcnt lgkmcnt(0)
	v_fma_f32 v36, v98, v130, v126
	ds_write2_b32 v220, v28, v29 offset1:65
	v_fma_f32 v28, v99, v131, v127
	ds_write2_b32 v221, v36, v28 offset1:65
	v_fma_f32 v28, v38, v30, v124
	v_fma_f32 v29, v100, v132, v128
	v_fmac_f32_e32 v125, v39, v31
	v_fmac_f32_e32 v129, v101, v133
	ds_write2_b32 v220, v28, v125 offset0:130 offset1:195
	ds_write2_b32 v221, v29, v129 offset0:130 offset1:195
	s_waitcnt vmcnt(2)
	ds_write_b128 v104, v[24:27] offset:41984
	s_mov_b32 s16, 0
	v_mov_b32_e32 v24, v112
	s_waitcnt lgkmcnt(0)
	s_barrier
	ds_read_b32 v200, v218
	ds_read_b32 v208, v219
	ds_read_b32 v201, v218 offset:520
	ds_read_b32 v209, v219 offset:256
	ds_read_b32 v202, v218 offset:1040
	ds_read_b32 v210, v219 offset:512
	ds_read_b32 v203, v218 offset:1560
	ds_read_b32 v211, v219 offset:768
	ds_read_b32 v204, v218 offset:2080
	ds_read_b32 v212, v219 offset:1024
	ds_read_b32 v205, v218 offset:2600
	ds_read_b32 v213, v219 offset:1280
	ds_read_b32 v206, v218 offset:3120
	ds_read_b32 v214, v219 offset:1536
	s_waitcnt lgkmcnt(12)
	v_mfma_f32_32x32x2_f32 v[4:19], v200, v208, v[4:19]
	ds_read_b32 v207, v218 offset:3640
	ds_read_b32 v215, v219 offset:1792
	s_waitcnt lgkmcnt(12)
	v_mfma_f32_32x32x2_f32 v[4:19], v201, v209, v[4:19]
	s_waitcnt lgkmcnt(10)
	v_mfma_f32_32x32x2_f32 v[4:19], v202, v210, v[4:19]
	s_waitcnt lgkmcnt(8)
	v_mfma_f32_32x32x2_f32 v[4:19], v203, v211, v[4:19]
	s_waitcnt lgkmcnt(6)
	v_mfma_f32_32x32x2_f32 v[4:19], v204, v212, v[4:19]
	s_waitcnt lgkmcnt(4)
	v_mfma_f32_32x32x2_f32 v[4:19], v205, v213, v[4:19]
	s_waitcnt lgkmcnt(2)
	v_mfma_f32_32x32x2_f32 v[4:19], v206, v214, v[4:19]
	s_waitcnt lgkmcnt(0)
	v_mfma_f32_32x32x2_f32 v[4:19], v207, v215, v[4:19]
	s_barrier
	global_load_dwordx4 v[28:31], v[94:95], off offset:1536 sc1
	global_load_dwordx4 v[24:27], v[74:75], off
	s_waitcnt vmcnt(3)
	v_cvt_f32_f16_sdwa v130, v32 dst_sel:DWORD dst_unused:UNUSED_PAD src0_sel:WORD_1
	v_cvt_f32_f16_e32 v32, v32
	v_cvt_f32_f16_e32 v131, v33
	v_cvt_f32_f16_sdwa v132, v34 dst_sel:DWORD dst_unused:UNUSED_PAD src0_sel:WORD_1
	v_cvt_f32_f16_e32 v135, v34
	ds_read_b128 v[36:39], v43 offset:15104
	ds_read_b128 v[98:101], v43 offset:15120
	ds_read_b128 v[122:125], v43 offset:19200
	ds_read_b128 v[126:129], v43 offset:19216
	v_cvt_f32_f16_sdwa v97, v33 dst_sel:DWORD dst_unused:UNUSED_PAD src0_sel:WORD_1
	v_cvt_f32_f16_sdwa v133, v35 dst_sel:DWORD dst_unused:UNUSED_PAD src0_sel:WORD_1
	v_cvt_f32_f16_e32 v134, v35
	v_sub_f32_e32 v32, v32, v0
	v_sub_f32_e32 v33, v130, v1
	v_sub_f32_e32 v34, v131, v2
	v_pk_mul_f32 v[32:33], v[90:91], v[32:33]
	v_sub_f32_e32 v130, v135, v0
	v_sub_f32_e32 v131, v132, v1
	v_sub_f32_e32 v35, v97, v3
	v_sub_f32_e32 v132, v134, v2
	v_sub_f32_e32 v133, v133, v3
	v_pk_mul_f32 v[130:131], v[90:91], v[130:131]
	s_waitcnt lgkmcnt(1)
	v_fma_f32 v32, v36, v32, v122
	v_fma_f32 v33, v37, v33, v123
	v_pk_mul_f32 v[34:35], v[92:93], v[34:35]
	v_pk_mul_f32 v[132:133], v[92:93], v[132:133]
	s_waitcnt lgkmcnt(0)
	v_fma_f32 v36, v98, v130, v126
	ds_write2_b32 v220, v32, v33 offset1:65
	v_fma_f32 v32, v99, v131, v127
	ds_write2_b32 v221, v36, v32 offset1:65
	v_fma_f32 v32, v38, v34, v124
	v_fma_f32 v33, v100, v132, v128
	v_fmac_f32_e32 v125, v39, v35
	v_fmac_f32_e32 v129, v101, v133
	ds_write2_b32 v220, v32, v125 offset0:130 offset1:195
	ds_write2_b32 v221, v33, v129 offset0:130 offset1:195
	s_waitcnt vmcnt(2)
	ds_write_b128 v104, v[20:23] offset:41984
	s_mov_b32 s16, 0
	v_mov_b32_e32 v20, v112
	s_waitcnt lgkmcnt(0)
	s_barrier
	ds_read_b32 v200, v218
	ds_read_b32 v208, v219
	ds_read_b32 v201, v218 offset:520
	ds_read_b32 v209, v219 offset:256
	ds_read_b32 v202, v218 offset:1040
	ds_read_b32 v210, v219 offset:512
	ds_read_b32 v203, v218 offset:1560
	ds_read_b32 v211, v219 offset:768
	ds_read_b32 v204, v218 offset:2080
	ds_read_b32 v212, v219 offset:1024
	ds_read_b32 v205, v218 offset:2600
	ds_read_b32 v213, v219 offset:1280
	ds_read_b32 v206, v218 offset:3120
	ds_read_b32 v214, v219 offset:1536
	s_waitcnt lgkmcnt(12)
	v_mfma_f32_32x32x2_f32 v[4:19], v200, v208, v[4:19]
	ds_read_b32 v207, v218 offset:3640
	ds_read_b32 v215, v219 offset:1792
	s_waitcnt lgkmcnt(12)
	v_mfma_f32_32x32x2_f32 v[4:19], v201, v209, v[4:19]
	s_waitcnt lgkmcnt(10)
	v_mfma_f32_32x32x2_f32 v[4:19], v202, v210, v[4:19]
	s_waitcnt lgkmcnt(8)
	v_mfma_f32_32x32x2_f32 v[4:19], v203, v211, v[4:19]
	s_waitcnt lgkmcnt(6)
	v_mfma_f32_32x32x2_f32 v[4:19], v204, v212, v[4:19]
	s_waitcnt lgkmcnt(4)
	v_mfma_f32_32x32x2_f32 v[4:19], v205, v213, v[4:19]
	s_waitcnt lgkmcnt(2)
	v_mfma_f32_32x32x2_f32 v[4:19], v206, v214, v[4:19]
	s_waitcnt lgkmcnt(0)
	v_mfma_f32_32x32x2_f32 v[4:19], v207, v215, v[4:19]
	s_barrier
	global_load_dwordx4 v[32:35], v[94:95], off offset:1664 sc1
	global_load_dwordx4 v[20:23], v[76:77], off
	s_waitcnt vmcnt(3)
	v_cvt_f32_f16_sdwa v130, v28 dst_sel:DWORD dst_unused:UNUSED_PAD src0_sel:WORD_1
	v_cvt_f32_f16_e32 v28, v28
	v_cvt_f32_f16_e32 v131, v29
	v_cvt_f32_f16_sdwa v132, v30 dst_sel:DWORD dst_unused:UNUSED_PAD src0_sel:WORD_1
	v_cvt_f32_f16_e32 v135, v30
	ds_read_b128 v[36:39], v43 offset:15360
	ds_read_b128 v[98:101], v43 offset:15376
	ds_read_b128 v[122:125], v43 offset:19456
	ds_read_b128 v[126:129], v43 offset:19472
	v_cvt_f32_f16_sdwa v97, v29 dst_sel:DWORD dst_unused:UNUSED_PAD src0_sel:WORD_1
	v_cvt_f32_f16_sdwa v133, v31 dst_sel:DWORD dst_unused:UNUSED_PAD src0_sel:WORD_1
	v_cvt_f32_f16_e32 v134, v31
	v_sub_f32_e32 v28, v28, v0
	v_sub_f32_e32 v29, v130, v1
	v_sub_f32_e32 v30, v131, v2
	v_pk_mul_f32 v[28:29], v[90:91], v[28:29]
	v_sub_f32_e32 v130, v135, v0
	v_sub_f32_e32 v131, v132, v1
	v_sub_f32_e32 v31, v97, v3
	v_sub_f32_e32 v132, v134, v2
	v_sub_f32_e32 v133, v133, v3
	v_pk_mul_f32 v[130:131], v[90:91], v[130:131]
	s_waitcnt lgkmcnt(1)
	v_fma_f32 v28, v36, v28, v122
	v_fma_f32 v29, v37, v29, v123
	v_pk_mul_f32 v[30:31], v[92:93], v[30:31]
	v_pk_mul_f32 v[132:133], v[92:93], v[132:133]
	s_waitcnt lgkmcnt(0)
	v_fma_f32 v36, v98, v130, v126
	ds_write2_b32 v220, v28, v29 offset1:65
	v_fma_f32 v28, v99, v131, v127
	ds_write2_b32 v221, v36, v28 offset1:65
	v_fma_f32 v28, v38, v30, v124
	v_fma_f32 v29, v100, v132, v128
	v_fmac_f32_e32 v125, v39, v31
	v_fmac_f32_e32 v129, v101, v133
	ds_write2_b32 v220, v28, v125 offset0:130 offset1:195
	ds_write2_b32 v221, v29, v129 offset0:130 offset1:195
	s_waitcnt vmcnt(2)
	ds_write_b128 v104, v[24:27] offset:41984
	s_mov_b32 s16, 0
	v_mov_b32_e32 v24, v112
	s_waitcnt lgkmcnt(0)
	s_barrier
	ds_read_b32 v200, v218
	ds_read_b32 v208, v219
	ds_read_b32 v201, v218 offset:520
	ds_read_b32 v209, v219 offset:256
	ds_read_b32 v202, v218 offset:1040
	ds_read_b32 v210, v219 offset:512
	ds_read_b32 v203, v218 offset:1560
	ds_read_b32 v211, v219 offset:768
	ds_read_b32 v204, v218 offset:2080
	ds_read_b32 v212, v219 offset:1024
	ds_read_b32 v205, v218 offset:2600
	ds_read_b32 v213, v219 offset:1280
	ds_read_b32 v206, v218 offset:3120
	ds_read_b32 v214, v219 offset:1536
	s_waitcnt lgkmcnt(12)
	v_mfma_f32_32x32x2_f32 v[4:19], v200, v208, v[4:19]
	ds_read_b32 v207, v218 offset:3640
	ds_read_b32 v215, v219 offset:1792
	s_waitcnt lgkmcnt(12)
	v_mfma_f32_32x32x2_f32 v[4:19], v201, v209, v[4:19]
	s_waitcnt lgkmcnt(10)
	v_mfma_f32_32x32x2_f32 v[4:19], v202, v210, v[4:19]
	s_waitcnt lgkmcnt(8)
	v_mfma_f32_32x32x2_f32 v[4:19], v203, v211, v[4:19]
	s_waitcnt lgkmcnt(6)
	v_mfma_f32_32x32x2_f32 v[4:19], v204, v212, v[4:19]
	s_waitcnt lgkmcnt(4)
	v_mfma_f32_32x32x2_f32 v[4:19], v205, v213, v[4:19]
	s_waitcnt lgkmcnt(2)
	v_mfma_f32_32x32x2_f32 v[4:19], v206, v214, v[4:19]
	s_waitcnt lgkmcnt(0)
	v_mfma_f32_32x32x2_f32 v[4:19], v207, v215, v[4:19]
	s_barrier
	global_load_dwordx4 v[28:31], v[94:95], off offset:1792 sc1
	global_load_dwordx4 v[24:27], v[78:79], off
	s_waitcnt vmcnt(3)
	v_cvt_f32_f16_sdwa v130, v32 dst_sel:DWORD dst_unused:UNUSED_PAD src0_sel:WORD_1
	v_cvt_f32_f16_e32 v32, v32
	v_cvt_f32_f16_e32 v131, v33
	v_cvt_f32_f16_sdwa v132, v34 dst_sel:DWORD dst_unused:UNUSED_PAD src0_sel:WORD_1
	v_cvt_f32_f16_e32 v135, v34
	ds_read_b128 v[36:39], v43 offset:15616
	ds_read_b128 v[98:101], v43 offset:15632
	ds_read_b128 v[122:125], v43 offset:19712
	ds_read_b128 v[126:129], v43 offset:19728
	v_cvt_f32_f16_sdwa v97, v33 dst_sel:DWORD dst_unused:UNUSED_PAD src0_sel:WORD_1
	v_cvt_f32_f16_sdwa v133, v35 dst_sel:DWORD dst_unused:UNUSED_PAD src0_sel:WORD_1
	v_cvt_f32_f16_e32 v134, v35
	v_sub_f32_e32 v32, v32, v0
	v_sub_f32_e32 v33, v130, v1
	v_sub_f32_e32 v34, v131, v2
	v_pk_mul_f32 v[32:33], v[90:91], v[32:33]
	v_sub_f32_e32 v130, v135, v0
	v_sub_f32_e32 v131, v132, v1
	v_sub_f32_e32 v35, v97, v3
	v_sub_f32_e32 v132, v134, v2
	v_sub_f32_e32 v133, v133, v3
	v_pk_mul_f32 v[130:131], v[90:91], v[130:131]
	s_waitcnt lgkmcnt(1)
	v_fma_f32 v32, v36, v32, v122
	v_fma_f32 v33, v37, v33, v123
	v_pk_mul_f32 v[34:35], v[92:93], v[34:35]
	v_pk_mul_f32 v[132:133], v[92:93], v[132:133]
	s_waitcnt lgkmcnt(0)
	v_fma_f32 v36, v98, v130, v126
	ds_write2_b32 v220, v32, v33 offset1:65
	v_fma_f32 v32, v99, v131, v127
	ds_write2_b32 v221, v36, v32 offset1:65
	v_fma_f32 v32, v38, v34, v124
	v_fma_f32 v33, v100, v132, v128
	v_fmac_f32_e32 v125, v39, v35
	v_fmac_f32_e32 v129, v101, v133
	ds_write2_b32 v220, v32, v125 offset0:130 offset1:195
	ds_write2_b32 v221, v33, v129 offset0:130 offset1:195
	s_waitcnt vmcnt(2)
	ds_write_b128 v104, v[20:23] offset:41984
	s_mov_b32 s16, 0
	v_mov_b32_e32 v20, v112
	s_waitcnt lgkmcnt(0)
	s_barrier
	ds_read_b32 v200, v218
	ds_read_b32 v208, v219
	ds_read_b32 v201, v218 offset:520
	ds_read_b32 v209, v219 offset:256
	ds_read_b32 v202, v218 offset:1040
	ds_read_b32 v210, v219 offset:512
	ds_read_b32 v203, v218 offset:1560
	ds_read_b32 v211, v219 offset:768
	ds_read_b32 v204, v218 offset:2080
	ds_read_b32 v212, v219 offset:1024
	ds_read_b32 v205, v218 offset:2600
	ds_read_b32 v213, v219 offset:1280
	ds_read_b32 v206, v218 offset:3120
	ds_read_b32 v214, v219 offset:1536
	s_waitcnt lgkmcnt(12)
	v_mfma_f32_32x32x2_f32 v[4:19], v200, v208, v[4:19]
	ds_read_b32 v207, v218 offset:3640
	ds_read_b32 v215, v219 offset:1792
	s_waitcnt lgkmcnt(12)
	v_mfma_f32_32x32x2_f32 v[4:19], v201, v209, v[4:19]
	s_waitcnt lgkmcnt(10)
	v_mfma_f32_32x32x2_f32 v[4:19], v202, v210, v[4:19]
	s_waitcnt lgkmcnt(8)
	v_mfma_f32_32x32x2_f32 v[4:19], v203, v211, v[4:19]
	s_waitcnt lgkmcnt(6)
	v_mfma_f32_32x32x2_f32 v[4:19], v204, v212, v[4:19]
	s_waitcnt lgkmcnt(4)
	v_mfma_f32_32x32x2_f32 v[4:19], v205, v213, v[4:19]
	s_waitcnt lgkmcnt(2)
	v_mfma_f32_32x32x2_f32 v[4:19], v206, v214, v[4:19]
	s_waitcnt lgkmcnt(0)
	v_mfma_f32_32x32x2_f32 v[4:19], v207, v215, v[4:19]
	s_barrier
	global_load_dwordx4 v[32:35], v[94:95], off offset:1920 sc1
	global_load_dwordx4 v[20:23], v[80:81], off
	s_waitcnt vmcnt(3)
	v_cvt_f32_f16_sdwa v95, v28 dst_sel:DWORD dst_unused:UNUSED_PAD src0_sel:WORD_1
	v_cvt_f32_f16_e32 v28, v28
	v_cvt_f32_f16_sdwa v94, v29 dst_sel:DWORD dst_unused:UNUSED_PAD src0_sel:WORD_1
	v_cvt_f32_f16_sdwa v130, v30 dst_sel:DWORD dst_unused:UNUSED_PAD src0_sel:WORD_1
	v_cvt_f32_f16_e32 v133, v30
	ds_read_b128 v[36:39], v43 offset:15872
	ds_read_b128 v[98:101], v43 offset:15888
	ds_read_b128 v[122:125], v43 offset:19968
	ds_read_b128 v[126:129], v43 offset:19984
	v_cvt_f32_f16_e32 v97, v29
	v_cvt_f32_f16_sdwa v131, v31 dst_sel:DWORD dst_unused:UNUSED_PAD src0_sel:WORD_1
	v_cvt_f32_f16_e32 v132, v31
	v_sub_f32_e32 v28, v28, v0
	v_sub_f32_e32 v29, v95, v1
	v_sub_f32_e32 v31, v94, v3
	v_pk_mul_f32 v[28:29], v[90:91], v[28:29]
	v_sub_f32_e32 v94, v133, v0
	v_sub_f32_e32 v95, v130, v1
	v_sub_f32_e32 v30, v97, v2
	v_sub_f32_e32 v130, v132, v2
	v_sub_f32_e32 v131, v131, v3
	v_pk_mul_f32 v[94:95], v[90:91], v[94:95]
	s_waitcnt lgkmcnt(1)
	v_fma_f32 v28, v36, v28, v122
	v_fma_f32 v29, v37, v29, v123
	v_pk_mul_f32 v[30:31], v[92:93], v[30:31]
	v_pk_mul_f32 v[130:131], v[92:93], v[130:131]
	s_waitcnt lgkmcnt(0)
	v_fma_f32 v36, v98, v94, v126
	ds_write2_b32 v220, v28, v29 offset1:65
	v_fma_f32 v28, v99, v95, v127
	ds_write2_b32 v221, v36, v28 offset1:65
	v_fma_f32 v28, v38, v30, v124
	v_fma_f32 v29, v100, v130, v128
	v_fmac_f32_e32 v125, v39, v31
	v_fmac_f32_e32 v129, v101, v131
	ds_write2_b32 v220, v28, v125 offset0:130 offset1:195
	ds_write2_b32 v221, v29, v129 offset0:130 offset1:195
	s_waitcnt vmcnt(2)
	ds_write_b128 v104, v[24:27] offset:41984
	s_mov_b32 s16, 0
	v_mov_b32_e32 v24, v112
	s_waitcnt lgkmcnt(0)
	s_barrier
	ds_read_b32 v200, v218
	ds_read_b32 v208, v219
	ds_read_b32 v201, v218 offset:520
	ds_read_b32 v209, v219 offset:256
	ds_read_b32 v202, v218 offset:1040
	ds_read_b32 v210, v219 offset:512
	ds_read_b32 v203, v218 offset:1560
	ds_read_b32 v211, v219 offset:768
	ds_read_b32 v204, v218 offset:2080
	ds_read_b32 v212, v219 offset:1024
	ds_read_b32 v205, v218 offset:2600
	ds_read_b32 v213, v219 offset:1280
	ds_read_b32 v206, v218 offset:3120
	ds_read_b32 v214, v219 offset:1536
	s_waitcnt lgkmcnt(12)
	v_mfma_f32_32x32x2_f32 v[4:19], v200, v208, v[4:19]
	ds_read_b32 v207, v218 offset:3640
	ds_read_b32 v215, v219 offset:1792
	s_waitcnt lgkmcnt(12)
	v_mfma_f32_32x32x2_f32 v[4:19], v201, v209, v[4:19]
	s_waitcnt lgkmcnt(10)
	v_mfma_f32_32x32x2_f32 v[4:19], v202, v210, v[4:19]
	s_waitcnt lgkmcnt(8)
	v_mfma_f32_32x32x2_f32 v[4:19], v203, v211, v[4:19]
	s_waitcnt lgkmcnt(6)
	v_mfma_f32_32x32x2_f32 v[4:19], v204, v212, v[4:19]
	s_waitcnt lgkmcnt(4)
	v_mfma_f32_32x32x2_f32 v[4:19], v205, v213, v[4:19]
	s_waitcnt lgkmcnt(2)
	v_mfma_f32_32x32x2_f32 v[4:19], v206, v214, v[4:19]
	s_waitcnt lgkmcnt(0)
	v_mfma_f32_32x32x2_f32 v[4:19], v207, v215, v[4:19]
	s_waitcnt vmcnt(1)
	v_cvt_f32_f16_sdwa v95, v32 dst_sel:DWORD dst_unused:UNUSED_PAD src0_sel:WORD_1
	v_cvt_f32_f16_e32 v32, v32
	v_cvt_f32_f16_sdwa v123, v34 dst_sel:DWORD dst_unused:UNUSED_PAD src0_sel:WORD_1
	v_cvt_f32_f16_e32 v125, v34
	s_barrier
	ds_read_b128 v[24:27], v43 offset:16128
	ds_read_b128 v[28:31], v43 offset:16144
	ds_read_b128 v[36:39], v43 offset:20224
	ds_read_b128 v[98:101], v43 offset:20240
	v_cvt_f32_f16_sdwa v94, v33 dst_sel:DWORD dst_unused:UNUSED_PAD src0_sel:WORD_1
	v_cvt_f32_f16_e32 v97, v33
	v_cvt_f32_f16_sdwa v122, v35 dst_sel:DWORD dst_unused:UNUSED_PAD src0_sel:WORD_1
	v_cvt_f32_f16_e32 v124, v35
	v_sub_f32_e32 v32, v32, v0
	v_sub_f32_e32 v33, v95, v1
	v_sub_f32_e32 v0, v125, v0
	v_sub_f32_e32 v1, v123, v1
	v_sub_f32_e32 v34, v97, v2
	v_sub_f32_e32 v35, v94, v3
	v_pk_mul_f32 v[0:1], v[90:91], v[0:1]
	v_pk_mul_f32 v[34:35], v[92:93], v[34:35]
	v_sub_f32_e32 v2, v124, v2
	v_sub_f32_e32 v3, v122, v3
	s_waitcnt lgkmcnt(0)
	v_fma_f32 v0, v28, v0, v98
	v_fma_f32 v1, v29, v1, v99
	v_pk_mul_f32 v[32:33], v[90:91], v[32:33]
	v_pk_mul_f32 v[2:3], v[92:93], v[2:3]
	ds_write2_b32 v221, v0, v1 offset1:65
	v_fma_f32 v0, v26, v34, v38
	v_fmac_f32_e32 v39, v27, v35
	v_fma_f32 v24, v24, v32, v36
	v_fma_f32 v25, v25, v33, v37
	v_fma_f32 v1, v30, v2, v100
	ds_write2_b32 v220, v0, v39 offset0:130 offset1:195
	v_fmac_f32_e32 v101, v31, v3
	s_mov_b32 s16, 0
	v_mov_b32_e32 v0, v112
	ds_write2_b32 v220, v24, v25 offset1:65
	ds_write2_b32 v221, v1, v101 offset0:130 offset1:195
	s_waitcnt vmcnt(0)
	ds_write_b128 v104, v[20:23] offset:41984
	s_waitcnt lgkmcnt(0)
	s_barrier
	ds_read_b32 v200, v218
	ds_read_b32 v208, v219
	ds_read_b32 v201, v218 offset:520
	ds_read_b32 v209, v219 offset:256
	ds_read_b32 v202, v218 offset:1040
	ds_read_b32 v210, v219 offset:512
	ds_read_b32 v203, v218 offset:1560
	ds_read_b32 v211, v219 offset:768
	ds_read_b32 v204, v218 offset:2080
	ds_read_b32 v212, v219 offset:1024
	ds_read_b32 v205, v218 offset:2600
	ds_read_b32 v213, v219 offset:1280
	ds_read_b32 v206, v218 offset:3120
	ds_read_b32 v214, v219 offset:1536
	s_waitcnt lgkmcnt(12)
	v_mfma_f32_32x32x2_f32 v[4:19], v200, v208, v[4:19]
	ds_read_b32 v207, v218 offset:3640
	ds_read_b32 v215, v219 offset:1792
	s_waitcnt lgkmcnt(12)
	v_mfma_f32_32x32x2_f32 v[4:19], v201, v209, v[4:19]
	s_waitcnt lgkmcnt(10)
	v_mfma_f32_32x32x2_f32 v[4:19], v202, v210, v[4:19]
	s_waitcnt lgkmcnt(8)
	v_mfma_f32_32x32x2_f32 v[4:19], v203, v211, v[4:19]
	s_waitcnt lgkmcnt(6)
	v_mfma_f32_32x32x2_f32 v[4:19], v204, v212, v[4:19]
	s_waitcnt lgkmcnt(4)
	v_mfma_f32_32x32x2_f32 v[4:19], v205, v213, v[4:19]
	s_waitcnt lgkmcnt(2)
	v_mfma_f32_32x32x2_f32 v[4:19], v206, v214, v[4:19]
	s_waitcnt lgkmcnt(0)
	v_mfma_f32_32x32x2_f32 v[4:19], v207, v215, v[4:19]
	s_barrier
	s_nop 15
	s_nop 3
	ds_write_b32 v217, v4 offset:58752
	ds_write_b32 v217, v5 offset:58880
	ds_write_b32 v217, v6 offset:59008
	ds_write_b32 v217, v7 offset:59136
	ds_write_b32 v217, v8 offset:59776
	ds_write_b32 v217, v9 offset:59904
	ds_write_b32 v217, v10 offset:60032
	ds_write_b32 v217, v11 offset:60160
	ds_write_b32 v217, v12 offset:60800
	ds_write_b32 v217, v13 offset:60928
	ds_write_b32 v217, v14 offset:61056
	ds_write_b32 v217, v15 offset:61184
	ds_write_b32 v217, v16 offset:61824
	ds_write_b32 v217, v17 offset:61952
	ds_write_b32 v217, v18 offset:62080
	ds_write_b32 v217, v19 offset:62208
	s_waitcnt lgkmcnt(0)
	s_barrier
	global_load_dwordx4 v[0:3], v[50:51], off
	ds_read_b128 v[4:7], v106 offset:58752
	ds_read_b128 v[8:11], v107 offset:8192
	ds_read_b128 v[12:15], v107 offset:16384
	ds_read_b128 v[16:19], v107 offset:24576
	v_add_u32_e32 v20, 0xc400, v108
	v_add_u32_e32 v21, 0xc408, v108
	s_waitcnt lgkmcnt(2)
	v_pk_add_f32 v[4:5], v[4:5], v[8:9]
	v_pk_add_f32 v[6:7], v[6:7], v[10:11]
	s_waitcnt lgkmcnt(1)
	v_pk_add_f32 v[4:5], v[12:13], v[4:5]
	v_pk_add_f32 v[6:7], v[14:15], v[6:7]
	s_waitcnt lgkmcnt(0)
	v_pk_add_f32 v[4:5], v[16:17], v[4:5]
	v_pk_add_f32 v[6:7], v[18:19], v[6:7]
	s_waitcnt vmcnt(0)
	v_pk_add_f32 v[0:1], v[0:1], v[4:5]
	v_pk_add_f32 v[2:3], v[6:7], v[2:3]
	ds_write2_b32 v20, v0, v1 offset1:1
	ds_write2_b32 v21, v2, v3 offset1:1
	s_waitcnt lgkmcnt(0)
	s_barrier
	s_and_saveexec_b64 s[28:29], s[6:7]
	s_cbranch_execz .LBB0_687
	v_add_u32_e32 v0, 0xc400, v117
	v_add_u32_e32 v1, 0xc408, v117
	v_add_u32_e32 v2, 0xc410, v117
	v_add_u32_e32 v3, 0xc418, v117
	ds_read2_b32 v[34:35], v0 offset1:1
	ds_read2_b32 v[30:31], v1 offset1:1
	ds_read2_b32 v[22:23], v2 offset1:1
	ds_read2_b32 v[10:11], v3 offset1:1
	s_mov_b32 s16, 0xff61b1e6
	s_waitcnt lgkmcnt(3)
	v_max_f32_e32 v0, v34, v34
	v_max_f32_e32 v0, 0xff61b1e6, v0
	v_cmp_lt_f32_e32 vcc, s16, v34
	v_cmp_gt_f32_e64 s[16:17], v35, v0
	v_add_u32_e32 v2, 0xc420, v117
	ds_read2_b32 v[24:25], v2 offset1:1
	v_cndmask_b32_e64 v0, v0, v35, s[16:17]
	v_cndmask_b32_e64 v1, 0, 1, s[16:17]
	s_waitcnt lgkmcnt(3)
	v_cmp_gt_f32_e64 s[16:17], v30, v0
	v_add_u32_e32 v2, 0xc428, v117
	v_add_u32_e32 v3, 0xc430, v117
	v_cndmask_b32_e64 v0, v0, v30, s[16:17]
	v_cndmask_b32_e64 v1, v1, 2, s[16:17]
	v_cmp_gt_f32_e64 s[16:17], v31, v0
	v_add_u32_e32 v4, 0xc438, v117
	ds_read2_b32 v[32:33], v2 offset1:1
	ds_read2_b32 v[20:21], v3 offset1:1
	ds_read2_b32 v[6:7], v4 offset1:1
	v_cndmask_b32_e64 v0, v0, v31, s[16:17]
	v_cndmask_b32_e64 v1, v1, 3, s[16:17]
	s_waitcnt lgkmcnt(5)
	v_cmp_gt_f32_e64 s[16:17], v22, v0
	v_add_u32_e32 v2, 0xc440, v117
	ds_read2_b32 v[18:19], v2 offset1:1
	v_cndmask_b32_e64 v0, v0, v22, s[16:17]
	v_cndmask_b32_e64 v1, v1, 4, s[16:17]
	v_cmp_gt_f32_e64 s[16:17], v23, v0
	v_add_u32_e32 v2, 0xc448, v117
	v_add_u32_e32 v4, 0xc458, v117
	v_cndmask_b32_e64 v0, v0, v23, s[16:17]
	v_cndmask_b32_e64 v1, v1, 5, s[16:17]
	s_waitcnt lgkmcnt(5)
	v_cmp_gt_f32_e64 s[16:17], v10, v0
	v_add_u32_e32 v3, 0xc450, v117
	ds_read2_b32 v[26:27], v2 offset1:1
	ds_read2_b32 v[12:13], v3 offset1:1
	ds_read2_b32 v[4:5], v4 offset1:1
	v_cndmask_b32_e64 v0, v0, v10, s[16:17]
	v_cndmask_b32_e64 v1, v1, 6, s[16:17]
	v_cmp_gt_f32_e64 s[16:17], v11, v0
	v_add_u32_e32 v2, 0xc460, v117
	ds_read2_b32 v[14:15], v2 offset1:1
	v_cndmask_b32_e64 v0, v0, v11, s[16:17]
	v_cndmask_b32_e64 v1, v1, 7, s[16:17]
	s_waitcnt lgkmcnt(8)
	v_cmp_gt_f32_e64 s[16:17], v24, v0
	v_add_u32_e32 v2, 0xc468, v117
	v_add_u32_e32 v8, 0xc478, v117
	v_cndmask_b32_e64 v0, v0, v24, s[16:17]
	v_cndmask_b32_e64 v1, v1, 8, s[16:17]
	v_cmp_gt_f32_e64 s[16:17], v25, v0
	v_add_u32_e32 v3, 0xc470, v117
	ds_read2_b32 v[28:29], v2 offset1:1
	ds_read2_b32 v[16:17], v3 offset1:1
	ds_read2_b32 v[8:9], v8 offset1:1
	v_cndmask_b32_e64 v0, v0, v25, s[16:17]
	v_cndmask_b32_e64 v1, v1, 9, s[16:17]
	s_waitcnt lgkmcnt(10)
	v_cmp_gt_f32_e64 s[16:17], v32, v0
	s_nop 1
	v_cndmask_b32_e64 v0, v0, v32, s[16:17]
	v_cndmask_b32_e64 v1, v1, 10, s[16:17]
	v_cmp_gt_f32_e64 s[16:17], v33, v0
	s_nop 1
	v_cndmask_b32_e64 v0, v0, v33, s[16:17]
	v_cndmask_b32_e64 v1, v1, 11, s[16:17]
	s_waitcnt lgkmcnt(9)
	v_cmp_gt_f32_e64 s[16:17], v20, v0
	s_nop 1
	v_cndmask_b32_e64 v0, v0, v20, s[16:17]
	v_cndmask_b32_e64 v1, v1, 12, s[16:17]
	v_cmp_gt_f32_e64 s[16:17], v21, v0
	s_nop 1
	v_cndmask_b32_e64 v0, v0, v21, s[16:17]
	v_cndmask_b32_e64 v1, v1, 13, s[16:17]
	s_waitcnt lgkmcnt(8)
	v_cmp_gt_f32_e64 s[16:17], v6, v0
	s_nop 1
	v_cndmask_b32_e64 v0, v0, v6, s[16:17]
	v_cndmask_b32_e64 v1, v1, 14, s[16:17]
	v_cmp_gt_f32_e64 s[16:17], v7, v0
	s_nop 1
	v_cndmask_b32_e64 v0, v0, v7, s[16:17]
	v_cndmask_b32_e64 v1, v1, 15, s[16:17]
	s_waitcnt lgkmcnt(7)
	v_cmp_gt_f32_e64 s[16:17], v18, v0
	s_nop 1
	v_cndmask_b32_e64 v0, v0, v18, s[16:17]
	v_cndmask_b32_e64 v1, v1, 16, s[16:17]
	v_cmp_gt_f32_e64 s[16:17], v19, v0
	s_nop 1
	v_cndmask_b32_e64 v0, v0, v19, s[16:17]
	v_cndmask_b32_e64 v1, v1, 17, s[16:17]
	s_waitcnt lgkmcnt(6)
	v_cmp_gt_f32_e64 s[16:17], v26, v0
	s_nop 1
	v_cndmask_b32_e64 v0, v0, v26, s[16:17]
	v_cndmask_b32_e64 v1, v1, 18, s[16:17]
	v_cmp_gt_f32_e64 s[16:17], v27, v0
	s_nop 1
	v_cndmask_b32_e64 v0, v0, v27, s[16:17]
	v_cndmask_b32_e64 v1, v1, 19, s[16:17]
	s_waitcnt lgkmcnt(5)
	v_cmp_gt_f32_e64 s[16:17], v12, v0
	s_nop 1
	v_cndmask_b32_e64 v0, v0, v12, s[16:17]
	v_cndmask_b32_e64 v1, v1, 20, s[16:17]
	v_cmp_gt_f32_e64 s[16:17], v13, v0
	s_nop 1
	v_cndmask_b32_e64 v0, v0, v13, s[16:17]
	v_cndmask_b32_e64 v1, v1, 21, s[16:17]
	s_waitcnt lgkmcnt(4)
	v_cmp_gt_f32_e64 s[16:17], v4, v0
	s_nop 1
	v_cndmask_b32_e64 v0, v0, v4, s[16:17]
	v_cndmask_b32_e64 v1, v1, 22, s[16:17]
	v_cmp_gt_f32_e64 s[16:17], v5, v0
	s_nop 1
	v_cndmask_b32_e64 v0, v0, v5, s[16:17]
	v_cndmask_b32_e64 v1, v1, 23, s[16:17]
	s_waitcnt lgkmcnt(3)
	v_cmp_gt_f32_e64 s[16:17], v14, v0
	s_nop 1
	v_cndmask_b32_e64 v0, v0, v14, s[16:17]
	v_cndmask_b32_e64 v1, v1, 24, s[16:17]
	v_cmp_gt_f32_e64 s[16:17], v15, v0
	s_nop 1
	v_cndmask_b32_e64 v0, v0, v15, s[16:17]
	v_cndmask_b32_e64 v1, v1, 25, s[16:17]
	s_waitcnt lgkmcnt(2)
	v_cmp_gt_f32_e64 s[16:17], v28, v0
	s_nop 1
	v_cndmask_b32_e64 v0, v0, v28, s[16:17]
	v_cndmask_b32_e64 v1, v1, 26, s[16:17]
	v_cmp_gt_f32_e64 s[16:17], v29, v0
	s_nop 1
	v_cndmask_b32_e64 v0, v0, v29, s[16:17]
	v_cndmask_b32_e64 v1, v1, 27, s[16:17]
	s_waitcnt lgkmcnt(1)
	v_cmp_gt_f32_e64 s[16:17], v16, v0
	s_nop 1
	v_cndmask_b32_e64 v0, v0, v16, s[16:17]
	v_cndmask_b32_e64 v1, v1, 28, s[16:17]
	v_cmp_gt_f32_e64 s[16:17], v17, v0
	s_nop 1
	v_cndmask_b32_e64 v0, v0, v17, s[16:17]
	v_cndmask_b32_e64 v1, v1, 29, s[16:17]
	s_waitcnt lgkmcnt(0)
	v_cmp_gt_f32_e64 s[16:17], v8, v0
	s_nop 1
	v_cndmask_b32_e64 v0, v0, v8, s[16:17]
	v_cndmask_b32_e64 v1, v1, 30, s[16:17]
	v_cmp_gt_f32_e64 s[16:17], v9, v0
	s_nop 1
	v_cndmask_b32_e64 v36, v0, v9, s[16:17]
	v_cndmask_b32_e64 v0, v1, 31, s[16:17]
	v_cmp_ne_u32_e64 s[16:17], 0, v0
	v_lshlrev_b32_e64 v2, v0, 1
	s_and_b64 s[16:17], s[16:17], vcc
	v_cndmask_b32_e64 v1, v121, v34, s[16:17]
	v_and_b32_e32 v3, 2, v2
	v_cmp_eq_u32_e64 s[16:17], 0, v3
	v_cmp_gt_f32_e64 s[18:19], v35, v1
	s_and_b64 s[16:17], s[16:17], s[18:19]
	v_cndmask_b32_e64 v1, v1, v35, s[16:17]
	v_and_b32_e32 v37, 4, v2
	v_cndmask_b32_e64 v3, 0, 1, s[16:17]
	v_cmp_eq_u32_e64 s[16:17], 0, v37
	v_cmp_gt_f32_e64 s[18:19], v30, v1
	s_and_b64 s[16:17], s[16:17], s[18:19]
	v_cndmask_b32_e64 v1, v1, v30, s[16:17]
	v_and_b32_e32 v37, 8, v2
	v_cndmask_b32_e64 v3, v3, 2, s[16:17]
	v_cmp_eq_u32_e64 s[16:17], 0, v37
	v_cmp_gt_f32_e64 s[18:19], v31, v1
	s_and_b64 s[16:17], s[16:17], s[18:19]
	v_cndmask_b32_e64 v1, v1, v31, s[16:17]
	v_and_b32_e32 v37, 16, v2
	v_cndmask_b32_e64 v3, v3, 3, s[16:17]
	v_cmp_eq_u32_e64 s[16:17], 0, v37
	v_cmp_gt_f32_e64 s[18:19], v22, v1
	s_and_b64 s[16:17], s[16:17], s[18:19]
	v_cndmask_b32_e64 v1, v1, v22, s[16:17]
	v_and_b32_e32 v37, 32, v2
	v_cndmask_b32_e64 v3, v3, 4, s[16:17]
	v_cmp_eq_u32_e64 s[16:17], 0, v37
	v_cmp_gt_f32_e64 s[18:19], v23, v1
	s_and_b64 s[16:17], s[16:17], s[18:19]
	v_cndmask_b32_e64 v1, v1, v23, s[16:17]
	v_and_b32_e32 v37, 64, v2
	v_cndmask_b32_e64 v3, v3, 5, s[16:17]
	v_cmp_eq_u32_e64 s[16:17], 0, v37
	v_cmp_gt_f32_e64 s[18:19], v10, v1
	s_and_b64 s[16:17], s[16:17], s[18:19]
	v_cndmask_b32_e64 v1, v1, v10, s[16:17]
	v_and_b32_e32 v37, 0x80, v2
	v_cndmask_b32_e64 v3, v3, 6, s[16:17]
	v_cmp_eq_u32_e64 s[16:17], 0, v37
	v_cmp_gt_f32_e64 s[18:19], v11, v1
	s_and_b64 s[16:17], s[16:17], s[18:19]
	v_cndmask_b32_e64 v1, v1, v11, s[16:17]
	v_and_b32_e32 v37, 0x100, v2
	v_cndmask_b32_e64 v3, v3, 7, s[16:17]
	v_cmp_eq_u32_e64 s[16:17], 0, v37
	v_cmp_gt_f32_e64 s[18:19], v24, v1
	s_and_b64 s[16:17], s[16:17], s[18:19]
	v_cndmask_b32_e64 v1, v1, v24, s[16:17]
	v_and_b32_e32 v37, 0x200, v2
	v_cndmask_b32_e64 v3, v3, 8, s[16:17]
	v_cmp_eq_u32_e64 s[16:17], 0, v37
	v_cmp_gt_f32_e64 s[18:19], v25, v1
	s_and_b64 s[16:17], s[16:17], s[18:19]
	v_cndmask_b32_e64 v1, v1, v25, s[16:17]
	v_and_b32_e32 v37, 0x400, v2
	v_cndmask_b32_e64 v3, v3, 9, s[16:17]
	v_cmp_eq_u32_e64 s[16:17], 0, v37
	v_cmp_gt_f32_e64 s[18:19], v32, v1
	s_and_b64 s[16:17], s[16:17], s[18:19]
	v_cndmask_b32_e64 v1, v1, v32, s[16:17]
	v_and_b32_e32 v37, 0x800, v2
	v_cndmask_b32_e64 v3, v3, 10, s[16:17]
	v_cmp_eq_u32_e64 s[16:17], 0, v37
	v_cmp_gt_f32_e64 s[18:19], v33, v1
	s_and_b64 s[16:17], s[16:17], s[18:19]
	v_cndmask_b32_e64 v1, v1, v33, s[16:17]
	v_and_b32_e32 v37, 0x1000, v2
	v_cndmask_b32_e64 v3, v3, 11, s[16:17]
	v_cmp_eq_u32_e64 s[16:17], 0, v37
	v_cmp_gt_f32_e64 s[18:19], v20, v1
	s_and_b64 s[16:17], s[16:17], s[18:19]
	v_cndmask_b32_e64 v1, v1, v20, s[16:17]
	v_and_b32_e32 v37, 0x2000, v2
	v_cndmask_b32_e64 v3, v3, 12, s[16:17]
	v_cmp_eq_u32_e64 s[16:17], 0, v37
	v_cmp_gt_f32_e64 s[18:19], v21, v1
	s_and_b64 s[16:17], s[16:17], s[18:19]
	v_cndmask_b32_e64 v1, v1, v21, s[16:17]
	v_and_b32_e32 v37, 0x4000, v2
	v_cndmask_b32_e64 v3, v3, 13, s[16:17]
	v_cmp_eq_u32_e64 s[16:17], 0, v37
	v_cmp_gt_f32_e64 s[18:19], v6, v1
	s_and_b64 s[16:17], s[16:17], s[18:19]
	v_cndmask_b32_e64 v1, v1, v6, s[16:17]
	v_and_b32_e32 v37, 0x8000, v2
	v_cndmask_b32_e64 v3, v3, 14, s[16:17]
	v_cmp_eq_u32_e64 s[16:17], 0, v37
	v_cmp_gt_f32_e64 s[18:19], v7, v1
	s_and_b64 s[16:17], s[16:17], s[18:19]
	v_cndmask_b32_e64 v1, v1, v7, s[16:17]
	v_and_b32_e32 v37, 0x10000, v2
	v_cndmask_b32_e64 v3, v3, 15, s[16:17]
	v_cmp_eq_u32_e64 s[16:17], 0, v37
	v_cmp_gt_f32_e64 s[18:19], v18, v1
	s_and_b64 s[16:17], s[16:17], s[18:19]
	v_cndmask_b32_e64 v1, v1, v18, s[16:17]
	v_and_b32_e32 v37, 0x20000, v2
	v_cndmask_b32_e64 v3, v3, 16, s[16:17]
	v_cmp_eq_u32_e64 s[16:17], 0, v37
	v_cmp_gt_f32_e64 s[18:19], v19, v1
	s_and_b64 s[16:17], s[16:17], s[18:19]
	v_cndmask_b32_e64 v1, v1, v19, s[16:17]
	v_and_b32_e32 v37, 0x40000, v2
	v_cndmask_b32_e64 v3, v3, 17, s[16:17]
	v_cmp_eq_u32_e64 s[16:17], 0, v37
	v_cmp_gt_f32_e64 s[18:19], v26, v1
	s_and_b64 s[16:17], s[16:17], s[18:19]
	v_cndmask_b32_e64 v1, v1, v26, s[16:17]
	v_and_b32_e32 v37, 0x80000, v2
	v_cndmask_b32_e64 v3, v3, 18, s[16:17]
	v_cmp_eq_u32_e64 s[16:17], 0, v37
	v_cmp_gt_f32_e64 s[18:19], v27, v1
	s_and_b64 s[16:17], s[16:17], s[18:19]
	v_cndmask_b32_e64 v1, v1, v27, s[16:17]
	v_and_b32_e32 v37, 0x100000, v2
	v_cndmask_b32_e64 v3, v3, 19, s[16:17]
	v_cmp_eq_u32_e64 s[16:17], 0, v37
	v_cmp_gt_f32_e64 s[18:19], v12, v1
	s_and_b64 s[16:17], s[16:17], s[18:19]
	v_cndmask_b32_e64 v1, v1, v12, s[16:17]
	v_and_b32_e32 v37, 0x200000, v2
	v_cndmask_b32_e64 v3, v3, 20, s[16:17]
	v_cmp_eq_u32_e64 s[16:17], 0, v37
	v_cmp_gt_f32_e64 s[18:19], v13, v1
	s_and_b64 s[16:17], s[16:17], s[18:19]
	v_cndmask_b32_e64 v1, v1, v13, s[16:17]
	v_and_b32_e32 v37, 0x400000, v2
	v_cndmask_b32_e64 v3, v3, 21, s[16:17]
	v_cmp_eq_u32_e64 s[16:17], 0, v37
	v_cmp_gt_f32_e64 s[18:19], v4, v1
	s_and_b64 s[16:17], s[16:17], s[18:19]
	v_cndmask_b32_e64 v1, v1, v4, s[16:17]
	v_and_b32_e32 v37, 0x800000, v2
	v_cndmask_b32_e64 v3, v3, 22, s[16:17]
	v_cmp_eq_u32_e64 s[16:17], 0, v37
	v_cmp_gt_f32_e64 s[18:19], v5, v1
	s_and_b64 s[16:17], s[16:17], s[18:19]
	v_cndmask_b32_e64 v1, v1, v5, s[16:17]
	v_and_b32_e32 v37, 0x1000000, v2
	v_cndmask_b32_e64 v3, v3, 23, s[16:17]
	v_cmp_eq_u32_e64 s[16:17], 0, v37
	v_cmp_gt_f32_e64 s[18:19], v14, v1
	s_and_b64 s[16:17], s[16:17], s[18:19]
	v_cndmask_b32_e64 v1, v1, v14, s[16:17]
	v_and_b32_e32 v37, 0x2000000, v2
	v_cndmask_b32_e64 v3, v3, 24, s[16:17]
	v_cmp_eq_u32_e64 s[16:17], 0, v37
	v_cmp_gt_f32_e64 s[18:19], v15, v1
	s_and_b64 s[16:17], s[16:17], s[18:19]
	v_cndmask_b32_e64 v1, v1, v15, s[16:17]
	v_and_b32_e32 v37, 0x4000000, v2
	v_cndmask_b32_e64 v3, v3, 25, s[16:17]
	v_cmp_eq_u32_e64 s[16:17], 0, v37
	v_cmp_gt_f32_e64 s[18:19], v28, v1
	s_and_b64 s[16:17], s[16:17], s[18:19]
	v_cndmask_b32_e64 v1, v1, v28, s[16:17]
	v_and_b32_e32 v37, 0x8000000, v2
	v_cndmask_b32_e64 v3, v3, 26, s[16:17]
	v_cmp_eq_u32_e64 s[16:17], 0, v37
	v_cmp_gt_f32_e64 s[18:19], v29, v1
	s_and_b64 s[16:17], s[16:17], s[18:19]
	v_cndmask_b32_e64 v1, v1, v29, s[16:17]
	v_and_b32_e32 v37, 0x10000000, v2
	v_cndmask_b32_e64 v3, v3, 27, s[16:17]
	v_cmp_eq_u32_e64 s[16:17], 0, v37
	v_cmp_gt_f32_e64 s[18:19], v16, v1
	s_and_b64 s[16:17], s[16:17], s[18:19]
	v_cndmask_b32_e64 v1, v1, v16, s[16:17]
	v_and_b32_e32 v37, 0x20000000, v2
	v_cndmask_b32_e64 v3, v3, 28, s[16:17]
	v_cmp_eq_u32_e64 s[16:17], 0, v37
	v_cmp_gt_f32_e64 s[18:19], v17, v1
	s_and_b64 s[16:17], s[16:17], s[18:19]
	v_cndmask_b32_e64 v1, v1, v17, s[16:17]
	v_and_b32_e32 v37, 2.0, v2
	v_cndmask_b32_e64 v3, v3, 29, s[16:17]
	v_cmp_eq_u32_e64 s[16:17], 0, v37
	v_cmp_gt_f32_e64 s[18:19], v8, v1
	s_and_b64 s[16:17], s[16:17], s[18:19]
	v_cndmask_b32_e64 v1, v1, v8, s[16:17]
	v_cndmask_b32_e64 v3, v3, 30, s[16:17]
	v_cmp_ne_u32_e64 s[16:17], 31, v0
	v_cmp_gt_f32_e64 s[18:19], v9, v1
	s_and_b64 s[16:17], s[16:17], s[18:19]
	v_cndmask_b32_e64 v37, v1, v9, s[16:17]
	v_cndmask_b32_e64 v1, v3, 31, s[16:17]
	v_lshl_or_b32 v3, 1, v1, v2
	v_and_b32_e32 v2, 1, v3
	v_cmp_eq_u32_e64 s[16:17], 0, v2
	s_and_b64 s[16:17], s[16:17], vcc
	v_and_b32_e32 v38, 2, v3
	v_cndmask_b32_e64 v2, v121, v34, s[16:17]
	v_cmp_eq_u32_e64 s[16:17], 0, v38
	v_cmp_gt_f32_e64 s[18:19], v35, v2
	s_and_b64 s[16:17], s[16:17], s[18:19]
	v_cndmask_b32_e64 v2, v2, v35, s[16:17]
	v_and_b32_e32 v39, 4, v3
	v_cndmask_b32_e64 v38, 0, 1, s[16:17]
	v_cmp_eq_u32_e64 s[16:17], 0, v39
	v_cmp_gt_f32_e64 s[18:19], v30, v2
	s_and_b64 s[16:17], s[16:17], s[18:19]
	v_cndmask_b32_e64 v2, v2, v30, s[16:17]
	v_and_b32_e32 v39, 8, v3
	v_cndmask_b32_e64 v38, v38, 2, s[16:17]
	v_cmp_eq_u32_e64 s[16:17], 0, v39
	v_cmp_gt_f32_e64 s[18:19], v31, v2
	s_and_b64 s[16:17], s[16:17], s[18:19]
	v_cndmask_b32_e64 v2, v2, v31, s[16:17]
	v_and_b32_e32 v39, 16, v3
	v_cndmask_b32_e64 v38, v38, 3, s[16:17]
	v_cmp_eq_u32_e64 s[16:17], 0, v39
	v_cmp_gt_f32_e64 s[18:19], v22, v2
	s_and_b64 s[16:17], s[16:17], s[18:19]
	v_cndmask_b32_e64 v2, v2, v22, s[16:17]
	v_and_b32_e32 v39, 32, v3
	v_cndmask_b32_e64 v38, v38, 4, s[16:17]
	v_cmp_eq_u32_e64 s[16:17], 0, v39
	v_cmp_gt_f32_e64 s[18:19], v23, v2
	s_and_b64 s[16:17], s[16:17], s[18:19]
	v_cndmask_b32_e64 v2, v2, v23, s[16:17]
	v_and_b32_e32 v39, 64, v3
	v_cndmask_b32_e64 v38, v38, 5, s[16:17]
	v_cmp_eq_u32_e64 s[16:17], 0, v39
	v_cmp_gt_f32_e64 s[18:19], v10, v2
	s_and_b64 s[16:17], s[16:17], s[18:19]
	v_cndmask_b32_e64 v2, v2, v10, s[16:17]
	v_and_b32_e32 v39, 0x80, v3
	v_cndmask_b32_e64 v38, v38, 6, s[16:17]
	v_cmp_eq_u32_e64 s[16:17], 0, v39
	v_cmp_gt_f32_e64 s[18:19], v11, v2
	s_and_b64 s[16:17], s[16:17], s[18:19]
	v_cndmask_b32_e64 v2, v2, v11, s[16:17]
	v_and_b32_e32 v39, 0x100, v3
	v_cndmask_b32_e64 v38, v38, 7, s[16:17]
	v_cmp_eq_u32_e64 s[16:17], 0, v39
	v_cmp_gt_f32_e64 s[18:19], v24, v2
	s_and_b64 s[16:17], s[16:17], s[18:19]
	v_cndmask_b32_e64 v2, v2, v24, s[16:17]
	v_and_b32_e32 v39, 0x200, v3
	v_cndmask_b32_e64 v38, v38, 8, s[16:17]
	v_cmp_eq_u32_e64 s[16:17], 0, v39
	v_cmp_gt_f32_e64 s[18:19], v25, v2
	s_and_b64 s[16:17], s[16:17], s[18:19]
	v_cndmask_b32_e64 v2, v2, v25, s[16:17]
	v_and_b32_e32 v39, 0x400, v3
	v_cndmask_b32_e64 v38, v38, 9, s[16:17]
	v_cmp_eq_u32_e64 s[16:17], 0, v39
	v_cmp_gt_f32_e64 s[18:19], v32, v2
	s_and_b64 s[16:17], s[16:17], s[18:19]
	v_cndmask_b32_e64 v2, v2, v32, s[16:17]
	v_and_b32_e32 v39, 0x800, v3
	v_cndmask_b32_e64 v38, v38, 10, s[16:17]
	v_cmp_eq_u32_e64 s[16:17], 0, v39
	v_cmp_gt_f32_e64 s[18:19], v33, v2
	s_and_b64 s[16:17], s[16:17], s[18:19]
	v_cndmask_b32_e64 v2, v2, v33, s[16:17]
	v_and_b32_e32 v39, 0x1000, v3
	v_cndmask_b32_e64 v38, v38, 11, s[16:17]
	v_cmp_eq_u32_e64 s[16:17], 0, v39
	v_cmp_gt_f32_e64 s[18:19], v20, v2
	s_and_b64 s[16:17], s[16:17], s[18:19]
	v_cndmask_b32_e64 v2, v2, v20, s[16:17]
	v_and_b32_e32 v39, 0x2000, v3
	v_cndmask_b32_e64 v38, v38, 12, s[16:17]
	v_cmp_eq_u32_e64 s[16:17], 0, v39
	v_cmp_gt_f32_e64 s[18:19], v21, v2
	s_and_b64 s[16:17], s[16:17], s[18:19]
	v_cndmask_b32_e64 v2, v2, v21, s[16:17]
	v_and_b32_e32 v39, 0x4000, v3
	v_cndmask_b32_e64 v38, v38, 13, s[16:17]
	v_cmp_eq_u32_e64 s[16:17], 0, v39
	v_cmp_gt_f32_e64 s[18:19], v6, v2
	s_and_b64 s[16:17], s[16:17], s[18:19]
	v_cndmask_b32_e64 v2, v2, v6, s[16:17]
	v_and_b32_e32 v39, 0x8000, v3
	v_cndmask_b32_e64 v38, v38, 14, s[16:17]
	v_cmp_eq_u32_e64 s[16:17], 0, v39
	v_cmp_gt_f32_e64 s[18:19], v7, v2
	s_and_b64 s[16:17], s[16:17], s[18:19]
	v_cndmask_b32_e64 v2, v2, v7, s[16:17]
	v_and_b32_e32 v39, 0x10000, v3
	v_cndmask_b32_e64 v38, v38, 15, s[16:17]
	v_cmp_eq_u32_e64 s[16:17], 0, v39
	v_cmp_gt_f32_e64 s[18:19], v18, v2
	s_and_b64 s[16:17], s[16:17], s[18:19]
	v_cndmask_b32_e64 v2, v2, v18, s[16:17]
	v_and_b32_e32 v39, 0x20000, v3
	v_cndmask_b32_e64 v38, v38, 16, s[16:17]
	v_cmp_eq_u32_e64 s[16:17], 0, v39
	v_cmp_gt_f32_e64 s[18:19], v19, v2
	s_and_b64 s[16:17], s[16:17], s[18:19]
	v_cndmask_b32_e64 v2, v2, v19, s[16:17]
	v_and_b32_e32 v39, 0x40000, v3
	v_cndmask_b32_e64 v38, v38, 17, s[16:17]
	v_cmp_eq_u32_e64 s[16:17], 0, v39
	v_cmp_gt_f32_e64 s[18:19], v26, v2
	s_and_b64 s[16:17], s[16:17], s[18:19]
	v_cndmask_b32_e64 v2, v2, v26, s[16:17]
	v_and_b32_e32 v39, 0x80000, v3
	v_cndmask_b32_e64 v38, v38, 18, s[16:17]
	v_cmp_eq_u32_e64 s[16:17], 0, v39
	v_cmp_gt_f32_e64 s[18:19], v27, v2
	s_and_b64 s[16:17], s[16:17], s[18:19]
	v_cndmask_b32_e64 v2, v2, v27, s[16:17]
	v_and_b32_e32 v39, 0x100000, v3
	v_cndmask_b32_e64 v38, v38, 19, s[16:17]
	v_cmp_eq_u32_e64 s[16:17], 0, v39
	v_cmp_gt_f32_e64 s[18:19], v12, v2
	s_and_b64 s[16:17], s[16:17], s[18:19]
	v_cndmask_b32_e64 v2, v2, v12, s[16:17]
	v_and_b32_e32 v39, 0x200000, v3
	v_cndmask_b32_e64 v38, v38, 20, s[16:17]
	v_cmp_eq_u32_e64 s[16:17], 0, v39
	v_cmp_gt_f32_e64 s[18:19], v13, v2
	s_and_b64 s[16:17], s[16:17], s[18:19]
	v_cndmask_b32_e64 v2, v2, v13, s[16:17]
	v_and_b32_e32 v39, 0x400000, v3
	v_cndmask_b32_e64 v38, v38, 21, s[16:17]
	v_cmp_eq_u32_e64 s[16:17], 0, v39
	v_cmp_gt_f32_e64 s[18:19], v4, v2
	s_and_b64 s[16:17], s[16:17], s[18:19]
	v_cndmask_b32_e64 v2, v2, v4, s[16:17]
	v_and_b32_e32 v39, 0x800000, v3
	v_cndmask_b32_e64 v38, v38, 22, s[16:17]
	v_cmp_eq_u32_e64 s[16:17], 0, v39
	v_cmp_gt_f32_e64 s[18:19], v5, v2
	s_and_b64 s[16:17], s[16:17], s[18:19]
	v_cndmask_b32_e64 v2, v2, v5, s[16:17]
	v_and_b32_e32 v39, 0x1000000, v3
	v_cndmask_b32_e64 v38, v38, 23, s[16:17]
	v_cmp_eq_u32_e64 s[16:17], 0, v39
	v_cmp_gt_f32_e64 s[18:19], v14, v2
	s_and_b64 s[16:17], s[16:17], s[18:19]
	v_cndmask_b32_e64 v2, v2, v14, s[16:17]
	v_and_b32_e32 v39, 0x2000000, v3
	v_cndmask_b32_e64 v38, v38, 24, s[16:17]
	v_cmp_eq_u32_e64 s[16:17], 0, v39
	v_cmp_gt_f32_e64 s[18:19], v15, v2
	s_and_b64 s[16:17], s[16:17], s[18:19]
	v_cndmask_b32_e64 v2, v2, v15, s[16:17]
	v_and_b32_e32 v39, 0x4000000, v3
	v_cndmask_b32_e64 v38, v38, 25, s[16:17]
	v_cmp_eq_u32_e64 s[16:17], 0, v39
	v_cmp_gt_f32_e64 s[18:19], v28, v2
	s_and_b64 s[16:17], s[16:17], s[18:19]
	v_cndmask_b32_e64 v2, v2, v28, s[16:17]
	v_and_b32_e32 v39, 0x8000000, v3
	v_cndmask_b32_e64 v38, v38, 26, s[16:17]
	v_cmp_eq_u32_e64 s[16:17], 0, v39
	v_cmp_gt_f32_e64 s[18:19], v29, v2
	s_and_b64 s[16:17], s[16:17], s[18:19]
	v_cndmask_b32_e64 v2, v2, v29, s[16:17]
	v_and_b32_e32 v39, 0x10000000, v3
	v_cndmask_b32_e64 v38, v38, 27, s[16:17]
	v_cmp_eq_u32_e64 s[16:17], 0, v39
	v_cmp_gt_f32_e64 s[18:19], v16, v2
	s_and_b64 s[16:17], s[16:17], s[18:19]
	v_cndmask_b32_e64 v2, v2, v16, s[16:17]
	v_and_b32_e32 v39, 0x20000000, v3
	v_cndmask_b32_e64 v38, v38, 28, s[16:17]
	v_cmp_eq_u32_e64 s[16:17], 0, v39
	v_cmp_gt_f32_e64 s[18:19], v17, v2
	s_and_b64 s[16:17], s[16:17], s[18:19]
	v_cndmask_b32_e64 v2, v2, v17, s[16:17]
	v_and_b32_e32 v39, 2.0, v3
	v_cndmask_b32_e64 v38, v38, 29, s[16:17]
	v_cmp_eq_u32_e64 s[16:17], 0, v39
	v_cmp_gt_f32_e64 s[18:19], v8, v2
	s_and_b64 s[16:17], s[16:17], s[18:19]
	v_cndmask_b32_e64 v2, v2, v8, s[16:17]
	v_cndmask_b32_e64 v38, v38, 30, s[16:17]
	v_cmp_lt_i32_e64 s[16:17], -1, v3
	v_cmp_gt_f32_e64 s[18:19], v9, v2
	s_and_b64 s[16:17], s[16:17], s[18:19]
	v_cndmask_b32_e64 v39, v2, v9, s[16:17]
	v_cndmask_b32_e64 v2, v38, 31, s[16:17]
	v_lshlrev_b32_e64 v38, v2, 1
	v_bitop3_b32 v90, v38, 1, v3 bitop3:0xc8
	v_cmp_eq_u32_e64 s[16:17], 0, v90
	s_and_b64 vcc, s[16:17], vcc
	v_cndmask_b32_e32 v34, v121, v34, vcc
	v_bitop3_b32 v90, v38, 2, v3 bitop3:0xc8
	v_cmp_eq_u32_e32 vcc, 0, v90
	v_cmp_gt_f32_e64 s[16:17], v35, v34
	s_and_b64 vcc, vcc, s[16:17]
	v_cndmask_b32_e32 v34, v34, v35, vcc
	v_bitop3_b32 v90, v38, 4, v3 bitop3:0xc8
	v_cndmask_b32_e64 v35, 0, 1, vcc
	v_cmp_eq_u32_e32 vcc, 0, v90
	v_cmp_gt_f32_e64 s[16:17], v30, v34
	s_and_b64 vcc, vcc, s[16:17]
	v_cndmask_b32_e32 v30, v34, v30, vcc
	v_cndmask_b32_e64 v34, v35, 2, vcc
	v_bitop3_b32 v35, v38, 8, v3 bitop3:0xc8
	v_cmp_eq_u32_e32 vcc, 0, v35
	v_cmp_gt_f32_e64 s[16:17], v31, v30
	s_and_b64 vcc, vcc, s[16:17]
	v_cndmask_b32_e32 v30, v30, v31, vcc
	v_cndmask_b32_e64 v31, v34, 3, vcc
	v_bitop3_b32 v34, v38, 16, v3 bitop3:0xc8
	v_cmp_eq_u32_e32 vcc, 0, v34
	v_cmp_gt_f32_e64 s[16:17], v22, v30
	s_and_b64 vcc, vcc, s[16:17]
	v_cndmask_b32_e32 v22, v30, v22, vcc
	v_cndmask_b32_e64 v30, v31, 4, vcc
	v_bitop3_b32 v31, v38, 32, v3 bitop3:0xc8
	v_cmp_eq_u32_e32 vcc, 0, v31
	v_cmp_gt_f32_e64 s[16:17], v23, v22
	s_and_b64 vcc, vcc, s[16:17]
	v_cndmask_b32_e32 v22, v22, v23, vcc
	v_cndmask_b32_e64 v23, v30, 5, vcc
	v_bitop3_b32 v30, v38, 64, v3 bitop3:0xc8
	v_cmp_eq_u32_e32 vcc, 0, v30
	v_cmp_gt_f32_e64 s[16:17], v10, v22
	s_and_b64 vcc, vcc, s[16:17]
	s_movk_i32 s16, 0x80
	v_cndmask_b32_e32 v10, v22, v10, vcc
	v_cndmask_b32_e64 v22, v23, 6, vcc
	v_bitop3_b32 v23, v38, s16, v3 bitop3:0xc8
	v_cmp_eq_u32_e32 vcc, 0, v23
	v_cmp_gt_f32_e64 s[16:17], v11, v10
	s_and_b64 vcc, vcc, s[16:17]
	s_movk_i32 s16, 0x100
	v_cndmask_b32_e32 v10, v10, v11, vcc
	v_cndmask_b32_e64 v11, v22, 7, vcc
	v_bitop3_b32 v22, v38, s16, v3 bitop3:0xc8
	v_cmp_eq_u32_e32 vcc, 0, v22
	v_cmp_gt_f32_e64 s[16:17], v24, v10
	s_and_b64 vcc, vcc, s[16:17]
	s_movk_i32 s16, 0x200
	v_cndmask_b32_e32 v10, v10, v24, vcc
	v_bitop3_b32 v22, v38, s16, v3 bitop3:0xc8
	v_cndmask_b32_e64 v11, v11, 8, vcc
	v_cmp_eq_u32_e32 vcc, 0, v22
	v_cmp_gt_f32_e64 s[16:17], v25, v10
	s_and_b64 vcc, vcc, s[16:17]
	v_cndmask_b32_e32 v10, v10, v25, vcc
	v_bitop3_b32 v22, v38, s46, v3 bitop3:0xc8
	v_cndmask_b32_e64 v11, v11, 9, vcc
	v_cmp_eq_u32_e32 vcc, 0, v22
	v_cmp_gt_f32_e64 s[16:17], v32, v10
	s_and_b64 vcc, vcc, s[16:17]
	s_movk_i32 s16, 0x800
	v_cndmask_b32_e32 v10, v10, v32, vcc
	v_bitop3_b32 v22, v38, s16, v3 bitop3:0xc8
	v_cndmask_b32_e64 v11, v11, 10, vcc
	v_cmp_eq_u32_e32 vcc, 0, v22
	v_cmp_gt_f32_e64 s[16:17], v33, v10
	s_and_b64 vcc, vcc, s[16:17]
	s_movk_i32 s16, 0x1000
	v_cndmask_b32_e32 v10, v10, v33, vcc
	v_bitop3_b32 v22, v38, s16, v3 bitop3:0xc8
	v_cndmask_b32_e64 v11, v11, 11, vcc
	v_cmp_eq_u32_e32 vcc, 0, v22
	v_cmp_gt_f32_e64 s[16:17], v20, v10
	s_and_b64 vcc, vcc, s[16:17]
	s_movk_i32 s16, 0x2000
	v_cndmask_b32_e32 v10, v10, v20, vcc
	v_bitop3_b32 v20, v38, s16, v3 bitop3:0xc8
	v_cndmask_b32_e64 v11, v11, 12, vcc
	v_cmp_eq_u32_e32 vcc, 0, v20
	v_cmp_gt_f32_e64 s[16:17], v21, v10
	s_and_b64 vcc, vcc, s[16:17]
	s_movk_i32 s16, 0x4000
	v_cndmask_b32_e32 v10, v10, v21, vcc
	v_bitop3_b32 v20, v38, s16, v3 bitop3:0xc8
	v_cndmask_b32_e64 v11, v11, 13, vcc
	v_cmp_eq_u32_e32 vcc, 0, v20
	v_cmp_gt_f32_e64 s[16:17], v6, v10
	s_and_b64 vcc, vcc, s[16:17]
	s_mov_b32 s16, 0x8000
	v_cndmask_b32_e32 v6, v10, v6, vcc
	v_cndmask_b32_e64 v10, v11, 14, vcc
	v_bitop3_b32 v11, v38, s16, v3 bitop3:0xc8
	v_cmp_eq_u32_e32 vcc, 0, v11
	v_cmp_gt_f32_e64 s[16:17], v7, v6
	s_and_b64 vcc, vcc, s[16:17]
	s_mov_b32 s16, 0x10000
	v_cndmask_b32_e32 v6, v6, v7, vcc
	v_cndmask_b32_e64 v7, v10, 15, vcc
	v_bitop3_b32 v10, v38, s16, v3 bitop3:0xc8
	v_cmp_eq_u32_e32 vcc, 0, v10
	v_cmp_gt_f32_e64 s[16:17], v18, v6
	s_and_b64 vcc, vcc, s[16:17]
	s_mov_b32 s16, 0x20000
	v_cndmask_b32_e32 v6, v6, v18, vcc
	v_bitop3_b32 v10, v38, s16, v3 bitop3:0xc8
	v_cndmask_b32_e64 v7, v7, 16, vcc
	v_cmp_eq_u32_e32 vcc, 0, v10
	v_cmp_gt_f32_e64 s[16:17], v19, v6
	s_and_b64 vcc, vcc, s[16:17]
	s_mov_b32 s16, 0x40000
	v_cndmask_b32_e32 v6, v6, v19, vcc
	v_bitop3_b32 v10, v38, s16, v3 bitop3:0xc8
	v_cndmask_b32_e64 v7, v7, 17, vcc
	v_cmp_eq_u32_e32 vcc, 0, v10
	v_cmp_gt_f32_e64 s[16:17], v26, v6
	s_and_b64 vcc, vcc, s[16:17]
	s_mov_b32 s16, 0x80000
	v_cndmask_b32_e32 v6, v6, v26, vcc
	v_bitop3_b32 v10, v38, s16, v3 bitop3:0xc8
	v_cndmask_b32_e64 v7, v7, 18, vcc
	v_cmp_eq_u32_e32 vcc, 0, v10
	v_cmp_gt_f32_e64 s[16:17], v27, v6
	s_and_b64 vcc, vcc, s[16:17]
	s_mov_b32 s16, 0x100000
	v_cndmask_b32_e32 v6, v6, v27, vcc
	v_bitop3_b32 v10, v38, s16, v3 bitop3:0xc8
	v_cndmask_b32_e64 v7, v7, 19, vcc
	v_cmp_eq_u32_e32 vcc, 0, v10
	v_cmp_gt_f32_e64 s[16:17], v12, v6
	s_and_b64 vcc, vcc, s[16:17]
	s_mov_b32 s16, 0x200000
	v_cndmask_b32_e32 v6, v6, v12, vcc
	v_bitop3_b32 v10, v38, s16, v3 bitop3:0xc8
	v_cndmask_b32_e64 v7, v7, 20, vcc
	v_cmp_eq_u32_e32 vcc, 0, v10
	v_cmp_gt_f32_e64 s[16:17], v13, v6
	s_and_b64 vcc, vcc, s[16:17]
	s_mov_b32 s16, 0x400000
	v_cndmask_b32_e32 v6, v6, v13, vcc
	v_bitop3_b32 v10, v38, s16, v3 bitop3:0xc8
	v_cndmask_b32_e64 v7, v7, 21, vcc
	v_cmp_eq_u32_e32 vcc, 0, v10
	v_cmp_gt_f32_e64 s[16:17], v4, v6
	s_and_b64 vcc, vcc, s[16:17]
	s_mov_b32 s16, 0x800000
	v_cndmask_b32_e32 v4, v6, v4, vcc
	v_cndmask_b32_e64 v6, v7, 22, vcc
	v_bitop3_b32 v7, v38, s16, v3 bitop3:0xc8
	v_cmp_eq_u32_e32 vcc, 0, v7
	v_cmp_gt_f32_e64 s[16:17], v5, v4
	s_and_b64 vcc, vcc, s[16:17]
	v_cndmask_b32_e32 v4, v4, v5, vcc
	v_cndmask_b32_e64 v5, v6, 23, vcc
	v_bitop3_b32 v6, v38, s55, v3 bitop3:0xc8
	v_cmp_eq_u32_e32 vcc, 0, v6
	v_cmp_gt_f32_e64 s[16:17], v14, v4
	s_and_b64 vcc, vcc, s[16:17]
	v_cndmask_b32_e32 v4, v4, v14, vcc
	v_bitop3_b32 v6, v38, s56, v3 bitop3:0xc8
	v_cndmask_b32_e64 v5, v5, 24, vcc
	v_cmp_eq_u32_e32 vcc, 0, v6
	v_cmp_gt_f32_e64 s[16:17], v15, v4
	s_and_b64 vcc, vcc, s[16:17]
	v_cndmask_b32_e32 v4, v4, v15, vcc
	v_bitop3_b32 v6, v38, s57, v3 bitop3:0xc8
	v_cndmask_b32_e64 v5, v5, 25, vcc
	v_cmp_eq_u32_e32 vcc, 0, v6
	v_cmp_gt_f32_e64 s[16:17], v28, v4
	s_and_b64 vcc, vcc, s[16:17]
	v_cndmask_b32_e32 v4, v4, v28, vcc
	v_bitop3_b32 v6, v38, s58, v3 bitop3:0xc8
	v_cndmask_b32_e64 v5, v5, 26, vcc
	v_cmp_eq_u32_e32 vcc, 0, v6
	v_cmp_gt_f32_e64 s[16:17], v29, v4
	s_and_b64 vcc, vcc, s[16:17]
	v_cndmask_b32_e32 v4, v4, v29, vcc
	v_bitop3_b32 v6, v38, s59, v3 bitop3:0xc8
	v_cndmask_b32_e64 v5, v5, 27, vcc
	v_cmp_eq_u32_e32 vcc, 0, v6
	v_cmp_gt_f32_e64 s[16:17], v16, v4
	s_and_b64 vcc, vcc, s[16:17]
	v_cndmask_b32_e32 v4, v4, v16, vcc
	v_bitop3_b32 v6, v38, s60, v3 bitop3:0xc8
	v_cndmask_b32_e64 v5, v5, 28, vcc
	v_cmp_eq_u32_e32 vcc, 0, v6
	v_cmp_gt_f32_e64 s[16:17], v17, v4
	s_and_b64 vcc, vcc, s[16:17]
	v_or_b32_e32 v44, v38, v3
	v_cndmask_b32_e32 v4, v4, v17, vcc
	v_bitop3_b32 v3, v38, 2.0, v3 bitop3:0xc8
	v_cndmask_b32_e64 v5, v5, 29, vcc
	v_cmp_eq_u32_e32 vcc, 0, v3
	v_cmp_gt_f32_e64 s[16:17], v8, v4
	s_and_b64 vcc, vcc, s[16:17]
	v_cndmask_b32_e32 v3, v4, v8, vcc
	v_cndmask_b32_e64 v4, v5, 30, vcc
	v_cmp_lt_i32_e32 vcc, -1, v44
	v_cmp_gt_f32_e64 s[16:17], v9, v3
	s_and_b64 vcc, vcc, s[16:17]
	v_cndmask_b32_e32 v5, v3, v9, vcc
	v_cndmask_b32_e64 v3, v4, 31, vcc
	v_sub_f32_e32 v4, v36, v36
	v_mul_f32_e32 v4, 0x3fb8aa3b, v4
	v_exp_f32_e32 v10, v4
	v_sub_f32_e32 v4, v37, v36
	v_mul_f32_e32 v4, 0x3fb8aa3b, v4
	v_exp_f32_e32 v11, v4
	v_sub_f32_e32 v4, v39, v36
	v_mul_f32_e32 v4, 0x3fb8aa3b, v4
	v_exp_f32_e32 v12, v4
	v_sub_f32_e32 v4, v5, v36
	v_mul_f32_e32 v4, 0x3fb8aa3b, v4
	v_exp_f32_e32 v13, v4
	v_add_f32_e32 v4, 0, v10
	v_add_f32_e32 v4, v4, v11
	v_add_f32_e32 v4, v4, v12
	v_add_f32_e32 v14, v4, v13
	v_div_scale_f32 v15, s[16:17], v14, v14, v10
	v_rcp_f32_e32 v16, v15
	v_lshl_add_u32 v4, s61, 8, v102
	v_ashrrev_i32_e32 v5, 31, v4
	v_lshlrev_b64 v[6:7], 2, v[4:5]
	v_fma_f32 v5, -v15, v16, 1.0
	v_fmac_f32_e32 v16, v5, v16
	v_div_scale_f32 v5, vcc, v10, v14, v10
	v_mul_f32_e32 v17, v5, v16
	v_fma_f32 v18, -v15, v17, v5
	v_fmac_f32_e32 v17, v18, v16
	v_fma_f32 v5, -v15, v17, v5
	v_div_fmas_f32 v5, v5, v16, v17
	v_div_fixup_f32 v5, v5, v14, v10
	v_div_scale_f32 v10, s[16:17], v14, v14, v11
	v_rcp_f32_e32 v15, v10
	v_lshl_add_u64 v[8:9], s[20:21], 0, v[6:7]
	v_lshl_add_u64 v[6:7], s[22:23], 0, v[6:7]
	global_store_dword v[6:7], v5, off
	v_or_b32_e32 v6, 1, v4
	v_fma_f32 v4, -v10, v15, 1.0
	v_lshl_add_u32 v5, v0, 2, 0
	v_fmac_f32_e32 v15, v4, v15
	v_div_scale_f32 v4, vcc, v11, v14, v11
	ds_add_u32 v5, v118 offset:58624
	v_mul_f32_e32 v5, v4, v15
	v_fma_f32 v16, -v10, v5, v4
	v_fmac_f32_e32 v5, v16, v15
	v_fma_f32 v4, -v10, v5, v4
	v_div_fmas_f32 v4, v4, v15, v5
	v_div_scale_f32 v5, s[16:17], v14, v14, v12
	v_rcp_f32_e32 v15, v5
	v_ashrrev_i32_e32 v7, 31, v6
	v_div_fixup_f32 v4, v4, v14, v11
	v_lshl_add_u64 v[10:11], v[6:7], 2, s[22:23]
	v_lshl_add_u32 v6, v1, 2, 0
	ds_add_u32 v6, v118 offset:58624
	v_fma_f32 v6, -v5, v15, 1.0
	v_fmac_f32_e32 v15, v6, v15
	v_div_scale_f32 v6, vcc, v12, v14, v12
	v_mul_f32_e32 v7, v6, v15
	v_fma_f32 v16, -v5, v7, v6
	v_fmac_f32_e32 v7, v16, v15
	v_fma_f32 v5, -v5, v7, v6
	v_div_scale_f32 v6, s[16:17], v14, v14, v13
	v_div_fmas_f32 v5, v5, v15, v7
	v_rcp_f32_e32 v7, v6
	v_div_fixup_f32 v5, v5, v14, v12
	v_lshl_add_u32 v12, v2, 2, 0
	ds_add_u32 v12, v118 offset:58624
	global_store_dwordx4 v[8:9], v[0:3], off
	s_nop 1
	v_fma_f32 v0, -v6, v7, 1.0
	v_fmac_f32_e32 v7, v0, v7
	v_div_scale_f32 v0, vcc, v13, v14, v13
	v_mul_f32_e32 v1, v0, v7
	v_fma_f32 v2, -v6, v1, v0
	v_fmac_f32_e32 v1, v2, v7
	v_fma_f32 v0, -v6, v1, v0
	v_div_fmas_f32 v0, v0, v7, v1
	v_div_fixup_f32 v6, v0, v14, v13
	global_store_dwordx3 v[10:11], v[4:6], off
	v_lshl_add_u32 v0, v3, 2, 0
	ds_add_u32 v0, v118 offset:58624

.LBB0_1474:
	s_waitcnt vmcnt(0)
	s_barrier
	s_waitcnt vmcnt(0)
	s_waitcnt vmcnt(0)
	v_readlane_b32 s98, v253, 20
	v_mbcnt_lo_u32_b32 v216, -1, 0
	v_mbcnt_hi_u32_b32 v216, -1, v216
	s_lshr_b32 s99, s98, 1
	s_and_b32 s100, s98, 1
	v_lshrrev_b32_e32 v217, 5, v216
	v_and_b32_e32 v216, 31, v216
	s_lshl_b32 s101, s99, 4
	v_add_u32_e32 v218, s101, v217
	v_lshlrev_b32_e32 v219, 7, v218
	v_lshl_add_u32 v219, v216, 2, v219
	v_add_u32_e32 v219, 0xa400, v219
	v_mul_u32_u24_e32 v218, 0x104, v218
	s_lshl_b32 s101, s100, 7
	v_add_u32_e32 v218, s101, v218
	v_lshl_add_u32 v218, v216, 2, v218
	v_add_u32_e32 v218, 0x6000, v218
	v_mov_b32_e32 v221, s98
	v_mbcnt_lo_u32_b32 v220, -1, 0
	v_mbcnt_hi_u32_b32 v220, -1, v220
	v_lshl_add_u32 v220, v221, 6, v220
	v_and_b32_e32 v221, 7, v220
	v_lshrrev_b32_e32 v220, 3, v220
	v_mul_u32_u24_e32 v221, 0x820, v221
	v_lshl_add_u32 v220, v220, 2, v221
	v_add_u32_e32 v220, 0x6000, v220
	v_add_u32_e32 v221, 0x410, v220
	s_lshl_b32 s101, s99, 13
	s_lshl_b32 s100, s100, 12
	s_add_i32 s101, s101, s100
	v_lshlrev_b32_e32 v217, 9, v217
	v_add_u32_e32 v217, s101, v217
	v_lshl_add_u32 v217, v216, 2, v217
	s_and_saveexec_b64 s[16:17], s[4:5]
	ds_write_b32 v95, v45 offset:58624
	s_or_b64 exec, exec, s[16:17]
	v_add_u32_e32 v0, s67, v42
	v_ashrrev_i32_e32 v1, 31, v0
	v_lshlrev_b64 v[0:1], 11, v[0:1]
	v_lshl_add_u64 v[92:93], v[46:47], 0, v[0:1]
	global_load_dwordx4 v[30:33], v[92:93], off sc1
	global_load_dwordx4 v[34:37], v[48:49], off
	global_load_dwordx4 v[20:23], v[52:53], off
	global_load_dwordx4 v[24:27], v[92:93], off offset:128 sc1
	ds_read_b64 v[38:39], v106 offset:20480
	ds_read_b128 v[116:119], v43 offset:12288
	ds_read_b128 v[120:123], v43 offset:12304
	ds_read_b128 v[124:127], v43 offset:16384
	ds_read_b128 v[128:131], v43 offset:16400
	v_add_u32_e32 v114, 0x6000, v97
	v_mov_b32_e32 v4, 0
	s_waitcnt lgkmcnt(4)
	v_mov_b32_e32 v0, v38
	v_mov_b32_e32 v1, v38
	v_mov_b32_e32 v2, v38
	v_mov_b32_e32 v3, v38
	v_mov_b32_e32 v88, v39
	v_mov_b32_e32 v89, v39
	v_mov_b32_e32 v90, v39
	v_mov_b32_e32 v91, v39
	v_add_u32_e32 v113, 0x6400, v97
	s_mov_b32 s16, 0
	v_mov_b32_e32 v28, v103
	v_mov_b32_e32 v5, v4
	v_mov_b32_e32 v6, v4
	v_mov_b32_e32 v7, v4
	v_mov_b32_e32 v8, v4
	v_mov_b32_e32 v9, v4
	v_mov_b32_e32 v10, v4
	v_mov_b32_e32 v11, v4
	v_mov_b32_e32 v12, v4
	v_mov_b32_e32 v13, v4
	v_mov_b32_e32 v14, v4
	v_mov_b32_e32 v15, v4
	v_mov_b32_e32 v16, v4
	v_mov_b32_e32 v17, v4
	v_mov_b32_e32 v18, v4
	s_waitcnt vmcnt(3)
	v_cvt_f32_f16_sdwa v19, v31 dst_sel:DWORD dst_unused:UNUSED_PAD src0_sel:WORD_1
	v_cvt_f32_f16_e32 v29, v31
	v_cvt_f32_f16_sdwa v31, v30 dst_sel:DWORD dst_unused:UNUSED_PAD src0_sel:WORD_1
	v_cvt_f32_f16_e32 v30, v30
	v_cvt_f32_f16_sdwa v115, v33 dst_sel:DWORD dst_unused:UNUSED_PAD src0_sel:WORD_1
	v_cvt_f32_f16_e32 v134, v33
	v_cvt_f32_f16_sdwa v133, v32 dst_sel:DWORD dst_unused:UNUSED_PAD src0_sel:WORD_1
	v_cvt_f32_f16_e32 v132, v32
	v_sub_f32_e32 v30, v30, v38
	v_sub_f32_e32 v31, v31, v38
	v_sub_f32_e32 v32, v29, v38
	v_sub_f32_e32 v33, v19, v38
	v_sub_f32_e32 v132, v132, v38
	v_sub_f32_e32 v133, v133, v38
	v_sub_f32_e32 v134, v134, v38
	v_sub_f32_e32 v135, v115, v38
	v_pk_mul_f32 v[30:31], v[38:39], v[30:31] op_sel:[1,0]
	v_pk_mul_f32 v[32:33], v[38:39], v[32:33] op_sel:[1,0]
	v_pk_mul_f32 v[134:135], v[38:39], v[134:135] op_sel:[1,0]
	v_pk_mul_f32 v[38:39], v[38:39], v[132:133] op_sel:[1,0]
	s_waitcnt lgkmcnt(1)
	v_fma_f32 v19, v116, v30, v124
	v_fma_f32 v30, v117, v31, v125
	s_waitcnt lgkmcnt(0)
	v_fma_f32 v29, v120, v38, v128
	v_fma_f32 v31, v121, v39, v129
	v_fma_f32 v32, v118, v32, v126
	v_fma_f32 v38, v122, v134, v130
	v_fmac_f32_e32 v127, v119, v33
	v_fmac_f32_e32 v131, v123, v135
	ds_write2_b32 v220, v19, v30 offset1:65
	ds_write2_b32 v221, v29, v31 offset1:65
	ds_write2_b32 v220, v32, v127 offset0:130 offset1:195
	ds_write2_b32 v221, v38, v131 offset0:130 offset1:195
	s_waitcnt vmcnt(2)
	ds_write_b128 v96, v[34:37] offset:41984
	v_mov_b32_e32 v19, v4
	s_waitcnt lgkmcnt(0)
	s_barrier
	ds_read_b32 v200, v218
	ds_read_b32 v208, v219
	ds_read_b32 v201, v218 offset:520
	ds_read_b32 v209, v219 offset:256
	ds_read_b32 v202, v218 offset:1040
	ds_read_b32 v210, v219 offset:512
	ds_read_b32 v203, v218 offset:1560
	ds_read_b32 v211, v219 offset:768
	ds_read_b32 v204, v218 offset:2080
	ds_read_b32 v212, v219 offset:1024
	ds_read_b32 v205, v218 offset:2600
	ds_read_b32 v213, v219 offset:1280
	ds_read_b32 v206, v218 offset:3120
	ds_read_b32 v214, v219 offset:1536
	s_waitcnt lgkmcnt(12)
	v_mfma_f32_32x32x2_f32 v[4:19], v200, v208, v[4:19]
	ds_read_b32 v207, v218 offset:3640
	ds_read_b32 v215, v219 offset:1792
	s_waitcnt lgkmcnt(12)
	v_mfma_f32_32x32x2_f32 v[4:19], v201, v209, v[4:19]
	s_waitcnt lgkmcnt(10)
	v_mfma_f32_32x32x2_f32 v[4:19], v202, v210, v[4:19]
	s_waitcnt lgkmcnt(8)
	v_mfma_f32_32x32x2_f32 v[4:19], v203, v211, v[4:19]
	s_waitcnt lgkmcnt(6)
	v_mfma_f32_32x32x2_f32 v[4:19], v204, v212, v[4:19]
	s_waitcnt lgkmcnt(4)
	v_mfma_f32_32x32x2_f32 v[4:19], v205, v213, v[4:19]
	s_waitcnt lgkmcnt(2)
	v_mfma_f32_32x32x2_f32 v[4:19], v206, v214, v[4:19]
	s_waitcnt lgkmcnt(0)
	v_mfma_f32_32x32x2_f32 v[4:19], v207, v215, v[4:19]
	s_barrier
	global_load_dwordx4 v[32:35], v[92:93], off offset:256 sc1
	global_load_dwordx4 v[28:31], v[54:55], off
	s_waitcnt vmcnt(2)
	v_cvt_f32_f16_sdwa v128, v24 dst_sel:DWORD dst_unused:UNUSED_PAD src0_sel:WORD_1
	v_cvt_f32_f16_e32 v24, v24
	v_cvt_f32_f16_e32 v129, v25
	v_cvt_f32_f16_sdwa v130, v26 dst_sel:DWORD dst_unused:UNUSED_PAD src0_sel:WORD_1
	v_cvt_f32_f16_e32 v133, v26
	ds_read_b128 v[36:39], v43 offset:12544
	ds_read_b128 v[116:119], v43 offset:12560
	ds_read_b128 v[120:123], v43 offset:16640
	ds_read_b128 v[124:127], v43 offset:16656
	v_cvt_f32_f16_sdwa v115, v25 dst_sel:DWORD dst_unused:UNUSED_PAD src0_sel:WORD_1
	v_cvt_f32_f16_sdwa v131, v27 dst_sel:DWORD dst_unused:UNUSED_PAD src0_sel:WORD_1
	v_cvt_f32_f16_e32 v132, v27
	v_sub_f32_e32 v24, v24, v0
	v_sub_f32_e32 v25, v128, v1
	v_sub_f32_e32 v26, v129, v2
	v_pk_mul_f32 v[24:25], v[88:89], v[24:25]
	v_sub_f32_e32 v128, v133, v0
	v_sub_f32_e32 v129, v130, v1
	v_sub_f32_e32 v27, v115, v3
	v_sub_f32_e32 v130, v132, v2
	v_sub_f32_e32 v131, v131, v3
	v_pk_mul_f32 v[128:129], v[88:89], v[128:129]
	s_waitcnt lgkmcnt(1)
	v_fma_f32 v24, v36, v24, v120
	v_fma_f32 v25, v37, v25, v121
	v_pk_mul_f32 v[26:27], v[90:91], v[26:27]
	v_pk_mul_f32 v[130:131], v[90:91], v[130:131]
	s_waitcnt lgkmcnt(0)
	v_fma_f32 v36, v116, v128, v124
	ds_write2_b32 v220, v24, v25 offset1:65
	v_fma_f32 v24, v117, v129, v125
	ds_write2_b32 v221, v36, v24 offset1:65
	v_fma_f32 v24, v38, v26, v122
	v_fma_f32 v25, v118, v130, v126
	v_fmac_f32_e32 v123, v39, v27
	v_fmac_f32_e32 v127, v119, v131
	ds_write2_b32 v220, v24, v123 offset0:130 offset1:195
	ds_write2_b32 v221, v25, v127 offset0:130 offset1:195
	ds_write_b128 v96, v[20:23] offset:41984
	s_mov_b32 s16, 0
	v_mov_b32_e32 v20, v103
	s_waitcnt lgkmcnt(0)
	s_barrier
	ds_read_b32 v200, v218
	ds_read_b32 v208, v219
	ds_read_b32 v201, v218 offset:520
	ds_read_b32 v209, v219 offset:256
	ds_read_b32 v202, v218 offset:1040
	ds_read_b32 v210, v219 offset:512
	ds_read_b32 v203, v218 offset:1560
	ds_read_b32 v211, v219 offset:768
	ds_read_b32 v204, v218 offset:2080
	ds_read_b32 v212, v219 offset:1024
	ds_read_b32 v205, v218 offset:2600
	ds_read_b32 v213, v219 offset:1280
	ds_read_b32 v206, v218 offset:3120
	ds_read_b32 v214, v219 offset:1536
	s_waitcnt lgkmcnt(12)
	v_mfma_f32_32x32x2_f32 v[4:19], v200, v208, v[4:19]
	ds_read_b32 v207, v218 offset:3640
	ds_read_b32 v215, v219 offset:1792
	s_waitcnt lgkmcnt(12)
	v_mfma_f32_32x32x2_f32 v[4:19], v201, v209, v[4:19]
	s_waitcnt lgkmcnt(10)
	v_mfma_f32_32x32x2_f32 v[4:19], v202, v210, v[4:19]
	s_waitcnt lgkmcnt(8)
	v_mfma_f32_32x32x2_f32 v[4:19], v203, v211, v[4:19]
	s_waitcnt lgkmcnt(6)
	v_mfma_f32_32x32x2_f32 v[4:19], v204, v212, v[4:19]
	s_waitcnt lgkmcnt(4)
	v_mfma_f32_32x32x2_f32 v[4:19], v205, v213, v[4:19]
	s_waitcnt lgkmcnt(2)
	v_mfma_f32_32x32x2_f32 v[4:19], v206, v214, v[4:19]
	s_waitcnt lgkmcnt(0)
	v_mfma_f32_32x32x2_f32 v[4:19], v207, v215, v[4:19]
	s_barrier
	global_load_dwordx4 v[36:39], v[92:93], off offset:384 sc1
	global_load_dwordx4 v[20:23], v[56:57], off
	s_waitcnt vmcnt(3)
	v_cvt_f32_f16_sdwa v128, v32 dst_sel:DWORD dst_unused:UNUSED_PAD src0_sel:WORD_1
	v_cvt_f32_f16_e32 v32, v32
	v_cvt_f32_f16_e32 v129, v33
	v_cvt_f32_f16_sdwa v130, v34 dst_sel:DWORD dst_unused:UNUSED_PAD src0_sel:WORD_1
	v_cvt_f32_f16_e32 v133, v34
	ds_read_b128 v[24:27], v43 offset:12800
	ds_read_b128 v[116:119], v43 offset:12816
	ds_read_b128 v[120:123], v43 offset:16896
	ds_read_b128 v[124:127], v43 offset:16912
	v_cvt_f32_f16_sdwa v115, v33 dst_sel:DWORD dst_unused:UNUSED_PAD src0_sel:WORD_1
	v_cvt_f32_f16_sdwa v131, v35 dst_sel:DWORD dst_unused:UNUSED_PAD src0_sel:WORD_1
	v_cvt_f32_f16_e32 v132, v35
	v_sub_f32_e32 v32, v32, v0
	v_sub_f32_e32 v33, v128, v1
	v_sub_f32_e32 v34, v129, v2
	v_pk_mul_f32 v[32:33], v[88:89], v[32:33]
	v_sub_f32_e32 v128, v133, v0
	v_sub_f32_e32 v129, v130, v1
	v_sub_f32_e32 v35, v115, v3
	v_pk_mul_f32 v[128:129], v[88:89], v[128:129]
	s_waitcnt lgkmcnt(1)
	v_fma_f32 v24, v24, v32, v120
	v_fma_f32 v25, v25, v33, v121
	v_pk_mul_f32 v[34:35], v[90:91], v[34:35]
	v_sub_f32_e32 v130, v132, v2
	v_sub_f32_e32 v131, v131, v3
	s_waitcnt lgkmcnt(0)
	v_fma_f32 v32, v116, v128, v124
	ds_write2_b32 v220, v24, v25 offset1:65
	v_fma_f32 v24, v117, v129, v125
	v_pk_mul_f32 v[130:131], v[90:91], v[130:131]
	ds_write2_b32 v221, v32, v24 offset1:65
	v_fma_f32 v24, v26, v34, v122
	v_fmac_f32_e32 v123, v27, v35
	v_fma_f32 v25, v118, v130, v126
	ds_write2_b32 v220, v24, v123 offset0:130 offset1:195
	v_fmac_f32_e32 v127, v119, v131
	s_mov_b32 s16, 0
	v_mov_b32_e32 v24, v103
	ds_write2_b32 v221, v25, v127 offset0:130 offset1:195
	s_waitcnt vmcnt(2)
	ds_write_b128 v96, v[28:31] offset:41984
	s_waitcnt lgkmcnt(0)
	s_barrier
	ds_read_b32 v200, v218
	ds_read_b32 v208, v219
	ds_read_b32 v201, v218 offset:520
	ds_read_b32 v209, v219 offset:256
	ds_read_b32 v202, v218 offset:1040
	ds_read_b32 v210, v219 offset:512
	ds_read_b32 v203, v218 offset:1560
	ds_read_b32 v211, v219 offset:768
	ds_read_b32 v204, v218 offset:2080
	ds_read_b32 v212, v219 offset:1024
	ds_read_b32 v205, v218 offset:2600
	ds_read_b32 v213, v219 offset:1280
	ds_read_b32 v206, v218 offset:3120
	ds_read_b32 v214, v219 offset:1536
	s_waitcnt lgkmcnt(12)
	v_mfma_f32_32x32x2_f32 v[4:19], v200, v208, v[4:19]
	ds_read_b32 v207, v218 offset:3640
	ds_read_b32 v215, v219 offset:1792
	s_waitcnt lgkmcnt(12)
	v_mfma_f32_32x32x2_f32 v[4:19], v201, v209, v[4:19]
	s_waitcnt lgkmcnt(10)
	v_mfma_f32_32x32x2_f32 v[4:19], v202, v210, v[4:19]
	s_waitcnt lgkmcnt(8)
	v_mfma_f32_32x32x2_f32 v[4:19], v203, v211, v[4:19]
	s_waitcnt lgkmcnt(6)
	v_mfma_f32_32x32x2_f32 v[4:19], v204, v212, v[4:19]
	s_waitcnt lgkmcnt(4)
	v_mfma_f32_32x32x2_f32 v[4:19], v205, v213, v[4:19]
	s_waitcnt lgkmcnt(2)
	v_mfma_f32_32x32x2_f32 v[4:19], v206, v214, v[4:19]
	s_waitcnt lgkmcnt(0)
	v_mfma_f32_32x32x2_f32 v[4:19], v207, v215, v[4:19]
	s_barrier
	global_load_dwordx4 v[28:31], v[92:93], off offset:512 sc1
	global_load_dwordx4 v[24:27], v[58:59], off
	s_waitcnt vmcnt(3)
	v_cvt_f32_f16_sdwa v128, v36 dst_sel:DWORD dst_unused:UNUSED_PAD src0_sel:WORD_1
	v_cvt_f32_f16_e32 v36, v36
	v_cvt_f32_f16_e32 v129, v37
	v_cvt_f32_f16_sdwa v130, v38 dst_sel:DWORD dst_unused:UNUSED_PAD src0_sel:WORD_1
	v_cvt_f32_f16_e32 v133, v38
	ds_read_b128 v[32:35], v43 offset:13056
	ds_read_b128 v[116:119], v43 offset:13072
	ds_read_b128 v[120:123], v43 offset:17152
	ds_read_b128 v[124:127], v43 offset:17168
	v_cvt_f32_f16_sdwa v115, v37 dst_sel:DWORD dst_unused:UNUSED_PAD src0_sel:WORD_1
	v_cvt_f32_f16_sdwa v131, v39 dst_sel:DWORD dst_unused:UNUSED_PAD src0_sel:WORD_1
	v_cvt_f32_f16_e32 v132, v39
	v_sub_f32_e32 v36, v36, v0
	v_sub_f32_e32 v37, v128, v1
	v_sub_f32_e32 v38, v129, v2
	v_pk_mul_f32 v[36:37], v[88:89], v[36:37]
	v_sub_f32_e32 v128, v133, v0
	v_sub_f32_e32 v129, v130, v1
	v_sub_f32_e32 v39, v115, v3
	v_sub_f32_e32 v130, v132, v2
	v_sub_f32_e32 v131, v131, v3
	v_pk_mul_f32 v[128:129], v[88:89], v[128:129]
	s_waitcnt lgkmcnt(1)
	v_fma_f32 v32, v32, v36, v120
	v_fma_f32 v33, v33, v37, v121
	v_pk_mul_f32 v[38:39], v[90:91], v[38:39]
	v_pk_mul_f32 v[130:131], v[90:91], v[130:131]
	s_waitcnt lgkmcnt(0)
	v_fma_f32 v36, v116, v128, v124
	ds_write2_b32 v220, v32, v33 offset1:65
	v_fma_f32 v32, v117, v129, v125
	ds_write2_b32 v221, v36, v32 offset1:65
	v_fma_f32 v32, v34, v38, v122
	v_fma_f32 v33, v118, v130, v126
	v_fmac_f32_e32 v123, v35, v39
	v_fmac_f32_e32 v127, v119, v131
	ds_write2_b32 v220, v32, v123 offset0:130 offset1:195
	ds_write2_b32 v221, v33, v127 offset0:130 offset1:195
	s_waitcnt vmcnt(2)
	ds_write_b128 v96, v[20:23] offset:41984
	s_mov_b32 s16, 0
	v_mov_b32_e32 v20, v103
	s_waitcnt lgkmcnt(0)
	s_barrier
	ds_read_b32 v200, v218
	ds_read_b32 v208, v219
	ds_read_b32 v201, v218 offset:520
	ds_read_b32 v209, v219 offset:256
	ds_read_b32 v202, v218 offset:1040
	ds_read_b32 v210, v219 offset:512
	ds_read_b32 v203, v218 offset:1560
	ds_read_b32 v211, v219 offset:768
	ds_read_b32 v204, v218 offset:2080
	ds_read_b32 v212, v219 offset:1024
	ds_read_b32 v205, v218 offset:2600
	ds_read_b32 v213, v219 offset:1280
	ds_read_b32 v206, v218 offset:3120
	ds_read_b32 v214, v219 offset:1536
	s_waitcnt lgkmcnt(12)
	v_mfma_f32_32x32x2_f32 v[4:19], v200, v208, v[4:19]
	ds_read_b32 v207, v218 offset:3640
	ds_read_b32 v215, v219 offset:1792
	s_waitcnt lgkmcnt(12)
	v_mfma_f32_32x32x2_f32 v[4:19], v201, v209, v[4:19]
	s_waitcnt lgkmcnt(10)
	v_mfma_f32_32x32x2_f32 v[4:19], v202, v210, v[4:19]
	s_waitcnt lgkmcnt(8)
	v_mfma_f32_32x32x2_f32 v[4:19], v203, v211, v[4:19]
	s_waitcnt lgkmcnt(6)
	v_mfma_f32_32x32x2_f32 v[4:19], v204, v212, v[4:19]
	s_waitcnt lgkmcnt(4)
	v_mfma_f32_32x32x2_f32 v[4:19], v205, v213, v[4:19]
	s_waitcnt lgkmcnt(2)
	v_mfma_f32_32x32x2_f32 v[4:19], v206, v214, v[4:19]
	s_waitcnt lgkmcnt(0)
	v_mfma_f32_32x32x2_f32 v[4:19], v207, v215, v[4:19]
	s_barrier
	global_load_dwordx4 v[32:35], v[92:93], off offset:640 sc1
	global_load_dwordx4 v[20:23], v[60:61], off
	s_waitcnt vmcnt(3)
	v_cvt_f32_f16_sdwa v128, v28 dst_sel:DWORD dst_unused:UNUSED_PAD src0_sel:WORD_1
	v_cvt_f32_f16_e32 v28, v28
	v_cvt_f32_f16_e32 v129, v29
	v_cvt_f32_f16_sdwa v130, v30 dst_sel:DWORD dst_unused:UNUSED_PAD src0_sel:WORD_1
	v_cvt_f32_f16_e32 v133, v30
	ds_read_b128 v[36:39], v43 offset:13312
	ds_read_b128 v[116:119], v43 offset:13328
	ds_read_b128 v[120:123], v43 offset:17408
	ds_read_b128 v[124:127], v43 offset:17424
	v_cvt_f32_f16_sdwa v115, v29 dst_sel:DWORD dst_unused:UNUSED_PAD src0_sel:WORD_1
	v_cvt_f32_f16_sdwa v131, v31 dst_sel:DWORD dst_unused:UNUSED_PAD src0_sel:WORD_1
	v_cvt_f32_f16_e32 v132, v31
	v_sub_f32_e32 v28, v28, v0
	v_sub_f32_e32 v29, v128, v1
	v_sub_f32_e32 v30, v129, v2
	v_pk_mul_f32 v[28:29], v[88:89], v[28:29]
	v_sub_f32_e32 v128, v133, v0
	v_sub_f32_e32 v129, v130, v1
	v_sub_f32_e32 v31, v115, v3
	v_sub_f32_e32 v130, v132, v2
	v_sub_f32_e32 v131, v131, v3
	v_pk_mul_f32 v[128:129], v[88:89], v[128:129]
	s_waitcnt lgkmcnt(1)
	v_fma_f32 v28, v36, v28, v120
	v_fma_f32 v29, v37, v29, v121
	v_pk_mul_f32 v[30:31], v[90:91], v[30:31]
	v_pk_mul_f32 v[130:131], v[90:91], v[130:131]
	s_waitcnt lgkmcnt(0)
	v_fma_f32 v36, v116, v128, v124
	ds_write2_b32 v220, v28, v29 offset1:65
	v_fma_f32 v28, v117, v129, v125
	ds_write2_b32 v221, v36, v28 offset1:65
	v_fma_f32 v28, v38, v30, v122
	v_fma_f32 v29, v118, v130, v126
	v_fmac_f32_e32 v123, v39, v31
	v_fmac_f32_e32 v127, v119, v131
	ds_write2_b32 v220, v28, v123 offset0:130 offset1:195
	ds_write2_b32 v221, v29, v127 offset0:130 offset1:195
	s_waitcnt vmcnt(2)
	ds_write_b128 v96, v[24:27] offset:41984
	s_mov_b32 s16, 0
	v_mov_b32_e32 v24, v103
	s_waitcnt lgkmcnt(0)
	s_barrier
	ds_read_b32 v200, v218
	ds_read_b32 v208, v219
	ds_read_b32 v201, v218 offset:520
	ds_read_b32 v209, v219 offset:256
	ds_read_b32 v202, v218 offset:1040
	ds_read_b32 v210, v219 offset:512
	ds_read_b32 v203, v218 offset:1560
	ds_read_b32 v211, v219 offset:768
	ds_read_b32 v204, v218 offset:2080
	ds_read_b32 v212, v219 offset:1024
	ds_read_b32 v205, v218 offset:2600
	ds_read_b32 v213, v219 offset:1280
	ds_read_b32 v206, v218 offset:3120
	ds_read_b32 v214, v219 offset:1536
	s_waitcnt lgkmcnt(12)
	v_mfma_f32_32x32x2_f32 v[4:19], v200, v208, v[4:19]
	ds_read_b32 v207, v218 offset:3640
	ds_read_b32 v215, v219 offset:1792
	s_waitcnt lgkmcnt(12)
	v_mfma_f32_32x32x2_f32 v[4:19], v201, v209, v[4:19]
	s_waitcnt lgkmcnt(10)
	v_mfma_f32_32x32x2_f32 v[4:19], v202, v210, v[4:19]
	s_waitcnt lgkmcnt(8)
	v_mfma_f32_32x32x2_f32 v[4:19], v203, v211, v[4:19]
	s_waitcnt lgkmcnt(6)
	v_mfma_f32_32x32x2_f32 v[4:19], v204, v212, v[4:19]
	s_waitcnt lgkmcnt(4)
	v_mfma_f32_32x32x2_f32 v[4:19], v205, v213, v[4:19]
	s_waitcnt lgkmcnt(2)
	v_mfma_f32_32x32x2_f32 v[4:19], v206, v214, v[4:19]
	s_waitcnt lgkmcnt(0)
	v_mfma_f32_32x32x2_f32 v[4:19], v207, v215, v[4:19]
	s_barrier
	global_load_dwordx4 v[28:31], v[92:93], off offset:768 sc1
	global_load_dwordx4 v[24:27], v[62:63], off
	s_waitcnt vmcnt(3)
	v_cvt_f32_f16_sdwa v128, v32 dst_sel:DWORD dst_unused:UNUSED_PAD src0_sel:WORD_1
	v_cvt_f32_f16_e32 v32, v32
	v_cvt_f32_f16_e32 v129, v33
	v_cvt_f32_f16_sdwa v130, v34 dst_sel:DWORD dst_unused:UNUSED_PAD src0_sel:WORD_1
	v_cvt_f32_f16_e32 v133, v34
	ds_read_b128 v[36:39], v43 offset:13568
	ds_read_b128 v[116:119], v43 offset:13584
	ds_read_b128 v[120:123], v43 offset:17664
	ds_read_b128 v[124:127], v43 offset:17680
	v_cvt_f32_f16_sdwa v115, v33 dst_sel:DWORD dst_unused:UNUSED_PAD src0_sel:WORD_1
	v_cvt_f32_f16_sdwa v131, v35 dst_sel:DWORD dst_unused:UNUSED_PAD src0_sel:WORD_1
	v_cvt_f32_f16_e32 v132, v35
	v_sub_f32_e32 v32, v32, v0
	v_sub_f32_e32 v33, v128, v1
	v_sub_f32_e32 v34, v129, v2
	v_pk_mul_f32 v[32:33], v[88:89], v[32:33]
	v_sub_f32_e32 v128, v133, v0
	v_sub_f32_e32 v129, v130, v1
	v_sub_f32_e32 v35, v115, v3
	v_sub_f32_e32 v130, v132, v2
	v_sub_f32_e32 v131, v131, v3
	v_pk_mul_f32 v[128:129], v[88:89], v[128:129]
	s_waitcnt lgkmcnt(1)
	v_fma_f32 v32, v36, v32, v120
	v_fma_f32 v33, v37, v33, v121
	v_pk_mul_f32 v[34:35], v[90:91], v[34:35]
	v_pk_mul_f32 v[130:131], v[90:91], v[130:131]
	s_waitcnt lgkmcnt(0)
	v_fma_f32 v36, v116, v128, v124
	ds_write2_b32 v220, v32, v33 offset1:65
	v_fma_f32 v32, v117, v129, v125
	ds_write2_b32 v221, v36, v32 offset1:65
	v_fma_f32 v32, v38, v34, v122
	v_fma_f32 v33, v118, v130, v126
	v_fmac_f32_e32 v123, v39, v35
	v_fmac_f32_e32 v127, v119, v131
	ds_write2_b32 v220, v32, v123 offset0:130 offset1:195
	ds_write2_b32 v221, v33, v127 offset0:130 offset1:195
	s_waitcnt vmcnt(2)
	ds_write_b128 v96, v[20:23] offset:41984
	s_mov_b32 s16, 0
	v_mov_b32_e32 v20, v103
	s_waitcnt lgkmcnt(0)
	s_barrier
	ds_read_b32 v200, v218
	ds_read_b32 v208, v219
	ds_read_b32 v201, v218 offset:520
	ds_read_b32 v209, v219 offset:256
	ds_read_b32 v202, v218 offset:1040
	ds_read_b32 v210, v219 offset:512
	ds_read_b32 v203, v218 offset:1560
	ds_read_b32 v211, v219 offset:768
	ds_read_b32 v204, v218 offset:2080
	ds_read_b32 v212, v219 offset:1024
	ds_read_b32 v205, v218 offset:2600
	ds_read_b32 v213, v219 offset:1280
	ds_read_b32 v206, v218 offset:3120
	ds_read_b32 v214, v219 offset:1536
	s_waitcnt lgkmcnt(12)
	v_mfma_f32_32x32x2_f32 v[4:19], v200, v208, v[4:19]
	ds_read_b32 v207, v218 offset:3640
	ds_read_b32 v215, v219 offset:1792
	s_waitcnt lgkmcnt(12)
	v_mfma_f32_32x32x2_f32 v[4:19], v201, v209, v[4:19]
	s_waitcnt lgkmcnt(10)
	v_mfma_f32_32x32x2_f32 v[4:19], v202, v210, v[4:19]
	s_waitcnt lgkmcnt(8)
	v_mfma_f32_32x32x2_f32 v[4:19], v203, v211, v[4:19]
	s_waitcnt lgkmcnt(6)
	v_mfma_f32_32x32x2_f32 v[4:19], v204, v212, v[4:19]
	s_waitcnt lgkmcnt(4)
	v_mfma_f32_32x32x2_f32 v[4:19], v205, v213, v[4:19]
	s_waitcnt lgkmcnt(2)
	v_mfma_f32_32x32x2_f32 v[4:19], v206, v214, v[4:19]
	s_waitcnt lgkmcnt(0)
	v_mfma_f32_32x32x2_f32 v[4:19], v207, v215, v[4:19]
	s_barrier
	global_load_dwordx4 v[32:35], v[92:93], off offset:896 sc1
	global_load_dwordx4 v[20:23], v[64:65], off
	s_waitcnt vmcnt(3)
	v_cvt_f32_f16_sdwa v128, v28 dst_sel:DWORD dst_unused:UNUSED_PAD src0_sel:WORD_1
	v_cvt_f32_f16_e32 v28, v28
	v_cvt_f32_f16_e32 v129, v29
	v_cvt_f32_f16_sdwa v130, v30 dst_sel:DWORD dst_unused:UNUSED_PAD src0_sel:WORD_1
	v_cvt_f32_f16_e32 v133, v30
	ds_read_b128 v[36:39], v43 offset:13824
	ds_read_b128 v[116:119], v43 offset:13840
	ds_read_b128 v[120:123], v43 offset:17920
	ds_read_b128 v[124:127], v43 offset:17936
	v_cvt_f32_f16_sdwa v115, v29 dst_sel:DWORD dst_unused:UNUSED_PAD src0_sel:WORD_1
	v_cvt_f32_f16_sdwa v131, v31 dst_sel:DWORD dst_unused:UNUSED_PAD src0_sel:WORD_1
	v_cvt_f32_f16_e32 v132, v31
	v_sub_f32_e32 v28, v28, v0
	v_sub_f32_e32 v29, v128, v1
	v_sub_f32_e32 v30, v129, v2
	v_pk_mul_f32 v[28:29], v[88:89], v[28:29]
	v_sub_f32_e32 v128, v133, v0
	v_sub_f32_e32 v129, v130, v1
	v_sub_f32_e32 v31, v115, v3
	v_sub_f32_e32 v130, v132, v2
	v_sub_f32_e32 v131, v131, v3
	v_pk_mul_f32 v[128:129], v[88:89], v[128:129]
	s_waitcnt lgkmcnt(1)
	v_fma_f32 v28, v36, v28, v120
	v_fma_f32 v29, v37, v29, v121
	v_pk_mul_f32 v[30:31], v[90:91], v[30:31]
	v_pk_mul_f32 v[130:131], v[90:91], v[130:131]
	s_waitcnt lgkmcnt(0)
	v_fma_f32 v36, v116, v128, v124
	ds_write2_b32 v220, v28, v29 offset1:65
	v_fma_f32 v28, v117, v129, v125
	ds_write2_b32 v221, v36, v28 offset1:65
	v_fma_f32 v28, v38, v30, v122
	v_fma_f32 v29, v118, v130, v126
	v_fmac_f32_e32 v123, v39, v31
	v_fmac_f32_e32 v127, v119, v131
	ds_write2_b32 v220, v28, v123 offset0:130 offset1:195
	ds_write2_b32 v221, v29, v127 offset0:130 offset1:195
	s_waitcnt vmcnt(2)
	ds_write_b128 v96, v[24:27] offset:41984
	s_mov_b32 s16, 0
	v_mov_b32_e32 v24, v103
	s_waitcnt lgkmcnt(0)
	s_barrier
	ds_read_b32 v200, v218
	ds_read_b32 v208, v219
	ds_read_b32 v201, v218 offset:520
	ds_read_b32 v209, v219 offset:256
	ds_read_b32 v202, v218 offset:1040
	ds_read_b32 v210, v219 offset:512
	ds_read_b32 v203, v218 offset:1560
	ds_read_b32 v211, v219 offset:768
	ds_read_b32 v204, v218 offset:2080
	ds_read_b32 v212, v219 offset:1024
	ds_read_b32 v205, v218 offset:2600
	ds_read_b32 v213, v219 offset:1280
	ds_read_b32 v206, v218 offset:3120
	ds_read_b32 v214, v219 offset:1536
	s_waitcnt lgkmcnt(12)
	v_mfma_f32_32x32x2_f32 v[4:19], v200, v208, v[4:19]
	ds_read_b32 v207, v218 offset:3640
	ds_read_b32 v215, v219 offset:1792
	s_waitcnt lgkmcnt(12)
	v_mfma_f32_32x32x2_f32 v[4:19], v201, v209, v[4:19]
	s_waitcnt lgkmcnt(10)
	v_mfma_f32_32x32x2_f32 v[4:19], v202, v210, v[4:19]
	s_waitcnt lgkmcnt(8)
	v_mfma_f32_32x32x2_f32 v[4:19], v203, v211, v[4:19]
	s_waitcnt lgkmcnt(6)
	v_mfma_f32_32x32x2_f32 v[4:19], v204, v212, v[4:19]
	s_waitcnt lgkmcnt(4)
	v_mfma_f32_32x32x2_f32 v[4:19], v205, v213, v[4:19]
	s_waitcnt lgkmcnt(2)
	v_mfma_f32_32x32x2_f32 v[4:19], v206, v214, v[4:19]
	s_waitcnt lgkmcnt(0)
	v_mfma_f32_32x32x2_f32 v[4:19], v207, v215, v[4:19]
	s_barrier
	global_load_dwordx4 v[28:31], v[92:93], off offset:1024 sc1
	global_load_dwordx4 v[24:27], v[66:67], off
	s_waitcnt vmcnt(3)
	v_cvt_f32_f16_sdwa v128, v32 dst_sel:DWORD dst_unused:UNUSED_PAD src0_sel:WORD_1
	v_cvt_f32_f16_e32 v32, v32
	v_cvt_f32_f16_e32 v129, v33
	v_cvt_f32_f16_sdwa v130, v34 dst_sel:DWORD dst_unused:UNUSED_PAD src0_sel:WORD_1
	v_cvt_f32_f16_e32 v133, v34
	ds_read_b128 v[36:39], v43 offset:14080
	ds_read_b128 v[116:119], v43 offset:14096
	ds_read_b128 v[120:123], v43 offset:18176
	ds_read_b128 v[124:127], v43 offset:18192
	v_cvt_f32_f16_sdwa v115, v33 dst_sel:DWORD dst_unused:UNUSED_PAD src0_sel:WORD_1
	v_cvt_f32_f16_sdwa v131, v35 dst_sel:DWORD dst_unused:UNUSED_PAD src0_sel:WORD_1
	v_cvt_f32_f16_e32 v132, v35
	v_sub_f32_e32 v32, v32, v0
	v_sub_f32_e32 v33, v128, v1
	v_sub_f32_e32 v34, v129, v2
	v_pk_mul_f32 v[32:33], v[88:89], v[32:33]
	v_sub_f32_e32 v128, v133, v0
	v_sub_f32_e32 v129, v130, v1
	v_sub_f32_e32 v35, v115, v3
	v_sub_f32_e32 v130, v132, v2
	v_sub_f32_e32 v131, v131, v3
	v_pk_mul_f32 v[128:129], v[88:89], v[128:129]
	s_waitcnt lgkmcnt(1)
	v_fma_f32 v32, v36, v32, v120
	v_fma_f32 v33, v37, v33, v121
	v_pk_mul_f32 v[34:35], v[90:91], v[34:35]
	v_pk_mul_f32 v[130:131], v[90:91], v[130:131]
	s_waitcnt lgkmcnt(0)
	v_fma_f32 v36, v116, v128, v124
	ds_write2_b32 v220, v32, v33 offset1:65
	v_fma_f32 v32, v117, v129, v125
	ds_write2_b32 v221, v36, v32 offset1:65
	v_fma_f32 v32, v38, v34, v122
	v_fma_f32 v33, v118, v130, v126
	v_fmac_f32_e32 v123, v39, v35
	v_fmac_f32_e32 v127, v119, v131
	ds_write2_b32 v220, v32, v123 offset0:130 offset1:195
	ds_write2_b32 v221, v33, v127 offset0:130 offset1:195
	s_waitcnt vmcnt(2)
	ds_write_b128 v96, v[20:23] offset:41984
	s_mov_b32 s16, 0
	v_mov_b32_e32 v20, v103
	s_waitcnt lgkmcnt(0)
	s_barrier
	ds_read_b32 v200, v218
	ds_read_b32 v208, v219
	ds_read_b32 v201, v218 offset:520
	ds_read_b32 v209, v219 offset:256
	ds_read_b32 v202, v218 offset:1040
	ds_read_b32 v210, v219 offset:512
	ds_read_b32 v203, v218 offset:1560
	ds_read_b32 v211, v219 offset:768
	ds_read_b32 v204, v218 offset:2080
	ds_read_b32 v212, v219 offset:1024
	ds_read_b32 v205, v218 offset:2600
	ds_read_b32 v213, v219 offset:1280
	ds_read_b32 v206, v218 offset:3120
	ds_read_b32 v214, v219 offset:1536
	s_waitcnt lgkmcnt(12)
	v_mfma_f32_32x32x2_f32 v[4:19], v200, v208, v[4:19]
	ds_read_b32 v207, v218 offset:3640
	ds_read_b32 v215, v219 offset:1792
	s_waitcnt lgkmcnt(12)
	v_mfma_f32_32x32x2_f32 v[4:19], v201, v209, v[4:19]
	s_waitcnt lgkmcnt(10)
	v_mfma_f32_32x32x2_f32 v[4:19], v202, v210, v[4:19]
	s_waitcnt lgkmcnt(8)
	v_mfma_f32_32x32x2_f32 v[4:19], v203, v211, v[4:19]
	s_waitcnt lgkmcnt(6)
	v_mfma_f32_32x32x2_f32 v[4:19], v204, v212, v[4:19]
	s_waitcnt lgkmcnt(4)
	v_mfma_f32_32x32x2_f32 v[4:19], v205, v213, v[4:19]
	s_waitcnt lgkmcnt(2)
	v_mfma_f32_32x32x2_f32 v[4:19], v206, v214, v[4:19]
	s_waitcnt lgkmcnt(0)
	v_mfma_f32_32x32x2_f32 v[4:19], v207, v215, v[4:19]
	s_barrier
	global_load_dwordx4 v[32:35], v[92:93], off offset:1152 sc1
	global_load_dwordx4 v[20:23], v[68:69], off
	s_waitcnt vmcnt(3)
	v_cvt_f32_f16_sdwa v128, v28 dst_sel:DWORD dst_unused:UNUSED_PAD src0_sel:WORD_1
	v_cvt_f32_f16_e32 v28, v28
	v_cvt_f32_f16_e32 v129, v29
	v_cvt_f32_f16_sdwa v130, v30 dst_sel:DWORD dst_unused:UNUSED_PAD src0_sel:WORD_1
	v_cvt_f32_f16_e32 v133, v30
	ds_read_b128 v[36:39], v43 offset:14336
	ds_read_b128 v[116:119], v43 offset:14352
	ds_read_b128 v[120:123], v43 offset:18432
	ds_read_b128 v[124:127], v43 offset:18448
	v_cvt_f32_f16_sdwa v115, v29 dst_sel:DWORD dst_unused:UNUSED_PAD src0_sel:WORD_1
	v_cvt_f32_f16_sdwa v131, v31 dst_sel:DWORD dst_unused:UNUSED_PAD src0_sel:WORD_1
	v_cvt_f32_f16_e32 v132, v31
	v_sub_f32_e32 v28, v28, v0
	v_sub_f32_e32 v29, v128, v1
	v_sub_f32_e32 v30, v129, v2
	v_pk_mul_f32 v[28:29], v[88:89], v[28:29]
	v_sub_f32_e32 v128, v133, v0
	v_sub_f32_e32 v129, v130, v1
	v_sub_f32_e32 v31, v115, v3
	v_sub_f32_e32 v130, v132, v2
	v_sub_f32_e32 v131, v131, v3
	v_pk_mul_f32 v[128:129], v[88:89], v[128:129]
	s_waitcnt lgkmcnt(1)
	v_fma_f32 v28, v36, v28, v120
	v_fma_f32 v29, v37, v29, v121
	v_pk_mul_f32 v[30:31], v[90:91], v[30:31]
	v_pk_mul_f32 v[130:131], v[90:91], v[130:131]
	s_waitcnt lgkmcnt(0)
	v_fma_f32 v36, v116, v128, v124
	ds_write2_b32 v220, v28, v29 offset1:65
	v_fma_f32 v28, v117, v129, v125
	ds_write2_b32 v221, v36, v28 offset1:65
	v_fma_f32 v28, v38, v30, v122
	v_fma_f32 v29, v118, v130, v126
	v_fmac_f32_e32 v123, v39, v31
	v_fmac_f32_e32 v127, v119, v131
	ds_write2_b32 v220, v28, v123 offset0:130 offset1:195
	ds_write2_b32 v221, v29, v127 offset0:130 offset1:195
	s_waitcnt vmcnt(2)
	ds_write_b128 v96, v[24:27] offset:41984
	s_mov_b32 s16, 0
	v_mov_b32_e32 v24, v103
	s_waitcnt lgkmcnt(0)
	s_barrier
	ds_read_b32 v200, v218
	ds_read_b32 v208, v219
	ds_read_b32 v201, v218 offset:520
	ds_read_b32 v209, v219 offset:256
	ds_read_b32 v202, v218 offset:1040
	ds_read_b32 v210, v219 offset:512
	ds_read_b32 v203, v218 offset:1560
	ds_read_b32 v211, v219 offset:768
	ds_read_b32 v204, v218 offset:2080
	ds_read_b32 v212, v219 offset:1024
	ds_read_b32 v205, v218 offset:2600
	ds_read_b32 v213, v219 offset:1280
	ds_read_b32 v206, v218 offset:3120
	ds_read_b32 v214, v219 offset:1536
	s_waitcnt lgkmcnt(12)
	v_mfma_f32_32x32x2_f32 v[4:19], v200, v208, v[4:19]
	ds_read_b32 v207, v218 offset:3640
	ds_read_b32 v215, v219 offset:1792
	s_waitcnt lgkmcnt(12)
	v_mfma_f32_32x32x2_f32 v[4:19], v201, v209, v[4:19]
	s_waitcnt lgkmcnt(10)
	v_mfma_f32_32x32x2_f32 v[4:19], v202, v210, v[4:19]
	s_waitcnt lgkmcnt(8)
	v_mfma_f32_32x32x2_f32 v[4:19], v203, v211, v[4:19]
	s_waitcnt lgkmcnt(6)
	v_mfma_f32_32x32x2_f32 v[4:19], v204, v212, v[4:19]
	s_waitcnt lgkmcnt(4)
	v_mfma_f32_32x32x2_f32 v[4:19], v205, v213, v[4:19]
	s_waitcnt lgkmcnt(2)
	v_mfma_f32_32x32x2_f32 v[4:19], v206, v214, v[4:19]
	s_waitcnt lgkmcnt(0)
	v_mfma_f32_32x32x2_f32 v[4:19], v207, v215, v[4:19]
	s_barrier
	global_load_dwordx4 v[28:31], v[92:93], off offset:1280 sc1
	global_load_dwordx4 v[24:27], v[70:71], off
	s_waitcnt vmcnt(3)
	v_cvt_f32_f16_sdwa v128, v32 dst_sel:DWORD dst_unused:UNUSED_PAD src0_sel:WORD_1
	v_cvt_f32_f16_e32 v32, v32
	v_cvt_f32_f16_e32 v129, v33
	v_cvt_f32_f16_sdwa v130, v34 dst_sel:DWORD dst_unused:UNUSED_PAD src0_sel:WORD_1
	v_cvt_f32_f16_e32 v133, v34
	ds_read_b128 v[36:39], v43 offset:14592
	ds_read_b128 v[116:119], v43 offset:14608
	ds_read_b128 v[120:123], v43 offset:18688
	ds_read_b128 v[124:127], v43 offset:18704
	v_cvt_f32_f16_sdwa v115, v33 dst_sel:DWORD dst_unused:UNUSED_PAD src0_sel:WORD_1
	v_cvt_f32_f16_sdwa v131, v35 dst_sel:DWORD dst_unused:UNUSED_PAD src0_sel:WORD_1
	v_cvt_f32_f16_e32 v132, v35
	v_sub_f32_e32 v32, v32, v0
	v_sub_f32_e32 v33, v128, v1
	v_sub_f32_e32 v34, v129, v2
	v_pk_mul_f32 v[32:33], v[88:89], v[32:33]
	v_sub_f32_e32 v128, v133, v0
	v_sub_f32_e32 v129, v130, v1
	v_sub_f32_e32 v35, v115, v3
	v_sub_f32_e32 v130, v132, v2
	v_sub_f32_e32 v131, v131, v3
	v_pk_mul_f32 v[128:129], v[88:89], v[128:129]
	s_waitcnt lgkmcnt(1)
	v_fma_f32 v32, v36, v32, v120
	v_fma_f32 v33, v37, v33, v121
	v_pk_mul_f32 v[34:35], v[90:91], v[34:35]
	v_pk_mul_f32 v[130:131], v[90:91], v[130:131]
	s_waitcnt lgkmcnt(0)
	v_fma_f32 v36, v116, v128, v124
	ds_write2_b32 v220, v32, v33 offset1:65
	v_fma_f32 v32, v117, v129, v125
	ds_write2_b32 v221, v36, v32 offset1:65
	v_fma_f32 v32, v38, v34, v122
	v_fma_f32 v33, v118, v130, v126
	v_fmac_f32_e32 v123, v39, v35
	v_fmac_f32_e32 v127, v119, v131
	ds_write2_b32 v220, v32, v123 offset0:130 offset1:195
	ds_write2_b32 v221, v33, v127 offset0:130 offset1:195
	s_waitcnt vmcnt(2)
	ds_write_b128 v96, v[20:23] offset:41984
	s_mov_b32 s16, 0
	v_mov_b32_e32 v20, v103
	s_waitcnt lgkmcnt(0)
	s_barrier
	ds_read_b32 v200, v218
	ds_read_b32 v208, v219
	ds_read_b32 v201, v218 offset:520
	ds_read_b32 v209, v219 offset:256
	ds_read_b32 v202, v218 offset:1040
	ds_read_b32 v210, v219 offset:512
	ds_read_b32 v203, v218 offset:1560
	ds_read_b32 v211, v219 offset:768
	ds_read_b32 v204, v218 offset:2080
	ds_read_b32 v212, v219 offset:1024
	ds_read_b32 v205, v218 offset:2600
	ds_read_b32 v213, v219 offset:1280
	ds_read_b32 v206, v218 offset:3120
	ds_read_b32 v214, v219 offset:1536
	s_waitcnt lgkmcnt(12)
	v_mfma_f32_32x32x2_f32 v[4:19], v200, v208, v[4:19]
	ds_read_b32 v207, v218 offset:3640
	ds_read_b32 v215, v219 offset:1792
	s_waitcnt lgkmcnt(12)
	v_mfma_f32_32x32x2_f32 v[4:19], v201, v209, v[4:19]
	s_waitcnt lgkmcnt(10)
	v_mfma_f32_32x32x2_f32 v[4:19], v202, v210, v[4:19]
	s_waitcnt lgkmcnt(8)
	v_mfma_f32_32x32x2_f32 v[4:19], v203, v211, v[4:19]
	s_waitcnt lgkmcnt(6)
	v_mfma_f32_32x32x2_f32 v[4:19], v204, v212, v[4:19]
	s_waitcnt lgkmcnt(4)
	v_mfma_f32_32x32x2_f32 v[4:19], v205, v213, v[4:19]
	s_waitcnt lgkmcnt(2)
	v_mfma_f32_32x32x2_f32 v[4:19], v206, v214, v[4:19]
	s_waitcnt lgkmcnt(0)
	v_mfma_f32_32x32x2_f32 v[4:19], v207, v215, v[4:19]
	s_barrier
	global_load_dwordx4 v[32:35], v[92:93], off offset:1408 sc1
	global_load_dwordx4 v[20:23], v[72:73], off
	s_waitcnt vmcnt(3)
	v_cvt_f32_f16_sdwa v128, v28 dst_sel:DWORD dst_unused:UNUSED_PAD src0_sel:WORD_1
	v_cvt_f32_f16_e32 v28, v28
	v_cvt_f32_f16_e32 v129, v29
	v_cvt_f32_f16_sdwa v130, v30 dst_sel:DWORD dst_unused:UNUSED_PAD src0_sel:WORD_1
	v_cvt_f32_f16_e32 v133, v30
	ds_read_b128 v[36:39], v43 offset:14848
	ds_read_b128 v[116:119], v43 offset:14864
	ds_read_b128 v[120:123], v43 offset:18944
	ds_read_b128 v[124:127], v43 offset:18960
	v_cvt_f32_f16_sdwa v115, v29 dst_sel:DWORD dst_unused:UNUSED_PAD src0_sel:WORD_1
	v_cvt_f32_f16_sdwa v131, v31 dst_sel:DWORD dst_unused:UNUSED_PAD src0_sel:WORD_1
	v_cvt_f32_f16_e32 v132, v31
	v_sub_f32_e32 v28, v28, v0
	v_sub_f32_e32 v29, v128, v1
	v_sub_f32_e32 v30, v129, v2
	v_pk_mul_f32 v[28:29], v[88:89], v[28:29]
	v_sub_f32_e32 v128, v133, v0
	v_sub_f32_e32 v129, v130, v1
	v_sub_f32_e32 v31, v115, v3
	v_sub_f32_e32 v130, v132, v2
	v_sub_f32_e32 v131, v131, v3
	v_pk_mul_f32 v[128:129], v[88:89], v[128:129]
	s_waitcnt lgkmcnt(1)
	v_fma_f32 v28, v36, v28, v120
	v_fma_f32 v29, v37, v29, v121
	v_pk_mul_f32 v[30:31], v[90:91], v[30:31]
	v_pk_mul_f32 v[130:131], v[90:91], v[130:131]
	s_waitcnt lgkmcnt(0)
	v_fma_f32 v36, v116, v128, v124
	ds_write2_b32 v220, v28, v29 offset1:65
	v_fma_f32 v28, v117, v129, v125
	ds_write2_b32 v221, v36, v28 offset1:65
	v_fma_f32 v28, v38, v30, v122
	v_fma_f32 v29, v118, v130, v126
	v_fmac_f32_e32 v123, v39, v31
	v_fmac_f32_e32 v127, v119, v131
	ds_write2_b32 v220, v28, v123 offset0:130 offset1:195
	ds_write2_b32 v221, v29, v127 offset0:130 offset1:195
	s_waitcnt vmcnt(2)
	ds_write_b128 v96, v[24:27] offset:41984
	s_mov_b32 s16, 0
	v_mov_b32_e32 v24, v103
	s_waitcnt lgkmcnt(0)
	s_barrier
	ds_read_b32 v200, v218
	ds_read_b32 v208, v219
	ds_read_b32 v201, v218 offset:520
	ds_read_b32 v209, v219 offset:256
	ds_read_b32 v202, v218 offset:1040
	ds_read_b32 v210, v219 offset:512
	ds_read_b32 v203, v218 offset:1560
	ds_read_b32 v211, v219 offset:768
	ds_read_b32 v204, v218 offset:2080
	ds_read_b32 v212, v219 offset:1024
	ds_read_b32 v205, v218 offset:2600
	ds_read_b32 v213, v219 offset:1280
	ds_read_b32 v206, v218 offset:3120
	ds_read_b32 v214, v219 offset:1536
	s_waitcnt lgkmcnt(12)
	v_mfma_f32_32x32x2_f32 v[4:19], v200, v208, v[4:19]
	ds_read_b32 v207, v218 offset:3640
	ds_read_b32 v215, v219 offset:1792
	s_waitcnt lgkmcnt(12)
	v_mfma_f32_32x32x2_f32 v[4:19], v201, v209, v[4:19]
	s_waitcnt lgkmcnt(10)
	v_mfma_f32_32x32x2_f32 v[4:19], v202, v210, v[4:19]
	s_waitcnt lgkmcnt(8)
	v_mfma_f32_32x32x2_f32 v[4:19], v203, v211, v[4:19]
	s_waitcnt lgkmcnt(6)
	v_mfma_f32_32x32x2_f32 v[4:19], v204, v212, v[4:19]
	s_waitcnt lgkmcnt(4)
	v_mfma_f32_32x32x2_f32 v[4:19], v205, v213, v[4:19]
	s_waitcnt lgkmcnt(2)
	v_mfma_f32_32x32x2_f32 v[4:19], v206, v214, v[4:19]
	s_waitcnt lgkmcnt(0)
	v_mfma_f32_32x32x2_f32 v[4:19], v207, v215, v[4:19]
	s_barrier
	global_load_dwordx4 v[28:31], v[92:93], off offset:1536 sc1
	global_load_dwordx4 v[24:27], v[74:75], off
	s_waitcnt vmcnt(3)
	v_cvt_f32_f16_sdwa v128, v32 dst_sel:DWORD dst_unused:UNUSED_PAD src0_sel:WORD_1
	v_cvt_f32_f16_e32 v32, v32
	v_cvt_f32_f16_e32 v129, v33
	v_cvt_f32_f16_sdwa v130, v34 dst_sel:DWORD dst_unused:UNUSED_PAD src0_sel:WORD_1
	v_cvt_f32_f16_e32 v133, v34
	ds_read_b128 v[36:39], v43 offset:15104
	ds_read_b128 v[116:119], v43 offset:15120
	ds_read_b128 v[120:123], v43 offset:19200
	ds_read_b128 v[124:127], v43 offset:19216
	v_cvt_f32_f16_sdwa v115, v33 dst_sel:DWORD dst_unused:UNUSED_PAD src0_sel:WORD_1
	v_cvt_f32_f16_sdwa v131, v35 dst_sel:DWORD dst_unused:UNUSED_PAD src0_sel:WORD_1
	v_cvt_f32_f16_e32 v132, v35
	v_sub_f32_e32 v32, v32, v0
	v_sub_f32_e32 v33, v128, v1
	v_sub_f32_e32 v34, v129, v2
	v_pk_mul_f32 v[32:33], v[88:89], v[32:33]
	v_sub_f32_e32 v128, v133, v0
	v_sub_f32_e32 v129, v130, v1
	v_sub_f32_e32 v35, v115, v3
	v_sub_f32_e32 v130, v132, v2
	v_sub_f32_e32 v131, v131, v3
	v_pk_mul_f32 v[128:129], v[88:89], v[128:129]
	s_waitcnt lgkmcnt(1)
	v_fma_f32 v32, v36, v32, v120
	v_fma_f32 v33, v37, v33, v121
	v_pk_mul_f32 v[34:35], v[90:91], v[34:35]
	v_pk_mul_f32 v[130:131], v[90:91], v[130:131]
	s_waitcnt lgkmcnt(0)
	v_fma_f32 v36, v116, v128, v124
	ds_write2_b32 v220, v32, v33 offset1:65
	v_fma_f32 v32, v117, v129, v125
	ds_write2_b32 v221, v36, v32 offset1:65
	v_fma_f32 v32, v38, v34, v122
	v_fma_f32 v33, v118, v130, v126
	v_fmac_f32_e32 v123, v39, v35
	v_fmac_f32_e32 v127, v119, v131
	ds_write2_b32 v220, v32, v123 offset0:130 offset1:195
	ds_write2_b32 v221, v33, v127 offset0:130 offset1:195
	s_waitcnt vmcnt(2)
	ds_write_b128 v96, v[20:23] offset:41984
	s_mov_b32 s16, 0
	v_mov_b32_e32 v20, v103
	s_waitcnt lgkmcnt(0)
	s_barrier
	ds_read_b32 v200, v218
	ds_read_b32 v208, v219
	ds_read_b32 v201, v218 offset:520
	ds_read_b32 v209, v219 offset:256
	ds_read_b32 v202, v218 offset:1040
	ds_read_b32 v210, v219 offset:512
	ds_read_b32 v203, v218 offset:1560
	ds_read_b32 v211, v219 offset:768
	ds_read_b32 v204, v218 offset:2080
	ds_read_b32 v212, v219 offset:1024
	ds_read_b32 v205, v218 offset:2600
	ds_read_b32 v213, v219 offset:1280
	ds_read_b32 v206, v218 offset:3120
	ds_read_b32 v214, v219 offset:1536
	s_waitcnt lgkmcnt(12)
	v_mfma_f32_32x32x2_f32 v[4:19], v200, v208, v[4:19]
	ds_read_b32 v207, v218 offset:3640
	ds_read_b32 v215, v219 offset:1792
	s_waitcnt lgkmcnt(12)
	v_mfma_f32_32x32x2_f32 v[4:19], v201, v209, v[4:19]
	s_waitcnt lgkmcnt(10)
	v_mfma_f32_32x32x2_f32 v[4:19], v202, v210, v[4:19]
	s_waitcnt lgkmcnt(8)
	v_mfma_f32_32x32x2_f32 v[4:19], v203, v211, v[4:19]
	s_waitcnt lgkmcnt(6)
	v_mfma_f32_32x32x2_f32 v[4:19], v204, v212, v[4:19]
	s_waitcnt lgkmcnt(4)
	v_mfma_f32_32x32x2_f32 v[4:19], v205, v213, v[4:19]
	s_waitcnt lgkmcnt(2)
	v_mfma_f32_32x32x2_f32 v[4:19], v206, v214, v[4:19]
	s_waitcnt lgkmcnt(0)
	v_mfma_f32_32x32x2_f32 v[4:19], v207, v215, v[4:19]
	s_barrier
	global_load_dwordx4 v[32:35], v[92:93], off offset:1664 sc1
	global_load_dwordx4 v[20:23], v[76:77], off
	s_waitcnt vmcnt(3)
	v_cvt_f32_f16_sdwa v128, v28 dst_sel:DWORD dst_unused:UNUSED_PAD src0_sel:WORD_1
	v_cvt_f32_f16_e32 v28, v28
	v_cvt_f32_f16_e32 v129, v29
	v_cvt_f32_f16_sdwa v130, v30 dst_sel:DWORD dst_unused:UNUSED_PAD src0_sel:WORD_1
	v_cvt_f32_f16_e32 v133, v30
	ds_read_b128 v[36:39], v43 offset:15360
	ds_read_b128 v[116:119], v43 offset:15376
	ds_read_b128 v[120:123], v43 offset:19456
	ds_read_b128 v[124:127], v43 offset:19472
	v_cvt_f32_f16_sdwa v115, v29 dst_sel:DWORD dst_unused:UNUSED_PAD src0_sel:WORD_1
	v_cvt_f32_f16_sdwa v131, v31 dst_sel:DWORD dst_unused:UNUSED_PAD src0_sel:WORD_1
	v_cvt_f32_f16_e32 v132, v31
	v_sub_f32_e32 v28, v28, v0
	v_sub_f32_e32 v29, v128, v1
	v_sub_f32_e32 v30, v129, v2
	v_pk_mul_f32 v[28:29], v[88:89], v[28:29]
	v_sub_f32_e32 v128, v133, v0
	v_sub_f32_e32 v129, v130, v1
	v_sub_f32_e32 v31, v115, v3
	v_sub_f32_e32 v130, v132, v2
	v_sub_f32_e32 v131, v131, v3
	v_pk_mul_f32 v[128:129], v[88:89], v[128:129]
	s_waitcnt lgkmcnt(1)
	v_fma_f32 v28, v36, v28, v120
	v_fma_f32 v29, v37, v29, v121
	v_pk_mul_f32 v[30:31], v[90:91], v[30:31]
	v_pk_mul_f32 v[130:131], v[90:91], v[130:131]
	s_waitcnt lgkmcnt(0)
	v_fma_f32 v36, v116, v128, v124
	ds_write2_b32 v220, v28, v29 offset1:65
	v_fma_f32 v28, v117, v129, v125
	ds_write2_b32 v221, v36, v28 offset1:65
	v_fma_f32 v28, v38, v30, v122
	v_fma_f32 v29, v118, v130, v126
	v_fmac_f32_e32 v123, v39, v31
	v_fmac_f32_e32 v127, v119, v131
	ds_write2_b32 v220, v28, v123 offset0:130 offset1:195
	ds_write2_b32 v221, v29, v127 offset0:130 offset1:195
	s_waitcnt vmcnt(2)
	ds_write_b128 v96, v[24:27] offset:41984
	s_mov_b32 s16, 0
	v_mov_b32_e32 v24, v103
	s_waitcnt lgkmcnt(0)
	s_barrier
	ds_read_b32 v200, v218
	ds_read_b32 v208, v219
	ds_read_b32 v201, v218 offset:520
	ds_read_b32 v209, v219 offset:256
	ds_read_b32 v202, v218 offset:1040
	ds_read_b32 v210, v219 offset:512
	ds_read_b32 v203, v218 offset:1560
	ds_read_b32 v211, v219 offset:768
	ds_read_b32 v204, v218 offset:2080
	ds_read_b32 v212, v219 offset:1024
	ds_read_b32 v205, v218 offset:2600
	ds_read_b32 v213, v219 offset:1280
	ds_read_b32 v206, v218 offset:3120
	ds_read_b32 v214, v219 offset:1536
	s_waitcnt lgkmcnt(12)
	v_mfma_f32_32x32x2_f32 v[4:19], v200, v208, v[4:19]
	ds_read_b32 v207, v218 offset:3640
	ds_read_b32 v215, v219 offset:1792
	s_waitcnt lgkmcnt(12)
	v_mfma_f32_32x32x2_f32 v[4:19], v201, v209, v[4:19]
	s_waitcnt lgkmcnt(10)
	v_mfma_f32_32x32x2_f32 v[4:19], v202, v210, v[4:19]
	s_waitcnt lgkmcnt(8)
	v_mfma_f32_32x32x2_f32 v[4:19], v203, v211, v[4:19]
	s_waitcnt lgkmcnt(6)
	v_mfma_f32_32x32x2_f32 v[4:19], v204, v212, v[4:19]
	s_waitcnt lgkmcnt(4)
	v_mfma_f32_32x32x2_f32 v[4:19], v205, v213, v[4:19]
	s_waitcnt lgkmcnt(2)
	v_mfma_f32_32x32x2_f32 v[4:19], v206, v214, v[4:19]
	s_waitcnt lgkmcnt(0)
	v_mfma_f32_32x32x2_f32 v[4:19], v207, v215, v[4:19]
	s_barrier
	global_load_dwordx4 v[28:31], v[92:93], off offset:1792 sc1
	global_load_dwordx4 v[24:27], v[78:79], off
	s_waitcnt vmcnt(3)
	v_cvt_f32_f16_sdwa v128, v32 dst_sel:DWORD dst_unused:UNUSED_PAD src0_sel:WORD_1
	v_cvt_f32_f16_e32 v32, v32
	v_cvt_f32_f16_e32 v129, v33
	v_cvt_f32_f16_sdwa v130, v34 dst_sel:DWORD dst_unused:UNUSED_PAD src0_sel:WORD_1
	v_cvt_f32_f16_e32 v133, v34
	ds_read_b128 v[36:39], v43 offset:15616
	ds_read_b128 v[116:119], v43 offset:15632
	ds_read_b128 v[120:123], v43 offset:19712
	ds_read_b128 v[124:127], v43 offset:19728
	v_cvt_f32_f16_sdwa v115, v33 dst_sel:DWORD dst_unused:UNUSED_PAD src0_sel:WORD_1
	v_cvt_f32_f16_sdwa v131, v35 dst_sel:DWORD dst_unused:UNUSED_PAD src0_sel:WORD_1
	v_cvt_f32_f16_e32 v132, v35
	v_sub_f32_e32 v32, v32, v0
	v_sub_f32_e32 v33, v128, v1
	v_sub_f32_e32 v34, v129, v2
	v_pk_mul_f32 v[32:33], v[88:89], v[32:33]
	v_sub_f32_e32 v128, v133, v0
	v_sub_f32_e32 v129, v130, v1
	v_sub_f32_e32 v35, v115, v3
	v_sub_f32_e32 v130, v132, v2
	v_sub_f32_e32 v131, v131, v3
	v_pk_mul_f32 v[128:129], v[88:89], v[128:129]
	s_waitcnt lgkmcnt(1)
	v_fma_f32 v32, v36, v32, v120
	v_fma_f32 v33, v37, v33, v121
	v_pk_mul_f32 v[34:35], v[90:91], v[34:35]
	v_pk_mul_f32 v[130:131], v[90:91], v[130:131]
	s_waitcnt lgkmcnt(0)
	v_fma_f32 v36, v116, v128, v124
	ds_write2_b32 v220, v32, v33 offset1:65
	v_fma_f32 v32, v117, v129, v125
	ds_write2_b32 v221, v36, v32 offset1:65
	v_fma_f32 v32, v38, v34, v122
	v_fma_f32 v33, v118, v130, v126
	v_fmac_f32_e32 v123, v39, v35
	v_fmac_f32_e32 v127, v119, v131
	ds_write2_b32 v220, v32, v123 offset0:130 offset1:195
	ds_write2_b32 v221, v33, v127 offset0:130 offset1:195
	s_waitcnt vmcnt(2)
	ds_write_b128 v96, v[20:23] offset:41984
	s_mov_b32 s16, 0
	v_mov_b32_e32 v20, v103
	s_waitcnt lgkmcnt(0)
	s_barrier
	ds_read_b32 v200, v218
	ds_read_b32 v208, v219
	ds_read_b32 v201, v218 offset:520
	ds_read_b32 v209, v219 offset:256
	ds_read_b32 v202, v218 offset:1040
	ds_read_b32 v210, v219 offset:512
	ds_read_b32 v203, v218 offset:1560
	ds_read_b32 v211, v219 offset:768
	ds_read_b32 v204, v218 offset:2080
	ds_read_b32 v212, v219 offset:1024
	ds_read_b32 v205, v218 offset:2600
	ds_read_b32 v213, v219 offset:1280
	ds_read_b32 v206, v218 offset:3120
	ds_read_b32 v214, v219 offset:1536
	s_waitcnt lgkmcnt(12)
	v_mfma_f32_32x32x2_f32 v[4:19], v200, v208, v[4:19]
	ds_read_b32 v207, v218 offset:3640
	ds_read_b32 v215, v219 offset:1792
	s_waitcnt lgkmcnt(12)
	v_mfma_f32_32x32x2_f32 v[4:19], v201, v209, v[4:19]
	s_waitcnt lgkmcnt(10)
	v_mfma_f32_32x32x2_f32 v[4:19], v202, v210, v[4:19]
	s_waitcnt lgkmcnt(8)
	v_mfma_f32_32x32x2_f32 v[4:19], v203, v211, v[4:19]
	s_waitcnt lgkmcnt(6)
	v_mfma_f32_32x32x2_f32 v[4:19], v204, v212, v[4:19]
	s_waitcnt lgkmcnt(4)
	v_mfma_f32_32x32x2_f32 v[4:19], v205, v213, v[4:19]
	s_waitcnt lgkmcnt(2)
	v_mfma_f32_32x32x2_f32 v[4:19], v206, v214, v[4:19]
	s_waitcnt lgkmcnt(0)
	v_mfma_f32_32x32x2_f32 v[4:19], v207, v215, v[4:19]
	s_barrier
	global_load_dwordx4 v[32:35], v[92:93], off offset:1920 sc1
	global_load_dwordx4 v[20:23], v[80:81], off
	s_waitcnt vmcnt(3)
	v_cvt_f32_f16_sdwa v93, v28 dst_sel:DWORD dst_unused:UNUSED_PAD src0_sel:WORD_1
	v_cvt_f32_f16_e32 v28, v28
	v_cvt_f32_f16_sdwa v92, v29 dst_sel:DWORD dst_unused:UNUSED_PAD src0_sel:WORD_1
	v_cvt_f32_f16_sdwa v128, v30 dst_sel:DWORD dst_unused:UNUSED_PAD src0_sel:WORD_1
	v_cvt_f32_f16_e32 v131, v30
	ds_read_b128 v[36:39], v43 offset:15872
	ds_read_b128 v[116:119], v43 offset:15888
	ds_read_b128 v[120:123], v43 offset:19968
	ds_read_b128 v[124:127], v43 offset:19984
	v_cvt_f32_f16_e32 v115, v29
	v_cvt_f32_f16_sdwa v129, v31 dst_sel:DWORD dst_unused:UNUSED_PAD src0_sel:WORD_1
	v_cvt_f32_f16_e32 v130, v31
	v_sub_f32_e32 v28, v28, v0
	v_sub_f32_e32 v29, v93, v1
	v_sub_f32_e32 v31, v92, v3
	v_pk_mul_f32 v[28:29], v[88:89], v[28:29]
	v_sub_f32_e32 v92, v131, v0
	v_sub_f32_e32 v93, v128, v1
	v_sub_f32_e32 v30, v115, v2
	v_sub_f32_e32 v128, v130, v2
	v_sub_f32_e32 v129, v129, v3
	v_pk_mul_f32 v[92:93], v[88:89], v[92:93]
	s_waitcnt lgkmcnt(1)
	v_fma_f32 v28, v36, v28, v120
	v_fma_f32 v29, v37, v29, v121
	v_pk_mul_f32 v[30:31], v[90:91], v[30:31]
	v_pk_mul_f32 v[128:129], v[90:91], v[128:129]
	s_waitcnt lgkmcnt(0)
	v_fma_f32 v36, v116, v92, v124
	ds_write2_b32 v220, v28, v29 offset1:65
	v_fma_f32 v28, v117, v93, v125
	ds_write2_b32 v221, v36, v28 offset1:65
	v_fma_f32 v28, v38, v30, v122
	v_fma_f32 v29, v118, v128, v126
	v_fmac_f32_e32 v123, v39, v31
	v_fmac_f32_e32 v127, v119, v129
	ds_write2_b32 v220, v28, v123 offset0:130 offset1:195
	ds_write2_b32 v221, v29, v127 offset0:130 offset1:195
	s_waitcnt vmcnt(2)
	ds_write_b128 v96, v[24:27] offset:41984
	s_mov_b32 s16, 0
	v_mov_b32_e32 v24, v103
	s_waitcnt lgkmcnt(0)
	s_barrier
	ds_read_b32 v200, v218
	ds_read_b32 v208, v219
	ds_read_b32 v201, v218 offset:520
	ds_read_b32 v209, v219 offset:256
	ds_read_b32 v202, v218 offset:1040
	ds_read_b32 v210, v219 offset:512
	ds_read_b32 v203, v218 offset:1560
	ds_read_b32 v211, v219 offset:768
	ds_read_b32 v204, v218 offset:2080
	ds_read_b32 v212, v219 offset:1024
	ds_read_b32 v205, v218 offset:2600
	ds_read_b32 v213, v219 offset:1280
	ds_read_b32 v206, v218 offset:3120
	ds_read_b32 v214, v219 offset:1536
	s_waitcnt lgkmcnt(12)
	v_mfma_f32_32x32x2_f32 v[4:19], v200, v208, v[4:19]
	ds_read_b32 v207, v218 offset:3640
	ds_read_b32 v215, v219 offset:1792
	s_waitcnt lgkmcnt(12)
	v_mfma_f32_32x32x2_f32 v[4:19], v201, v209, v[4:19]
	s_waitcnt lgkmcnt(10)
	v_mfma_f32_32x32x2_f32 v[4:19], v202, v210, v[4:19]
	s_waitcnt lgkmcnt(8)
	v_mfma_f32_32x32x2_f32 v[4:19], v203, v211, v[4:19]
	s_waitcnt lgkmcnt(6)
	v_mfma_f32_32x32x2_f32 v[4:19], v204, v212, v[4:19]
	s_waitcnt lgkmcnt(4)
	v_mfma_f32_32x32x2_f32 v[4:19], v205, v213, v[4:19]
	s_waitcnt lgkmcnt(2)
	v_mfma_f32_32x32x2_f32 v[4:19], v206, v214, v[4:19]
	s_waitcnt lgkmcnt(0)
	v_mfma_f32_32x32x2_f32 v[4:19], v207, v215, v[4:19]
	s_waitcnt vmcnt(1)
	v_cvt_f32_f16_sdwa v93, v32 dst_sel:DWORD dst_unused:UNUSED_PAD src0_sel:WORD_1
	v_cvt_f32_f16_e32 v32, v32
	v_cvt_f32_f16_sdwa v121, v34 dst_sel:DWORD dst_unused:UNUSED_PAD src0_sel:WORD_1
	v_cvt_f32_f16_e32 v123, v34
	s_barrier
	ds_read_b128 v[24:27], v43 offset:16128
	ds_read_b128 v[28:31], v43 offset:16144
	ds_read_b128 v[36:39], v43 offset:20224
	ds_read_b128 v[116:119], v43 offset:20240
	v_cvt_f32_f16_sdwa v92, v33 dst_sel:DWORD dst_unused:UNUSED_PAD src0_sel:WORD_1
	v_cvt_f32_f16_e32 v115, v33
	v_cvt_f32_f16_sdwa v120, v35 dst_sel:DWORD dst_unused:UNUSED_PAD src0_sel:WORD_1
	v_cvt_f32_f16_e32 v122, v35
	v_sub_f32_e32 v32, v32, v0
	v_sub_f32_e32 v33, v93, v1
	v_sub_f32_e32 v0, v123, v0
	v_sub_f32_e32 v1, v121, v1
	v_sub_f32_e32 v34, v115, v2
	v_sub_f32_e32 v35, v92, v3
	v_pk_mul_f32 v[0:1], v[88:89], v[0:1]
	v_pk_mul_f32 v[34:35], v[90:91], v[34:35]
	v_sub_f32_e32 v2, v122, v2
	v_sub_f32_e32 v3, v120, v3
	s_waitcnt lgkmcnt(0)
	v_fma_f32 v0, v28, v0, v116
	v_fma_f32 v1, v29, v1, v117
	v_pk_mul_f32 v[32:33], v[88:89], v[32:33]
	v_pk_mul_f32 v[2:3], v[90:91], v[2:3]
	ds_write2_b32 v221, v0, v1 offset1:65
	v_fma_f32 v0, v26, v34, v38
	v_fmac_f32_e32 v39, v27, v35
	v_fma_f32 v24, v24, v32, v36
	v_fma_f32 v25, v25, v33, v37
	v_fma_f32 v1, v30, v2, v118
	ds_write2_b32 v220, v0, v39 offset0:130 offset1:195
	v_fmac_f32_e32 v119, v31, v3
	s_mov_b32 s16, 0
	v_mov_b32_e32 v0, v103
	ds_write2_b32 v220, v24, v25 offset1:65
	ds_write2_b32 v221, v1, v119 offset0:130 offset1:195
	s_waitcnt vmcnt(0)
	ds_write_b128 v96, v[20:23] offset:41984
	s_waitcnt lgkmcnt(0)
	s_barrier
	ds_read_b32 v200, v218
	ds_read_b32 v208, v219
	ds_read_b32 v201, v218 offset:520
	ds_read_b32 v209, v219 offset:256
	ds_read_b32 v202, v218 offset:1040
	ds_read_b32 v210, v219 offset:512
	ds_read_b32 v203, v218 offset:1560
	ds_read_b32 v211, v219 offset:768
	ds_read_b32 v204, v218 offset:2080
	ds_read_b32 v212, v219 offset:1024
	ds_read_b32 v205, v218 offset:2600
	ds_read_b32 v213, v219 offset:1280
	ds_read_b32 v206, v218 offset:3120
	ds_read_b32 v214, v219 offset:1536
	s_waitcnt lgkmcnt(12)
	v_mfma_f32_32x32x2_f32 v[4:19], v200, v208, v[4:19]
	ds_read_b32 v207, v218 offset:3640
	ds_read_b32 v215, v219 offset:1792
	s_waitcnt lgkmcnt(12)
	v_mfma_f32_32x32x2_f32 v[4:19], v201, v209, v[4:19]
	s_waitcnt lgkmcnt(10)
	v_mfma_f32_32x32x2_f32 v[4:19], v202, v210, v[4:19]
	s_waitcnt lgkmcnt(8)
	v_mfma_f32_32x32x2_f32 v[4:19], v203, v211, v[4:19]
	s_waitcnt lgkmcnt(6)
	v_mfma_f32_32x32x2_f32 v[4:19], v204, v212, v[4:19]
	s_waitcnt lgkmcnt(4)
	v_mfma_f32_32x32x2_f32 v[4:19], v205, v213, v[4:19]
	s_waitcnt lgkmcnt(2)
	v_mfma_f32_32x32x2_f32 v[4:19], v206, v214, v[4:19]
	s_waitcnt lgkmcnt(0)
	v_mfma_f32_32x32x2_f32 v[4:19], v207, v215, v[4:19]
	s_barrier
	s_nop 15
	s_nop 3
	ds_write_b32 v217, v4 offset:58752
	ds_write_b32 v217, v5 offset:58880
	ds_write_b32 v217, v6 offset:59008
	ds_write_b32 v217, v7 offset:59136
	ds_write_b32 v217, v8 offset:59776
	ds_write_b32 v217, v9 offset:59904
	ds_write_b32 v217, v10 offset:60032
	ds_write_b32 v217, v11 offset:60160
	ds_write_b32 v217, v12 offset:60800
	ds_write_b32 v217, v13 offset:60928
	ds_write_b32 v217, v14 offset:61056
	ds_write_b32 v217, v15 offset:61184
	ds_write_b32 v217, v16 offset:61824
	ds_write_b32 v217, v17 offset:61952
	ds_write_b32 v217, v18 offset:62080
	ds_write_b32 v217, v19 offset:62208
	s_waitcnt lgkmcnt(0)
	s_barrier
	global_load_dwordx4 v[0:3], v[50:51], off offset:128
	ds_read_b128 v[4:7], v98 offset:58752
	ds_read_b128 v[8:11], v99 offset:8192
	ds_read_b128 v[12:15], v99 offset:16384
	ds_read_b128 v[16:19], v99 offset:24576
	v_add_u32_e32 v20, 0xc400, v100
	v_add_u32_e32 v21, 0xc408, v100
	s_waitcnt lgkmcnt(2)
	v_pk_add_f32 v[4:5], v[4:5], v[8:9]
	v_pk_add_f32 v[6:7], v[6:7], v[10:11]
	s_waitcnt lgkmcnt(1)
	v_pk_add_f32 v[4:5], v[12:13], v[4:5]
	v_pk_add_f32 v[6:7], v[14:15], v[6:7]
	s_waitcnt lgkmcnt(0)
	v_pk_add_f32 v[4:5], v[16:17], v[4:5]
	v_pk_add_f32 v[6:7], v[18:19], v[6:7]
	s_waitcnt vmcnt(0)
	v_pk_add_f32 v[0:1], v[0:1], v[4:5]
	v_pk_add_f32 v[2:3], v[6:7], v[2:3]
	ds_write2_b32 v20, v0, v1 offset1:1
	ds_write2_b32 v21, v2, v3 offset1:1
	s_waitcnt lgkmcnt(0)
	s_barrier
	s_and_saveexec_b64 s[36:37], s[6:7]
	s_cbranch_execz .LBB0_1510
	v_add_u32_e32 v0, 0xc400, v108
	v_add_u32_e32 v1, 0xc408, v108
	v_add_u32_e32 v2, 0xc410, v108
	v_add_u32_e32 v3, 0xc418, v108
	ds_read2_b32 v[34:35], v0 offset1:1
	ds_read2_b32 v[30:31], v1 offset1:1
	ds_read2_b32 v[22:23], v2 offset1:1
	ds_read2_b32 v[10:11], v3 offset1:1
	s_mov_b32 s16, 0xff61b1e6
	s_waitcnt lgkmcnt(3)
	v_max_f32_e32 v0, v34, v34
	v_max_f32_e32 v0, 0xff61b1e6, v0
	v_cmp_lt_f32_e32 vcc, s16, v34
	v_cmp_gt_f32_e64 s[16:17], v35, v0
	v_add_u32_e32 v2, 0xc420, v108
	ds_read2_b32 v[24:25], v2 offset1:1
	v_cndmask_b32_e64 v0, v0, v35, s[16:17]
	v_cndmask_b32_e64 v1, 0, 1, s[16:17]
	s_waitcnt lgkmcnt(3)
	v_cmp_gt_f32_e64 s[16:17], v30, v0
	v_add_u32_e32 v2, 0xc428, v108
	v_add_u32_e32 v3, 0xc430, v108
	v_cndmask_b32_e64 v0, v0, v30, s[16:17]
	v_cndmask_b32_e64 v1, v1, 2, s[16:17]
	v_cmp_gt_f32_e64 s[16:17], v31, v0
	v_add_u32_e32 v4, 0xc438, v108
	ds_read2_b32 v[32:33], v2 offset1:1
	ds_read2_b32 v[20:21], v3 offset1:1
	ds_read2_b32 v[6:7], v4 offset1:1
	v_cndmask_b32_e64 v0, v0, v31, s[16:17]
	v_cndmask_b32_e64 v1, v1, 3, s[16:17]
	s_waitcnt lgkmcnt(5)
	v_cmp_gt_f32_e64 s[16:17], v22, v0
	v_add_u32_e32 v2, 0xc440, v108
	ds_read2_b32 v[18:19], v2 offset1:1
	v_cndmask_b32_e64 v0, v0, v22, s[16:17]
	v_cndmask_b32_e64 v1, v1, 4, s[16:17]
	v_cmp_gt_f32_e64 s[16:17], v23, v0
	v_add_u32_e32 v2, 0xc448, v108
	v_add_u32_e32 v4, 0xc458, v108
	v_cndmask_b32_e64 v0, v0, v23, s[16:17]
	v_cndmask_b32_e64 v1, v1, 5, s[16:17]
	s_waitcnt lgkmcnt(5)
	v_cmp_gt_f32_e64 s[16:17], v10, v0
	v_add_u32_e32 v3, 0xc450, v108
	ds_read2_b32 v[28:29], v2 offset1:1
	ds_read2_b32 v[12:13], v3 offset1:1
	ds_read2_b32 v[4:5], v4 offset1:1
	v_cndmask_b32_e64 v0, v0, v10, s[16:17]
	v_cndmask_b32_e64 v1, v1, 6, s[16:17]
	v_cmp_gt_f32_e64 s[16:17], v11, v0
	v_add_u32_e32 v2, 0xc460, v108
	ds_read2_b32 v[14:15], v2 offset1:1
	v_cndmask_b32_e64 v0, v0, v11, s[16:17]
	v_cndmask_b32_e64 v1, v1, 7, s[16:17]
	s_waitcnt lgkmcnt(8)
	v_cmp_gt_f32_e64 s[16:17], v24, v0
	v_add_u32_e32 v2, 0xc468, v108
	v_add_u32_e32 v8, 0xc478, v108
	v_cndmask_b32_e64 v0, v0, v24, s[16:17]
	v_cndmask_b32_e64 v1, v1, 8, s[16:17]
	v_cmp_gt_f32_e64 s[16:17], v25, v0
	v_add_u32_e32 v3, 0xc470, v108
	ds_read2_b32 v[26:27], v2 offset1:1
	ds_read2_b32 v[16:17], v3 offset1:1
	ds_read2_b32 v[8:9], v8 offset1:1
	v_cndmask_b32_e64 v0, v0, v25, s[16:17]
	v_cndmask_b32_e64 v1, v1, 9, s[16:17]
	s_waitcnt lgkmcnt(10)
	v_cmp_gt_f32_e64 s[16:17], v32, v0
	s_nop 1
	v_cndmask_b32_e64 v0, v0, v32, s[16:17]
	v_cndmask_b32_e64 v1, v1, 10, s[16:17]
	v_cmp_gt_f32_e64 s[16:17], v33, v0
	s_nop 1
	v_cndmask_b32_e64 v0, v0, v33, s[16:17]
	v_cndmask_b32_e64 v1, v1, 11, s[16:17]
	s_waitcnt lgkmcnt(9)
	v_cmp_gt_f32_e64 s[16:17], v20, v0
	s_nop 1
	v_cndmask_b32_e64 v0, v0, v20, s[16:17]
	v_cndmask_b32_e64 v1, v1, 12, s[16:17]
	v_cmp_gt_f32_e64 s[16:17], v21, v0
	s_nop 1
	v_cndmask_b32_e64 v0, v0, v21, s[16:17]
	v_cndmask_b32_e64 v1, v1, 13, s[16:17]
	s_waitcnt lgkmcnt(8)
	v_cmp_gt_f32_e64 s[16:17], v6, v0
	s_nop 1
	v_cndmask_b32_e64 v0, v0, v6, s[16:17]
	v_cndmask_b32_e64 v1, v1, 14, s[16:17]
	v_cmp_gt_f32_e64 s[16:17], v7, v0
	s_nop 1
	v_cndmask_b32_e64 v0, v0, v7, s[16:17]
	v_cndmask_b32_e64 v1, v1, 15, s[16:17]
	s_waitcnt lgkmcnt(7)
	v_cmp_gt_f32_e64 s[16:17], v18, v0
	s_nop 1
	v_cndmask_b32_e64 v0, v0, v18, s[16:17]
	v_cndmask_b32_e64 v1, v1, 16, s[16:17]
	v_cmp_gt_f32_e64 s[16:17], v19, v0
	s_nop 1
	v_cndmask_b32_e64 v0, v0, v19, s[16:17]
	v_cndmask_b32_e64 v1, v1, 17, s[16:17]
	s_waitcnt lgkmcnt(6)
	v_cmp_gt_f32_e64 s[16:17], v28, v0
	s_nop 1
	v_cndmask_b32_e64 v0, v0, v28, s[16:17]
	v_cndmask_b32_e64 v1, v1, 18, s[16:17]
	v_cmp_gt_f32_e64 s[16:17], v29, v0
	s_nop 1
	v_cndmask_b32_e64 v0, v0, v29, s[16:17]
	v_cndmask_b32_e64 v1, v1, 19, s[16:17]
	s_waitcnt lgkmcnt(5)
	v_cmp_gt_f32_e64 s[16:17], v12, v0
	s_nop 1
	v_cndmask_b32_e64 v0, v0, v12, s[16:17]
	v_cndmask_b32_e64 v1, v1, 20, s[16:17]
	v_cmp_gt_f32_e64 s[16:17], v13, v0
	s_nop 1
	v_cndmask_b32_e64 v0, v0, v13, s[16:17]
	v_cndmask_b32_e64 v1, v1, 21, s[16:17]
	s_waitcnt lgkmcnt(4)
	v_cmp_gt_f32_e64 s[16:17], v4, v0
	s_nop 1
	v_cndmask_b32_e64 v0, v0, v4, s[16:17]
	v_cndmask_b32_e64 v1, v1, 22, s[16:17]
	v_cmp_gt_f32_e64 s[16:17], v5, v0
	s_nop 1
	v_cndmask_b32_e64 v0, v0, v5, s[16:17]
	v_cndmask_b32_e64 v1, v1, 23, s[16:17]
	s_waitcnt lgkmcnt(3)
	v_cmp_gt_f32_e64 s[16:17], v14, v0
	s_nop 1
	v_cndmask_b32_e64 v0, v0, v14, s[16:17]
	v_cndmask_b32_e64 v1, v1, 24, s[16:17]
	v_cmp_gt_f32_e64 s[16:17], v15, v0
	s_nop 1
	v_cndmask_b32_e64 v0, v0, v15, s[16:17]
	v_cndmask_b32_e64 v1, v1, 25, s[16:17]
	s_waitcnt lgkmcnt(2)
	v_cmp_gt_f32_e64 s[16:17], v26, v0
	s_nop 1
	v_cndmask_b32_e64 v0, v0, v26, s[16:17]
	v_cndmask_b32_e64 v1, v1, 26, s[16:17]
	v_cmp_gt_f32_e64 s[16:17], v27, v0
	s_nop 1
	v_cndmask_b32_e64 v0, v0, v27, s[16:17]
	v_cndmask_b32_e64 v1, v1, 27, s[16:17]
	s_waitcnt lgkmcnt(1)
	v_cmp_gt_f32_e64 s[16:17], v16, v0
	s_nop 1
	v_cndmask_b32_e64 v0, v0, v16, s[16:17]
	v_cndmask_b32_e64 v1, v1, 28, s[16:17]
	v_cmp_gt_f32_e64 s[16:17], v17, v0
	s_nop 1
	v_cndmask_b32_e64 v0, v0, v17, s[16:17]
	v_cndmask_b32_e64 v1, v1, 29, s[16:17]
	s_waitcnt lgkmcnt(0)
	v_cmp_gt_f32_e64 s[16:17], v8, v0
	s_nop 1
	v_cndmask_b32_e64 v0, v0, v8, s[16:17]
	v_cndmask_b32_e64 v1, v1, 30, s[16:17]
	v_cmp_gt_f32_e64 s[16:17], v9, v0
	s_nop 1
	v_cndmask_b32_e64 v36, v0, v9, s[16:17]
	v_cndmask_b32_e64 v0, v1, 31, s[16:17]
	v_cmp_ne_u32_e64 s[16:17], 0, v0
	v_lshlrev_b32_e64 v2, v0, 1
	s_and_b64 s[16:17], s[16:17], vcc
	v_cndmask_b32_e64 v1, v112, v34, s[16:17]
	v_and_b32_e32 v3, 2, v2
	v_cmp_eq_u32_e64 s[16:17], 0, v3
	v_cmp_gt_f32_e64 s[18:19], v35, v1
	s_and_b64 s[16:17], s[16:17], s[18:19]
	v_cndmask_b32_e64 v1, v1, v35, s[16:17]
	v_and_b32_e32 v37, 4, v2
	v_cndmask_b32_e64 v3, 0, 1, s[16:17]
	v_cmp_eq_u32_e64 s[16:17], 0, v37
	v_cmp_gt_f32_e64 s[18:19], v30, v1
	s_and_b64 s[16:17], s[16:17], s[18:19]
	v_cndmask_b32_e64 v1, v1, v30, s[16:17]
	v_and_b32_e32 v37, 8, v2
	v_cndmask_b32_e64 v3, v3, 2, s[16:17]
	v_cmp_eq_u32_e64 s[16:17], 0, v37
	v_cmp_gt_f32_e64 s[18:19], v31, v1
	s_and_b64 s[16:17], s[16:17], s[18:19]
	v_cndmask_b32_e64 v1, v1, v31, s[16:17]
	v_and_b32_e32 v37, 16, v2
	v_cndmask_b32_e64 v3, v3, 3, s[16:17]
	v_cmp_eq_u32_e64 s[16:17], 0, v37
	v_cmp_gt_f32_e64 s[18:19], v22, v1
	s_and_b64 s[16:17], s[16:17], s[18:19]
	v_cndmask_b32_e64 v1, v1, v22, s[16:17]
	v_and_b32_e32 v37, 32, v2
	v_cndmask_b32_e64 v3, v3, 4, s[16:17]
	v_cmp_eq_u32_e64 s[16:17], 0, v37
	v_cmp_gt_f32_e64 s[18:19], v23, v1
	s_and_b64 s[16:17], s[16:17], s[18:19]
	v_cndmask_b32_e64 v1, v1, v23, s[16:17]
	v_and_b32_e32 v37, 64, v2
	v_cndmask_b32_e64 v3, v3, 5, s[16:17]
	v_cmp_eq_u32_e64 s[16:17], 0, v37
	v_cmp_gt_f32_e64 s[18:19], v10, v1
	s_and_b64 s[16:17], s[16:17], s[18:19]
	v_cndmask_b32_e64 v1, v1, v10, s[16:17]
	v_and_b32_e32 v37, 0x80, v2
	v_cndmask_b32_e64 v3, v3, 6, s[16:17]
	v_cmp_eq_u32_e64 s[16:17], 0, v37
	v_cmp_gt_f32_e64 s[18:19], v11, v1
	s_and_b64 s[16:17], s[16:17], s[18:19]
	v_cndmask_b32_e64 v1, v1, v11, s[16:17]
	v_and_b32_e32 v37, 0x100, v2
	v_cndmask_b32_e64 v3, v3, 7, s[16:17]
	v_cmp_eq_u32_e64 s[16:17], 0, v37
	v_cmp_gt_f32_e64 s[18:19], v24, v1
	s_and_b64 s[16:17], s[16:17], s[18:19]
	v_cndmask_b32_e64 v1, v1, v24, s[16:17]
	v_and_b32_e32 v37, 0x200, v2
	v_cndmask_b32_e64 v3, v3, 8, s[16:17]
	v_cmp_eq_u32_e64 s[16:17], 0, v37
	v_cmp_gt_f32_e64 s[18:19], v25, v1
	s_and_b64 s[16:17], s[16:17], s[18:19]
	v_cndmask_b32_e64 v1, v1, v25, s[16:17]
	v_and_b32_e32 v37, 0x400, v2
	v_cndmask_b32_e64 v3, v3, 9, s[16:17]
	v_cmp_eq_u32_e64 s[16:17], 0, v37
	v_cmp_gt_f32_e64 s[18:19], v32, v1
	s_and_b64 s[16:17], s[16:17], s[18:19]
	v_cndmask_b32_e64 v1, v1, v32, s[16:17]
	v_and_b32_e32 v37, 0x800, v2
	v_cndmask_b32_e64 v3, v3, 10, s[16:17]
	v_cmp_eq_u32_e64 s[16:17], 0, v37
	v_cmp_gt_f32_e64 s[18:19], v33, v1
	s_and_b64 s[16:17], s[16:17], s[18:19]
	v_cndmask_b32_e64 v1, v1, v33, s[16:17]
	v_and_b32_e32 v37, 0x1000, v2
	v_cndmask_b32_e64 v3, v3, 11, s[16:17]
	v_cmp_eq_u32_e64 s[16:17], 0, v37
	v_cmp_gt_f32_e64 s[18:19], v20, v1
	s_and_b64 s[16:17], s[16:17], s[18:19]
	v_cndmask_b32_e64 v1, v1, v20, s[16:17]
	v_and_b32_e32 v37, 0x2000, v2
	v_cndmask_b32_e64 v3, v3, 12, s[16:17]
	v_cmp_eq_u32_e64 s[16:17], 0, v37
	v_cmp_gt_f32_e64 s[18:19], v21, v1
	s_and_b64 s[16:17], s[16:17], s[18:19]
	v_cndmask_b32_e64 v1, v1, v21, s[16:17]
	v_and_b32_e32 v37, 0x4000, v2
	v_cndmask_b32_e64 v3, v3, 13, s[16:17]
	v_cmp_eq_u32_e64 s[16:17], 0, v37
	v_cmp_gt_f32_e64 s[18:19], v6, v1
	s_and_b64 s[16:17], s[16:17], s[18:19]
	v_cndmask_b32_e64 v1, v1, v6, s[16:17]
	v_and_b32_e32 v37, 0x8000, v2
	v_cndmask_b32_e64 v3, v3, 14, s[16:17]
	v_cmp_eq_u32_e64 s[16:17], 0, v37
	v_cmp_gt_f32_e64 s[18:19], v7, v1
	s_and_b64 s[16:17], s[16:17], s[18:19]
	v_cndmask_b32_e64 v1, v1, v7, s[16:17]
	v_and_b32_e32 v37, 0x10000, v2
	v_cndmask_b32_e64 v3, v3, 15, s[16:17]
	v_cmp_eq_u32_e64 s[16:17], 0, v37
	v_cmp_gt_f32_e64 s[18:19], v18, v1
	s_and_b64 s[16:17], s[16:17], s[18:19]
	v_cndmask_b32_e64 v1, v1, v18, s[16:17]
	v_and_b32_e32 v37, 0x20000, v2
	v_cndmask_b32_e64 v3, v3, 16, s[16:17]
	v_cmp_eq_u32_e64 s[16:17], 0, v37
	v_cmp_gt_f32_e64 s[18:19], v19, v1
	s_and_b64 s[16:17], s[16:17], s[18:19]
	v_cndmask_b32_e64 v1, v1, v19, s[16:17]
	v_and_b32_e32 v37, 0x40000, v2
	v_cndmask_b32_e64 v3, v3, 17, s[16:17]
	v_cmp_eq_u32_e64 s[16:17], 0, v37
	v_cmp_gt_f32_e64 s[18:19], v28, v1
	s_and_b64 s[16:17], s[16:17], s[18:19]
	v_cndmask_b32_e64 v1, v1, v28, s[16:17]
	v_and_b32_e32 v37, 0x80000, v2
	v_cndmask_b32_e64 v3, v3, 18, s[16:17]
	v_cmp_eq_u32_e64 s[16:17], 0, v37
	v_cmp_gt_f32_e64 s[18:19], v29, v1
	s_and_b64 s[16:17], s[16:17], s[18:19]
	v_cndmask_b32_e64 v1, v1, v29, s[16:17]
	v_and_b32_e32 v37, 0x100000, v2
	v_cndmask_b32_e64 v3, v3, 19, s[16:17]
	v_cmp_eq_u32_e64 s[16:17], 0, v37
	v_cmp_gt_f32_e64 s[18:19], v12, v1
	s_and_b64 s[16:17], s[16:17], s[18:19]
	v_cndmask_b32_e64 v1, v1, v12, s[16:17]
	v_and_b32_e32 v37, 0x200000, v2
	v_cndmask_b32_e64 v3, v3, 20, s[16:17]
	v_cmp_eq_u32_e64 s[16:17], 0, v37
	v_cmp_gt_f32_e64 s[18:19], v13, v1
	s_and_b64 s[16:17], s[16:17], s[18:19]
	v_cndmask_b32_e64 v1, v1, v13, s[16:17]
	v_and_b32_e32 v37, 0x400000, v2
	v_cndmask_b32_e64 v3, v3, 21, s[16:17]
	v_cmp_eq_u32_e64 s[16:17], 0, v37
	v_cmp_gt_f32_e64 s[18:19], v4, v1
	s_and_b64 s[16:17], s[16:17], s[18:19]
	v_cndmask_b32_e64 v1, v1, v4, s[16:17]
	v_and_b32_e32 v37, 0x800000, v2
	v_cndmask_b32_e64 v3, v3, 22, s[16:17]
	v_cmp_eq_u32_e64 s[16:17], 0, v37
	v_cmp_gt_f32_e64 s[18:19], v5, v1
	s_and_b64 s[16:17], s[16:17], s[18:19]
	v_cndmask_b32_e64 v1, v1, v5, s[16:17]
	v_and_b32_e32 v37, 0x1000000, v2
	v_cndmask_b32_e64 v3, v3, 23, s[16:17]
	v_cmp_eq_u32_e64 s[16:17], 0, v37
	v_cmp_gt_f32_e64 s[18:19], v14, v1
	s_and_b64 s[16:17], s[16:17], s[18:19]
	v_cndmask_b32_e64 v1, v1, v14, s[16:17]
	v_and_b32_e32 v37, 0x2000000, v2
	v_cndmask_b32_e64 v3, v3, 24, s[16:17]
	v_cmp_eq_u32_e64 s[16:17], 0, v37
	v_cmp_gt_f32_e64 s[18:19], v15, v1
	s_and_b64 s[16:17], s[16:17], s[18:19]
	v_cndmask_b32_e64 v1, v1, v15, s[16:17]
	v_and_b32_e32 v37, 0x4000000, v2
	v_cndmask_b32_e64 v3, v3, 25, s[16:17]
	v_cmp_eq_u32_e64 s[16:17], 0, v37
	v_cmp_gt_f32_e64 s[18:19], v26, v1
	s_and_b64 s[16:17], s[16:17], s[18:19]
	v_cndmask_b32_e64 v1, v1, v26, s[16:17]
	v_and_b32_e32 v37, 0x8000000, v2
	v_cndmask_b32_e64 v3, v3, 26, s[16:17]
	v_cmp_eq_u32_e64 s[16:17], 0, v37
	v_cmp_gt_f32_e64 s[18:19], v27, v1
	s_and_b64 s[16:17], s[16:17], s[18:19]
	v_cndmask_b32_e64 v1, v1, v27, s[16:17]
	v_and_b32_e32 v37, 0x10000000, v2
	v_cndmask_b32_e64 v3, v3, 27, s[16:17]
	v_cmp_eq_u32_e64 s[16:17], 0, v37
	v_cmp_gt_f32_e64 s[18:19], v16, v1
	s_and_b64 s[16:17], s[16:17], s[18:19]
	v_cndmask_b32_e64 v1, v1, v16, s[16:17]
	v_and_b32_e32 v37, 0x20000000, v2
	v_cndmask_b32_e64 v3, v3, 28, s[16:17]
	v_cmp_eq_u32_e64 s[16:17], 0, v37
	v_cmp_gt_f32_e64 s[18:19], v17, v1
	s_and_b64 s[16:17], s[16:17], s[18:19]
	v_cndmask_b32_e64 v1, v1, v17, s[16:17]
	v_and_b32_e32 v37, 2.0, v2
	v_cndmask_b32_e64 v3, v3, 29, s[16:17]
	v_cmp_eq_u32_e64 s[16:17], 0, v37
	v_cmp_gt_f32_e64 s[18:19], v8, v1
	s_and_b64 s[16:17], s[16:17], s[18:19]
	v_cndmask_b32_e64 v1, v1, v8, s[16:17]
	v_cndmask_b32_e64 v3, v3, 30, s[16:17]
	v_cmp_ne_u32_e64 s[16:17], 31, v0
	v_cmp_gt_f32_e64 s[18:19], v9, v1
	s_and_b64 s[16:17], s[16:17], s[18:19]
	v_cndmask_b32_e64 v37, v1, v9, s[16:17]
	v_cndmask_b32_e64 v1, v3, 31, s[16:17]
	v_lshl_or_b32 v3, 1, v1, v2
	v_and_b32_e32 v2, 1, v3
	v_cmp_eq_u32_e64 s[16:17], 0, v2
	s_and_b64 s[16:17], s[16:17], vcc
	v_and_b32_e32 v38, 2, v3
	v_cndmask_b32_e64 v2, v112, v34, s[16:17]
	v_cmp_eq_u32_e64 s[16:17], 0, v38
	v_cmp_gt_f32_e64 s[18:19], v35, v2
	s_and_b64 s[16:17], s[16:17], s[18:19]
	v_cndmask_b32_e64 v2, v2, v35, s[16:17]
	v_and_b32_e32 v39, 4, v3
	v_cndmask_b32_e64 v38, 0, 1, s[16:17]
	v_cmp_eq_u32_e64 s[16:17], 0, v39
	v_cmp_gt_f32_e64 s[18:19], v30, v2
	s_and_b64 s[16:17], s[16:17], s[18:19]
	v_cndmask_b32_e64 v2, v2, v30, s[16:17]
	v_and_b32_e32 v39, 8, v3
	v_cndmask_b32_e64 v38, v38, 2, s[16:17]
	v_cmp_eq_u32_e64 s[16:17], 0, v39
	v_cmp_gt_f32_e64 s[18:19], v31, v2
	s_and_b64 s[16:17], s[16:17], s[18:19]
	v_cndmask_b32_e64 v2, v2, v31, s[16:17]
	v_and_b32_e32 v39, 16, v3
	v_cndmask_b32_e64 v38, v38, 3, s[16:17]
	v_cmp_eq_u32_e64 s[16:17], 0, v39
	v_cmp_gt_f32_e64 s[18:19], v22, v2
	s_and_b64 s[16:17], s[16:17], s[18:19]
	v_cndmask_b32_e64 v2, v2, v22, s[16:17]
	v_and_b32_e32 v39, 32, v3
	v_cndmask_b32_e64 v38, v38, 4, s[16:17]
	v_cmp_eq_u32_e64 s[16:17], 0, v39
	v_cmp_gt_f32_e64 s[18:19], v23, v2
	s_and_b64 s[16:17], s[16:17], s[18:19]
	v_cndmask_b32_e64 v2, v2, v23, s[16:17]
	v_and_b32_e32 v39, 64, v3
	v_cndmask_b32_e64 v38, v38, 5, s[16:17]
	v_cmp_eq_u32_e64 s[16:17], 0, v39
	v_cmp_gt_f32_e64 s[18:19], v10, v2
	s_and_b64 s[16:17], s[16:17], s[18:19]
	v_cndmask_b32_e64 v2, v2, v10, s[16:17]
	v_and_b32_e32 v39, 0x80, v3
	v_cndmask_b32_e64 v38, v38, 6, s[16:17]
	v_cmp_eq_u32_e64 s[16:17], 0, v39
	v_cmp_gt_f32_e64 s[18:19], v11, v2
	s_and_b64 s[16:17], s[16:17], s[18:19]
	v_cndmask_b32_e64 v2, v2, v11, s[16:17]
	v_and_b32_e32 v39, 0x100, v3
	v_cndmask_b32_e64 v38, v38, 7, s[16:17]
	v_cmp_eq_u32_e64 s[16:17], 0, v39
	v_cmp_gt_f32_e64 s[18:19], v24, v2
	s_and_b64 s[16:17], s[16:17], s[18:19]
	v_cndmask_b32_e64 v2, v2, v24, s[16:17]
	v_and_b32_e32 v39, 0x200, v3
	v_cndmask_b32_e64 v38, v38, 8, s[16:17]
	v_cmp_eq_u32_e64 s[16:17], 0, v39
	v_cmp_gt_f32_e64 s[18:19], v25, v2
	s_and_b64 s[16:17], s[16:17], s[18:19]
	v_cndmask_b32_e64 v2, v2, v25, s[16:17]
	v_and_b32_e32 v39, 0x400, v3
	v_cndmask_b32_e64 v38, v38, 9, s[16:17]
	v_cmp_eq_u32_e64 s[16:17], 0, v39
	v_cmp_gt_f32_e64 s[18:19], v32, v2
	s_and_b64 s[16:17], s[16:17], s[18:19]
	v_cndmask_b32_e64 v2, v2, v32, s[16:17]
	v_and_b32_e32 v39, 0x800, v3
	v_cndmask_b32_e64 v38, v38, 10, s[16:17]
	v_cmp_eq_u32_e64 s[16:17], 0, v39
	v_cmp_gt_f32_e64 s[18:19], v33, v2
	s_and_b64 s[16:17], s[16:17], s[18:19]
	v_cndmask_b32_e64 v2, v2, v33, s[16:17]
	v_and_b32_e32 v39, 0x1000, v3
	v_cndmask_b32_e64 v38, v38, 11, s[16:17]
	v_cmp_eq_u32_e64 s[16:17], 0, v39
	v_cmp_gt_f32_e64 s[18:19], v20, v2
	s_and_b64 s[16:17], s[16:17], s[18:19]
	v_cndmask_b32_e64 v2, v2, v20, s[16:17]
	v_and_b32_e32 v39, 0x2000, v3
	v_cndmask_b32_e64 v38, v38, 12, s[16:17]
	v_cmp_eq_u32_e64 s[16:17], 0, v39
	v_cmp_gt_f32_e64 s[18:19], v21, v2
	s_and_b64 s[16:17], s[16:17], s[18:19]
	v_cndmask_b32_e64 v2, v2, v21, s[16:17]
	v_and_b32_e32 v39, 0x4000, v3
	v_cndmask_b32_e64 v38, v38, 13, s[16:17]
	v_cmp_eq_u32_e64 s[16:17], 0, v39
	v_cmp_gt_f32_e64 s[18:19], v6, v2
	s_and_b64 s[16:17], s[16:17], s[18:19]
	v_cndmask_b32_e64 v2, v2, v6, s[16:17]
	v_and_b32_e32 v39, 0x8000, v3
	v_cndmask_b32_e64 v38, v38, 14, s[16:17]
	v_cmp_eq_u32_e64 s[16:17], 0, v39
	v_cmp_gt_f32_e64 s[18:19], v7, v2
	s_and_b64 s[16:17], s[16:17], s[18:19]
	v_cndmask_b32_e64 v2, v2, v7, s[16:17]
	v_and_b32_e32 v39, 0x10000, v3
	v_cndmask_b32_e64 v38, v38, 15, s[16:17]
	v_cmp_eq_u32_e64 s[16:17], 0, v39
	v_cmp_gt_f32_e64 s[18:19], v18, v2
	s_and_b64 s[16:17], s[16:17], s[18:19]
	v_cndmask_b32_e64 v2, v2, v18, s[16:17]
	v_and_b32_e32 v39, 0x20000, v3
	v_cndmask_b32_e64 v38, v38, 16, s[16:17]
	v_cmp_eq_u32_e64 s[16:17], 0, v39
	v_cmp_gt_f32_e64 s[18:19], v19, v2
	s_and_b64 s[16:17], s[16:17], s[18:19]
	v_cndmask_b32_e64 v2, v2, v19, s[16:17]
	v_and_b32_e32 v39, 0x40000, v3
	v_cndmask_b32_e64 v38, v38, 17, s[16:17]
	v_cmp_eq_u32_e64 s[16:17], 0, v39
	v_cmp_gt_f32_e64 s[18:19], v28, v2
	s_and_b64 s[16:17], s[16:17], s[18:19]
	v_cndmask_b32_e64 v2, v2, v28, s[16:17]
	v_and_b32_e32 v39, 0x80000, v3
	v_cndmask_b32_e64 v38, v38, 18, s[16:17]
	v_cmp_eq_u32_e64 s[16:17], 0, v39
	v_cmp_gt_f32_e64 s[18:19], v29, v2
	s_and_b64 s[16:17], s[16:17], s[18:19]
	v_cndmask_b32_e64 v2, v2, v29, s[16:17]
	v_and_b32_e32 v39, 0x100000, v3
	v_cndmask_b32_e64 v38, v38, 19, s[16:17]
	v_cmp_eq_u32_e64 s[16:17], 0, v39
	v_cmp_gt_f32_e64 s[18:19], v12, v2
	s_and_b64 s[16:17], s[16:17], s[18:19]
	v_cndmask_b32_e64 v2, v2, v12, s[16:17]
	v_and_b32_e32 v39, 0x200000, v3
	v_cndmask_b32_e64 v38, v38, 20, s[16:17]
	v_cmp_eq_u32_e64 s[16:17], 0, v39
	v_cmp_gt_f32_e64 s[18:19], v13, v2
	s_and_b64 s[16:17], s[16:17], s[18:19]
	v_cndmask_b32_e64 v2, v2, v13, s[16:17]
	v_and_b32_e32 v39, 0x400000, v3
	v_cndmask_b32_e64 v38, v38, 21, s[16:17]
	v_cmp_eq_u32_e64 s[16:17], 0, v39
	v_cmp_gt_f32_e64 s[18:19], v4, v2
	s_and_b64 s[16:17], s[16:17], s[18:19]
	v_cndmask_b32_e64 v2, v2, v4, s[16:17]
	v_and_b32_e32 v39, 0x800000, v3
	v_cndmask_b32_e64 v38, v38, 22, s[16:17]
	v_cmp_eq_u32_e64 s[16:17], 0, v39
	v_cmp_gt_f32_e64 s[18:19], v5, v2
	s_and_b64 s[16:17], s[16:17], s[18:19]
	v_cndmask_b32_e64 v2, v2, v5, s[16:17]
	v_and_b32_e32 v39, 0x1000000, v3
	v_cndmask_b32_e64 v38, v38, 23, s[16:17]
	v_cmp_eq_u32_e64 s[16:17], 0, v39
	v_cmp_gt_f32_e64 s[18:19], v14, v2
	s_and_b64 s[16:17], s[16:17], s[18:19]
	v_cndmask_b32_e64 v2, v2, v14, s[16:17]
	v_and_b32_e32 v39, 0x2000000, v3
	v_cndmask_b32_e64 v38, v38, 24, s[16:17]
	v_cmp_eq_u32_e64 s[16:17], 0, v39
	v_cmp_gt_f32_e64 s[18:19], v15, v2
	s_and_b64 s[16:17], s[16:17], s[18:19]
	v_cndmask_b32_e64 v2, v2, v15, s[16:17]
	v_and_b32_e32 v39, 0x4000000, v3
	v_cndmask_b32_e64 v38, v38, 25, s[16:17]
	v_cmp_eq_u32_e64 s[16:17], 0, v39
	v_cmp_gt_f32_e64 s[18:19], v26, v2
	s_and_b64 s[16:17], s[16:17], s[18:19]
	v_cndmask_b32_e64 v2, v2, v26, s[16:17]
	v_and_b32_e32 v39, 0x8000000, v3
	v_cndmask_b32_e64 v38, v38, 26, s[16:17]
	v_cmp_eq_u32_e64 s[16:17], 0, v39
	v_cmp_gt_f32_e64 s[18:19], v27, v2
	s_and_b64 s[16:17], s[16:17], s[18:19]
	v_cndmask_b32_e64 v2, v2, v27, s[16:17]
	v_and_b32_e32 v39, 0x10000000, v3
	v_cndmask_b32_e64 v38, v38, 27, s[16:17]
	v_cmp_eq_u32_e64 s[16:17], 0, v39
	v_cmp_gt_f32_e64 s[18:19], v16, v2
	s_and_b64 s[16:17], s[16:17], s[18:19]
	v_cndmask_b32_e64 v2, v2, v16, s[16:17]
	v_and_b32_e32 v39, 0x20000000, v3
	v_cndmask_b32_e64 v38, v38, 28, s[16:17]
	v_cmp_eq_u32_e64 s[16:17], 0, v39
	v_cmp_gt_f32_e64 s[18:19], v17, v2
	s_and_b64 s[16:17], s[16:17], s[18:19]
	v_cndmask_b32_e64 v2, v2, v17, s[16:17]
	v_and_b32_e32 v39, 2.0, v3
	v_cndmask_b32_e64 v38, v38, 29, s[16:17]
	v_cmp_eq_u32_e64 s[16:17], 0, v39
	v_cmp_gt_f32_e64 s[18:19], v8, v2
	s_and_b64 s[16:17], s[16:17], s[18:19]
	v_cndmask_b32_e64 v2, v2, v8, s[16:17]
	v_cndmask_b32_e64 v38, v38, 30, s[16:17]
	v_cmp_lt_i32_e64 s[16:17], -1, v3
	v_cmp_gt_f32_e64 s[18:19], v9, v2
	s_and_b64 s[16:17], s[16:17], s[18:19]
	v_cndmask_b32_e64 v39, v2, v9, s[16:17]
	v_cndmask_b32_e64 v2, v38, 31, s[16:17]
	v_lshlrev_b32_e64 v38, v2, 1
	v_bitop3_b32 v89, v38, 1, v3 bitop3:0xc8
	v_cmp_eq_u32_e64 s[16:17], 0, v89
	s_and_b64 vcc, s[16:17], vcc
	v_cndmask_b32_e32 v34, v112, v34, vcc
	v_bitop3_b32 v89, v38, 2, v3 bitop3:0xc8
	v_cmp_eq_u32_e32 vcc, 0, v89
	v_cmp_gt_f32_e64 s[16:17], v35, v34
	s_and_b64 vcc, vcc, s[16:17]
	v_cndmask_b32_e32 v34, v34, v35, vcc
	v_bitop3_b32 v89, v38, 4, v3 bitop3:0xc8
	v_cndmask_b32_e64 v35, 0, 1, vcc
	v_cmp_eq_u32_e32 vcc, 0, v89
	v_cmp_gt_f32_e64 s[16:17], v30, v34
	s_and_b64 vcc, vcc, s[16:17]
	v_cndmask_b32_e32 v30, v34, v30, vcc
	v_cndmask_b32_e64 v34, v35, 2, vcc
	v_bitop3_b32 v35, v38, 8, v3 bitop3:0xc8
	v_cmp_eq_u32_e32 vcc, 0, v35
	v_cmp_gt_f32_e64 s[16:17], v31, v30
	s_and_b64 vcc, vcc, s[16:17]
	v_cndmask_b32_e32 v30, v30, v31, vcc
	v_cndmask_b32_e64 v31, v34, 3, vcc
	v_bitop3_b32 v34, v38, 16, v3 bitop3:0xc8
	v_cmp_eq_u32_e32 vcc, 0, v34
	v_cmp_gt_f32_e64 s[16:17], v22, v30
	s_and_b64 vcc, vcc, s[16:17]
	v_cndmask_b32_e32 v22, v30, v22, vcc
	v_cndmask_b32_e64 v30, v31, 4, vcc
	v_bitop3_b32 v31, v38, 32, v3 bitop3:0xc8
	v_cmp_eq_u32_e32 vcc, 0, v31
	v_cmp_gt_f32_e64 s[16:17], v23, v22
	s_and_b64 vcc, vcc, s[16:17]
	v_cndmask_b32_e32 v22, v22, v23, vcc
	v_cndmask_b32_e64 v23, v30, 5, vcc
	v_bitop3_b32 v30, v38, 64, v3 bitop3:0xc8
	v_cmp_eq_u32_e32 vcc, 0, v30
	v_cmp_gt_f32_e64 s[16:17], v10, v22
	s_and_b64 vcc, vcc, s[16:17]
	s_movk_i32 s16, 0x80
	v_cndmask_b32_e32 v10, v22, v10, vcc
	v_cndmask_b32_e64 v22, v23, 6, vcc
	v_bitop3_b32 v23, v38, s16, v3 bitop3:0xc8
	v_cmp_eq_u32_e32 vcc, 0, v23
	v_cmp_gt_f32_e64 s[16:17], v11, v10
	s_and_b64 vcc, vcc, s[16:17]
	s_movk_i32 s16, 0x100
	v_cndmask_b32_e32 v10, v10, v11, vcc
	v_cndmask_b32_e64 v11, v22, 7, vcc
	v_bitop3_b32 v22, v38, s16, v3 bitop3:0xc8
	v_cmp_eq_u32_e32 vcc, 0, v22
	v_cmp_gt_f32_e64 s[16:17], v24, v10
	s_and_b64 vcc, vcc, s[16:17]
	s_movk_i32 s16, 0x200
	v_cndmask_b32_e32 v10, v10, v24, vcc
	v_bitop3_b32 v22, v38, s16, v3 bitop3:0xc8
	v_cndmask_b32_e64 v11, v11, 8, vcc
	v_cmp_eq_u32_e32 vcc, 0, v22
	v_cmp_gt_f32_e64 s[16:17], v25, v10
	s_and_b64 vcc, vcc, s[16:17]
	v_cndmask_b32_e32 v10, v10, v25, vcc
	v_bitop3_b32 v22, v38, s52, v3 bitop3:0xc8
	v_cndmask_b32_e64 v11, v11, 9, vcc
	v_cmp_eq_u32_e32 vcc, 0, v22
	v_cmp_gt_f32_e64 s[16:17], v32, v10
	s_and_b64 vcc, vcc, s[16:17]
	s_movk_i32 s16, 0x800
	v_cndmask_b32_e32 v10, v10, v32, vcc
	v_bitop3_b32 v22, v38, s16, v3 bitop3:0xc8
	v_cndmask_b32_e64 v11, v11, 10, vcc
	v_cmp_eq_u32_e32 vcc, 0, v22
	v_cmp_gt_f32_e64 s[16:17], v33, v10
	s_and_b64 vcc, vcc, s[16:17]
	s_movk_i32 s16, 0x1000
	v_cndmask_b32_e32 v10, v10, v33, vcc
	v_bitop3_b32 v22, v38, s16, v3 bitop3:0xc8
	v_cndmask_b32_e64 v11, v11, 11, vcc
	v_cmp_eq_u32_e32 vcc, 0, v22
	v_cmp_gt_f32_e64 s[16:17], v20, v10
	s_and_b64 vcc, vcc, s[16:17]
	s_movk_i32 s16, 0x2000
	v_cndmask_b32_e32 v10, v10, v20, vcc
	v_bitop3_b32 v20, v38, s16, v3 bitop3:0xc8
	v_cndmask_b32_e64 v11, v11, 12, vcc
	v_cmp_eq_u32_e32 vcc, 0, v20
	v_cmp_gt_f32_e64 s[16:17], v21, v10
	s_and_b64 vcc, vcc, s[16:17]
	s_movk_i32 s16, 0x4000
	v_cndmask_b32_e32 v10, v10, v21, vcc
	v_bitop3_b32 v20, v38, s16, v3 bitop3:0xc8
	v_cndmask_b32_e64 v11, v11, 13, vcc
	v_cmp_eq_u32_e32 vcc, 0, v20
	v_cmp_gt_f32_e64 s[16:17], v6, v10
	s_and_b64 vcc, vcc, s[16:17]
	s_mov_b32 s16, 0x8000
	v_cndmask_b32_e32 v6, v10, v6, vcc
	v_cndmask_b32_e64 v10, v11, 14, vcc
	v_bitop3_b32 v11, v38, s16, v3 bitop3:0xc8
	v_cmp_eq_u32_e32 vcc, 0, v11
	v_cmp_gt_f32_e64 s[16:17], v7, v6
	s_and_b64 vcc, vcc, s[16:17]
	s_mov_b32 s16, 0x10000
	v_cndmask_b32_e32 v6, v6, v7, vcc
	v_cndmask_b32_e64 v7, v10, 15, vcc
	v_bitop3_b32 v10, v38, s16, v3 bitop3:0xc8
	v_cmp_eq_u32_e32 vcc, 0, v10
	v_cmp_gt_f32_e64 s[16:17], v18, v6
	s_and_b64 vcc, vcc, s[16:17]
	s_mov_b32 s16, 0x20000
	v_cndmask_b32_e32 v6, v6, v18, vcc
	v_bitop3_b32 v10, v38, s16, v3 bitop3:0xc8
	v_cndmask_b32_e64 v7, v7, 16, vcc
	v_cmp_eq_u32_e32 vcc, 0, v10
	v_cmp_gt_f32_e64 s[16:17], v19, v6
	s_and_b64 vcc, vcc, s[16:17]
	s_mov_b32 s16, 0x40000
	v_cndmask_b32_e32 v6, v6, v19, vcc
	v_bitop3_b32 v10, v38, s16, v3 bitop3:0xc8
	v_cndmask_b32_e64 v7, v7, 17, vcc
	v_cmp_eq_u32_e32 vcc, 0, v10
	v_cmp_gt_f32_e64 s[16:17], v28, v6
	s_and_b64 vcc, vcc, s[16:17]
	s_mov_b32 s16, 0x80000
	v_cndmask_b32_e32 v6, v6, v28, vcc
	v_bitop3_b32 v10, v38, s16, v3 bitop3:0xc8
	v_cndmask_b32_e64 v7, v7, 18, vcc
	v_cmp_eq_u32_e32 vcc, 0, v10
	v_cmp_gt_f32_e64 s[16:17], v29, v6
	s_and_b64 vcc, vcc, s[16:17]
	s_mov_b32 s16, 0x100000
	v_cndmask_b32_e32 v6, v6, v29, vcc
	v_bitop3_b32 v10, v38, s16, v3 bitop3:0xc8
	v_cndmask_b32_e64 v7, v7, 19, vcc
	v_cmp_eq_u32_e32 vcc, 0, v10
	v_cmp_gt_f32_e64 s[16:17], v12, v6
	s_and_b64 vcc, vcc, s[16:17]
	s_mov_b32 s16, 0x200000
	v_cndmask_b32_e32 v6, v6, v12, vcc
	v_bitop3_b32 v10, v38, s16, v3 bitop3:0xc8
	v_cndmask_b32_e64 v7, v7, 20, vcc
	v_cmp_eq_u32_e32 vcc, 0, v10
	v_cmp_gt_f32_e64 s[16:17], v13, v6
	s_and_b64 vcc, vcc, s[16:17]
	s_mov_b32 s16, 0x400000
	v_cndmask_b32_e32 v6, v6, v13, vcc
	v_bitop3_b32 v10, v38, s16, v3 bitop3:0xc8
	v_cndmask_b32_e64 v7, v7, 21, vcc
	v_cmp_eq_u32_e32 vcc, 0, v10
	v_cmp_gt_f32_e64 s[16:17], v4, v6
	s_and_b64 vcc, vcc, s[16:17]
	s_mov_b32 s16, 0x800000
	v_cndmask_b32_e32 v4, v6, v4, vcc
	v_cndmask_b32_e64 v6, v7, 22, vcc
	v_bitop3_b32 v7, v38, s16, v3 bitop3:0xc8
	v_cmp_eq_u32_e32 vcc, 0, v7
	v_cmp_gt_f32_e64 s[16:17], v5, v4
	s_and_b64 vcc, vcc, s[16:17]
	s_mov_b32 s16, 0x1000000
	v_cndmask_b32_e32 v4, v4, v5, vcc
	v_cndmask_b32_e64 v5, v6, 23, vcc
	v_bitop3_b32 v6, v38, s16, v3 bitop3:0xc8
	v_cmp_eq_u32_e32 vcc, 0, v6
	v_cmp_gt_f32_e64 s[16:17], v14, v4
	s_and_b64 vcc, vcc, s[16:17]
	v_cndmask_b32_e32 v4, v4, v14, vcc
	v_bitop3_b32 v6, v38, s61, v3 bitop3:0xc8
	v_cndmask_b32_e64 v5, v5, 24, vcc
	v_cmp_eq_u32_e32 vcc, 0, v6
	v_cmp_gt_f32_e64 s[16:17], v15, v4
	s_and_b64 vcc, vcc, s[16:17]
	v_cndmask_b32_e32 v4, v4, v15, vcc
	v_bitop3_b32 v6, v38, s62, v3 bitop3:0xc8
	v_cndmask_b32_e64 v5, v5, 25, vcc
	v_cmp_eq_u32_e32 vcc, 0, v6
	v_cmp_gt_f32_e64 s[16:17], v26, v4
	s_and_b64 vcc, vcc, s[16:17]
	v_cndmask_b32_e32 v4, v4, v26, vcc
	v_bitop3_b32 v6, v38, s63, v3 bitop3:0xc8
	v_cndmask_b32_e64 v5, v5, 26, vcc
	v_cmp_eq_u32_e32 vcc, 0, v6
	v_cmp_gt_f32_e64 s[16:17], v27, v4
	s_and_b64 vcc, vcc, s[16:17]
	v_cndmask_b32_e32 v4, v4, v27, vcc
	v_bitop3_b32 v6, v38, s64, v3 bitop3:0xc8
	v_cndmask_b32_e64 v5, v5, 27, vcc
	v_cmp_eq_u32_e32 vcc, 0, v6
	v_cmp_gt_f32_e64 s[16:17], v16, v4
	s_and_b64 vcc, vcc, s[16:17]
	v_cndmask_b32_e32 v4, v4, v16, vcc
	v_bitop3_b32 v6, v38, s65, v3 bitop3:0xc8
	v_cndmask_b32_e64 v5, v5, 28, vcc
	v_cmp_eq_u32_e32 vcc, 0, v6
	v_cmp_gt_f32_e64 s[16:17], v17, v4
	s_and_b64 vcc, vcc, s[16:17]
	v_or_b32_e32 v88, v38, v3
	v_cndmask_b32_e32 v4, v4, v17, vcc
	v_bitop3_b32 v3, v38, 2.0, v3 bitop3:0xc8
	v_cndmask_b32_e64 v5, v5, 29, vcc
	v_cmp_eq_u32_e32 vcc, 0, v3
	v_cmp_gt_f32_e64 s[16:17], v8, v4
	s_and_b64 vcc, vcc, s[16:17]
	v_cndmask_b32_e32 v3, v4, v8, vcc
	v_cndmask_b32_e64 v4, v5, 30, vcc
	v_cmp_lt_i32_e32 vcc, -1, v88
	v_cmp_gt_f32_e64 s[16:17], v9, v3
	s_and_b64 vcc, vcc, s[16:17]
	v_cndmask_b32_e32 v5, v3, v9, vcc
	v_cndmask_b32_e64 v3, v4, 31, vcc
	v_sub_f32_e32 v4, v36, v36
	v_mul_f32_e32 v4, 0x3fb8aa3b, v4
	v_exp_f32_e32 v10, v4
	v_sub_f32_e32 v4, v37, v36
	v_mul_f32_e32 v4, 0x3fb8aa3b, v4
	v_exp_f32_e32 v11, v4
	v_sub_f32_e32 v4, v39, v36
	v_mul_f32_e32 v4, 0x3fb8aa3b, v4
	v_exp_f32_e32 v12, v4
	v_sub_f32_e32 v4, v5, v36
	v_mul_f32_e32 v4, 0x3fb8aa3b, v4
	v_exp_f32_e32 v13, v4
	v_add_f32_e32 v4, 0, v10
	v_add_f32_e32 v4, v4, v11
	v_add_f32_e32 v4, v4, v12
	v_add_f32_e32 v14, v4, v13
	v_div_scale_f32 v15, s[16:17], v14, v14, v10
	v_rcp_f32_e32 v16, v15
	v_lshl_add_u32 v4, s66, 8, v94
	v_ashrrev_i32_e32 v5, 31, v4
	v_lshlrev_b64 v[6:7], 2, v[4:5]
	v_fma_f32 v5, -v15, v16, 1.0
	v_fmac_f32_e32 v16, v5, v16
	v_div_scale_f32 v5, vcc, v10, v14, v10
	v_mul_f32_e32 v17, v5, v16
	v_fma_f32 v18, -v15, v17, v5
	v_fmac_f32_e32 v17, v18, v16
	v_fma_f32 v5, -v15, v17, v5
	v_div_fmas_f32 v5, v5, v16, v17
	v_div_fixup_f32 v5, v5, v14, v10
	v_div_scale_f32 v10, s[16:17], v14, v14, v11
	v_rcp_f32_e32 v15, v10
	v_lshl_add_u64 v[8:9], s[20:21], 0, v[6:7]
	v_lshl_add_u64 v[6:7], s[22:23], 0, v[6:7]
	global_store_dword v[6:7], v5, off
	v_or_b32_e32 v6, 1, v4
	v_fma_f32 v4, -v10, v15, 1.0
	v_lshl_add_u32 v5, v0, 2, 0
	v_fmac_f32_e32 v15, v4, v15
	v_div_scale_f32 v4, vcc, v11, v14, v11
	ds_add_u32 v5, v109 offset:58624
	v_mul_f32_e32 v5, v4, v15
	v_fma_f32 v16, -v10, v5, v4
	v_fmac_f32_e32 v5, v16, v15
	v_fma_f32 v4, -v10, v5, v4
	v_div_fmas_f32 v4, v4, v15, v5
	v_div_scale_f32 v5, s[16:17], v14, v14, v12
	v_rcp_f32_e32 v15, v5
	v_ashrrev_i32_e32 v7, 31, v6
	v_div_fixup_f32 v4, v4, v14, v11
	v_lshl_add_u64 v[10:11], v[6:7], 2, s[22:23]
	v_lshl_add_u32 v6, v1, 2, 0
	ds_add_u32 v6, v109 offset:58624
	v_fma_f32 v6, -v5, v15, 1.0
	v_fmac_f32_e32 v15, v6, v15
	v_div_scale_f32 v6, vcc, v12, v14, v12
	v_mul_f32_e32 v7, v6, v15
	v_fma_f32 v16, -v5, v7, v6
	v_fmac_f32_e32 v7, v16, v15
	v_fma_f32 v5, -v5, v7, v6
	v_div_scale_f32 v6, s[16:17], v14, v14, v13
	v_div_fmas_f32 v5, v5, v15, v7
	v_rcp_f32_e32 v7, v6
	v_div_fixup_f32 v5, v5, v14, v12
	v_lshl_add_u32 v12, v2, 2, 0
	ds_add_u32 v12, v109 offset:58624
	global_store_dwordx4 v[8:9], v[0:3], off
	s_nop 1
	v_fma_f32 v0, -v6, v7, 1.0
	v_fmac_f32_e32 v7, v0, v7
	v_div_scale_f32 v0, vcc, v13, v14, v13
	v_mul_f32_e32 v1, v0, v7
	v_fma_f32 v2, -v6, v1, v0
	v_fmac_f32_e32 v1, v2, v7
	v_fma_f32 v0, -v6, v1, v0
	v_div_fmas_f32 v0, v0, v7, v1
	v_div_fixup_f32 v6, v0, v14, v13
	global_store_dwordx3 v[10:11], v[4:6], off
	v_lshl_add_u32 v0, v3, 2, 0
	ds_add_u32 v0, v109 offset:58624

.LBB0_2382:
	s_waitcnt vmcnt(0)
	s_barrier
	s_waitcnt vmcnt(0)
	s_waitcnt vmcnt(0)
	v_readlane_b32 s98, v253, 20
	v_mbcnt_lo_u32_b32 v216, -1, 0
	v_mbcnt_hi_u32_b32 v216, -1, v216
	s_lshr_b32 s99, s98, 1
	s_and_b32 s100, s98, 1
	v_lshrrev_b32_e32 v217, 5, v216
	v_and_b32_e32 v216, 31, v216
	s_lshl_b32 s101, s99, 4
	v_add_u32_e32 v218, s101, v217
	v_lshlrev_b32_e32 v219, 7, v218
	v_lshl_add_u32 v219, v216, 2, v219
	v_add_u32_e32 v219, 0xa400, v219
	v_mul_u32_u24_e32 v218, 0x104, v218
	s_lshl_b32 s101, s100, 7
	v_add_u32_e32 v218, s101, v218
	v_lshl_add_u32 v218, v216, 2, v218
	v_add_u32_e32 v218, 0x6000, v218
	v_mov_b32_e32 v221, s98
	v_mbcnt_lo_u32_b32 v220, -1, 0
	v_mbcnt_hi_u32_b32 v220, -1, v220
	v_lshl_add_u32 v220, v221, 6, v220
	v_and_b32_e32 v221, 7, v220
	v_lshrrev_b32_e32 v220, 3, v220
	v_mul_u32_u24_e32 v221, 0x820, v221
	v_lshl_add_u32 v220, v220, 2, v221
	v_add_u32_e32 v220, 0x6000, v220
	v_add_u32_e32 v221, 0x410, v220
	s_lshl_b32 s101, s99, 13
	s_lshl_b32 s100, s100, 12
	s_add_i32 s101, s101, s100
	v_lshlrev_b32_e32 v217, 9, v217
	v_add_u32_e32 v217, s101, v217
	v_lshl_add_u32 v217, v216, 2, v217
	s_and_saveexec_b64 s[16:17], s[4:5]
	ds_write_b32 v95, v45 offset:58624
	s_or_b64 exec, exec, s[16:17]
	v_add_u32_e32 v0, s67, v42
	v_ashrrev_i32_e32 v1, 31, v0
	v_lshlrev_b64 v[0:1], 11, v[0:1]
	v_lshl_add_u64 v[92:93], v[46:47], 0, v[0:1]
	global_load_dwordx4 v[30:33], v[92:93], off sc1
	global_load_dwordx4 v[34:37], v[48:49], off
	global_load_dwordx4 v[20:23], v[52:53], off
	global_load_dwordx4 v[24:27], v[92:93], off offset:128 sc1
	ds_read_b64 v[38:39], v106 offset:20480
	ds_read_b128 v[116:119], v43 offset:12288
	ds_read_b128 v[120:123], v43 offset:12304
	ds_read_b128 v[124:127], v43 offset:16384
	ds_read_b128 v[128:131], v43 offset:16400
	v_add_u32_e32 v114, 0x6000, v97
	v_mov_b32_e32 v4, 0
	s_waitcnt lgkmcnt(4)
	v_mov_b32_e32 v0, v38
	v_mov_b32_e32 v1, v38
	v_mov_b32_e32 v2, v38
	v_mov_b32_e32 v3, v38
	v_mov_b32_e32 v88, v39
	v_mov_b32_e32 v89, v39
	v_mov_b32_e32 v90, v39
	v_mov_b32_e32 v91, v39
	v_add_u32_e32 v113, 0x6400, v97
	s_mov_b32 s16, 0
	v_mov_b32_e32 v28, v103
	v_mov_b32_e32 v5, v4
	v_mov_b32_e32 v6, v4
	v_mov_b32_e32 v7, v4
	v_mov_b32_e32 v8, v4
	v_mov_b32_e32 v9, v4
	v_mov_b32_e32 v10, v4
	v_mov_b32_e32 v11, v4
	v_mov_b32_e32 v12, v4
	v_mov_b32_e32 v13, v4
	v_mov_b32_e32 v14, v4
	v_mov_b32_e32 v15, v4
	v_mov_b32_e32 v16, v4
	v_mov_b32_e32 v17, v4
	v_mov_b32_e32 v18, v4
	s_waitcnt vmcnt(3)
	v_cvt_f32_f16_sdwa v19, v31 dst_sel:DWORD dst_unused:UNUSED_PAD src0_sel:WORD_1
	v_cvt_f32_f16_e32 v29, v31
	v_cvt_f32_f16_sdwa v31, v30 dst_sel:DWORD dst_unused:UNUSED_PAD src0_sel:WORD_1
	v_cvt_f32_f16_e32 v30, v30
	v_cvt_f32_f16_sdwa v115, v33 dst_sel:DWORD dst_unused:UNUSED_PAD src0_sel:WORD_1
	v_cvt_f32_f16_e32 v134, v33
	v_cvt_f32_f16_sdwa v133, v32 dst_sel:DWORD dst_unused:UNUSED_PAD src0_sel:WORD_1
	v_cvt_f32_f16_e32 v132, v32
	v_sub_f32_e32 v30, v30, v38
	v_sub_f32_e32 v31, v31, v38
	v_sub_f32_e32 v32, v29, v38
	v_sub_f32_e32 v33, v19, v38
	v_sub_f32_e32 v132, v132, v38
	v_sub_f32_e32 v133, v133, v38
	v_sub_f32_e32 v134, v134, v38
	v_sub_f32_e32 v135, v115, v38
	v_pk_mul_f32 v[30:31], v[38:39], v[30:31] op_sel:[1,0]
	v_pk_mul_f32 v[32:33], v[38:39], v[32:33] op_sel:[1,0]
	v_pk_mul_f32 v[134:135], v[38:39], v[134:135] op_sel:[1,0]
	v_pk_mul_f32 v[38:39], v[38:39], v[132:133] op_sel:[1,0]
	s_waitcnt lgkmcnt(1)
	v_fma_f32 v19, v116, v30, v124
	v_fma_f32 v30, v117, v31, v125
	s_waitcnt lgkmcnt(0)
	v_fma_f32 v29, v120, v38, v128
	v_fma_f32 v31, v121, v39, v129
	v_fma_f32 v32, v118, v32, v126
	v_fma_f32 v38, v122, v134, v130
	v_fmac_f32_e32 v127, v119, v33
	v_fmac_f32_e32 v131, v123, v135
	ds_write2_b32 v220, v19, v30 offset1:65
	ds_write2_b32 v221, v29, v31 offset1:65
	ds_write2_b32 v220, v32, v127 offset0:130 offset1:195
	ds_write2_b32 v221, v38, v131 offset0:130 offset1:195
	s_waitcnt vmcnt(2)
	ds_write_b128 v96, v[34:37] offset:41984
	v_mov_b32_e32 v19, v4
	s_waitcnt lgkmcnt(0)
	s_barrier
	ds_read_b32 v200, v218
	ds_read_b32 v208, v219
	ds_read_b32 v201, v218 offset:520
	ds_read_b32 v209, v219 offset:256
	ds_read_b32 v202, v218 offset:1040
	ds_read_b32 v210, v219 offset:512
	ds_read_b32 v203, v218 offset:1560
	ds_read_b32 v211, v219 offset:768
	ds_read_b32 v204, v218 offset:2080
	ds_read_b32 v212, v219 offset:1024
	ds_read_b32 v205, v218 offset:2600
	ds_read_b32 v213, v219 offset:1280
	ds_read_b32 v206, v218 offset:3120
	ds_read_b32 v214, v219 offset:1536
	s_waitcnt lgkmcnt(12)
	v_mfma_f32_32x32x2_f32 v[4:19], v200, v208, v[4:19]
	ds_read_b32 v207, v218 offset:3640
	ds_read_b32 v215, v219 offset:1792
	s_waitcnt lgkmcnt(12)
	v_mfma_f32_32x32x2_f32 v[4:19], v201, v209, v[4:19]
	s_waitcnt lgkmcnt(10)
	v_mfma_f32_32x32x2_f32 v[4:19], v202, v210, v[4:19]
	s_waitcnt lgkmcnt(8)
	v_mfma_f32_32x32x2_f32 v[4:19], v203, v211, v[4:19]
	s_waitcnt lgkmcnt(6)
	v_mfma_f32_32x32x2_f32 v[4:19], v204, v212, v[4:19]
	s_waitcnt lgkmcnt(4)
	v_mfma_f32_32x32x2_f32 v[4:19], v205, v213, v[4:19]
	s_waitcnt lgkmcnt(2)
	v_mfma_f32_32x32x2_f32 v[4:19], v206, v214, v[4:19]
	s_waitcnt lgkmcnt(0)
	v_mfma_f32_32x32x2_f32 v[4:19], v207, v215, v[4:19]
	s_barrier
	global_load_dwordx4 v[32:35], v[92:93], off offset:256 sc1
	global_load_dwordx4 v[28:31], v[54:55], off
	s_waitcnt vmcnt(2)
	v_cvt_f32_f16_sdwa v128, v24 dst_sel:DWORD dst_unused:UNUSED_PAD src0_sel:WORD_1
	v_cvt_f32_f16_e32 v24, v24
	v_cvt_f32_f16_e32 v129, v25
	v_cvt_f32_f16_sdwa v130, v26 dst_sel:DWORD dst_unused:UNUSED_PAD src0_sel:WORD_1
	v_cvt_f32_f16_e32 v133, v26
	ds_read_b128 v[36:39], v43 offset:12544
	ds_read_b128 v[116:119], v43 offset:12560
	ds_read_b128 v[120:123], v43 offset:16640
	ds_read_b128 v[124:127], v43 offset:16656
	v_cvt_f32_f16_sdwa v115, v25 dst_sel:DWORD dst_unused:UNUSED_PAD src0_sel:WORD_1
	v_cvt_f32_f16_sdwa v131, v27 dst_sel:DWORD dst_unused:UNUSED_PAD src0_sel:WORD_1
	v_cvt_f32_f16_e32 v132, v27
	v_sub_f32_e32 v24, v24, v0
	v_sub_f32_e32 v25, v128, v1
	v_sub_f32_e32 v26, v129, v2
	v_pk_mul_f32 v[24:25], v[88:89], v[24:25]
	v_sub_f32_e32 v128, v133, v0
	v_sub_f32_e32 v129, v130, v1
	v_sub_f32_e32 v27, v115, v3
	v_sub_f32_e32 v130, v132, v2
	v_sub_f32_e32 v131, v131, v3
	v_pk_mul_f32 v[128:129], v[88:89], v[128:129]
	s_waitcnt lgkmcnt(1)
	v_fma_f32 v24, v36, v24, v120
	v_fma_f32 v25, v37, v25, v121
	v_pk_mul_f32 v[26:27], v[90:91], v[26:27]
	v_pk_mul_f32 v[130:131], v[90:91], v[130:131]
	s_waitcnt lgkmcnt(0)
	v_fma_f32 v36, v116, v128, v124
	ds_write2_b32 v220, v24, v25 offset1:65
	v_fma_f32 v24, v117, v129, v125
	ds_write2_b32 v221, v36, v24 offset1:65
	v_fma_f32 v24, v38, v26, v122
	v_fma_f32 v25, v118, v130, v126
	v_fmac_f32_e32 v123, v39, v27
	v_fmac_f32_e32 v127, v119, v131
	ds_write2_b32 v220, v24, v123 offset0:130 offset1:195
	ds_write2_b32 v221, v25, v127 offset0:130 offset1:195
	ds_write_b128 v96, v[20:23] offset:41984
	s_mov_b32 s16, 0
	v_mov_b32_e32 v20, v103
	s_waitcnt lgkmcnt(0)
	s_barrier
	ds_read_b32 v200, v218
	ds_read_b32 v208, v219
	ds_read_b32 v201, v218 offset:520
	ds_read_b32 v209, v219 offset:256
	ds_read_b32 v202, v218 offset:1040
	ds_read_b32 v210, v219 offset:512
	ds_read_b32 v203, v218 offset:1560
	ds_read_b32 v211, v219 offset:768
	ds_read_b32 v204, v218 offset:2080
	ds_read_b32 v212, v219 offset:1024
	ds_read_b32 v205, v218 offset:2600
	ds_read_b32 v213, v219 offset:1280
	ds_read_b32 v206, v218 offset:3120
	ds_read_b32 v214, v219 offset:1536
	s_waitcnt lgkmcnt(12)
	v_mfma_f32_32x32x2_f32 v[4:19], v200, v208, v[4:19]
	ds_read_b32 v207, v218 offset:3640
	ds_read_b32 v215, v219 offset:1792
	s_waitcnt lgkmcnt(12)
	v_mfma_f32_32x32x2_f32 v[4:19], v201, v209, v[4:19]
	s_waitcnt lgkmcnt(10)
	v_mfma_f32_32x32x2_f32 v[4:19], v202, v210, v[4:19]
	s_waitcnt lgkmcnt(8)
	v_mfma_f32_32x32x2_f32 v[4:19], v203, v211, v[4:19]
	s_waitcnt lgkmcnt(6)
	v_mfma_f32_32x32x2_f32 v[4:19], v204, v212, v[4:19]
	s_waitcnt lgkmcnt(4)
	v_mfma_f32_32x32x2_f32 v[4:19], v205, v213, v[4:19]
	s_waitcnt lgkmcnt(2)
	v_mfma_f32_32x32x2_f32 v[4:19], v206, v214, v[4:19]
	s_waitcnt lgkmcnt(0)
	v_mfma_f32_32x32x2_f32 v[4:19], v207, v215, v[4:19]
	s_barrier
	global_load_dwordx4 v[36:39], v[92:93], off offset:384 sc1
	global_load_dwordx4 v[20:23], v[56:57], off
	s_waitcnt vmcnt(3)
	v_cvt_f32_f16_sdwa v128, v32 dst_sel:DWORD dst_unused:UNUSED_PAD src0_sel:WORD_1
	v_cvt_f32_f16_e32 v32, v32
	v_cvt_f32_f16_e32 v129, v33
	v_cvt_f32_f16_sdwa v130, v34 dst_sel:DWORD dst_unused:UNUSED_PAD src0_sel:WORD_1
	v_cvt_f32_f16_e32 v133, v34
	ds_read_b128 v[24:27], v43 offset:12800
	ds_read_b128 v[116:119], v43 offset:12816
	ds_read_b128 v[120:123], v43 offset:16896
	ds_read_b128 v[124:127], v43 offset:16912
	v_cvt_f32_f16_sdwa v115, v33 dst_sel:DWORD dst_unused:UNUSED_PAD src0_sel:WORD_1
	v_cvt_f32_f16_sdwa v131, v35 dst_sel:DWORD dst_unused:UNUSED_PAD src0_sel:WORD_1
	v_cvt_f32_f16_e32 v132, v35
	v_sub_f32_e32 v32, v32, v0
	v_sub_f32_e32 v33, v128, v1
	v_sub_f32_e32 v34, v129, v2
	v_pk_mul_f32 v[32:33], v[88:89], v[32:33]
	v_sub_f32_e32 v128, v133, v0
	v_sub_f32_e32 v129, v130, v1
	v_sub_f32_e32 v35, v115, v3
	v_pk_mul_f32 v[128:129], v[88:89], v[128:129]
	s_waitcnt lgkmcnt(1)
	v_fma_f32 v24, v24, v32, v120
	v_fma_f32 v25, v25, v33, v121
	v_pk_mul_f32 v[34:35], v[90:91], v[34:35]
	v_sub_f32_e32 v130, v132, v2
	v_sub_f32_e32 v131, v131, v3
	s_waitcnt lgkmcnt(0)
	v_fma_f32 v32, v116, v128, v124
	ds_write2_b32 v220, v24, v25 offset1:65
	v_fma_f32 v24, v117, v129, v125
	v_pk_mul_f32 v[130:131], v[90:91], v[130:131]
	ds_write2_b32 v221, v32, v24 offset1:65
	v_fma_f32 v24, v26, v34, v122
	v_fmac_f32_e32 v123, v27, v35
	v_fma_f32 v25, v118, v130, v126
	ds_write2_b32 v220, v24, v123 offset0:130 offset1:195
	v_fmac_f32_e32 v127, v119, v131
	s_mov_b32 s16, 0
	v_mov_b32_e32 v24, v103
	ds_write2_b32 v221, v25, v127 offset0:130 offset1:195
	s_waitcnt vmcnt(2)
	ds_write_b128 v96, v[28:31] offset:41984
	s_waitcnt lgkmcnt(0)
	s_barrier
	ds_read_b32 v200, v218
	ds_read_b32 v208, v219
	ds_read_b32 v201, v218 offset:520
	ds_read_b32 v209, v219 offset:256
	ds_read_b32 v202, v218 offset:1040
	ds_read_b32 v210, v219 offset:512
	ds_read_b32 v203, v218 offset:1560
	ds_read_b32 v211, v219 offset:768
	ds_read_b32 v204, v218 offset:2080
	ds_read_b32 v212, v219 offset:1024
	ds_read_b32 v205, v218 offset:2600
	ds_read_b32 v213, v219 offset:1280
	ds_read_b32 v206, v218 offset:3120
	ds_read_b32 v214, v219 offset:1536
	s_waitcnt lgkmcnt(12)
	v_mfma_f32_32x32x2_f32 v[4:19], v200, v208, v[4:19]
	ds_read_b32 v207, v218 offset:3640
	ds_read_b32 v215, v219 offset:1792
	s_waitcnt lgkmcnt(12)
	v_mfma_f32_32x32x2_f32 v[4:19], v201, v209, v[4:19]
	s_waitcnt lgkmcnt(10)
	v_mfma_f32_32x32x2_f32 v[4:19], v202, v210, v[4:19]
	s_waitcnt lgkmcnt(8)
	v_mfma_f32_32x32x2_f32 v[4:19], v203, v211, v[4:19]
	s_waitcnt lgkmcnt(6)
	v_mfma_f32_32x32x2_f32 v[4:19], v204, v212, v[4:19]
	s_waitcnt lgkmcnt(4)
	v_mfma_f32_32x32x2_f32 v[4:19], v205, v213, v[4:19]
	s_waitcnt lgkmcnt(2)
	v_mfma_f32_32x32x2_f32 v[4:19], v206, v214, v[4:19]
	s_waitcnt lgkmcnt(0)
	v_mfma_f32_32x32x2_f32 v[4:19], v207, v215, v[4:19]
	s_barrier
	global_load_dwordx4 v[28:31], v[92:93], off offset:512 sc1
	global_load_dwordx4 v[24:27], v[58:59], off
	s_waitcnt vmcnt(3)
	v_cvt_f32_f16_sdwa v128, v36 dst_sel:DWORD dst_unused:UNUSED_PAD src0_sel:WORD_1
	v_cvt_f32_f16_e32 v36, v36
	v_cvt_f32_f16_e32 v129, v37
	v_cvt_f32_f16_sdwa v130, v38 dst_sel:DWORD dst_unused:UNUSED_PAD src0_sel:WORD_1
	v_cvt_f32_f16_e32 v133, v38
	ds_read_b128 v[32:35], v43 offset:13056
	ds_read_b128 v[116:119], v43 offset:13072
	ds_read_b128 v[120:123], v43 offset:17152
	ds_read_b128 v[124:127], v43 offset:17168
	v_cvt_f32_f16_sdwa v115, v37 dst_sel:DWORD dst_unused:UNUSED_PAD src0_sel:WORD_1
	v_cvt_f32_f16_sdwa v131, v39 dst_sel:DWORD dst_unused:UNUSED_PAD src0_sel:WORD_1
	v_cvt_f32_f16_e32 v132, v39
	v_sub_f32_e32 v36, v36, v0
	v_sub_f32_e32 v37, v128, v1
	v_sub_f32_e32 v38, v129, v2
	v_pk_mul_f32 v[36:37], v[88:89], v[36:37]
	v_sub_f32_e32 v128, v133, v0
	v_sub_f32_e32 v129, v130, v1
	v_sub_f32_e32 v39, v115, v3
	v_sub_f32_e32 v130, v132, v2
	v_sub_f32_e32 v131, v131, v3
	v_pk_mul_f32 v[128:129], v[88:89], v[128:129]
	s_waitcnt lgkmcnt(1)
	v_fma_f32 v32, v32, v36, v120
	v_fma_f32 v33, v33, v37, v121
	v_pk_mul_f32 v[38:39], v[90:91], v[38:39]
	v_pk_mul_f32 v[130:131], v[90:91], v[130:131]
	s_waitcnt lgkmcnt(0)
	v_fma_f32 v36, v116, v128, v124
	ds_write2_b32 v220, v32, v33 offset1:65
	v_fma_f32 v32, v117, v129, v125
	ds_write2_b32 v221, v36, v32 offset1:65
	v_fma_f32 v32, v34, v38, v122
	v_fma_f32 v33, v118, v130, v126
	v_fmac_f32_e32 v123, v35, v39
	v_fmac_f32_e32 v127, v119, v131
	ds_write2_b32 v220, v32, v123 offset0:130 offset1:195
	ds_write2_b32 v221, v33, v127 offset0:130 offset1:195
	s_waitcnt vmcnt(2)
	ds_write_b128 v96, v[20:23] offset:41984
	s_mov_b32 s16, 0
	v_mov_b32_e32 v20, v103
	s_waitcnt lgkmcnt(0)
	s_barrier
	ds_read_b32 v200, v218
	ds_read_b32 v208, v219
	ds_read_b32 v201, v218 offset:520
	ds_read_b32 v209, v219 offset:256
	ds_read_b32 v202, v218 offset:1040
	ds_read_b32 v210, v219 offset:512
	ds_read_b32 v203, v218 offset:1560
	ds_read_b32 v211, v219 offset:768
	ds_read_b32 v204, v218 offset:2080
	ds_read_b32 v212, v219 offset:1024
	ds_read_b32 v205, v218 offset:2600
	ds_read_b32 v213, v219 offset:1280
	ds_read_b32 v206, v218 offset:3120
	ds_read_b32 v214, v219 offset:1536
	s_waitcnt lgkmcnt(12)
	v_mfma_f32_32x32x2_f32 v[4:19], v200, v208, v[4:19]
	ds_read_b32 v207, v218 offset:3640
	ds_read_b32 v215, v219 offset:1792
	s_waitcnt lgkmcnt(12)
	v_mfma_f32_32x32x2_f32 v[4:19], v201, v209, v[4:19]
	s_waitcnt lgkmcnt(10)
	v_mfma_f32_32x32x2_f32 v[4:19], v202, v210, v[4:19]
	s_waitcnt lgkmcnt(8)
	v_mfma_f32_32x32x2_f32 v[4:19], v203, v211, v[4:19]
	s_waitcnt lgkmcnt(6)
	v_mfma_f32_32x32x2_f32 v[4:19], v204, v212, v[4:19]
	s_waitcnt lgkmcnt(4)
	v_mfma_f32_32x32x2_f32 v[4:19], v205, v213, v[4:19]
	s_waitcnt lgkmcnt(2)
	v_mfma_f32_32x32x2_f32 v[4:19], v206, v214, v[4:19]
	s_waitcnt lgkmcnt(0)
	v_mfma_f32_32x32x2_f32 v[4:19], v207, v215, v[4:19]
	s_barrier
	global_load_dwordx4 v[32:35], v[92:93], off offset:640 sc1
	global_load_dwordx4 v[20:23], v[60:61], off
	s_waitcnt vmcnt(3)
	v_cvt_f32_f16_sdwa v128, v28 dst_sel:DWORD dst_unused:UNUSED_PAD src0_sel:WORD_1
	v_cvt_f32_f16_e32 v28, v28
	v_cvt_f32_f16_e32 v129, v29
	v_cvt_f32_f16_sdwa v130, v30 dst_sel:DWORD dst_unused:UNUSED_PAD src0_sel:WORD_1
	v_cvt_f32_f16_e32 v133, v30
	ds_read_b128 v[36:39], v43 offset:13312
	ds_read_b128 v[116:119], v43 offset:13328
	ds_read_b128 v[120:123], v43 offset:17408
	ds_read_b128 v[124:127], v43 offset:17424
	v_cvt_f32_f16_sdwa v115, v29 dst_sel:DWORD dst_unused:UNUSED_PAD src0_sel:WORD_1
	v_cvt_f32_f16_sdwa v131, v31 dst_sel:DWORD dst_unused:UNUSED_PAD src0_sel:WORD_1
	v_cvt_f32_f16_e32 v132, v31
	v_sub_f32_e32 v28, v28, v0
	v_sub_f32_e32 v29, v128, v1
	v_sub_f32_e32 v30, v129, v2
	v_pk_mul_f32 v[28:29], v[88:89], v[28:29]
	v_sub_f32_e32 v128, v133, v0
	v_sub_f32_e32 v129, v130, v1
	v_sub_f32_e32 v31, v115, v3
	v_sub_f32_e32 v130, v132, v2
	v_sub_f32_e32 v131, v131, v3
	v_pk_mul_f32 v[128:129], v[88:89], v[128:129]
	s_waitcnt lgkmcnt(1)
	v_fma_f32 v28, v36, v28, v120
	v_fma_f32 v29, v37, v29, v121
	v_pk_mul_f32 v[30:31], v[90:91], v[30:31]
	v_pk_mul_f32 v[130:131], v[90:91], v[130:131]
	s_waitcnt lgkmcnt(0)
	v_fma_f32 v36, v116, v128, v124
	ds_write2_b32 v220, v28, v29 offset1:65
	v_fma_f32 v28, v117, v129, v125
	ds_write2_b32 v221, v36, v28 offset1:65
	v_fma_f32 v28, v38, v30, v122
	v_fma_f32 v29, v118, v130, v126
	v_fmac_f32_e32 v123, v39, v31
	v_fmac_f32_e32 v127, v119, v131
	ds_write2_b32 v220, v28, v123 offset0:130 offset1:195
	ds_write2_b32 v221, v29, v127 offset0:130 offset1:195
	s_waitcnt vmcnt(2)
	ds_write_b128 v96, v[24:27] offset:41984
	s_mov_b32 s16, 0
	v_mov_b32_e32 v24, v103
	s_waitcnt lgkmcnt(0)
	s_barrier
	ds_read_b32 v200, v218
	ds_read_b32 v208, v219
	ds_read_b32 v201, v218 offset:520
	ds_read_b32 v209, v219 offset:256
	ds_read_b32 v202, v218 offset:1040
	ds_read_b32 v210, v219 offset:512
	ds_read_b32 v203, v218 offset:1560
	ds_read_b32 v211, v219 offset:768
	ds_read_b32 v204, v218 offset:2080
	ds_read_b32 v212, v219 offset:1024
	ds_read_b32 v205, v218 offset:2600
	ds_read_b32 v213, v219 offset:1280
	ds_read_b32 v206, v218 offset:3120
	ds_read_b32 v214, v219 offset:1536
	s_waitcnt lgkmcnt(12)
	v_mfma_f32_32x32x2_f32 v[4:19], v200, v208, v[4:19]
	ds_read_b32 v207, v218 offset:3640
	ds_read_b32 v215, v219 offset:1792
	s_waitcnt lgkmcnt(12)
	v_mfma_f32_32x32x2_f32 v[4:19], v201, v209, v[4:19]
	s_waitcnt lgkmcnt(10)
	v_mfma_f32_32x32x2_f32 v[4:19], v202, v210, v[4:19]
	s_waitcnt lgkmcnt(8)
	v_mfma_f32_32x32x2_f32 v[4:19], v203, v211, v[4:19]
	s_waitcnt lgkmcnt(6)
	v_mfma_f32_32x32x2_f32 v[4:19], v204, v212, v[4:19]
	s_waitcnt lgkmcnt(4)
	v_mfma_f32_32x32x2_f32 v[4:19], v205, v213, v[4:19]
	s_waitcnt lgkmcnt(2)
	v_mfma_f32_32x32x2_f32 v[4:19], v206, v214, v[4:19]
	s_waitcnt lgkmcnt(0)
	v_mfma_f32_32x32x2_f32 v[4:19], v207, v215, v[4:19]
	s_barrier
	global_load_dwordx4 v[28:31], v[92:93], off offset:768 sc1
	global_load_dwordx4 v[24:27], v[62:63], off
	s_waitcnt vmcnt(3)
	v_cvt_f32_f16_sdwa v128, v32 dst_sel:DWORD dst_unused:UNUSED_PAD src0_sel:WORD_1
	v_cvt_f32_f16_e32 v32, v32
	v_cvt_f32_f16_e32 v129, v33
	v_cvt_f32_f16_sdwa v130, v34 dst_sel:DWORD dst_unused:UNUSED_PAD src0_sel:WORD_1
	v_cvt_f32_f16_e32 v133, v34
	ds_read_b128 v[36:39], v43 offset:13568
	ds_read_b128 v[116:119], v43 offset:13584
	ds_read_b128 v[120:123], v43 offset:17664
	ds_read_b128 v[124:127], v43 offset:17680
	v_cvt_f32_f16_sdwa v115, v33 dst_sel:DWORD dst_unused:UNUSED_PAD src0_sel:WORD_1
	v_cvt_f32_f16_sdwa v131, v35 dst_sel:DWORD dst_unused:UNUSED_PAD src0_sel:WORD_1
	v_cvt_f32_f16_e32 v132, v35
	v_sub_f32_e32 v32, v32, v0
	v_sub_f32_e32 v33, v128, v1
	v_sub_f32_e32 v34, v129, v2
	v_pk_mul_f32 v[32:33], v[88:89], v[32:33]
	v_sub_f32_e32 v128, v133, v0
	v_sub_f32_e32 v129, v130, v1
	v_sub_f32_e32 v35, v115, v3
	v_sub_f32_e32 v130, v132, v2
	v_sub_f32_e32 v131, v131, v3
	v_pk_mul_f32 v[128:129], v[88:89], v[128:129]
	s_waitcnt lgkmcnt(1)
	v_fma_f32 v32, v36, v32, v120
	v_fma_f32 v33, v37, v33, v121
	v_pk_mul_f32 v[34:35], v[90:91], v[34:35]
	v_pk_mul_f32 v[130:131], v[90:91], v[130:131]
	s_waitcnt lgkmcnt(0)
	v_fma_f32 v36, v116, v128, v124
	ds_write2_b32 v220, v32, v33 offset1:65
	v_fma_f32 v32, v117, v129, v125
	ds_write2_b32 v221, v36, v32 offset1:65
	v_fma_f32 v32, v38, v34, v122
	v_fma_f32 v33, v118, v130, v126
	v_fmac_f32_e32 v123, v39, v35
	v_fmac_f32_e32 v127, v119, v131
	ds_write2_b32 v220, v32, v123 offset0:130 offset1:195
	ds_write2_b32 v221, v33, v127 offset0:130 offset1:195
	s_waitcnt vmcnt(2)
	ds_write_b128 v96, v[20:23] offset:41984
	s_mov_b32 s16, 0
	v_mov_b32_e32 v20, v103
	s_waitcnt lgkmcnt(0)
	s_barrier
	ds_read_b32 v200, v218
	ds_read_b32 v208, v219
	ds_read_b32 v201, v218 offset:520
	ds_read_b32 v209, v219 offset:256
	ds_read_b32 v202, v218 offset:1040
	ds_read_b32 v210, v219 offset:512
	ds_read_b32 v203, v218 offset:1560
	ds_read_b32 v211, v219 offset:768
	ds_read_b32 v204, v218 offset:2080
	ds_read_b32 v212, v219 offset:1024
	ds_read_b32 v205, v218 offset:2600
	ds_read_b32 v213, v219 offset:1280
	ds_read_b32 v206, v218 offset:3120
	ds_read_b32 v214, v219 offset:1536
	s_waitcnt lgkmcnt(12)
	v_mfma_f32_32x32x2_f32 v[4:19], v200, v208, v[4:19]
	ds_read_b32 v207, v218 offset:3640
	ds_read_b32 v215, v219 offset:1792
	s_waitcnt lgkmcnt(12)
	v_mfma_f32_32x32x2_f32 v[4:19], v201, v209, v[4:19]
	s_waitcnt lgkmcnt(10)
	v_mfma_f32_32x32x2_f32 v[4:19], v202, v210, v[4:19]
	s_waitcnt lgkmcnt(8)
	v_mfma_f32_32x32x2_f32 v[4:19], v203, v211, v[4:19]
	s_waitcnt lgkmcnt(6)
	v_mfma_f32_32x32x2_f32 v[4:19], v204, v212, v[4:19]
	s_waitcnt lgkmcnt(4)
	v_mfma_f32_32x32x2_f32 v[4:19], v205, v213, v[4:19]
	s_waitcnt lgkmcnt(2)
	v_mfma_f32_32x32x2_f32 v[4:19], v206, v214, v[4:19]
	s_waitcnt lgkmcnt(0)
	v_mfma_f32_32x32x2_f32 v[4:19], v207, v215, v[4:19]
	s_barrier
	global_load_dwordx4 v[32:35], v[92:93], off offset:896 sc1
	global_load_dwordx4 v[20:23], v[64:65], off
	s_waitcnt vmcnt(3)
	v_cvt_f32_f16_sdwa v128, v28 dst_sel:DWORD dst_unused:UNUSED_PAD src0_sel:WORD_1
	v_cvt_f32_f16_e32 v28, v28
	v_cvt_f32_f16_e32 v129, v29
	v_cvt_f32_f16_sdwa v130, v30 dst_sel:DWORD dst_unused:UNUSED_PAD src0_sel:WORD_1
	v_cvt_f32_f16_e32 v133, v30
	ds_read_b128 v[36:39], v43 offset:13824
	ds_read_b128 v[116:119], v43 offset:13840
	ds_read_b128 v[120:123], v43 offset:17920
	ds_read_b128 v[124:127], v43 offset:17936
	v_cvt_f32_f16_sdwa v115, v29 dst_sel:DWORD dst_unused:UNUSED_PAD src0_sel:WORD_1
	v_cvt_f32_f16_sdwa v131, v31 dst_sel:DWORD dst_unused:UNUSED_PAD src0_sel:WORD_1
	v_cvt_f32_f16_e32 v132, v31
	v_sub_f32_e32 v28, v28, v0
	v_sub_f32_e32 v29, v128, v1
	v_sub_f32_e32 v30, v129, v2
	v_pk_mul_f32 v[28:29], v[88:89], v[28:29]
	v_sub_f32_e32 v128, v133, v0
	v_sub_f32_e32 v129, v130, v1
	v_sub_f32_e32 v31, v115, v3
	v_sub_f32_e32 v130, v132, v2
	v_sub_f32_e32 v131, v131, v3
	v_pk_mul_f32 v[128:129], v[88:89], v[128:129]
	s_waitcnt lgkmcnt(1)
	v_fma_f32 v28, v36, v28, v120
	v_fma_f32 v29, v37, v29, v121
	v_pk_mul_f32 v[30:31], v[90:91], v[30:31]
	v_pk_mul_f32 v[130:131], v[90:91], v[130:131]
	s_waitcnt lgkmcnt(0)
	v_fma_f32 v36, v116, v128, v124
	ds_write2_b32 v220, v28, v29 offset1:65
	v_fma_f32 v28, v117, v129, v125
	ds_write2_b32 v221, v36, v28 offset1:65
	v_fma_f32 v28, v38, v30, v122
	v_fma_f32 v29, v118, v130, v126
	v_fmac_f32_e32 v123, v39, v31
	v_fmac_f32_e32 v127, v119, v131
	ds_write2_b32 v220, v28, v123 offset0:130 offset1:195
	ds_write2_b32 v221, v29, v127 offset0:130 offset1:195
	s_waitcnt vmcnt(2)
	ds_write_b128 v96, v[24:27] offset:41984
	s_mov_b32 s16, 0
	v_mov_b32_e32 v24, v103
	s_waitcnt lgkmcnt(0)
	s_barrier
	ds_read_b32 v200, v218
	ds_read_b32 v208, v219
	ds_read_b32 v201, v218 offset:520
	ds_read_b32 v209, v219 offset:256
	ds_read_b32 v202, v218 offset:1040
	ds_read_b32 v210, v219 offset:512
	ds_read_b32 v203, v218 offset:1560
	ds_read_b32 v211, v219 offset:768
	ds_read_b32 v204, v218 offset:2080
	ds_read_b32 v212, v219 offset:1024
	ds_read_b32 v205, v218 offset:2600
	ds_read_b32 v213, v219 offset:1280
	ds_read_b32 v206, v218 offset:3120
	ds_read_b32 v214, v219 offset:1536
	s_waitcnt lgkmcnt(12)
	v_mfma_f32_32x32x2_f32 v[4:19], v200, v208, v[4:19]
	ds_read_b32 v207, v218 offset:3640
	ds_read_b32 v215, v219 offset:1792
	s_waitcnt lgkmcnt(12)
	v_mfma_f32_32x32x2_f32 v[4:19], v201, v209, v[4:19]
	s_waitcnt lgkmcnt(10)
	v_mfma_f32_32x32x2_f32 v[4:19], v202, v210, v[4:19]
	s_waitcnt lgkmcnt(8)
	v_mfma_f32_32x32x2_f32 v[4:19], v203, v211, v[4:19]
	s_waitcnt lgkmcnt(6)
	v_mfma_f32_32x32x2_f32 v[4:19], v204, v212, v[4:19]
	s_waitcnt lgkmcnt(4)
	v_mfma_f32_32x32x2_f32 v[4:19], v205, v213, v[4:19]
	s_waitcnt lgkmcnt(2)
	v_mfma_f32_32x32x2_f32 v[4:19], v206, v214, v[4:19]
	s_waitcnt lgkmcnt(0)
	v_mfma_f32_32x32x2_f32 v[4:19], v207, v215, v[4:19]
	s_barrier
	global_load_dwordx4 v[28:31], v[92:93], off offset:1024 sc1
	global_load_dwordx4 v[24:27], v[66:67], off
	s_waitcnt vmcnt(3)
	v_cvt_f32_f16_sdwa v128, v32 dst_sel:DWORD dst_unused:UNUSED_PAD src0_sel:WORD_1
	v_cvt_f32_f16_e32 v32, v32
	v_cvt_f32_f16_e32 v129, v33
	v_cvt_f32_f16_sdwa v130, v34 dst_sel:DWORD dst_unused:UNUSED_PAD src0_sel:WORD_1
	v_cvt_f32_f16_e32 v133, v34
	ds_read_b128 v[36:39], v43 offset:14080
	ds_read_b128 v[116:119], v43 offset:14096
	ds_read_b128 v[120:123], v43 offset:18176
	ds_read_b128 v[124:127], v43 offset:18192
	v_cvt_f32_f16_sdwa v115, v33 dst_sel:DWORD dst_unused:UNUSED_PAD src0_sel:WORD_1
	v_cvt_f32_f16_sdwa v131, v35 dst_sel:DWORD dst_unused:UNUSED_PAD src0_sel:WORD_1
	v_cvt_f32_f16_e32 v132, v35
	v_sub_f32_e32 v32, v32, v0
	v_sub_f32_e32 v33, v128, v1
	v_sub_f32_e32 v34, v129, v2
	v_pk_mul_f32 v[32:33], v[88:89], v[32:33]
	v_sub_f32_e32 v128, v133, v0
	v_sub_f32_e32 v129, v130, v1
	v_sub_f32_e32 v35, v115, v3
	v_sub_f32_e32 v130, v132, v2
	v_sub_f32_e32 v131, v131, v3
	v_pk_mul_f32 v[128:129], v[88:89], v[128:129]
	s_waitcnt lgkmcnt(1)
	v_fma_f32 v32, v36, v32, v120
	v_fma_f32 v33, v37, v33, v121
	v_pk_mul_f32 v[34:35], v[90:91], v[34:35]
	v_pk_mul_f32 v[130:131], v[90:91], v[130:131]
	s_waitcnt lgkmcnt(0)
	v_fma_f32 v36, v116, v128, v124
	ds_write2_b32 v220, v32, v33 offset1:65
	v_fma_f32 v32, v117, v129, v125
	ds_write2_b32 v221, v36, v32 offset1:65
	v_fma_f32 v32, v38, v34, v122
	v_fma_f32 v33, v118, v130, v126
	v_fmac_f32_e32 v123, v39, v35
	v_fmac_f32_e32 v127, v119, v131
	ds_write2_b32 v220, v32, v123 offset0:130 offset1:195
	ds_write2_b32 v221, v33, v127 offset0:130 offset1:195
	s_waitcnt vmcnt(2)
	ds_write_b128 v96, v[20:23] offset:41984
	s_mov_b32 s16, 0
	v_mov_b32_e32 v20, v103
	s_waitcnt lgkmcnt(0)
	s_barrier
	ds_read_b32 v200, v218
	ds_read_b32 v208, v219
	ds_read_b32 v201, v218 offset:520
	ds_read_b32 v209, v219 offset:256
	ds_read_b32 v202, v218 offset:1040
	ds_read_b32 v210, v219 offset:512
	ds_read_b32 v203, v218 offset:1560
	ds_read_b32 v211, v219 offset:768
	ds_read_b32 v204, v218 offset:2080
	ds_read_b32 v212, v219 offset:1024
	ds_read_b32 v205, v218 offset:2600
	ds_read_b32 v213, v219 offset:1280
	ds_read_b32 v206, v218 offset:3120
	ds_read_b32 v214, v219 offset:1536
	s_waitcnt lgkmcnt(12)
	v_mfma_f32_32x32x2_f32 v[4:19], v200, v208, v[4:19]
	ds_read_b32 v207, v218 offset:3640
	ds_read_b32 v215, v219 offset:1792
	s_waitcnt lgkmcnt(12)
	v_mfma_f32_32x32x2_f32 v[4:19], v201, v209, v[4:19]
	s_waitcnt lgkmcnt(10)
	v_mfma_f32_32x32x2_f32 v[4:19], v202, v210, v[4:19]
	s_waitcnt lgkmcnt(8)
	v_mfma_f32_32x32x2_f32 v[4:19], v203, v211, v[4:19]
	s_waitcnt lgkmcnt(6)
	v_mfma_f32_32x32x2_f32 v[4:19], v204, v212, v[4:19]
	s_waitcnt lgkmcnt(4)
	v_mfma_f32_32x32x2_f32 v[4:19], v205, v213, v[4:19]
	s_waitcnt lgkmcnt(2)
	v_mfma_f32_32x32x2_f32 v[4:19], v206, v214, v[4:19]
	s_waitcnt lgkmcnt(0)
	v_mfma_f32_32x32x2_f32 v[4:19], v207, v215, v[4:19]
	s_barrier
	global_load_dwordx4 v[32:35], v[92:93], off offset:1152 sc1
	global_load_dwordx4 v[20:23], v[68:69], off
	s_waitcnt vmcnt(3)
	v_cvt_f32_f16_sdwa v128, v28 dst_sel:DWORD dst_unused:UNUSED_PAD src0_sel:WORD_1
	v_cvt_f32_f16_e32 v28, v28
	v_cvt_f32_f16_e32 v129, v29
	v_cvt_f32_f16_sdwa v130, v30 dst_sel:DWORD dst_unused:UNUSED_PAD src0_sel:WORD_1
	v_cvt_f32_f16_e32 v133, v30
	ds_read_b128 v[36:39], v43 offset:14336
	ds_read_b128 v[116:119], v43 offset:14352
	ds_read_b128 v[120:123], v43 offset:18432
	ds_read_b128 v[124:127], v43 offset:18448
	v_cvt_f32_f16_sdwa v115, v29 dst_sel:DWORD dst_unused:UNUSED_PAD src0_sel:WORD_1
	v_cvt_f32_f16_sdwa v131, v31 dst_sel:DWORD dst_unused:UNUSED_PAD src0_sel:WORD_1
	v_cvt_f32_f16_e32 v132, v31
	v_sub_f32_e32 v28, v28, v0
	v_sub_f32_e32 v29, v128, v1
	v_sub_f32_e32 v30, v129, v2
	v_pk_mul_f32 v[28:29], v[88:89], v[28:29]
	v_sub_f32_e32 v128, v133, v0
	v_sub_f32_e32 v129, v130, v1
	v_sub_f32_e32 v31, v115, v3
	v_sub_f32_e32 v130, v132, v2
	v_sub_f32_e32 v131, v131, v3
	v_pk_mul_f32 v[128:129], v[88:89], v[128:129]
	s_waitcnt lgkmcnt(1)
	v_fma_f32 v28, v36, v28, v120
	v_fma_f32 v29, v37, v29, v121
	v_pk_mul_f32 v[30:31], v[90:91], v[30:31]
	v_pk_mul_f32 v[130:131], v[90:91], v[130:131]
	s_waitcnt lgkmcnt(0)
	v_fma_f32 v36, v116, v128, v124
	ds_write2_b32 v220, v28, v29 offset1:65
	v_fma_f32 v28, v117, v129, v125
	ds_write2_b32 v221, v36, v28 offset1:65
	v_fma_f32 v28, v38, v30, v122
	v_fma_f32 v29, v118, v130, v126
	v_fmac_f32_e32 v123, v39, v31
	v_fmac_f32_e32 v127, v119, v131
	ds_write2_b32 v220, v28, v123 offset0:130 offset1:195
	ds_write2_b32 v221, v29, v127 offset0:130 offset1:195
	s_waitcnt vmcnt(2)
	ds_write_b128 v96, v[24:27] offset:41984
	s_mov_b32 s16, 0
	v_mov_b32_e32 v24, v103
	s_waitcnt lgkmcnt(0)
	s_barrier
	ds_read_b32 v200, v218
	ds_read_b32 v208, v219
	ds_read_b32 v201, v218 offset:520
	ds_read_b32 v209, v219 offset:256
	ds_read_b32 v202, v218 offset:1040
	ds_read_b32 v210, v219 offset:512
	ds_read_b32 v203, v218 offset:1560
	ds_read_b32 v211, v219 offset:768
	ds_read_b32 v204, v218 offset:2080
	ds_read_b32 v212, v219 offset:1024
	ds_read_b32 v205, v218 offset:2600
	ds_read_b32 v213, v219 offset:1280
	ds_read_b32 v206, v218 offset:3120
	ds_read_b32 v214, v219 offset:1536
	s_waitcnt lgkmcnt(12)
	v_mfma_f32_32x32x2_f32 v[4:19], v200, v208, v[4:19]
	ds_read_b32 v207, v218 offset:3640
	ds_read_b32 v215, v219 offset:1792
	s_waitcnt lgkmcnt(12)
	v_mfma_f32_32x32x2_f32 v[4:19], v201, v209, v[4:19]
	s_waitcnt lgkmcnt(10)
	v_mfma_f32_32x32x2_f32 v[4:19], v202, v210, v[4:19]
	s_waitcnt lgkmcnt(8)
	v_mfma_f32_32x32x2_f32 v[4:19], v203, v211, v[4:19]
	s_waitcnt lgkmcnt(6)
	v_mfma_f32_32x32x2_f32 v[4:19], v204, v212, v[4:19]
	s_waitcnt lgkmcnt(4)
	v_mfma_f32_32x32x2_f32 v[4:19], v205, v213, v[4:19]
	s_waitcnt lgkmcnt(2)
	v_mfma_f32_32x32x2_f32 v[4:19], v206, v214, v[4:19]
	s_waitcnt lgkmcnt(0)
	v_mfma_f32_32x32x2_f32 v[4:19], v207, v215, v[4:19]
	s_barrier
	global_load_dwordx4 v[28:31], v[92:93], off offset:1280 sc1
	global_load_dwordx4 v[24:27], v[70:71], off
	s_waitcnt vmcnt(3)
	v_cvt_f32_f16_sdwa v128, v32 dst_sel:DWORD dst_unused:UNUSED_PAD src0_sel:WORD_1
	v_cvt_f32_f16_e32 v32, v32
	v_cvt_f32_f16_e32 v129, v33
	v_cvt_f32_f16_sdwa v130, v34 dst_sel:DWORD dst_unused:UNUSED_PAD src0_sel:WORD_1
	v_cvt_f32_f16_e32 v133, v34
	ds_read_b128 v[36:39], v43 offset:14592
	ds_read_b128 v[116:119], v43 offset:14608
	ds_read_b128 v[120:123], v43 offset:18688
	ds_read_b128 v[124:127], v43 offset:18704
	v_cvt_f32_f16_sdwa v115, v33 dst_sel:DWORD dst_unused:UNUSED_PAD src0_sel:WORD_1
	v_cvt_f32_f16_sdwa v131, v35 dst_sel:DWORD dst_unused:UNUSED_PAD src0_sel:WORD_1
	v_cvt_f32_f16_e32 v132, v35
	v_sub_f32_e32 v32, v32, v0
	v_sub_f32_e32 v33, v128, v1
	v_sub_f32_e32 v34, v129, v2
	v_pk_mul_f32 v[32:33], v[88:89], v[32:33]
	v_sub_f32_e32 v128, v133, v0
	v_sub_f32_e32 v129, v130, v1
	v_sub_f32_e32 v35, v115, v3
	v_sub_f32_e32 v130, v132, v2
	v_sub_f32_e32 v131, v131, v3
	v_pk_mul_f32 v[128:129], v[88:89], v[128:129]
	s_waitcnt lgkmcnt(1)
	v_fma_f32 v32, v36, v32, v120
	v_fma_f32 v33, v37, v33, v121
	v_pk_mul_f32 v[34:35], v[90:91], v[34:35]
	v_pk_mul_f32 v[130:131], v[90:91], v[130:131]
	s_waitcnt lgkmcnt(0)
	v_fma_f32 v36, v116, v128, v124
	ds_write2_b32 v220, v32, v33 offset1:65
	v_fma_f32 v32, v117, v129, v125
	ds_write2_b32 v221, v36, v32 offset1:65
	v_fma_f32 v32, v38, v34, v122
	v_fma_f32 v33, v118, v130, v126
	v_fmac_f32_e32 v123, v39, v35
	v_fmac_f32_e32 v127, v119, v131
	ds_write2_b32 v220, v32, v123 offset0:130 offset1:195
	ds_write2_b32 v221, v33, v127 offset0:130 offset1:195
	s_waitcnt vmcnt(2)
	ds_write_b128 v96, v[20:23] offset:41984
	s_mov_b32 s16, 0
	v_mov_b32_e32 v20, v103
	s_waitcnt lgkmcnt(0)
	s_barrier
	ds_read_b32 v200, v218
	ds_read_b32 v208, v219
	ds_read_b32 v201, v218 offset:520
	ds_read_b32 v209, v219 offset:256
	ds_read_b32 v202, v218 offset:1040
	ds_read_b32 v210, v219 offset:512
	ds_read_b32 v203, v218 offset:1560
	ds_read_b32 v211, v219 offset:768
	ds_read_b32 v204, v218 offset:2080
	ds_read_b32 v212, v219 offset:1024
	ds_read_b32 v205, v218 offset:2600
	ds_read_b32 v213, v219 offset:1280
	ds_read_b32 v206, v218 offset:3120
	ds_read_b32 v214, v219 offset:1536
	s_waitcnt lgkmcnt(12)
	v_mfma_f32_32x32x2_f32 v[4:19], v200, v208, v[4:19]
	ds_read_b32 v207, v218 offset:3640
	ds_read_b32 v215, v219 offset:1792
	s_waitcnt lgkmcnt(12)
	v_mfma_f32_32x32x2_f32 v[4:19], v201, v209, v[4:19]
	s_waitcnt lgkmcnt(10)
	v_mfma_f32_32x32x2_f32 v[4:19], v202, v210, v[4:19]
	s_waitcnt lgkmcnt(8)
	v_mfma_f32_32x32x2_f32 v[4:19], v203, v211, v[4:19]
	s_waitcnt lgkmcnt(6)
	v_mfma_f32_32x32x2_f32 v[4:19], v204, v212, v[4:19]
	s_waitcnt lgkmcnt(4)
	v_mfma_f32_32x32x2_f32 v[4:19], v205, v213, v[4:19]
	s_waitcnt lgkmcnt(2)
	v_mfma_f32_32x32x2_f32 v[4:19], v206, v214, v[4:19]
	s_waitcnt lgkmcnt(0)
	v_mfma_f32_32x32x2_f32 v[4:19], v207, v215, v[4:19]
	s_barrier
	global_load_dwordx4 v[32:35], v[92:93], off offset:1408 sc1
	global_load_dwordx4 v[20:23], v[72:73], off
	s_waitcnt vmcnt(3)
	v_cvt_f32_f16_sdwa v128, v28 dst_sel:DWORD dst_unused:UNUSED_PAD src0_sel:WORD_1
	v_cvt_f32_f16_e32 v28, v28
	v_cvt_f32_f16_e32 v129, v29
	v_cvt_f32_f16_sdwa v130, v30 dst_sel:DWORD dst_unused:UNUSED_PAD src0_sel:WORD_1
	v_cvt_f32_f16_e32 v133, v30
	ds_read_b128 v[36:39], v43 offset:14848
	ds_read_b128 v[116:119], v43 offset:14864
	ds_read_b128 v[120:123], v43 offset:18944
	ds_read_b128 v[124:127], v43 offset:18960
	v_cvt_f32_f16_sdwa v115, v29 dst_sel:DWORD dst_unused:UNUSED_PAD src0_sel:WORD_1
	v_cvt_f32_f16_sdwa v131, v31 dst_sel:DWORD dst_unused:UNUSED_PAD src0_sel:WORD_1
	v_cvt_f32_f16_e32 v132, v31
	v_sub_f32_e32 v28, v28, v0
	v_sub_f32_e32 v29, v128, v1
	v_sub_f32_e32 v30, v129, v2
	v_pk_mul_f32 v[28:29], v[88:89], v[28:29]
	v_sub_f32_e32 v128, v133, v0
	v_sub_f32_e32 v129, v130, v1
	v_sub_f32_e32 v31, v115, v3
	v_sub_f32_e32 v130, v132, v2
	v_sub_f32_e32 v131, v131, v3
	v_pk_mul_f32 v[128:129], v[88:89], v[128:129]
	s_waitcnt lgkmcnt(1)
	v_fma_f32 v28, v36, v28, v120
	v_fma_f32 v29, v37, v29, v121
	v_pk_mul_f32 v[30:31], v[90:91], v[30:31]
	v_pk_mul_f32 v[130:131], v[90:91], v[130:131]
	s_waitcnt lgkmcnt(0)
	v_fma_f32 v36, v116, v128, v124
	ds_write2_b32 v220, v28, v29 offset1:65
	v_fma_f32 v28, v117, v129, v125
	ds_write2_b32 v221, v36, v28 offset1:65
	v_fma_f32 v28, v38, v30, v122
	v_fma_f32 v29, v118, v130, v126
	v_fmac_f32_e32 v123, v39, v31
	v_fmac_f32_e32 v127, v119, v131
	ds_write2_b32 v220, v28, v123 offset0:130 offset1:195
	ds_write2_b32 v221, v29, v127 offset0:130 offset1:195
	s_waitcnt vmcnt(2)
	ds_write_b128 v96, v[24:27] offset:41984
	s_mov_b32 s16, 0
	v_mov_b32_e32 v24, v103
	s_waitcnt lgkmcnt(0)
	s_barrier
	ds_read_b32 v200, v218
	ds_read_b32 v208, v219
	ds_read_b32 v201, v218 offset:520
	ds_read_b32 v209, v219 offset:256
	ds_read_b32 v202, v218 offset:1040
	ds_read_b32 v210, v219 offset:512
	ds_read_b32 v203, v218 offset:1560
	ds_read_b32 v211, v219 offset:768
	ds_read_b32 v204, v218 offset:2080
	ds_read_b32 v212, v219 offset:1024
	ds_read_b32 v205, v218 offset:2600
	ds_read_b32 v213, v219 offset:1280
	ds_read_b32 v206, v218 offset:3120
	ds_read_b32 v214, v219 offset:1536
	s_waitcnt lgkmcnt(12)
	v_mfma_f32_32x32x2_f32 v[4:19], v200, v208, v[4:19]
	ds_read_b32 v207, v218 offset:3640
	ds_read_b32 v215, v219 offset:1792
	s_waitcnt lgkmcnt(12)
	v_mfma_f32_32x32x2_f32 v[4:19], v201, v209, v[4:19]
	s_waitcnt lgkmcnt(10)
	v_mfma_f32_32x32x2_f32 v[4:19], v202, v210, v[4:19]
	s_waitcnt lgkmcnt(8)
	v_mfma_f32_32x32x2_f32 v[4:19], v203, v211, v[4:19]
	s_waitcnt lgkmcnt(6)
	v_mfma_f32_32x32x2_f32 v[4:19], v204, v212, v[4:19]
	s_waitcnt lgkmcnt(4)
	v_mfma_f32_32x32x2_f32 v[4:19], v205, v213, v[4:19]
	s_waitcnt lgkmcnt(2)
	v_mfma_f32_32x32x2_f32 v[4:19], v206, v214, v[4:19]
	s_waitcnt lgkmcnt(0)
	v_mfma_f32_32x32x2_f32 v[4:19], v207, v215, v[4:19]
	s_barrier
	global_load_dwordx4 v[28:31], v[92:93], off offset:1536 sc1
	global_load_dwordx4 v[24:27], v[74:75], off
	s_waitcnt vmcnt(3)
	v_cvt_f32_f16_sdwa v128, v32 dst_sel:DWORD dst_unused:UNUSED_PAD src0_sel:WORD_1
	v_cvt_f32_f16_e32 v32, v32
	v_cvt_f32_f16_e32 v129, v33
	v_cvt_f32_f16_sdwa v130, v34 dst_sel:DWORD dst_unused:UNUSED_PAD src0_sel:WORD_1
	v_cvt_f32_f16_e32 v133, v34
	ds_read_b128 v[36:39], v43 offset:15104
	ds_read_b128 v[116:119], v43 offset:15120
	ds_read_b128 v[120:123], v43 offset:19200
	ds_read_b128 v[124:127], v43 offset:19216
	v_cvt_f32_f16_sdwa v115, v33 dst_sel:DWORD dst_unused:UNUSED_PAD src0_sel:WORD_1
	v_cvt_f32_f16_sdwa v131, v35 dst_sel:DWORD dst_unused:UNUSED_PAD src0_sel:WORD_1
	v_cvt_f32_f16_e32 v132, v35
	v_sub_f32_e32 v32, v32, v0
	v_sub_f32_e32 v33, v128, v1
	v_sub_f32_e32 v34, v129, v2
	v_pk_mul_f32 v[32:33], v[88:89], v[32:33]
	v_sub_f32_e32 v128, v133, v0
	v_sub_f32_e32 v129, v130, v1
	v_sub_f32_e32 v35, v115, v3
	v_sub_f32_e32 v130, v132, v2
	v_sub_f32_e32 v131, v131, v3
	v_pk_mul_f32 v[128:129], v[88:89], v[128:129]
	s_waitcnt lgkmcnt(1)
	v_fma_f32 v32, v36, v32, v120
	v_fma_f32 v33, v37, v33, v121
	v_pk_mul_f32 v[34:35], v[90:91], v[34:35]
	v_pk_mul_f32 v[130:131], v[90:91], v[130:131]
	s_waitcnt lgkmcnt(0)
	v_fma_f32 v36, v116, v128, v124
	ds_write2_b32 v220, v32, v33 offset1:65
	v_fma_f32 v32, v117, v129, v125
	ds_write2_b32 v221, v36, v32 offset1:65
	v_fma_f32 v32, v38, v34, v122
	v_fma_f32 v33, v118, v130, v126
	v_fmac_f32_e32 v123, v39, v35
	v_fmac_f32_e32 v127, v119, v131
	ds_write2_b32 v220, v32, v123 offset0:130 offset1:195
	ds_write2_b32 v221, v33, v127 offset0:130 offset1:195
	s_waitcnt vmcnt(2)
	ds_write_b128 v96, v[20:23] offset:41984
	s_mov_b32 s16, 0
	v_mov_b32_e32 v20, v103
	s_waitcnt lgkmcnt(0)
	s_barrier
	ds_read_b32 v200, v218
	ds_read_b32 v208, v219
	ds_read_b32 v201, v218 offset:520
	ds_read_b32 v209, v219 offset:256
	ds_read_b32 v202, v218 offset:1040
	ds_read_b32 v210, v219 offset:512
	ds_read_b32 v203, v218 offset:1560
	ds_read_b32 v211, v219 offset:768
	ds_read_b32 v204, v218 offset:2080
	ds_read_b32 v212, v219 offset:1024
	ds_read_b32 v205, v218 offset:2600
	ds_read_b32 v213, v219 offset:1280
	ds_read_b32 v206, v218 offset:3120
	ds_read_b32 v214, v219 offset:1536
	s_waitcnt lgkmcnt(12)
	v_mfma_f32_32x32x2_f32 v[4:19], v200, v208, v[4:19]
	ds_read_b32 v207, v218 offset:3640
	ds_read_b32 v215, v219 offset:1792
	s_waitcnt lgkmcnt(12)
	v_mfma_f32_32x32x2_f32 v[4:19], v201, v209, v[4:19]
	s_waitcnt lgkmcnt(10)
	v_mfma_f32_32x32x2_f32 v[4:19], v202, v210, v[4:19]
	s_waitcnt lgkmcnt(8)
	v_mfma_f32_32x32x2_f32 v[4:19], v203, v211, v[4:19]
	s_waitcnt lgkmcnt(6)
	v_mfma_f32_32x32x2_f32 v[4:19], v204, v212, v[4:19]
	s_waitcnt lgkmcnt(4)
	v_mfma_f32_32x32x2_f32 v[4:19], v205, v213, v[4:19]
	s_waitcnt lgkmcnt(2)
	v_mfma_f32_32x32x2_f32 v[4:19], v206, v214, v[4:19]
	s_waitcnt lgkmcnt(0)
	v_mfma_f32_32x32x2_f32 v[4:19], v207, v215, v[4:19]
	s_barrier
	global_load_dwordx4 v[32:35], v[92:93], off offset:1664 sc1
	global_load_dwordx4 v[20:23], v[76:77], off
	s_waitcnt vmcnt(3)
	v_cvt_f32_f16_sdwa v128, v28 dst_sel:DWORD dst_unused:UNUSED_PAD src0_sel:WORD_1
	v_cvt_f32_f16_e32 v28, v28
	v_cvt_f32_f16_e32 v129, v29
	v_cvt_f32_f16_sdwa v130, v30 dst_sel:DWORD dst_unused:UNUSED_PAD src0_sel:WORD_1
	v_cvt_f32_f16_e32 v133, v30
	ds_read_b128 v[36:39], v43 offset:15360
	ds_read_b128 v[116:119], v43 offset:15376
	ds_read_b128 v[120:123], v43 offset:19456
	ds_read_b128 v[124:127], v43 offset:19472
	v_cvt_f32_f16_sdwa v115, v29 dst_sel:DWORD dst_unused:UNUSED_PAD src0_sel:WORD_1
	v_cvt_f32_f16_sdwa v131, v31 dst_sel:DWORD dst_unused:UNUSED_PAD src0_sel:WORD_1
	v_cvt_f32_f16_e32 v132, v31
	v_sub_f32_e32 v28, v28, v0
	v_sub_f32_e32 v29, v128, v1
	v_sub_f32_e32 v30, v129, v2
	v_pk_mul_f32 v[28:29], v[88:89], v[28:29]
	v_sub_f32_e32 v128, v133, v0
	v_sub_f32_e32 v129, v130, v1
	v_sub_f32_e32 v31, v115, v3
	v_sub_f32_e32 v130, v132, v2
	v_sub_f32_e32 v131, v131, v3
	v_pk_mul_f32 v[128:129], v[88:89], v[128:129]
	s_waitcnt lgkmcnt(1)
	v_fma_f32 v28, v36, v28, v120
	v_fma_f32 v29, v37, v29, v121
	v_pk_mul_f32 v[30:31], v[90:91], v[30:31]
	v_pk_mul_f32 v[130:131], v[90:91], v[130:131]
	s_waitcnt lgkmcnt(0)
	v_fma_f32 v36, v116, v128, v124
	ds_write2_b32 v220, v28, v29 offset1:65
	v_fma_f32 v28, v117, v129, v125
	ds_write2_b32 v221, v36, v28 offset1:65
	v_fma_f32 v28, v38, v30, v122
	v_fma_f32 v29, v118, v130, v126
	v_fmac_f32_e32 v123, v39, v31
	v_fmac_f32_e32 v127, v119, v131
	ds_write2_b32 v220, v28, v123 offset0:130 offset1:195
	ds_write2_b32 v221, v29, v127 offset0:130 offset1:195
	s_waitcnt vmcnt(2)
	ds_write_b128 v96, v[24:27] offset:41984
	s_mov_b32 s16, 0
	v_mov_b32_e32 v24, v103
	s_waitcnt lgkmcnt(0)
	s_barrier
	ds_read_b32 v200, v218
	ds_read_b32 v208, v219
	ds_read_b32 v201, v218 offset:520
	ds_read_b32 v209, v219 offset:256
	ds_read_b32 v202, v218 offset:1040
	ds_read_b32 v210, v219 offset:512
	ds_read_b32 v203, v218 offset:1560
	ds_read_b32 v211, v219 offset:768
	ds_read_b32 v204, v218 offset:2080
	ds_read_b32 v212, v219 offset:1024
	ds_read_b32 v205, v218 offset:2600
	ds_read_b32 v213, v219 offset:1280
	ds_read_b32 v206, v218 offset:3120
	ds_read_b32 v214, v219 offset:1536
	s_waitcnt lgkmcnt(12)
	v_mfma_f32_32x32x2_f32 v[4:19], v200, v208, v[4:19]
	ds_read_b32 v207, v218 offset:3640
	ds_read_b32 v215, v219 offset:1792
	s_waitcnt lgkmcnt(12)
	v_mfma_f32_32x32x2_f32 v[4:19], v201, v209, v[4:19]
	s_waitcnt lgkmcnt(10)
	v_mfma_f32_32x32x2_f32 v[4:19], v202, v210, v[4:19]
	s_waitcnt lgkmcnt(8)
	v_mfma_f32_32x32x2_f32 v[4:19], v203, v211, v[4:19]
	s_waitcnt lgkmcnt(6)
	v_mfma_f32_32x32x2_f32 v[4:19], v204, v212, v[4:19]
	s_waitcnt lgkmcnt(4)
	v_mfma_f32_32x32x2_f32 v[4:19], v205, v213, v[4:19]
	s_waitcnt lgkmcnt(2)
	v_mfma_f32_32x32x2_f32 v[4:19], v206, v214, v[4:19]
	s_waitcnt lgkmcnt(0)
	v_mfma_f32_32x32x2_f32 v[4:19], v207, v215, v[4:19]
	s_barrier
	global_load_dwordx4 v[28:31], v[92:93], off offset:1792 sc1
	global_load_dwordx4 v[24:27], v[78:79], off
	s_waitcnt vmcnt(3)
	v_cvt_f32_f16_sdwa v128, v32 dst_sel:DWORD dst_unused:UNUSED_PAD src0_sel:WORD_1
	v_cvt_f32_f16_e32 v32, v32
	v_cvt_f32_f16_e32 v129, v33
	v_cvt_f32_f16_sdwa v130, v34 dst_sel:DWORD dst_unused:UNUSED_PAD src0_sel:WORD_1
	v_cvt_f32_f16_e32 v133, v34
	ds_read_b128 v[36:39], v43 offset:15616
	ds_read_b128 v[116:119], v43 offset:15632
	ds_read_b128 v[120:123], v43 offset:19712
	ds_read_b128 v[124:127], v43 offset:19728
	v_cvt_f32_f16_sdwa v115, v33 dst_sel:DWORD dst_unused:UNUSED_PAD src0_sel:WORD_1
	v_cvt_f32_f16_sdwa v131, v35 dst_sel:DWORD dst_unused:UNUSED_PAD src0_sel:WORD_1
	v_cvt_f32_f16_e32 v132, v35
	v_sub_f32_e32 v32, v32, v0
	v_sub_f32_e32 v33, v128, v1
	v_sub_f32_e32 v34, v129, v2
	v_pk_mul_f32 v[32:33], v[88:89], v[32:33]
	v_sub_f32_e32 v128, v133, v0
	v_sub_f32_e32 v129, v130, v1
	v_sub_f32_e32 v35, v115, v3
	v_sub_f32_e32 v130, v132, v2
	v_sub_f32_e32 v131, v131, v3
	v_pk_mul_f32 v[128:129], v[88:89], v[128:129]
	s_waitcnt lgkmcnt(1)
	v_fma_f32 v32, v36, v32, v120
	v_fma_f32 v33, v37, v33, v121
	v_pk_mul_f32 v[34:35], v[90:91], v[34:35]
	v_pk_mul_f32 v[130:131], v[90:91], v[130:131]
	s_waitcnt lgkmcnt(0)
	v_fma_f32 v36, v116, v128, v124
	ds_write2_b32 v220, v32, v33 offset1:65
	v_fma_f32 v32, v117, v129, v125
	ds_write2_b32 v221, v36, v32 offset1:65
	v_fma_f32 v32, v38, v34, v122
	v_fma_f32 v33, v118, v130, v126
	v_fmac_f32_e32 v123, v39, v35
	v_fmac_f32_e32 v127, v119, v131
	ds_write2_b32 v220, v32, v123 offset0:130 offset1:195
	ds_write2_b32 v221, v33, v127 offset0:130 offset1:195
	s_waitcnt vmcnt(2)
	ds_write_b128 v96, v[20:23] offset:41984
	s_mov_b32 s16, 0
	v_mov_b32_e32 v20, v103
	s_waitcnt lgkmcnt(0)
	s_barrier
	ds_read_b32 v200, v218
	ds_read_b32 v208, v219
	ds_read_b32 v201, v218 offset:520
	ds_read_b32 v209, v219 offset:256
	ds_read_b32 v202, v218 offset:1040
	ds_read_b32 v210, v219 offset:512
	ds_read_b32 v203, v218 offset:1560
	ds_read_b32 v211, v219 offset:768
	ds_read_b32 v204, v218 offset:2080
	ds_read_b32 v212, v219 offset:1024
	ds_read_b32 v205, v218 offset:2600
	ds_read_b32 v213, v219 offset:1280
	ds_read_b32 v206, v218 offset:3120
	ds_read_b32 v214, v219 offset:1536
	s_waitcnt lgkmcnt(12)
	v_mfma_f32_32x32x2_f32 v[4:19], v200, v208, v[4:19]
	ds_read_b32 v207, v218 offset:3640
	ds_read_b32 v215, v219 offset:1792
	s_waitcnt lgkmcnt(12)
	v_mfma_f32_32x32x2_f32 v[4:19], v201, v209, v[4:19]
	s_waitcnt lgkmcnt(10)
	v_mfma_f32_32x32x2_f32 v[4:19], v202, v210, v[4:19]
	s_waitcnt lgkmcnt(8)
	v_mfma_f32_32x32x2_f32 v[4:19], v203, v211, v[4:19]
	s_waitcnt lgkmcnt(6)
	v_mfma_f32_32x32x2_f32 v[4:19], v204, v212, v[4:19]
	s_waitcnt lgkmcnt(4)
	v_mfma_f32_32x32x2_f32 v[4:19], v205, v213, v[4:19]
	s_waitcnt lgkmcnt(2)
	v_mfma_f32_32x32x2_f32 v[4:19], v206, v214, v[4:19]
	s_waitcnt lgkmcnt(0)
	v_mfma_f32_32x32x2_f32 v[4:19], v207, v215, v[4:19]
	s_barrier
	global_load_dwordx4 v[32:35], v[92:93], off offset:1920 sc1
	global_load_dwordx4 v[20:23], v[80:81], off
	s_waitcnt vmcnt(3)
	v_cvt_f32_f16_sdwa v93, v28 dst_sel:DWORD dst_unused:UNUSED_PAD src0_sel:WORD_1
	v_cvt_f32_f16_e32 v28, v28
	v_cvt_f32_f16_sdwa v92, v29 dst_sel:DWORD dst_unused:UNUSED_PAD src0_sel:WORD_1
	v_cvt_f32_f16_sdwa v128, v30 dst_sel:DWORD dst_unused:UNUSED_PAD src0_sel:WORD_1
	v_cvt_f32_f16_e32 v131, v30
	ds_read_b128 v[36:39], v43 offset:15872
	ds_read_b128 v[116:119], v43 offset:15888
	ds_read_b128 v[120:123], v43 offset:19968
	ds_read_b128 v[124:127], v43 offset:19984
	v_cvt_f32_f16_e32 v115, v29
	v_cvt_f32_f16_sdwa v129, v31 dst_sel:DWORD dst_unused:UNUSED_PAD src0_sel:WORD_1
	v_cvt_f32_f16_e32 v130, v31
	v_sub_f32_e32 v28, v28, v0
	v_sub_f32_e32 v29, v93, v1
	v_sub_f32_e32 v31, v92, v3
	v_pk_mul_f32 v[28:29], v[88:89], v[28:29]
	v_sub_f32_e32 v92, v131, v0
	v_sub_f32_e32 v93, v128, v1
	v_sub_f32_e32 v30, v115, v2
	v_sub_f32_e32 v128, v130, v2
	v_sub_f32_e32 v129, v129, v3
	v_pk_mul_f32 v[92:93], v[88:89], v[92:93]
	s_waitcnt lgkmcnt(1)
	v_fma_f32 v28, v36, v28, v120
	v_fma_f32 v29, v37, v29, v121
	v_pk_mul_f32 v[30:31], v[90:91], v[30:31]
	v_pk_mul_f32 v[128:129], v[90:91], v[128:129]
	s_waitcnt lgkmcnt(0)
	v_fma_f32 v36, v116, v92, v124
	ds_write2_b32 v220, v28, v29 offset1:65
	v_fma_f32 v28, v117, v93, v125
	ds_write2_b32 v221, v36, v28 offset1:65
	v_fma_f32 v28, v38, v30, v122
	v_fma_f32 v29, v118, v128, v126
	v_fmac_f32_e32 v123, v39, v31
	v_fmac_f32_e32 v127, v119, v129
	ds_write2_b32 v220, v28, v123 offset0:130 offset1:195
	ds_write2_b32 v221, v29, v127 offset0:130 offset1:195
	s_waitcnt vmcnt(2)
	ds_write_b128 v96, v[24:27] offset:41984
	s_mov_b32 s16, 0
	v_mov_b32_e32 v24, v103
	s_waitcnt lgkmcnt(0)
	s_barrier
	ds_read_b32 v200, v218
	ds_read_b32 v208, v219
	ds_read_b32 v201, v218 offset:520
	ds_read_b32 v209, v219 offset:256
	ds_read_b32 v202, v218 offset:1040
	ds_read_b32 v210, v219 offset:512
	ds_read_b32 v203, v218 offset:1560
	ds_read_b32 v211, v219 offset:768
	ds_read_b32 v204, v218 offset:2080
	ds_read_b32 v212, v219 offset:1024
	ds_read_b32 v205, v218 offset:2600
	ds_read_b32 v213, v219 offset:1280
	ds_read_b32 v206, v218 offset:3120
	ds_read_b32 v214, v219 offset:1536
	s_waitcnt lgkmcnt(12)
	v_mfma_f32_32x32x2_f32 v[4:19], v200, v208, v[4:19]
	ds_read_b32 v207, v218 offset:3640
	ds_read_b32 v215, v219 offset:1792
	s_waitcnt lgkmcnt(12)
	v_mfma_f32_32x32x2_f32 v[4:19], v201, v209, v[4:19]
	s_waitcnt lgkmcnt(10)
	v_mfma_f32_32x32x2_f32 v[4:19], v202, v210, v[4:19]
	s_waitcnt lgkmcnt(8)
	v_mfma_f32_32x32x2_f32 v[4:19], v203, v211, v[4:19]
	s_waitcnt lgkmcnt(6)
	v_mfma_f32_32x32x2_f32 v[4:19], v204, v212, v[4:19]
	s_waitcnt lgkmcnt(4)
	v_mfma_f32_32x32x2_f32 v[4:19], v205, v213, v[4:19]
	s_waitcnt lgkmcnt(2)
	v_mfma_f32_32x32x2_f32 v[4:19], v206, v214, v[4:19]
	s_waitcnt lgkmcnt(0)
	v_mfma_f32_32x32x2_f32 v[4:19], v207, v215, v[4:19]
	s_waitcnt vmcnt(1)
	v_cvt_f32_f16_sdwa v93, v32 dst_sel:DWORD dst_unused:UNUSED_PAD src0_sel:WORD_1
	v_cvt_f32_f16_e32 v32, v32
	v_cvt_f32_f16_sdwa v121, v34 dst_sel:DWORD dst_unused:UNUSED_PAD src0_sel:WORD_1
	v_cvt_f32_f16_e32 v123, v34
	s_barrier
	ds_read_b128 v[24:27], v43 offset:16128
	ds_read_b128 v[28:31], v43 offset:16144
	ds_read_b128 v[36:39], v43 offset:20224
	ds_read_b128 v[116:119], v43 offset:20240
	v_cvt_f32_f16_sdwa v92, v33 dst_sel:DWORD dst_unused:UNUSED_PAD src0_sel:WORD_1
	v_cvt_f32_f16_e32 v115, v33
	v_cvt_f32_f16_sdwa v120, v35 dst_sel:DWORD dst_unused:UNUSED_PAD src0_sel:WORD_1
	v_cvt_f32_f16_e32 v122, v35
	v_sub_f32_e32 v32, v32, v0
	v_sub_f32_e32 v33, v93, v1
	v_sub_f32_e32 v0, v123, v0
	v_sub_f32_e32 v1, v121, v1
	v_sub_f32_e32 v34, v115, v2
	v_sub_f32_e32 v35, v92, v3
	v_pk_mul_f32 v[0:1], v[88:89], v[0:1]
	v_pk_mul_f32 v[34:35], v[90:91], v[34:35]
	v_sub_f32_e32 v2, v122, v2
	v_sub_f32_e32 v3, v120, v3
	s_waitcnt lgkmcnt(0)
	v_fma_f32 v0, v28, v0, v116
	v_fma_f32 v1, v29, v1, v117
	v_pk_mul_f32 v[32:33], v[88:89], v[32:33]
	v_pk_mul_f32 v[2:3], v[90:91], v[2:3]
	ds_write2_b32 v221, v0, v1 offset1:65
	v_fma_f32 v0, v26, v34, v38
	v_fmac_f32_e32 v39, v27, v35
	v_fma_f32 v24, v24, v32, v36
	v_fma_f32 v25, v25, v33, v37
	v_fma_f32 v1, v30, v2, v118
	ds_write2_b32 v220, v0, v39 offset0:130 offset1:195
	v_fmac_f32_e32 v119, v31, v3
	s_mov_b32 s16, 0
	v_mov_b32_e32 v0, v103
	ds_write2_b32 v220, v24, v25 offset1:65
	ds_write2_b32 v221, v1, v119 offset0:130 offset1:195
	s_waitcnt vmcnt(0)
	ds_write_b128 v96, v[20:23] offset:41984
	s_waitcnt lgkmcnt(0)
	s_barrier
	ds_read_b32 v200, v218
	ds_read_b32 v208, v219
	ds_read_b32 v201, v218 offset:520
	ds_read_b32 v209, v219 offset:256
	ds_read_b32 v202, v218 offset:1040
	ds_read_b32 v210, v219 offset:512
	ds_read_b32 v203, v218 offset:1560
	ds_read_b32 v211, v219 offset:768
	ds_read_b32 v204, v218 offset:2080
	ds_read_b32 v212, v219 offset:1024
	ds_read_b32 v205, v218 offset:2600
	ds_read_b32 v213, v219 offset:1280
	ds_read_b32 v206, v218 offset:3120
	ds_read_b32 v214, v219 offset:1536
	s_waitcnt lgkmcnt(12)
	v_mfma_f32_32x32x2_f32 v[4:19], v200, v208, v[4:19]
	ds_read_b32 v207, v218 offset:3640
	ds_read_b32 v215, v219 offset:1792
	s_waitcnt lgkmcnt(12)
	v_mfma_f32_32x32x2_f32 v[4:19], v201, v209, v[4:19]
	s_waitcnt lgkmcnt(10)
	v_mfma_f32_32x32x2_f32 v[4:19], v202, v210, v[4:19]
	s_waitcnt lgkmcnt(8)
	v_mfma_f32_32x32x2_f32 v[4:19], v203, v211, v[4:19]
	s_waitcnt lgkmcnt(6)
	v_mfma_f32_32x32x2_f32 v[4:19], v204, v212, v[4:19]
	s_waitcnt lgkmcnt(4)
	v_mfma_f32_32x32x2_f32 v[4:19], v205, v213, v[4:19]
	s_waitcnt lgkmcnt(2)
	v_mfma_f32_32x32x2_f32 v[4:19], v206, v214, v[4:19]
	s_waitcnt lgkmcnt(0)
	v_mfma_f32_32x32x2_f32 v[4:19], v207, v215, v[4:19]
	s_barrier
	s_nop 15
	s_nop 3
	ds_write_b32 v217, v4 offset:58752
	ds_write_b32 v217, v5 offset:58880
	ds_write_b32 v217, v6 offset:59008
	ds_write_b32 v217, v7 offset:59136
	ds_write_b32 v217, v8 offset:59776
	ds_write_b32 v217, v9 offset:59904
	ds_write_b32 v217, v10 offset:60032
	ds_write_b32 v217, v11 offset:60160
	ds_write_b32 v217, v12 offset:60800
	ds_write_b32 v217, v13 offset:60928
	ds_write_b32 v217, v14 offset:61056
	ds_write_b32 v217, v15 offset:61184
	ds_write_b32 v217, v16 offset:61824
	ds_write_b32 v217, v17 offset:61952
	ds_write_b32 v217, v18 offset:62080
	ds_write_b32 v217, v19 offset:62208
	s_waitcnt lgkmcnt(0)
	s_barrier
	global_load_dwordx4 v[0:3], v[50:51], off offset:256
	ds_read_b128 v[4:7], v98 offset:58752
	ds_read_b128 v[8:11], v99 offset:8192
	ds_read_b128 v[12:15], v99 offset:16384
	ds_read_b128 v[16:19], v99 offset:24576
	v_add_u32_e32 v20, 0xc400, v100
	v_add_u32_e32 v21, 0xc408, v100
	s_waitcnt lgkmcnt(2)
	v_pk_add_f32 v[4:5], v[4:5], v[8:9]
	v_pk_add_f32 v[6:7], v[6:7], v[10:11]
	s_waitcnt lgkmcnt(1)
	v_pk_add_f32 v[4:5], v[12:13], v[4:5]
	v_pk_add_f32 v[6:7], v[14:15], v[6:7]
	s_waitcnt lgkmcnt(0)
	v_pk_add_f32 v[4:5], v[16:17], v[4:5]
	v_pk_add_f32 v[6:7], v[18:19], v[6:7]
	s_waitcnt vmcnt(0)
	v_pk_add_f32 v[0:1], v[0:1], v[4:5]
	v_pk_add_f32 v[2:3], v[6:7], v[2:3]
	ds_write2_b32 v20, v0, v1 offset1:1
	ds_write2_b32 v21, v2, v3 offset1:1
	s_waitcnt lgkmcnt(0)
	s_barrier
	s_and_saveexec_b64 s[36:37], s[6:7]
	s_cbranch_execz .LBB0_2418
	v_add_u32_e32 v0, 0xc400, v108
	v_add_u32_e32 v1, 0xc408, v108
	v_add_u32_e32 v2, 0xc410, v108
	v_add_u32_e32 v3, 0xc418, v108
	ds_read2_b32 v[34:35], v0 offset1:1
	ds_read2_b32 v[30:31], v1 offset1:1
	ds_read2_b32 v[22:23], v2 offset1:1
	ds_read2_b32 v[10:11], v3 offset1:1
	s_mov_b32 s16, 0xff61b1e6
	s_waitcnt lgkmcnt(3)
	v_max_f32_e32 v0, v34, v34
	v_max_f32_e32 v0, 0xff61b1e6, v0
	v_cmp_lt_f32_e32 vcc, s16, v34
	v_cmp_gt_f32_e64 s[16:17], v35, v0
	v_add_u32_e32 v2, 0xc420, v108
	ds_read2_b32 v[24:25], v2 offset1:1
	v_cndmask_b32_e64 v0, v0, v35, s[16:17]
	v_cndmask_b32_e64 v1, 0, 1, s[16:17]
	s_waitcnt lgkmcnt(3)
	v_cmp_gt_f32_e64 s[16:17], v30, v0
	v_add_u32_e32 v2, 0xc428, v108
	v_add_u32_e32 v3, 0xc430, v108
	v_cndmask_b32_e64 v0, v0, v30, s[16:17]
	v_cndmask_b32_e64 v1, v1, 2, s[16:17]
	v_cmp_gt_f32_e64 s[16:17], v31, v0
	v_add_u32_e32 v4, 0xc438, v108
	ds_read2_b32 v[32:33], v2 offset1:1
	ds_read2_b32 v[20:21], v3 offset1:1
	ds_read2_b32 v[6:7], v4 offset1:1
	v_cndmask_b32_e64 v0, v0, v31, s[16:17]
	v_cndmask_b32_e64 v1, v1, 3, s[16:17]
	s_waitcnt lgkmcnt(5)
	v_cmp_gt_f32_e64 s[16:17], v22, v0
	v_add_u32_e32 v2, 0xc440, v108
	ds_read2_b32 v[18:19], v2 offset1:1
	v_cndmask_b32_e64 v0, v0, v22, s[16:17]
	v_cndmask_b32_e64 v1, v1, 4, s[16:17]
	v_cmp_gt_f32_e64 s[16:17], v23, v0
	v_add_u32_e32 v2, 0xc448, v108
	v_add_u32_e32 v4, 0xc458, v108
	v_cndmask_b32_e64 v0, v0, v23, s[16:17]
	v_cndmask_b32_e64 v1, v1, 5, s[16:17]
	s_waitcnt lgkmcnt(5)
	v_cmp_gt_f32_e64 s[16:17], v10, v0
	v_add_u32_e32 v3, 0xc450, v108
	ds_read2_b32 v[28:29], v2 offset1:1
	ds_read2_b32 v[12:13], v3 offset1:1
	ds_read2_b32 v[4:5], v4 offset1:1
	v_cndmask_b32_e64 v0, v0, v10, s[16:17]
	v_cndmask_b32_e64 v1, v1, 6, s[16:17]
	v_cmp_gt_f32_e64 s[16:17], v11, v0
	v_add_u32_e32 v2, 0xc460, v108
	ds_read2_b32 v[14:15], v2 offset1:1
	v_cndmask_b32_e64 v0, v0, v11, s[16:17]
	v_cndmask_b32_e64 v1, v1, 7, s[16:17]
	s_waitcnt lgkmcnt(8)
	v_cmp_gt_f32_e64 s[16:17], v24, v0
	v_add_u32_e32 v2, 0xc468, v108
	v_add_u32_e32 v8, 0xc478, v108
	v_cndmask_b32_e64 v0, v0, v24, s[16:17]
	v_cndmask_b32_e64 v1, v1, 8, s[16:17]
	v_cmp_gt_f32_e64 s[16:17], v25, v0
	v_add_u32_e32 v3, 0xc470, v108
	ds_read2_b32 v[26:27], v2 offset1:1
	ds_read2_b32 v[16:17], v3 offset1:1
	ds_read2_b32 v[8:9], v8 offset1:1
	v_cndmask_b32_e64 v0, v0, v25, s[16:17]
	v_cndmask_b32_e64 v1, v1, 9, s[16:17]
	s_waitcnt lgkmcnt(10)
	v_cmp_gt_f32_e64 s[16:17], v32, v0
	s_nop 1
	v_cndmask_b32_e64 v0, v0, v32, s[16:17]
	v_cndmask_b32_e64 v1, v1, 10, s[16:17]
	v_cmp_gt_f32_e64 s[16:17], v33, v0
	s_nop 1
	v_cndmask_b32_e64 v0, v0, v33, s[16:17]
	v_cndmask_b32_e64 v1, v1, 11, s[16:17]
	s_waitcnt lgkmcnt(9)
	v_cmp_gt_f32_e64 s[16:17], v20, v0
	s_nop 1
	v_cndmask_b32_e64 v0, v0, v20, s[16:17]
	v_cndmask_b32_e64 v1, v1, 12, s[16:17]
	v_cmp_gt_f32_e64 s[16:17], v21, v0
	s_nop 1
	v_cndmask_b32_e64 v0, v0, v21, s[16:17]
	v_cndmask_b32_e64 v1, v1, 13, s[16:17]
	s_waitcnt lgkmcnt(8)
	v_cmp_gt_f32_e64 s[16:17], v6, v0
	s_nop 1
	v_cndmask_b32_e64 v0, v0, v6, s[16:17]
	v_cndmask_b32_e64 v1, v1, 14, s[16:17]
	v_cmp_gt_f32_e64 s[16:17], v7, v0
	s_nop 1
	v_cndmask_b32_e64 v0, v0, v7, s[16:17]
	v_cndmask_b32_e64 v1, v1, 15, s[16:17]
	s_waitcnt lgkmcnt(7)
	v_cmp_gt_f32_e64 s[16:17], v18, v0
	s_nop 1
	v_cndmask_b32_e64 v0, v0, v18, s[16:17]
	v_cndmask_b32_e64 v1, v1, 16, s[16:17]
	v_cmp_gt_f32_e64 s[16:17], v19, v0
	s_nop 1
	v_cndmask_b32_e64 v0, v0, v19, s[16:17]
	v_cndmask_b32_e64 v1, v1, 17, s[16:17]
	s_waitcnt lgkmcnt(6)
	v_cmp_gt_f32_e64 s[16:17], v28, v0
	s_nop 1
	v_cndmask_b32_e64 v0, v0, v28, s[16:17]
	v_cndmask_b32_e64 v1, v1, 18, s[16:17]
	v_cmp_gt_f32_e64 s[16:17], v29, v0
	s_nop 1
	v_cndmask_b32_e64 v0, v0, v29, s[16:17]
	v_cndmask_b32_e64 v1, v1, 19, s[16:17]
	s_waitcnt lgkmcnt(5)
	v_cmp_gt_f32_e64 s[16:17], v12, v0
	s_nop 1
	v_cndmask_b32_e64 v0, v0, v12, s[16:17]
	v_cndmask_b32_e64 v1, v1, 20, s[16:17]
	v_cmp_gt_f32_e64 s[16:17], v13, v0
	s_nop 1
	v_cndmask_b32_e64 v0, v0, v13, s[16:17]
	v_cndmask_b32_e64 v1, v1, 21, s[16:17]
	s_waitcnt lgkmcnt(4)
	v_cmp_gt_f32_e64 s[16:17], v4, v0
	s_nop 1
	v_cndmask_b32_e64 v0, v0, v4, s[16:17]
	v_cndmask_b32_e64 v1, v1, 22, s[16:17]
	v_cmp_gt_f32_e64 s[16:17], v5, v0
	s_nop 1
	v_cndmask_b32_e64 v0, v0, v5, s[16:17]
	v_cndmask_b32_e64 v1, v1, 23, s[16:17]
	s_waitcnt lgkmcnt(3)
	v_cmp_gt_f32_e64 s[16:17], v14, v0
	s_nop 1
	v_cndmask_b32_e64 v0, v0, v14, s[16:17]
	v_cndmask_b32_e64 v1, v1, 24, s[16:17]
	v_cmp_gt_f32_e64 s[16:17], v15, v0
	s_nop 1
	v_cndmask_b32_e64 v0, v0, v15, s[16:17]
	v_cndmask_b32_e64 v1, v1, 25, s[16:17]
	s_waitcnt lgkmcnt(2)
	v_cmp_gt_f32_e64 s[16:17], v26, v0
	s_nop 1
	v_cndmask_b32_e64 v0, v0, v26, s[16:17]
	v_cndmask_b32_e64 v1, v1, 26, s[16:17]
	v_cmp_gt_f32_e64 s[16:17], v27, v0
	s_nop 1
	v_cndmask_b32_e64 v0, v0, v27, s[16:17]
	v_cndmask_b32_e64 v1, v1, 27, s[16:17]
	s_waitcnt lgkmcnt(1)
	v_cmp_gt_f32_e64 s[16:17], v16, v0
	s_nop 1
	v_cndmask_b32_e64 v0, v0, v16, s[16:17]
	v_cndmask_b32_e64 v1, v1, 28, s[16:17]
	v_cmp_gt_f32_e64 s[16:17], v17, v0
	s_nop 1
	v_cndmask_b32_e64 v0, v0, v17, s[16:17]
	v_cndmask_b32_e64 v1, v1, 29, s[16:17]
	s_waitcnt lgkmcnt(0)
	v_cmp_gt_f32_e64 s[16:17], v8, v0
	s_nop 1
	v_cndmask_b32_e64 v0, v0, v8, s[16:17]
	v_cndmask_b32_e64 v1, v1, 30, s[16:17]
	v_cmp_gt_f32_e64 s[16:17], v9, v0
	s_nop 1
	v_cndmask_b32_e64 v36, v0, v9, s[16:17]
	v_cndmask_b32_e64 v0, v1, 31, s[16:17]
	v_cmp_ne_u32_e64 s[16:17], 0, v0
	v_lshlrev_b32_e64 v2, v0, 1
	s_and_b64 s[16:17], s[16:17], vcc
	v_cndmask_b32_e64 v1, v112, v34, s[16:17]
	v_and_b32_e32 v3, 2, v2
	v_cmp_eq_u32_e64 s[16:17], 0, v3
	v_cmp_gt_f32_e64 s[18:19], v35, v1
	s_and_b64 s[16:17], s[16:17], s[18:19]
	v_cndmask_b32_e64 v1, v1, v35, s[16:17]
	v_and_b32_e32 v37, 4, v2
	v_cndmask_b32_e64 v3, 0, 1, s[16:17]
	v_cmp_eq_u32_e64 s[16:17], 0, v37
	v_cmp_gt_f32_e64 s[18:19], v30, v1
	s_and_b64 s[16:17], s[16:17], s[18:19]
	v_cndmask_b32_e64 v1, v1, v30, s[16:17]
	v_and_b32_e32 v37, 8, v2
	v_cndmask_b32_e64 v3, v3, 2, s[16:17]
	v_cmp_eq_u32_e64 s[16:17], 0, v37
	v_cmp_gt_f32_e64 s[18:19], v31, v1
	s_and_b64 s[16:17], s[16:17], s[18:19]
	v_cndmask_b32_e64 v1, v1, v31, s[16:17]
	v_and_b32_e32 v37, 16, v2
	v_cndmask_b32_e64 v3, v3, 3, s[16:17]
	v_cmp_eq_u32_e64 s[16:17], 0, v37
	v_cmp_gt_f32_e64 s[18:19], v22, v1
	s_and_b64 s[16:17], s[16:17], s[18:19]
	v_cndmask_b32_e64 v1, v1, v22, s[16:17]
	v_and_b32_e32 v37, 32, v2
	v_cndmask_b32_e64 v3, v3, 4, s[16:17]
	v_cmp_eq_u32_e64 s[16:17], 0, v37
	v_cmp_gt_f32_e64 s[18:19], v23, v1
	s_and_b64 s[16:17], s[16:17], s[18:19]
	v_cndmask_b32_e64 v1, v1, v23, s[16:17]
	v_and_b32_e32 v37, 64, v2
	v_cndmask_b32_e64 v3, v3, 5, s[16:17]
	v_cmp_eq_u32_e64 s[16:17], 0, v37
	v_cmp_gt_f32_e64 s[18:19], v10, v1
	s_and_b64 s[16:17], s[16:17], s[18:19]
	v_cndmask_b32_e64 v1, v1, v10, s[16:17]
	v_and_b32_e32 v37, 0x80, v2
	v_cndmask_b32_e64 v3, v3, 6, s[16:17]
	v_cmp_eq_u32_e64 s[16:17], 0, v37
	v_cmp_gt_f32_e64 s[18:19], v11, v1
	s_and_b64 s[16:17], s[16:17], s[18:19]
	v_cndmask_b32_e64 v1, v1, v11, s[16:17]
	v_and_b32_e32 v37, 0x100, v2
	v_cndmask_b32_e64 v3, v3, 7, s[16:17]
	v_cmp_eq_u32_e64 s[16:17], 0, v37
	v_cmp_gt_f32_e64 s[18:19], v24, v1
	s_and_b64 s[16:17], s[16:17], s[18:19]
	v_cndmask_b32_e64 v1, v1, v24, s[16:17]
	v_and_b32_e32 v37, 0x200, v2
	v_cndmask_b32_e64 v3, v3, 8, s[16:17]
	v_cmp_eq_u32_e64 s[16:17], 0, v37
	v_cmp_gt_f32_e64 s[18:19], v25, v1
	s_and_b64 s[16:17], s[16:17], s[18:19]
	v_cndmask_b32_e64 v1, v1, v25, s[16:17]
	v_and_b32_e32 v37, 0x400, v2
	v_cndmask_b32_e64 v3, v3, 9, s[16:17]
	v_cmp_eq_u32_e64 s[16:17], 0, v37
	v_cmp_gt_f32_e64 s[18:19], v32, v1
	s_and_b64 s[16:17], s[16:17], s[18:19]
	v_cndmask_b32_e64 v1, v1, v32, s[16:17]
	v_and_b32_e32 v37, 0x800, v2
	v_cndmask_b32_e64 v3, v3, 10, s[16:17]
	v_cmp_eq_u32_e64 s[16:17], 0, v37
	v_cmp_gt_f32_e64 s[18:19], v33, v1
	s_and_b64 s[16:17], s[16:17], s[18:19]
	v_cndmask_b32_e64 v1, v1, v33, s[16:17]
	v_and_b32_e32 v37, 0x1000, v2
	v_cndmask_b32_e64 v3, v3, 11, s[16:17]
	v_cmp_eq_u32_e64 s[16:17], 0, v37
	v_cmp_gt_f32_e64 s[18:19], v20, v1
	s_and_b64 s[16:17], s[16:17], s[18:19]
	v_cndmask_b32_e64 v1, v1, v20, s[16:17]
	v_and_b32_e32 v37, 0x2000, v2
	v_cndmask_b32_e64 v3, v3, 12, s[16:17]
	v_cmp_eq_u32_e64 s[16:17], 0, v37
	v_cmp_gt_f32_e64 s[18:19], v21, v1
	s_and_b64 s[16:17], s[16:17], s[18:19]
	v_cndmask_b32_e64 v1, v1, v21, s[16:17]
	v_and_b32_e32 v37, 0x4000, v2
	v_cndmask_b32_e64 v3, v3, 13, s[16:17]
	v_cmp_eq_u32_e64 s[16:17], 0, v37
	v_cmp_gt_f32_e64 s[18:19], v6, v1
	s_and_b64 s[16:17], s[16:17], s[18:19]
	v_cndmask_b32_e64 v1, v1, v6, s[16:17]
	v_and_b32_e32 v37, 0x8000, v2
	v_cndmask_b32_e64 v3, v3, 14, s[16:17]
	v_cmp_eq_u32_e64 s[16:17], 0, v37
	v_cmp_gt_f32_e64 s[18:19], v7, v1
	s_and_b64 s[16:17], s[16:17], s[18:19]
	v_cndmask_b32_e64 v1, v1, v7, s[16:17]
	v_and_b32_e32 v37, 0x10000, v2
	v_cndmask_b32_e64 v3, v3, 15, s[16:17]
	v_cmp_eq_u32_e64 s[16:17], 0, v37
	v_cmp_gt_f32_e64 s[18:19], v18, v1
	s_and_b64 s[16:17], s[16:17], s[18:19]
	v_cndmask_b32_e64 v1, v1, v18, s[16:17]
	v_and_b32_e32 v37, 0x20000, v2
	v_cndmask_b32_e64 v3, v3, 16, s[16:17]
	v_cmp_eq_u32_e64 s[16:17], 0, v37
	v_cmp_gt_f32_e64 s[18:19], v19, v1
	s_and_b64 s[16:17], s[16:17], s[18:19]
	v_cndmask_b32_e64 v1, v1, v19, s[16:17]
	v_and_b32_e32 v37, 0x40000, v2
	v_cndmask_b32_e64 v3, v3, 17, s[16:17]
	v_cmp_eq_u32_e64 s[16:17], 0, v37
	v_cmp_gt_f32_e64 s[18:19], v28, v1
	s_and_b64 s[16:17], s[16:17], s[18:19]
	v_cndmask_b32_e64 v1, v1, v28, s[16:17]
	v_and_b32_e32 v37, 0x80000, v2
	v_cndmask_b32_e64 v3, v3, 18, s[16:17]
	v_cmp_eq_u32_e64 s[16:17], 0, v37
	v_cmp_gt_f32_e64 s[18:19], v29, v1
	s_and_b64 s[16:17], s[16:17], s[18:19]
	v_cndmask_b32_e64 v1, v1, v29, s[16:17]
	v_and_b32_e32 v37, 0x100000, v2
	v_cndmask_b32_e64 v3, v3, 19, s[16:17]
	v_cmp_eq_u32_e64 s[16:17], 0, v37
	v_cmp_gt_f32_e64 s[18:19], v12, v1
	s_and_b64 s[16:17], s[16:17], s[18:19]
	v_cndmask_b32_e64 v1, v1, v12, s[16:17]
	v_and_b32_e32 v37, 0x200000, v2
	v_cndmask_b32_e64 v3, v3, 20, s[16:17]
	v_cmp_eq_u32_e64 s[16:17], 0, v37
	v_cmp_gt_f32_e64 s[18:19], v13, v1
	s_and_b64 s[16:17], s[16:17], s[18:19]
	v_cndmask_b32_e64 v1, v1, v13, s[16:17]
	v_and_b32_e32 v37, 0x400000, v2
	v_cndmask_b32_e64 v3, v3, 21, s[16:17]
	v_cmp_eq_u32_e64 s[16:17], 0, v37
	v_cmp_gt_f32_e64 s[18:19], v4, v1
	s_and_b64 s[16:17], s[16:17], s[18:19]
	v_cndmask_b32_e64 v1, v1, v4, s[16:17]
	v_and_b32_e32 v37, 0x800000, v2
	v_cndmask_b32_e64 v3, v3, 22, s[16:17]
	v_cmp_eq_u32_e64 s[16:17], 0, v37
	v_cmp_gt_f32_e64 s[18:19], v5, v1
	s_and_b64 s[16:17], s[16:17], s[18:19]
	v_cndmask_b32_e64 v1, v1, v5, s[16:17]
	v_and_b32_e32 v37, 0x1000000, v2
	v_cndmask_b32_e64 v3, v3, 23, s[16:17]
	v_cmp_eq_u32_e64 s[16:17], 0, v37
	v_cmp_gt_f32_e64 s[18:19], v14, v1
	s_and_b64 s[16:17], s[16:17], s[18:19]
	v_cndmask_b32_e64 v1, v1, v14, s[16:17]
	v_and_b32_e32 v37, 0x2000000, v2
	v_cndmask_b32_e64 v3, v3, 24, s[16:17]
	v_cmp_eq_u32_e64 s[16:17], 0, v37
	v_cmp_gt_f32_e64 s[18:19], v15, v1
	s_and_b64 s[16:17], s[16:17], s[18:19]
	v_cndmask_b32_e64 v1, v1, v15, s[16:17]
	v_and_b32_e32 v37, 0x4000000, v2
	v_cndmask_b32_e64 v3, v3, 25, s[16:17]
	v_cmp_eq_u32_e64 s[16:17], 0, v37
	v_cmp_gt_f32_e64 s[18:19], v26, v1
	s_and_b64 s[16:17], s[16:17], s[18:19]
	v_cndmask_b32_e64 v1, v1, v26, s[16:17]
	v_and_b32_e32 v37, 0x8000000, v2
	v_cndmask_b32_e64 v3, v3, 26, s[16:17]
	v_cmp_eq_u32_e64 s[16:17], 0, v37
	v_cmp_gt_f32_e64 s[18:19], v27, v1
	s_and_b64 s[16:17], s[16:17], s[18:19]
	v_cndmask_b32_e64 v1, v1, v27, s[16:17]
	v_and_b32_e32 v37, 0x10000000, v2
	v_cndmask_b32_e64 v3, v3, 27, s[16:17]
	v_cmp_eq_u32_e64 s[16:17], 0, v37
	v_cmp_gt_f32_e64 s[18:19], v16, v1
	s_and_b64 s[16:17], s[16:17], s[18:19]
	v_cndmask_b32_e64 v1, v1, v16, s[16:17]
	v_and_b32_e32 v37, 0x20000000, v2
	v_cndmask_b32_e64 v3, v3, 28, s[16:17]
	v_cmp_eq_u32_e64 s[16:17], 0, v37
	v_cmp_gt_f32_e64 s[18:19], v17, v1
	s_and_b64 s[16:17], s[16:17], s[18:19]
	v_cndmask_b32_e64 v1, v1, v17, s[16:17]
	v_and_b32_e32 v37, 2.0, v2
	v_cndmask_b32_e64 v3, v3, 29, s[16:17]
	v_cmp_eq_u32_e64 s[16:17], 0, v37
	v_cmp_gt_f32_e64 s[18:19], v8, v1
	s_and_b64 s[16:17], s[16:17], s[18:19]
	v_cndmask_b32_e64 v1, v1, v8, s[16:17]
	v_cndmask_b32_e64 v3, v3, 30, s[16:17]
	v_cmp_ne_u32_e64 s[16:17], 31, v0
	v_cmp_gt_f32_e64 s[18:19], v9, v1
	s_and_b64 s[16:17], s[16:17], s[18:19]
	v_cndmask_b32_e64 v37, v1, v9, s[16:17]
	v_cndmask_b32_e64 v1, v3, 31, s[16:17]
	v_lshl_or_b32 v3, 1, v1, v2
	v_and_b32_e32 v2, 1, v3
	v_cmp_eq_u32_e64 s[16:17], 0, v2
	s_and_b64 s[16:17], s[16:17], vcc
	v_and_b32_e32 v38, 2, v3
	v_cndmask_b32_e64 v2, v112, v34, s[16:17]
	v_cmp_eq_u32_e64 s[16:17], 0, v38
	v_cmp_gt_f32_e64 s[18:19], v35, v2
	s_and_b64 s[16:17], s[16:17], s[18:19]
	v_cndmask_b32_e64 v2, v2, v35, s[16:17]
	v_and_b32_e32 v39, 4, v3
	v_cndmask_b32_e64 v38, 0, 1, s[16:17]
	v_cmp_eq_u32_e64 s[16:17], 0, v39
	v_cmp_gt_f32_e64 s[18:19], v30, v2
	s_and_b64 s[16:17], s[16:17], s[18:19]
	v_cndmask_b32_e64 v2, v2, v30, s[16:17]
	v_and_b32_e32 v39, 8, v3
	v_cndmask_b32_e64 v38, v38, 2, s[16:17]
	v_cmp_eq_u32_e64 s[16:17], 0, v39
	v_cmp_gt_f32_e64 s[18:19], v31, v2
	s_and_b64 s[16:17], s[16:17], s[18:19]
	v_cndmask_b32_e64 v2, v2, v31, s[16:17]
	v_and_b32_e32 v39, 16, v3
	v_cndmask_b32_e64 v38, v38, 3, s[16:17]
	v_cmp_eq_u32_e64 s[16:17], 0, v39
	v_cmp_gt_f32_e64 s[18:19], v22, v2
	s_and_b64 s[16:17], s[16:17], s[18:19]
	v_cndmask_b32_e64 v2, v2, v22, s[16:17]
	v_and_b32_e32 v39, 32, v3
	v_cndmask_b32_e64 v38, v38, 4, s[16:17]
	v_cmp_eq_u32_e64 s[16:17], 0, v39
	v_cmp_gt_f32_e64 s[18:19], v23, v2
	s_and_b64 s[16:17], s[16:17], s[18:19]
	v_cndmask_b32_e64 v2, v2, v23, s[16:17]
	v_and_b32_e32 v39, 64, v3
	v_cndmask_b32_e64 v38, v38, 5, s[16:17]
	v_cmp_eq_u32_e64 s[16:17], 0, v39
	v_cmp_gt_f32_e64 s[18:19], v10, v2
	s_and_b64 s[16:17], s[16:17], s[18:19]
	v_cndmask_b32_e64 v2, v2, v10, s[16:17]
	v_and_b32_e32 v39, 0x80, v3
	v_cndmask_b32_e64 v38, v38, 6, s[16:17]
	v_cmp_eq_u32_e64 s[16:17], 0, v39
	v_cmp_gt_f32_e64 s[18:19], v11, v2
	s_and_b64 s[16:17], s[16:17], s[18:19]
	v_cndmask_b32_e64 v2, v2, v11, s[16:17]
	v_and_b32_e32 v39, 0x100, v3
	v_cndmask_b32_e64 v38, v38, 7, s[16:17]
	v_cmp_eq_u32_e64 s[16:17], 0, v39
	v_cmp_gt_f32_e64 s[18:19], v24, v2
	s_and_b64 s[16:17], s[16:17], s[18:19]
	v_cndmask_b32_e64 v2, v2, v24, s[16:17]
	v_and_b32_e32 v39, 0x200, v3
	v_cndmask_b32_e64 v38, v38, 8, s[16:17]
	v_cmp_eq_u32_e64 s[16:17], 0, v39
	v_cmp_gt_f32_e64 s[18:19], v25, v2
	s_and_b64 s[16:17], s[16:17], s[18:19]
	v_cndmask_b32_e64 v2, v2, v25, s[16:17]
	v_and_b32_e32 v39, 0x400, v3
	v_cndmask_b32_e64 v38, v38, 9, s[16:17]
	v_cmp_eq_u32_e64 s[16:17], 0, v39
	v_cmp_gt_f32_e64 s[18:19], v32, v2
	s_and_b64 s[16:17], s[16:17], s[18:19]
	v_cndmask_b32_e64 v2, v2, v32, s[16:17]
	v_and_b32_e32 v39, 0x800, v3
	v_cndmask_b32_e64 v38, v38, 10, s[16:17]
	v_cmp_eq_u32_e64 s[16:17], 0, v39
	v_cmp_gt_f32_e64 s[18:19], v33, v2
	s_and_b64 s[16:17], s[16:17], s[18:19]
	v_cndmask_b32_e64 v2, v2, v33, s[16:17]
	v_and_b32_e32 v39, 0x1000, v3
	v_cndmask_b32_e64 v38, v38, 11, s[16:17]
	v_cmp_eq_u32_e64 s[16:17], 0, v39
	v_cmp_gt_f32_e64 s[18:19], v20, v2
	s_and_b64 s[16:17], s[16:17], s[18:19]
	v_cndmask_b32_e64 v2, v2, v20, s[16:17]
	v_and_b32_e32 v39, 0x2000, v3
	v_cndmask_b32_e64 v38, v38, 12, s[16:17]
	v_cmp_eq_u32_e64 s[16:17], 0, v39
	v_cmp_gt_f32_e64 s[18:19], v21, v2
	s_and_b64 s[16:17], s[16:17], s[18:19]
	v_cndmask_b32_e64 v2, v2, v21, s[16:17]
	v_and_b32_e32 v39, 0x4000, v3
	v_cndmask_b32_e64 v38, v38, 13, s[16:17]
	v_cmp_eq_u32_e64 s[16:17], 0, v39
	v_cmp_gt_f32_e64 s[18:19], v6, v2
	s_and_b64 s[16:17], s[16:17], s[18:19]
	v_cndmask_b32_e64 v2, v2, v6, s[16:17]
	v_and_b32_e32 v39, 0x8000, v3
	v_cndmask_b32_e64 v38, v38, 14, s[16:17]
	v_cmp_eq_u32_e64 s[16:17], 0, v39
	v_cmp_gt_f32_e64 s[18:19], v7, v2
	s_and_b64 s[16:17], s[16:17], s[18:19]
	v_cndmask_b32_e64 v2, v2, v7, s[16:17]
	v_and_b32_e32 v39, 0x10000, v3
	v_cndmask_b32_e64 v38, v38, 15, s[16:17]
	v_cmp_eq_u32_e64 s[16:17], 0, v39
	v_cmp_gt_f32_e64 s[18:19], v18, v2
	s_and_b64 s[16:17], s[16:17], s[18:19]
	v_cndmask_b32_e64 v2, v2, v18, s[16:17]
	v_and_b32_e32 v39, 0x20000, v3
	v_cndmask_b32_e64 v38, v38, 16, s[16:17]
	v_cmp_eq_u32_e64 s[16:17], 0, v39
	v_cmp_gt_f32_e64 s[18:19], v19, v2
	s_and_b64 s[16:17], s[16:17], s[18:19]
	v_cndmask_b32_e64 v2, v2, v19, s[16:17]
	v_and_b32_e32 v39, 0x40000, v3
	v_cndmask_b32_e64 v38, v38, 17, s[16:17]
	v_cmp_eq_u32_e64 s[16:17], 0, v39
	v_cmp_gt_f32_e64 s[18:19], v28, v2
	s_and_b64 s[16:17], s[16:17], s[18:19]
	v_cndmask_b32_e64 v2, v2, v28, s[16:17]
	v_and_b32_e32 v39, 0x80000, v3
	v_cndmask_b32_e64 v38, v38, 18, s[16:17]
	v_cmp_eq_u32_e64 s[16:17], 0, v39
	v_cmp_gt_f32_e64 s[18:19], v29, v2
	s_and_b64 s[16:17], s[16:17], s[18:19]
	v_cndmask_b32_e64 v2, v2, v29, s[16:17]
	v_and_b32_e32 v39, 0x100000, v3
	v_cndmask_b32_e64 v38, v38, 19, s[16:17]
	v_cmp_eq_u32_e64 s[16:17], 0, v39
	v_cmp_gt_f32_e64 s[18:19], v12, v2
	s_and_b64 s[16:17], s[16:17], s[18:19]
	v_cndmask_b32_e64 v2, v2, v12, s[16:17]
	v_and_b32_e32 v39, 0x200000, v3
	v_cndmask_b32_e64 v38, v38, 20, s[16:17]
	v_cmp_eq_u32_e64 s[16:17], 0, v39
	v_cmp_gt_f32_e64 s[18:19], v13, v2
	s_and_b64 s[16:17], s[16:17], s[18:19]
	v_cndmask_b32_e64 v2, v2, v13, s[16:17]
	v_and_b32_e32 v39, 0x400000, v3
	v_cndmask_b32_e64 v38, v38, 21, s[16:17]
	v_cmp_eq_u32_e64 s[16:17], 0, v39
	v_cmp_gt_f32_e64 s[18:19], v4, v2
	s_and_b64 s[16:17], s[16:17], s[18:19]
	v_cndmask_b32_e64 v2, v2, v4, s[16:17]
	v_and_b32_e32 v39, 0x800000, v3
	v_cndmask_b32_e64 v38, v38, 22, s[16:17]
	v_cmp_eq_u32_e64 s[16:17], 0, v39
	v_cmp_gt_f32_e64 s[18:19], v5, v2
	s_and_b64 s[16:17], s[16:17], s[18:19]
	v_cndmask_b32_e64 v2, v2, v5, s[16:17]
	v_and_b32_e32 v39, 0x1000000, v3
	v_cndmask_b32_e64 v38, v38, 23, s[16:17]
	v_cmp_eq_u32_e64 s[16:17], 0, v39
	v_cmp_gt_f32_e64 s[18:19], v14, v2
	s_and_b64 s[16:17], s[16:17], s[18:19]
	v_cndmask_b32_e64 v2, v2, v14, s[16:17]
	v_and_b32_e32 v39, 0x2000000, v3
	v_cndmask_b32_e64 v38, v38, 24, s[16:17]
	v_cmp_eq_u32_e64 s[16:17], 0, v39
	v_cmp_gt_f32_e64 s[18:19], v15, v2
	s_and_b64 s[16:17], s[16:17], s[18:19]
	v_cndmask_b32_e64 v2, v2, v15, s[16:17]
	v_and_b32_e32 v39, 0x4000000, v3
	v_cndmask_b32_e64 v38, v38, 25, s[16:17]
	v_cmp_eq_u32_e64 s[16:17], 0, v39
	v_cmp_gt_f32_e64 s[18:19], v26, v2
	s_and_b64 s[16:17], s[16:17], s[18:19]
	v_cndmask_b32_e64 v2, v2, v26, s[16:17]
	v_and_b32_e32 v39, 0x8000000, v3
	v_cndmask_b32_e64 v38, v38, 26, s[16:17]
	v_cmp_eq_u32_e64 s[16:17], 0, v39
	v_cmp_gt_f32_e64 s[18:19], v27, v2
	s_and_b64 s[16:17], s[16:17], s[18:19]
	v_cndmask_b32_e64 v2, v2, v27, s[16:17]
	v_and_b32_e32 v39, 0x10000000, v3
	v_cndmask_b32_e64 v38, v38, 27, s[16:17]
	v_cmp_eq_u32_e64 s[16:17], 0, v39
	v_cmp_gt_f32_e64 s[18:19], v16, v2
	s_and_b64 s[16:17], s[16:17], s[18:19]
	v_cndmask_b32_e64 v2, v2, v16, s[16:17]
	v_and_b32_e32 v39, 0x20000000, v3
	v_cndmask_b32_e64 v38, v38, 28, s[16:17]
	v_cmp_eq_u32_e64 s[16:17], 0, v39
	v_cmp_gt_f32_e64 s[18:19], v17, v2
	s_and_b64 s[16:17], s[16:17], s[18:19]
	v_cndmask_b32_e64 v2, v2, v17, s[16:17]
	v_and_b32_e32 v39, 2.0, v3
	v_cndmask_b32_e64 v38, v38, 29, s[16:17]
	v_cmp_eq_u32_e64 s[16:17], 0, v39
	v_cmp_gt_f32_e64 s[18:19], v8, v2
	s_and_b64 s[16:17], s[16:17], s[18:19]
	v_cndmask_b32_e64 v2, v2, v8, s[16:17]
	v_cndmask_b32_e64 v38, v38, 30, s[16:17]
	v_cmp_lt_i32_e64 s[16:17], -1, v3
	v_cmp_gt_f32_e64 s[18:19], v9, v2
	s_and_b64 s[16:17], s[16:17], s[18:19]
	v_cndmask_b32_e64 v39, v2, v9, s[16:17]
	v_cndmask_b32_e64 v2, v38, 31, s[16:17]
	v_lshlrev_b32_e64 v38, v2, 1
	v_bitop3_b32 v89, v38, 1, v3 bitop3:0xc8
	v_cmp_eq_u32_e64 s[16:17], 0, v89
	s_and_b64 vcc, s[16:17], vcc
	v_cndmask_b32_e32 v34, v112, v34, vcc
	v_bitop3_b32 v89, v38, 2, v3 bitop3:0xc8
	v_cmp_eq_u32_e32 vcc, 0, v89
	v_cmp_gt_f32_e64 s[16:17], v35, v34
	s_and_b64 vcc, vcc, s[16:17]
	v_cndmask_b32_e32 v34, v34, v35, vcc
	v_bitop3_b32 v89, v38, 4, v3 bitop3:0xc8
	v_cndmask_b32_e64 v35, 0, 1, vcc
	v_cmp_eq_u32_e32 vcc, 0, v89
	v_cmp_gt_f32_e64 s[16:17], v30, v34
	s_and_b64 vcc, vcc, s[16:17]
	v_cndmask_b32_e32 v30, v34, v30, vcc
	v_cndmask_b32_e64 v34, v35, 2, vcc
	v_bitop3_b32 v35, v38, 8, v3 bitop3:0xc8
	v_cmp_eq_u32_e32 vcc, 0, v35
	v_cmp_gt_f32_e64 s[16:17], v31, v30
	s_and_b64 vcc, vcc, s[16:17]
	v_cndmask_b32_e32 v30, v30, v31, vcc
	v_cndmask_b32_e64 v31, v34, 3, vcc
	v_bitop3_b32 v34, v38, 16, v3 bitop3:0xc8
	v_cmp_eq_u32_e32 vcc, 0, v34
	v_cmp_gt_f32_e64 s[16:17], v22, v30
	s_and_b64 vcc, vcc, s[16:17]
	v_cndmask_b32_e32 v22, v30, v22, vcc
	v_cndmask_b32_e64 v30, v31, 4, vcc
	v_bitop3_b32 v31, v38, 32, v3 bitop3:0xc8
	v_cmp_eq_u32_e32 vcc, 0, v31
	v_cmp_gt_f32_e64 s[16:17], v23, v22
	s_and_b64 vcc, vcc, s[16:17]
	v_cndmask_b32_e32 v22, v22, v23, vcc
	v_cndmask_b32_e64 v23, v30, 5, vcc
	v_bitop3_b32 v30, v38, 64, v3 bitop3:0xc8
	v_cmp_eq_u32_e32 vcc, 0, v30
	v_cmp_gt_f32_e64 s[16:17], v10, v22
	s_and_b64 vcc, vcc, s[16:17]
	s_movk_i32 s16, 0x80
	v_cndmask_b32_e32 v10, v22, v10, vcc
	v_cndmask_b32_e64 v22, v23, 6, vcc
	v_bitop3_b32 v23, v38, s16, v3 bitop3:0xc8
	v_cmp_eq_u32_e32 vcc, 0, v23
	v_cmp_gt_f32_e64 s[16:17], v11, v10
	s_and_b64 vcc, vcc, s[16:17]
	s_movk_i32 s16, 0x100
	v_cndmask_b32_e32 v10, v10, v11, vcc
	v_cndmask_b32_e64 v11, v22, 7, vcc
	v_bitop3_b32 v22, v38, s16, v3 bitop3:0xc8
	v_cmp_eq_u32_e32 vcc, 0, v22
	v_cmp_gt_f32_e64 s[16:17], v24, v10
	s_and_b64 vcc, vcc, s[16:17]
	s_movk_i32 s16, 0x200
	v_cndmask_b32_e32 v10, v10, v24, vcc
	v_bitop3_b32 v22, v38, s16, v3 bitop3:0xc8
	v_cndmask_b32_e64 v11, v11, 8, vcc
	v_cmp_eq_u32_e32 vcc, 0, v22
	v_cmp_gt_f32_e64 s[16:17], v25, v10
	s_and_b64 vcc, vcc, s[16:17]
	v_cndmask_b32_e32 v10, v10, v25, vcc
	v_bitop3_b32 v22, v38, s52, v3 bitop3:0xc8
	v_cndmask_b32_e64 v11, v11, 9, vcc
	v_cmp_eq_u32_e32 vcc, 0, v22
	v_cmp_gt_f32_e64 s[16:17], v32, v10
	s_and_b64 vcc, vcc, s[16:17]
	s_movk_i32 s16, 0x800
	v_cndmask_b32_e32 v10, v10, v32, vcc
	v_bitop3_b32 v22, v38, s16, v3 bitop3:0xc8
	v_cndmask_b32_e64 v11, v11, 10, vcc
	v_cmp_eq_u32_e32 vcc, 0, v22
	v_cmp_gt_f32_e64 s[16:17], v33, v10
	s_and_b64 vcc, vcc, s[16:17]
	s_movk_i32 s16, 0x1000
	v_cndmask_b32_e32 v10, v10, v33, vcc
	v_bitop3_b32 v22, v38, s16, v3 bitop3:0xc8
	v_cndmask_b32_e64 v11, v11, 11, vcc
	v_cmp_eq_u32_e32 vcc, 0, v22
	v_cmp_gt_f32_e64 s[16:17], v20, v10
	s_and_b64 vcc, vcc, s[16:17]
	s_movk_i32 s16, 0x2000
	v_cndmask_b32_e32 v10, v10, v20, vcc
	v_bitop3_b32 v20, v38, s16, v3 bitop3:0xc8
	v_cndmask_b32_e64 v11, v11, 12, vcc
	v_cmp_eq_u32_e32 vcc, 0, v20
	v_cmp_gt_f32_e64 s[16:17], v21, v10
	s_and_b64 vcc, vcc, s[16:17]
	s_movk_i32 s16, 0x4000
	v_cndmask_b32_e32 v10, v10, v21, vcc
	v_bitop3_b32 v20, v38, s16, v3 bitop3:0xc8
	v_cndmask_b32_e64 v11, v11, 13, vcc
	v_cmp_eq_u32_e32 vcc, 0, v20
	v_cmp_gt_f32_e64 s[16:17], v6, v10
	s_and_b64 vcc, vcc, s[16:17]
	s_mov_b32 s16, 0x8000
	v_cndmask_b32_e32 v6, v10, v6, vcc
	v_cndmask_b32_e64 v10, v11, 14, vcc
	v_bitop3_b32 v11, v38, s16, v3 bitop3:0xc8
	v_cmp_eq_u32_e32 vcc, 0, v11
	v_cmp_gt_f32_e64 s[16:17], v7, v6
	s_and_b64 vcc, vcc, s[16:17]
	s_mov_b32 s16, 0x10000
	v_cndmask_b32_e32 v6, v6, v7, vcc
	v_cndmask_b32_e64 v7, v10, 15, vcc
	v_bitop3_b32 v10, v38, s16, v3 bitop3:0xc8
	v_cmp_eq_u32_e32 vcc, 0, v10
	v_cmp_gt_f32_e64 s[16:17], v18, v6
	s_and_b64 vcc, vcc, s[16:17]
	s_mov_b32 s16, 0x20000
	v_cndmask_b32_e32 v6, v6, v18, vcc
	v_bitop3_b32 v10, v38, s16, v3 bitop3:0xc8
	v_cndmask_b32_e64 v7, v7, 16, vcc
	v_cmp_eq_u32_e32 vcc, 0, v10
	v_cmp_gt_f32_e64 s[16:17], v19, v6
	s_and_b64 vcc, vcc, s[16:17]
	s_mov_b32 s16, 0x40000
	v_cndmask_b32_e32 v6, v6, v19, vcc
	v_bitop3_b32 v10, v38, s16, v3 bitop3:0xc8
	v_cndmask_b32_e64 v7, v7, 17, vcc
	v_cmp_eq_u32_e32 vcc, 0, v10
	v_cmp_gt_f32_e64 s[16:17], v28, v6
	s_and_b64 vcc, vcc, s[16:17]
	s_mov_b32 s16, 0x80000
	v_cndmask_b32_e32 v6, v6, v28, vcc
	v_bitop3_b32 v10, v38, s16, v3 bitop3:0xc8
	v_cndmask_b32_e64 v7, v7, 18, vcc
	v_cmp_eq_u32_e32 vcc, 0, v10
	v_cmp_gt_f32_e64 s[16:17], v29, v6
	s_and_b64 vcc, vcc, s[16:17]
	s_mov_b32 s16, 0x100000
	v_cndmask_b32_e32 v6, v6, v29, vcc
	v_bitop3_b32 v10, v38, s16, v3 bitop3:0xc8
	v_cndmask_b32_e64 v7, v7, 19, vcc
	v_cmp_eq_u32_e32 vcc, 0, v10
	v_cmp_gt_f32_e64 s[16:17], v12, v6
	s_and_b64 vcc, vcc, s[16:17]
	s_mov_b32 s16, 0x200000
	v_cndmask_b32_e32 v6, v6, v12, vcc
	v_bitop3_b32 v10, v38, s16, v3 bitop3:0xc8
	v_cndmask_b32_e64 v7, v7, 20, vcc
	v_cmp_eq_u32_e32 vcc, 0, v10
	v_cmp_gt_f32_e64 s[16:17], v13, v6
	s_and_b64 vcc, vcc, s[16:17]
	s_mov_b32 s16, 0x400000
	v_cndmask_b32_e32 v6, v6, v13, vcc
	v_bitop3_b32 v10, v38, s16, v3 bitop3:0xc8
	v_cndmask_b32_e64 v7, v7, 21, vcc
	v_cmp_eq_u32_e32 vcc, 0, v10
	v_cmp_gt_f32_e64 s[16:17], v4, v6
	s_and_b64 vcc, vcc, s[16:17]
	s_mov_b32 s16, 0x800000
	v_cndmask_b32_e32 v4, v6, v4, vcc
	v_cndmask_b32_e64 v6, v7, 22, vcc
	v_bitop3_b32 v7, v38, s16, v3 bitop3:0xc8
	v_cmp_eq_u32_e32 vcc, 0, v7
	v_cmp_gt_f32_e64 s[16:17], v5, v4
	s_and_b64 vcc, vcc, s[16:17]
	s_mov_b32 s16, 0x1000000
	v_cndmask_b32_e32 v4, v4, v5, vcc
	v_cndmask_b32_e64 v5, v6, 23, vcc
	v_bitop3_b32 v6, v38, s16, v3 bitop3:0xc8
	v_cmp_eq_u32_e32 vcc, 0, v6
	v_cmp_gt_f32_e64 s[16:17], v14, v4
	s_and_b64 vcc, vcc, s[16:17]
	v_cndmask_b32_e32 v4, v4, v14, vcc
	v_bitop3_b32 v6, v38, s61, v3 bitop3:0xc8
	v_cndmask_b32_e64 v5, v5, 24, vcc
	v_cmp_eq_u32_e32 vcc, 0, v6
	v_cmp_gt_f32_e64 s[16:17], v15, v4
	s_and_b64 vcc, vcc, s[16:17]
	v_cndmask_b32_e32 v4, v4, v15, vcc
	v_bitop3_b32 v6, v38, s62, v3 bitop3:0xc8
	v_cndmask_b32_e64 v5, v5, 25, vcc
	v_cmp_eq_u32_e32 vcc, 0, v6
	v_cmp_gt_f32_e64 s[16:17], v26, v4
	s_and_b64 vcc, vcc, s[16:17]
	v_cndmask_b32_e32 v4, v4, v26, vcc
	v_bitop3_b32 v6, v38, s63, v3 bitop3:0xc8
	v_cndmask_b32_e64 v5, v5, 26, vcc
	v_cmp_eq_u32_e32 vcc, 0, v6
	v_cmp_gt_f32_e64 s[16:17], v27, v4
	s_and_b64 vcc, vcc, s[16:17]
	v_cndmask_b32_e32 v4, v4, v27, vcc
	v_bitop3_b32 v6, v38, s64, v3 bitop3:0xc8
	v_cndmask_b32_e64 v5, v5, 27, vcc
	v_cmp_eq_u32_e32 vcc, 0, v6
	v_cmp_gt_f32_e64 s[16:17], v16, v4
	s_and_b64 vcc, vcc, s[16:17]
	v_cndmask_b32_e32 v4, v4, v16, vcc
	v_bitop3_b32 v6, v38, s65, v3 bitop3:0xc8
	v_cndmask_b32_e64 v5, v5, 28, vcc
	v_cmp_eq_u32_e32 vcc, 0, v6
	v_cmp_gt_f32_e64 s[16:17], v17, v4
	s_and_b64 vcc, vcc, s[16:17]
	v_or_b32_e32 v88, v38, v3
	v_cndmask_b32_e32 v4, v4, v17, vcc
	v_bitop3_b32 v3, v38, 2.0, v3 bitop3:0xc8
	v_cndmask_b32_e64 v5, v5, 29, vcc
	v_cmp_eq_u32_e32 vcc, 0, v3
	v_cmp_gt_f32_e64 s[16:17], v8, v4
	s_and_b64 vcc, vcc, s[16:17]
	v_cndmask_b32_e32 v3, v4, v8, vcc
	v_cndmask_b32_e64 v4, v5, 30, vcc
	v_cmp_lt_i32_e32 vcc, -1, v88
	v_cmp_gt_f32_e64 s[16:17], v9, v3
	s_and_b64 vcc, vcc, s[16:17]
	v_cndmask_b32_e32 v5, v3, v9, vcc
	v_cndmask_b32_e64 v3, v4, 31, vcc
	v_sub_f32_e32 v4, v36, v36
	v_mul_f32_e32 v4, 0x3fb8aa3b, v4
	v_exp_f32_e32 v10, v4
	v_sub_f32_e32 v4, v37, v36
	v_mul_f32_e32 v4, 0x3fb8aa3b, v4
	v_exp_f32_e32 v11, v4
	v_sub_f32_e32 v4, v39, v36
	v_mul_f32_e32 v4, 0x3fb8aa3b, v4
	v_exp_f32_e32 v12, v4
	v_sub_f32_e32 v4, v5, v36
	v_mul_f32_e32 v4, 0x3fb8aa3b, v4
	v_exp_f32_e32 v13, v4
	v_add_f32_e32 v4, 0, v10
	v_add_f32_e32 v4, v4, v11
	v_add_f32_e32 v4, v4, v12
	v_add_f32_e32 v14, v4, v13
	v_div_scale_f32 v15, s[16:17], v14, v14, v10
	v_rcp_f32_e32 v16, v15
	v_lshl_add_u32 v4, s66, 8, v94
	v_ashrrev_i32_e32 v5, 31, v4
	v_lshlrev_b64 v[6:7], 2, v[4:5]
	v_fma_f32 v5, -v15, v16, 1.0
	v_fmac_f32_e32 v16, v5, v16
	v_div_scale_f32 v5, vcc, v10, v14, v10
	v_mul_f32_e32 v17, v5, v16
	v_fma_f32 v18, -v15, v17, v5
	v_fmac_f32_e32 v17, v18, v16
	v_fma_f32 v5, -v15, v17, v5
	v_div_fmas_f32 v5, v5, v16, v17
	v_div_fixup_f32 v5, v5, v14, v10
	v_div_scale_f32 v10, s[16:17], v14, v14, v11
	v_rcp_f32_e32 v15, v10
	v_lshl_add_u64 v[8:9], s[20:21], 0, v[6:7]
	v_lshl_add_u64 v[6:7], s[22:23], 0, v[6:7]
	global_store_dword v[6:7], v5, off
	v_or_b32_e32 v6, 1, v4
	v_fma_f32 v4, -v10, v15, 1.0
	v_lshl_add_u32 v5, v0, 2, 0
	v_fmac_f32_e32 v15, v4, v15
	v_div_scale_f32 v4, vcc, v11, v14, v11
	ds_add_u32 v5, v109 offset:58624
	v_mul_f32_e32 v5, v4, v15
	v_fma_f32 v16, -v10, v5, v4
	v_fmac_f32_e32 v5, v16, v15
	v_fma_f32 v4, -v10, v5, v4
	v_div_fmas_f32 v4, v4, v15, v5
	v_div_scale_f32 v5, s[16:17], v14, v14, v12
	v_rcp_f32_e32 v15, v5
	v_ashrrev_i32_e32 v7, 31, v6
	v_div_fixup_f32 v4, v4, v14, v11
	v_lshl_add_u64 v[10:11], v[6:7], 2, s[22:23]
	v_lshl_add_u32 v6, v1, 2, 0
	ds_add_u32 v6, v109 offset:58624
	v_fma_f32 v6, -v5, v15, 1.0
	v_fmac_f32_e32 v15, v6, v15
	v_div_scale_f32 v6, vcc, v12, v14, v12
	v_mul_f32_e32 v7, v6, v15
	v_fma_f32 v16, -v5, v7, v6
	v_fmac_f32_e32 v7, v16, v15
	v_fma_f32 v5, -v5, v7, v6
	v_div_scale_f32 v6, s[16:17], v14, v14, v13
	v_div_fmas_f32 v5, v5, v15, v7
	v_rcp_f32_e32 v7, v6
	v_div_fixup_f32 v5, v5, v14, v12
	v_lshl_add_u32 v12, v2, 2, 0
	ds_add_u32 v12, v109 offset:58624
	global_store_dwordx4 v[8:9], v[0:3], off
	s_nop 1
	v_fma_f32 v0, -v6, v7, 1.0
	v_fmac_f32_e32 v7, v0, v7
	v_div_scale_f32 v0, vcc, v13, v14, v13
	v_mul_f32_e32 v1, v0, v7
	v_fma_f32 v2, -v6, v1, v0
	v_fmac_f32_e32 v1, v2, v7
	v_fma_f32 v0, -v6, v1, v0
	v_div_fmas_f32 v0, v0, v7, v1
	v_div_fixup_f32 v6, v0, v14, v13
	global_store_dwordx3 v[10:11], v[4:6], off
	v_lshl_add_u32 v0, v3, 2, 0
	ds_add_u32 v0, v109 offset:58624

.LBB0_3329:
	s_waitcnt vmcnt(0)
	s_barrier
	s_waitcnt vmcnt(0)
	s_waitcnt vmcnt(0)
	v_readlane_b32 s98, v253, 20
	v_mbcnt_lo_u32_b32 v216, -1, 0
	v_mbcnt_hi_u32_b32 v216, -1, v216
	s_lshr_b32 s99, s98, 1
	s_and_b32 s100, s98, 1
	v_lshrrev_b32_e32 v217, 5, v216
	v_and_b32_e32 v216, 31, v216
	s_lshl_b32 s101, s99, 4
	v_add_u32_e32 v218, s101, v217
	v_lshlrev_b32_e32 v219, 7, v218
	v_lshl_add_u32 v219, v216, 2, v219
	v_add_u32_e32 v219, 0xa400, v219
	v_mul_u32_u24_e32 v218, 0x104, v218
	s_lshl_b32 s101, s100, 7
	v_add_u32_e32 v218, s101, v218
	v_lshl_add_u32 v218, v216, 2, v218
	v_add_u32_e32 v218, 0x6000, v218
	v_mov_b32_e32 v221, s98
	v_mbcnt_lo_u32_b32 v220, -1, 0
	v_mbcnt_hi_u32_b32 v220, -1, v220
	v_lshl_add_u32 v220, v221, 6, v220
	v_and_b32_e32 v221, 7, v220
	v_lshrrev_b32_e32 v220, 3, v220
	v_mul_u32_u24_e32 v221, 0x820, v221
	v_lshl_add_u32 v220, v220, 2, v221
	v_add_u32_e32 v220, 0x6000, v220
	v_add_u32_e32 v221, 0x410, v220
	s_lshl_b32 s101, s99, 13
	s_lshl_b32 s100, s100, 12
	s_add_i32 s101, s101, s100
	v_lshlrev_b32_e32 v217, 9, v217
	v_add_u32_e32 v217, s101, v217
	v_lshl_add_u32 v217, v216, 2, v217
	s_and_saveexec_b64 s[16:17], s[4:5]
	ds_write_b32 v95, v45 offset:58624
	s_or_b64 exec, exec, s[16:17]
	v_add_u32_e32 v0, s96, v42
	v_ashrrev_i32_e32 v1, 31, v0
	v_lshlrev_b64 v[0:1], 11, v[0:1]
	v_lshl_add_u64 v[92:93], v[46:47], 0, v[0:1]
	global_load_dwordx4 v[30:33], v[92:93], off sc1
	global_load_dwordx4 v[34:37], v[48:49], off
	global_load_dwordx4 v[20:23], v[52:53], off
	global_load_dwordx4 v[24:27], v[92:93], off offset:128 sc1
	ds_read_b64 v[38:39], v106 offset:20480
	ds_read_b128 v[116:119], v43 offset:12288
	ds_read_b128 v[120:123], v43 offset:12304
	ds_read_b128 v[124:127], v43 offset:16384
	ds_read_b128 v[128:131], v43 offset:16400
	v_add_u32_e32 v114, 0x6000, v97
	v_mov_b32_e32 v4, 0
	s_waitcnt lgkmcnt(4)
	v_mov_b32_e32 v0, v38
	v_mov_b32_e32 v1, v38
	v_mov_b32_e32 v2, v38
	v_mov_b32_e32 v3, v38
	v_mov_b32_e32 v88, v39
	v_mov_b32_e32 v89, v39
	v_mov_b32_e32 v90, v39
	v_mov_b32_e32 v91, v39
	v_add_u32_e32 v113, 0x6400, v97
	s_mov_b32 s16, 0
	v_mov_b32_e32 v28, v103
	v_mov_b32_e32 v5, v4
	v_mov_b32_e32 v6, v4
	v_mov_b32_e32 v7, v4
	v_mov_b32_e32 v8, v4
	v_mov_b32_e32 v9, v4
	v_mov_b32_e32 v10, v4
	v_mov_b32_e32 v11, v4
	v_mov_b32_e32 v12, v4
	v_mov_b32_e32 v13, v4
	v_mov_b32_e32 v14, v4
	v_mov_b32_e32 v15, v4
	v_mov_b32_e32 v16, v4
	v_mov_b32_e32 v17, v4
	v_mov_b32_e32 v18, v4
	s_waitcnt vmcnt(3)
	v_cvt_f32_f16_sdwa v19, v31 dst_sel:DWORD dst_unused:UNUSED_PAD src0_sel:WORD_1
	v_cvt_f32_f16_e32 v29, v31
	v_cvt_f32_f16_sdwa v31, v30 dst_sel:DWORD dst_unused:UNUSED_PAD src0_sel:WORD_1
	v_cvt_f32_f16_e32 v30, v30
	v_cvt_f32_f16_sdwa v115, v33 dst_sel:DWORD dst_unused:UNUSED_PAD src0_sel:WORD_1
	v_cvt_f32_f16_e32 v134, v33
	v_cvt_f32_f16_sdwa v133, v32 dst_sel:DWORD dst_unused:UNUSED_PAD src0_sel:WORD_1
	v_cvt_f32_f16_e32 v132, v32
	v_sub_f32_e32 v30, v30, v38
	v_sub_f32_e32 v31, v31, v38
	v_sub_f32_e32 v32, v29, v38
	v_sub_f32_e32 v33, v19, v38
	v_sub_f32_e32 v132, v132, v38
	v_sub_f32_e32 v133, v133, v38
	v_sub_f32_e32 v134, v134, v38
	v_sub_f32_e32 v135, v115, v38
	v_pk_mul_f32 v[30:31], v[38:39], v[30:31] op_sel:[1,0]
	v_pk_mul_f32 v[32:33], v[38:39], v[32:33] op_sel:[1,0]
	v_pk_mul_f32 v[134:135], v[38:39], v[134:135] op_sel:[1,0]
	v_pk_mul_f32 v[38:39], v[38:39], v[132:133] op_sel:[1,0]
	s_waitcnt lgkmcnt(1)
	v_fma_f32 v19, v116, v30, v124
	v_fma_f32 v30, v117, v31, v125
	s_waitcnt lgkmcnt(0)
	v_fma_f32 v29, v120, v38, v128
	v_fma_f32 v31, v121, v39, v129
	v_fma_f32 v32, v118, v32, v126
	v_fma_f32 v38, v122, v134, v130
	v_fmac_f32_e32 v127, v119, v33
	v_fmac_f32_e32 v131, v123, v135
	ds_write2_b32 v220, v19, v30 offset1:65
	ds_write2_b32 v221, v29, v31 offset1:65
	ds_write2_b32 v220, v32, v127 offset0:130 offset1:195
	ds_write2_b32 v221, v38, v131 offset0:130 offset1:195
	s_waitcnt vmcnt(2)
	ds_write_b128 v96, v[34:37] offset:41984
	v_mov_b32_e32 v19, v4
	s_waitcnt lgkmcnt(0)
	s_barrier
	ds_read_b32 v200, v218
	ds_read_b32 v208, v219
	ds_read_b32 v201, v218 offset:520
	ds_read_b32 v209, v219 offset:256
	ds_read_b32 v202, v218 offset:1040
	ds_read_b32 v210, v219 offset:512
	ds_read_b32 v203, v218 offset:1560
	ds_read_b32 v211, v219 offset:768
	ds_read_b32 v204, v218 offset:2080
	ds_read_b32 v212, v219 offset:1024
	ds_read_b32 v205, v218 offset:2600
	ds_read_b32 v213, v219 offset:1280
	ds_read_b32 v206, v218 offset:3120
	ds_read_b32 v214, v219 offset:1536
	s_waitcnt lgkmcnt(12)
	v_mfma_f32_32x32x2_f32 v[4:19], v200, v208, v[4:19]
	ds_read_b32 v207, v218 offset:3640
	ds_read_b32 v215, v219 offset:1792
	s_waitcnt lgkmcnt(12)
	v_mfma_f32_32x32x2_f32 v[4:19], v201, v209, v[4:19]
	s_waitcnt lgkmcnt(10)
	v_mfma_f32_32x32x2_f32 v[4:19], v202, v210, v[4:19]
	s_waitcnt lgkmcnt(8)
	v_mfma_f32_32x32x2_f32 v[4:19], v203, v211, v[4:19]
	s_waitcnt lgkmcnt(6)
	v_mfma_f32_32x32x2_f32 v[4:19], v204, v212, v[4:19]
	s_waitcnt lgkmcnt(4)
	v_mfma_f32_32x32x2_f32 v[4:19], v205, v213, v[4:19]
	s_waitcnt lgkmcnt(2)
	v_mfma_f32_32x32x2_f32 v[4:19], v206, v214, v[4:19]
	s_waitcnt lgkmcnt(0)
	v_mfma_f32_32x32x2_f32 v[4:19], v207, v215, v[4:19]
	s_barrier
	global_load_dwordx4 v[32:35], v[92:93], off offset:256 sc1
	global_load_dwordx4 v[28:31], v[54:55], off
	s_waitcnt vmcnt(2)
	v_cvt_f32_f16_sdwa v128, v24 dst_sel:DWORD dst_unused:UNUSED_PAD src0_sel:WORD_1
	v_cvt_f32_f16_e32 v24, v24
	v_cvt_f32_f16_e32 v129, v25
	v_cvt_f32_f16_sdwa v130, v26 dst_sel:DWORD dst_unused:UNUSED_PAD src0_sel:WORD_1
	v_cvt_f32_f16_e32 v133, v26
	ds_read_b128 v[36:39], v43 offset:12544
	ds_read_b128 v[116:119], v43 offset:12560
	ds_read_b128 v[120:123], v43 offset:16640
	ds_read_b128 v[124:127], v43 offset:16656
	v_cvt_f32_f16_sdwa v115, v25 dst_sel:DWORD dst_unused:UNUSED_PAD src0_sel:WORD_1
	v_cvt_f32_f16_sdwa v131, v27 dst_sel:DWORD dst_unused:UNUSED_PAD src0_sel:WORD_1
	v_cvt_f32_f16_e32 v132, v27
	v_sub_f32_e32 v24, v24, v0
	v_sub_f32_e32 v25, v128, v1
	v_sub_f32_e32 v26, v129, v2
	v_pk_mul_f32 v[24:25], v[88:89], v[24:25]
	v_sub_f32_e32 v128, v133, v0
	v_sub_f32_e32 v129, v130, v1
	v_sub_f32_e32 v27, v115, v3
	v_sub_f32_e32 v130, v132, v2
	v_sub_f32_e32 v131, v131, v3
	v_pk_mul_f32 v[128:129], v[88:89], v[128:129]
	s_waitcnt lgkmcnt(1)
	v_fma_f32 v24, v36, v24, v120
	v_fma_f32 v25, v37, v25, v121
	v_pk_mul_f32 v[26:27], v[90:91], v[26:27]
	v_pk_mul_f32 v[130:131], v[90:91], v[130:131]
	s_waitcnt lgkmcnt(0)
	v_fma_f32 v36, v116, v128, v124
	ds_write2_b32 v220, v24, v25 offset1:65
	v_fma_f32 v24, v117, v129, v125
	ds_write2_b32 v221, v36, v24 offset1:65
	v_fma_f32 v24, v38, v26, v122
	v_fma_f32 v25, v118, v130, v126
	v_fmac_f32_e32 v123, v39, v27
	v_fmac_f32_e32 v127, v119, v131
	ds_write2_b32 v220, v24, v123 offset0:130 offset1:195
	ds_write2_b32 v221, v25, v127 offset0:130 offset1:195
	ds_write_b128 v96, v[20:23] offset:41984
	s_mov_b32 s16, 0
	v_mov_b32_e32 v20, v103
	s_waitcnt lgkmcnt(0)
	s_barrier
	ds_read_b32 v200, v218
	ds_read_b32 v208, v219
	ds_read_b32 v201, v218 offset:520
	ds_read_b32 v209, v219 offset:256
	ds_read_b32 v202, v218 offset:1040
	ds_read_b32 v210, v219 offset:512
	ds_read_b32 v203, v218 offset:1560
	ds_read_b32 v211, v219 offset:768
	ds_read_b32 v204, v218 offset:2080
	ds_read_b32 v212, v219 offset:1024
	ds_read_b32 v205, v218 offset:2600
	ds_read_b32 v213, v219 offset:1280
	ds_read_b32 v206, v218 offset:3120
	ds_read_b32 v214, v219 offset:1536
	s_waitcnt lgkmcnt(12)
	v_mfma_f32_32x32x2_f32 v[4:19], v200, v208, v[4:19]
	ds_read_b32 v207, v218 offset:3640
	ds_read_b32 v215, v219 offset:1792
	s_waitcnt lgkmcnt(12)
	v_mfma_f32_32x32x2_f32 v[4:19], v201, v209, v[4:19]
	s_waitcnt lgkmcnt(10)
	v_mfma_f32_32x32x2_f32 v[4:19], v202, v210, v[4:19]
	s_waitcnt lgkmcnt(8)
	v_mfma_f32_32x32x2_f32 v[4:19], v203, v211, v[4:19]
	s_waitcnt lgkmcnt(6)
	v_mfma_f32_32x32x2_f32 v[4:19], v204, v212, v[4:19]
	s_waitcnt lgkmcnt(4)
	v_mfma_f32_32x32x2_f32 v[4:19], v205, v213, v[4:19]
	s_waitcnt lgkmcnt(2)
	v_mfma_f32_32x32x2_f32 v[4:19], v206, v214, v[4:19]
	s_waitcnt lgkmcnt(0)
	v_mfma_f32_32x32x2_f32 v[4:19], v207, v215, v[4:19]
	s_barrier
	global_load_dwordx4 v[36:39], v[92:93], off offset:384 sc1
	global_load_dwordx4 v[20:23], v[56:57], off
	s_waitcnt vmcnt(3)
	v_cvt_f32_f16_sdwa v128, v32 dst_sel:DWORD dst_unused:UNUSED_PAD src0_sel:WORD_1
	v_cvt_f32_f16_e32 v32, v32
	v_cvt_f32_f16_e32 v129, v33
	v_cvt_f32_f16_sdwa v130, v34 dst_sel:DWORD dst_unused:UNUSED_PAD src0_sel:WORD_1
	v_cvt_f32_f16_e32 v133, v34
	ds_read_b128 v[24:27], v43 offset:12800
	ds_read_b128 v[116:119], v43 offset:12816
	ds_read_b128 v[120:123], v43 offset:16896
	ds_read_b128 v[124:127], v43 offset:16912
	v_cvt_f32_f16_sdwa v115, v33 dst_sel:DWORD dst_unused:UNUSED_PAD src0_sel:WORD_1
	v_cvt_f32_f16_sdwa v131, v35 dst_sel:DWORD dst_unused:UNUSED_PAD src0_sel:WORD_1
	v_cvt_f32_f16_e32 v132, v35
	v_sub_f32_e32 v32, v32, v0
	v_sub_f32_e32 v33, v128, v1
	v_sub_f32_e32 v34, v129, v2
	v_pk_mul_f32 v[32:33], v[88:89], v[32:33]
	v_sub_f32_e32 v128, v133, v0
	v_sub_f32_e32 v129, v130, v1
	v_sub_f32_e32 v35, v115, v3
	v_pk_mul_f32 v[128:129], v[88:89], v[128:129]
	s_waitcnt lgkmcnt(1)
	v_fma_f32 v24, v24, v32, v120
	v_fma_f32 v25, v25, v33, v121
	v_pk_mul_f32 v[34:35], v[90:91], v[34:35]
	v_sub_f32_e32 v130, v132, v2
	v_sub_f32_e32 v131, v131, v3
	s_waitcnt lgkmcnt(0)
	v_fma_f32 v32, v116, v128, v124
	ds_write2_b32 v220, v24, v25 offset1:65
	v_fma_f32 v24, v117, v129, v125
	v_pk_mul_f32 v[130:131], v[90:91], v[130:131]
	ds_write2_b32 v221, v32, v24 offset1:65
	v_fma_f32 v24, v26, v34, v122
	v_fmac_f32_e32 v123, v27, v35
	v_fma_f32 v25, v118, v130, v126
	ds_write2_b32 v220, v24, v123 offset0:130 offset1:195
	v_fmac_f32_e32 v127, v119, v131
	s_mov_b32 s16, 0
	v_mov_b32_e32 v24, v103
	ds_write2_b32 v221, v25, v127 offset0:130 offset1:195
	s_waitcnt vmcnt(2)
	ds_write_b128 v96, v[28:31] offset:41984
	s_waitcnt lgkmcnt(0)
	s_barrier
	ds_read_b32 v200, v218
	ds_read_b32 v208, v219
	ds_read_b32 v201, v218 offset:520
	ds_read_b32 v209, v219 offset:256
	ds_read_b32 v202, v218 offset:1040
	ds_read_b32 v210, v219 offset:512
	ds_read_b32 v203, v218 offset:1560
	ds_read_b32 v211, v219 offset:768
	ds_read_b32 v204, v218 offset:2080
	ds_read_b32 v212, v219 offset:1024
	ds_read_b32 v205, v218 offset:2600
	ds_read_b32 v213, v219 offset:1280
	ds_read_b32 v206, v218 offset:3120
	ds_read_b32 v214, v219 offset:1536
	s_waitcnt lgkmcnt(12)
	v_mfma_f32_32x32x2_f32 v[4:19], v200, v208, v[4:19]
	ds_read_b32 v207, v218 offset:3640
	ds_read_b32 v215, v219 offset:1792
	s_waitcnt lgkmcnt(12)
	v_mfma_f32_32x32x2_f32 v[4:19], v201, v209, v[4:19]
	s_waitcnt lgkmcnt(10)
	v_mfma_f32_32x32x2_f32 v[4:19], v202, v210, v[4:19]
	s_waitcnt lgkmcnt(8)
	v_mfma_f32_32x32x2_f32 v[4:19], v203, v211, v[4:19]
	s_waitcnt lgkmcnt(6)
	v_mfma_f32_32x32x2_f32 v[4:19], v204, v212, v[4:19]
	s_waitcnt lgkmcnt(4)
	v_mfma_f32_32x32x2_f32 v[4:19], v205, v213, v[4:19]
	s_waitcnt lgkmcnt(2)
	v_mfma_f32_32x32x2_f32 v[4:19], v206, v214, v[4:19]
	s_waitcnt lgkmcnt(0)
	v_mfma_f32_32x32x2_f32 v[4:19], v207, v215, v[4:19]
	s_barrier
	global_load_dwordx4 v[28:31], v[92:93], off offset:512 sc1
	global_load_dwordx4 v[24:27], v[58:59], off
	s_waitcnt vmcnt(3)
	v_cvt_f32_f16_sdwa v128, v36 dst_sel:DWORD dst_unused:UNUSED_PAD src0_sel:WORD_1
	v_cvt_f32_f16_e32 v36, v36
	v_cvt_f32_f16_e32 v129, v37
	v_cvt_f32_f16_sdwa v130, v38 dst_sel:DWORD dst_unused:UNUSED_PAD src0_sel:WORD_1
	v_cvt_f32_f16_e32 v133, v38
	ds_read_b128 v[32:35], v43 offset:13056
	ds_read_b128 v[116:119], v43 offset:13072
	ds_read_b128 v[120:123], v43 offset:17152
	ds_read_b128 v[124:127], v43 offset:17168
	v_cvt_f32_f16_sdwa v115, v37 dst_sel:DWORD dst_unused:UNUSED_PAD src0_sel:WORD_1
	v_cvt_f32_f16_sdwa v131, v39 dst_sel:DWORD dst_unused:UNUSED_PAD src0_sel:WORD_1
	v_cvt_f32_f16_e32 v132, v39
	v_sub_f32_e32 v36, v36, v0
	v_sub_f32_e32 v37, v128, v1
	v_sub_f32_e32 v38, v129, v2
	v_pk_mul_f32 v[36:37], v[88:89], v[36:37]
	v_sub_f32_e32 v128, v133, v0
	v_sub_f32_e32 v129, v130, v1
	v_sub_f32_e32 v39, v115, v3
	v_sub_f32_e32 v130, v132, v2
	v_sub_f32_e32 v131, v131, v3
	v_pk_mul_f32 v[128:129], v[88:89], v[128:129]
	s_waitcnt lgkmcnt(1)
	v_fma_f32 v32, v32, v36, v120
	v_fma_f32 v33, v33, v37, v121
	v_pk_mul_f32 v[38:39], v[90:91], v[38:39]
	v_pk_mul_f32 v[130:131], v[90:91], v[130:131]
	s_waitcnt lgkmcnt(0)
	v_fma_f32 v36, v116, v128, v124
	ds_write2_b32 v220, v32, v33 offset1:65
	v_fma_f32 v32, v117, v129, v125
	ds_write2_b32 v221, v36, v32 offset1:65
	v_fma_f32 v32, v34, v38, v122
	v_fma_f32 v33, v118, v130, v126
	v_fmac_f32_e32 v123, v35, v39
	v_fmac_f32_e32 v127, v119, v131
	ds_write2_b32 v220, v32, v123 offset0:130 offset1:195
	ds_write2_b32 v221, v33, v127 offset0:130 offset1:195
	s_waitcnt vmcnt(2)
	ds_write_b128 v96, v[20:23] offset:41984
	s_mov_b32 s16, 0
	v_mov_b32_e32 v20, v103
	s_waitcnt lgkmcnt(0)
	s_barrier
	ds_read_b32 v200, v218
	ds_read_b32 v208, v219
	ds_read_b32 v201, v218 offset:520
	ds_read_b32 v209, v219 offset:256
	ds_read_b32 v202, v218 offset:1040
	ds_read_b32 v210, v219 offset:512
	ds_read_b32 v203, v218 offset:1560
	ds_read_b32 v211, v219 offset:768
	ds_read_b32 v204, v218 offset:2080
	ds_read_b32 v212, v219 offset:1024
	ds_read_b32 v205, v218 offset:2600
	ds_read_b32 v213, v219 offset:1280
	ds_read_b32 v206, v218 offset:3120
	ds_read_b32 v214, v219 offset:1536
	s_waitcnt lgkmcnt(12)
	v_mfma_f32_32x32x2_f32 v[4:19], v200, v208, v[4:19]
	ds_read_b32 v207, v218 offset:3640
	ds_read_b32 v215, v219 offset:1792
	s_waitcnt lgkmcnt(12)
	v_mfma_f32_32x32x2_f32 v[4:19], v201, v209, v[4:19]
	s_waitcnt lgkmcnt(10)
	v_mfma_f32_32x32x2_f32 v[4:19], v202, v210, v[4:19]
	s_waitcnt lgkmcnt(8)
	v_mfma_f32_32x32x2_f32 v[4:19], v203, v211, v[4:19]
	s_waitcnt lgkmcnt(6)
	v_mfma_f32_32x32x2_f32 v[4:19], v204, v212, v[4:19]
	s_waitcnt lgkmcnt(4)
	v_mfma_f32_32x32x2_f32 v[4:19], v205, v213, v[4:19]
	s_waitcnt lgkmcnt(2)
	v_mfma_f32_32x32x2_f32 v[4:19], v206, v214, v[4:19]
	s_waitcnt lgkmcnt(0)
	v_mfma_f32_32x32x2_f32 v[4:19], v207, v215, v[4:19]
	s_barrier
	global_load_dwordx4 v[32:35], v[92:93], off offset:640 sc1
	global_load_dwordx4 v[20:23], v[60:61], off
	s_waitcnt vmcnt(3)
	v_cvt_f32_f16_sdwa v128, v28 dst_sel:DWORD dst_unused:UNUSED_PAD src0_sel:WORD_1
	v_cvt_f32_f16_e32 v28, v28
	v_cvt_f32_f16_e32 v129, v29
	v_cvt_f32_f16_sdwa v130, v30 dst_sel:DWORD dst_unused:UNUSED_PAD src0_sel:WORD_1
	v_cvt_f32_f16_e32 v133, v30
	ds_read_b128 v[36:39], v43 offset:13312
	ds_read_b128 v[116:119], v43 offset:13328
	ds_read_b128 v[120:123], v43 offset:17408
	ds_read_b128 v[124:127], v43 offset:17424
	v_cvt_f32_f16_sdwa v115, v29 dst_sel:DWORD dst_unused:UNUSED_PAD src0_sel:WORD_1
	v_cvt_f32_f16_sdwa v131, v31 dst_sel:DWORD dst_unused:UNUSED_PAD src0_sel:WORD_1
	v_cvt_f32_f16_e32 v132, v31
	v_sub_f32_e32 v28, v28, v0
	v_sub_f32_e32 v29, v128, v1
	v_sub_f32_e32 v30, v129, v2
	v_pk_mul_f32 v[28:29], v[88:89], v[28:29]
	v_sub_f32_e32 v128, v133, v0
	v_sub_f32_e32 v129, v130, v1
	v_sub_f32_e32 v31, v115, v3
	v_sub_f32_e32 v130, v132, v2
	v_sub_f32_e32 v131, v131, v3
	v_pk_mul_f32 v[128:129], v[88:89], v[128:129]
	s_waitcnt lgkmcnt(1)
	v_fma_f32 v28, v36, v28, v120
	v_fma_f32 v29, v37, v29, v121
	v_pk_mul_f32 v[30:31], v[90:91], v[30:31]
	v_pk_mul_f32 v[130:131], v[90:91], v[130:131]
	s_waitcnt lgkmcnt(0)
	v_fma_f32 v36, v116, v128, v124
	ds_write2_b32 v220, v28, v29 offset1:65
	v_fma_f32 v28, v117, v129, v125
	ds_write2_b32 v221, v36, v28 offset1:65
	v_fma_f32 v28, v38, v30, v122
	v_fma_f32 v29, v118, v130, v126
	v_fmac_f32_e32 v123, v39, v31
	v_fmac_f32_e32 v127, v119, v131
	ds_write2_b32 v220, v28, v123 offset0:130 offset1:195
	ds_write2_b32 v221, v29, v127 offset0:130 offset1:195
	s_waitcnt vmcnt(2)
	ds_write_b128 v96, v[24:27] offset:41984
	s_mov_b32 s16, 0
	v_mov_b32_e32 v24, v103
	s_waitcnt lgkmcnt(0)
	s_barrier
	ds_read_b32 v200, v218
	ds_read_b32 v208, v219
	ds_read_b32 v201, v218 offset:520
	ds_read_b32 v209, v219 offset:256
	ds_read_b32 v202, v218 offset:1040
	ds_read_b32 v210, v219 offset:512
	ds_read_b32 v203, v218 offset:1560
	ds_read_b32 v211, v219 offset:768
	ds_read_b32 v204, v218 offset:2080
	ds_read_b32 v212, v219 offset:1024
	ds_read_b32 v205, v218 offset:2600
	ds_read_b32 v213, v219 offset:1280
	ds_read_b32 v206, v218 offset:3120
	ds_read_b32 v214, v219 offset:1536
	s_waitcnt lgkmcnt(12)
	v_mfma_f32_32x32x2_f32 v[4:19], v200, v208, v[4:19]
	ds_read_b32 v207, v218 offset:3640
	ds_read_b32 v215, v219 offset:1792
	s_waitcnt lgkmcnt(12)
	v_mfma_f32_32x32x2_f32 v[4:19], v201, v209, v[4:19]
	s_waitcnt lgkmcnt(10)
	v_mfma_f32_32x32x2_f32 v[4:19], v202, v210, v[4:19]
	s_waitcnt lgkmcnt(8)
	v_mfma_f32_32x32x2_f32 v[4:19], v203, v211, v[4:19]
	s_waitcnt lgkmcnt(6)
	v_mfma_f32_32x32x2_f32 v[4:19], v204, v212, v[4:19]
	s_waitcnt lgkmcnt(4)
	v_mfma_f32_32x32x2_f32 v[4:19], v205, v213, v[4:19]
	s_waitcnt lgkmcnt(2)
	v_mfma_f32_32x32x2_f32 v[4:19], v206, v214, v[4:19]
	s_waitcnt lgkmcnt(0)
	v_mfma_f32_32x32x2_f32 v[4:19], v207, v215, v[4:19]
	s_barrier
	global_load_dwordx4 v[28:31], v[92:93], off offset:768 sc1
	global_load_dwordx4 v[24:27], v[62:63], off
	s_waitcnt vmcnt(3)
	v_cvt_f32_f16_sdwa v128, v32 dst_sel:DWORD dst_unused:UNUSED_PAD src0_sel:WORD_1
	v_cvt_f32_f16_e32 v32, v32
	v_cvt_f32_f16_e32 v129, v33
	v_cvt_f32_f16_sdwa v130, v34 dst_sel:DWORD dst_unused:UNUSED_PAD src0_sel:WORD_1
	v_cvt_f32_f16_e32 v133, v34
	ds_read_b128 v[36:39], v43 offset:13568
	ds_read_b128 v[116:119], v43 offset:13584
	ds_read_b128 v[120:123], v43 offset:17664
	ds_read_b128 v[124:127], v43 offset:17680
	v_cvt_f32_f16_sdwa v115, v33 dst_sel:DWORD dst_unused:UNUSED_PAD src0_sel:WORD_1
	v_cvt_f32_f16_sdwa v131, v35 dst_sel:DWORD dst_unused:UNUSED_PAD src0_sel:WORD_1
	v_cvt_f32_f16_e32 v132, v35
	v_sub_f32_e32 v32, v32, v0
	v_sub_f32_e32 v33, v128, v1
	v_sub_f32_e32 v34, v129, v2
	v_pk_mul_f32 v[32:33], v[88:89], v[32:33]
	v_sub_f32_e32 v128, v133, v0
	v_sub_f32_e32 v129, v130, v1
	v_sub_f32_e32 v35, v115, v3
	v_sub_f32_e32 v130, v132, v2
	v_sub_f32_e32 v131, v131, v3
	v_pk_mul_f32 v[128:129], v[88:89], v[128:129]
	s_waitcnt lgkmcnt(1)
	v_fma_f32 v32, v36, v32, v120
	v_fma_f32 v33, v37, v33, v121
	v_pk_mul_f32 v[34:35], v[90:91], v[34:35]
	v_pk_mul_f32 v[130:131], v[90:91], v[130:131]
	s_waitcnt lgkmcnt(0)
	v_fma_f32 v36, v116, v128, v124
	ds_write2_b32 v220, v32, v33 offset1:65
	v_fma_f32 v32, v117, v129, v125
	ds_write2_b32 v221, v36, v32 offset1:65
	v_fma_f32 v32, v38, v34, v122
	v_fma_f32 v33, v118, v130, v126
	v_fmac_f32_e32 v123, v39, v35
	v_fmac_f32_e32 v127, v119, v131
	ds_write2_b32 v220, v32, v123 offset0:130 offset1:195
	ds_write2_b32 v221, v33, v127 offset0:130 offset1:195
	s_waitcnt vmcnt(2)
	ds_write_b128 v96, v[20:23] offset:41984
	s_mov_b32 s16, 0
	v_mov_b32_e32 v20, v103
	s_waitcnt lgkmcnt(0)
	s_barrier
	ds_read_b32 v200, v218
	ds_read_b32 v208, v219
	ds_read_b32 v201, v218 offset:520
	ds_read_b32 v209, v219 offset:256
	ds_read_b32 v202, v218 offset:1040
	ds_read_b32 v210, v219 offset:512
	ds_read_b32 v203, v218 offset:1560
	ds_read_b32 v211, v219 offset:768
	ds_read_b32 v204, v218 offset:2080
	ds_read_b32 v212, v219 offset:1024
	ds_read_b32 v205, v218 offset:2600
	ds_read_b32 v213, v219 offset:1280
	ds_read_b32 v206, v218 offset:3120
	ds_read_b32 v214, v219 offset:1536
	s_waitcnt lgkmcnt(12)
	v_mfma_f32_32x32x2_f32 v[4:19], v200, v208, v[4:19]
	ds_read_b32 v207, v218 offset:3640
	ds_read_b32 v215, v219 offset:1792
	s_waitcnt lgkmcnt(12)
	v_mfma_f32_32x32x2_f32 v[4:19], v201, v209, v[4:19]
	s_waitcnt lgkmcnt(10)
	v_mfma_f32_32x32x2_f32 v[4:19], v202, v210, v[4:19]
	s_waitcnt lgkmcnt(8)
	v_mfma_f32_32x32x2_f32 v[4:19], v203, v211, v[4:19]
	s_waitcnt lgkmcnt(6)
	v_mfma_f32_32x32x2_f32 v[4:19], v204, v212, v[4:19]
	s_waitcnt lgkmcnt(4)
	v_mfma_f32_32x32x2_f32 v[4:19], v205, v213, v[4:19]
	s_waitcnt lgkmcnt(2)
	v_mfma_f32_32x32x2_f32 v[4:19], v206, v214, v[4:19]
	s_waitcnt lgkmcnt(0)
	v_mfma_f32_32x32x2_f32 v[4:19], v207, v215, v[4:19]
	s_barrier
	global_load_dwordx4 v[32:35], v[92:93], off offset:896 sc1
	global_load_dwordx4 v[20:23], v[64:65], off
	s_waitcnt vmcnt(3)
	v_cvt_f32_f16_sdwa v128, v28 dst_sel:DWORD dst_unused:UNUSED_PAD src0_sel:WORD_1
	v_cvt_f32_f16_e32 v28, v28
	v_cvt_f32_f16_e32 v129, v29
	v_cvt_f32_f16_sdwa v130, v30 dst_sel:DWORD dst_unused:UNUSED_PAD src0_sel:WORD_1
	v_cvt_f32_f16_e32 v133, v30
	ds_read_b128 v[36:39], v43 offset:13824
	ds_read_b128 v[116:119], v43 offset:13840
	ds_read_b128 v[120:123], v43 offset:17920
	ds_read_b128 v[124:127], v43 offset:17936
	v_cvt_f32_f16_sdwa v115, v29 dst_sel:DWORD dst_unused:UNUSED_PAD src0_sel:WORD_1
	v_cvt_f32_f16_sdwa v131, v31 dst_sel:DWORD dst_unused:UNUSED_PAD src0_sel:WORD_1
	v_cvt_f32_f16_e32 v132, v31
	v_sub_f32_e32 v28, v28, v0
	v_sub_f32_e32 v29, v128, v1
	v_sub_f32_e32 v30, v129, v2
	v_pk_mul_f32 v[28:29], v[88:89], v[28:29]
	v_sub_f32_e32 v128, v133, v0
	v_sub_f32_e32 v129, v130, v1
	v_sub_f32_e32 v31, v115, v3
	v_sub_f32_e32 v130, v132, v2
	v_sub_f32_e32 v131, v131, v3
	v_pk_mul_f32 v[128:129], v[88:89], v[128:129]
	s_waitcnt lgkmcnt(1)
	v_fma_f32 v28, v36, v28, v120
	v_fma_f32 v29, v37, v29, v121
	v_pk_mul_f32 v[30:31], v[90:91], v[30:31]
	v_pk_mul_f32 v[130:131], v[90:91], v[130:131]
	s_waitcnt lgkmcnt(0)
	v_fma_f32 v36, v116, v128, v124
	ds_write2_b32 v220, v28, v29 offset1:65
	v_fma_f32 v28, v117, v129, v125
	ds_write2_b32 v221, v36, v28 offset1:65
	v_fma_f32 v28, v38, v30, v122
	v_fma_f32 v29, v118, v130, v126
	v_fmac_f32_e32 v123, v39, v31
	v_fmac_f32_e32 v127, v119, v131
	ds_write2_b32 v220, v28, v123 offset0:130 offset1:195
	ds_write2_b32 v221, v29, v127 offset0:130 offset1:195
	s_waitcnt vmcnt(2)
	ds_write_b128 v96, v[24:27] offset:41984
	s_mov_b32 s16, 0
	v_mov_b32_e32 v24, v103
	s_waitcnt lgkmcnt(0)
	s_barrier
	ds_read_b32 v200, v218
	ds_read_b32 v208, v219
	ds_read_b32 v201, v218 offset:520
	ds_read_b32 v209, v219 offset:256
	ds_read_b32 v202, v218 offset:1040
	ds_read_b32 v210, v219 offset:512
	ds_read_b32 v203, v218 offset:1560
	ds_read_b32 v211, v219 offset:768
	ds_read_b32 v204, v218 offset:2080
	ds_read_b32 v212, v219 offset:1024
	ds_read_b32 v205, v218 offset:2600
	ds_read_b32 v213, v219 offset:1280
	ds_read_b32 v206, v218 offset:3120
	ds_read_b32 v214, v219 offset:1536
	s_waitcnt lgkmcnt(12)
	v_mfma_f32_32x32x2_f32 v[4:19], v200, v208, v[4:19]
	ds_read_b32 v207, v218 offset:3640
	ds_read_b32 v215, v219 offset:1792
	s_waitcnt lgkmcnt(12)
	v_mfma_f32_32x32x2_f32 v[4:19], v201, v209, v[4:19]
	s_waitcnt lgkmcnt(10)
	v_mfma_f32_32x32x2_f32 v[4:19], v202, v210, v[4:19]
	s_waitcnt lgkmcnt(8)
	v_mfma_f32_32x32x2_f32 v[4:19], v203, v211, v[4:19]
	s_waitcnt lgkmcnt(6)
	v_mfma_f32_32x32x2_f32 v[4:19], v204, v212, v[4:19]
	s_waitcnt lgkmcnt(4)
	v_mfma_f32_32x32x2_f32 v[4:19], v205, v213, v[4:19]
	s_waitcnt lgkmcnt(2)
	v_mfma_f32_32x32x2_f32 v[4:19], v206, v214, v[4:19]
	s_waitcnt lgkmcnt(0)
	v_mfma_f32_32x32x2_f32 v[4:19], v207, v215, v[4:19]
	s_barrier
	global_load_dwordx4 v[28:31], v[92:93], off offset:1024 sc1
	global_load_dwordx4 v[24:27], v[66:67], off
	s_waitcnt vmcnt(3)
	v_cvt_f32_f16_sdwa v128, v32 dst_sel:DWORD dst_unused:UNUSED_PAD src0_sel:WORD_1
	v_cvt_f32_f16_e32 v32, v32
	v_cvt_f32_f16_e32 v129, v33
	v_cvt_f32_f16_sdwa v130, v34 dst_sel:DWORD dst_unused:UNUSED_PAD src0_sel:WORD_1
	v_cvt_f32_f16_e32 v133, v34
	ds_read_b128 v[36:39], v43 offset:14080
	ds_read_b128 v[116:119], v43 offset:14096
	ds_read_b128 v[120:123], v43 offset:18176
	ds_read_b128 v[124:127], v43 offset:18192
	v_cvt_f32_f16_sdwa v115, v33 dst_sel:DWORD dst_unused:UNUSED_PAD src0_sel:WORD_1
	v_cvt_f32_f16_sdwa v131, v35 dst_sel:DWORD dst_unused:UNUSED_PAD src0_sel:WORD_1
	v_cvt_f32_f16_e32 v132, v35
	v_sub_f32_e32 v32, v32, v0
	v_sub_f32_e32 v33, v128, v1
	v_sub_f32_e32 v34, v129, v2
	v_pk_mul_f32 v[32:33], v[88:89], v[32:33]
	v_sub_f32_e32 v128, v133, v0
	v_sub_f32_e32 v129, v130, v1
	v_sub_f32_e32 v35, v115, v3
	v_sub_f32_e32 v130, v132, v2
	v_sub_f32_e32 v131, v131, v3
	v_pk_mul_f32 v[128:129], v[88:89], v[128:129]
	s_waitcnt lgkmcnt(1)
	v_fma_f32 v32, v36, v32, v120
	v_fma_f32 v33, v37, v33, v121
	v_pk_mul_f32 v[34:35], v[90:91], v[34:35]
	v_pk_mul_f32 v[130:131], v[90:91], v[130:131]
	s_waitcnt lgkmcnt(0)
	v_fma_f32 v36, v116, v128, v124
	ds_write2_b32 v220, v32, v33 offset1:65
	v_fma_f32 v32, v117, v129, v125
	ds_write2_b32 v221, v36, v32 offset1:65
	v_fma_f32 v32, v38, v34, v122
	v_fma_f32 v33, v118, v130, v126
	v_fmac_f32_e32 v123, v39, v35
	v_fmac_f32_e32 v127, v119, v131
	ds_write2_b32 v220, v32, v123 offset0:130 offset1:195
	ds_write2_b32 v221, v33, v127 offset0:130 offset1:195
	s_waitcnt vmcnt(2)
	ds_write_b128 v96, v[20:23] offset:41984
	s_mov_b32 s16, 0
	v_mov_b32_e32 v20, v103
	s_waitcnt lgkmcnt(0)
	s_barrier
	ds_read_b32 v200, v218
	ds_read_b32 v208, v219
	ds_read_b32 v201, v218 offset:520
	ds_read_b32 v209, v219 offset:256
	ds_read_b32 v202, v218 offset:1040
	ds_read_b32 v210, v219 offset:512
	ds_read_b32 v203, v218 offset:1560
	ds_read_b32 v211, v219 offset:768
	ds_read_b32 v204, v218 offset:2080
	ds_read_b32 v212, v219 offset:1024
	ds_read_b32 v205, v218 offset:2600
	ds_read_b32 v213, v219 offset:1280
	ds_read_b32 v206, v218 offset:3120
	ds_read_b32 v214, v219 offset:1536
	s_waitcnt lgkmcnt(12)
	v_mfma_f32_32x32x2_f32 v[4:19], v200, v208, v[4:19]
	ds_read_b32 v207, v218 offset:3640
	ds_read_b32 v215, v219 offset:1792
	s_waitcnt lgkmcnt(12)
	v_mfma_f32_32x32x2_f32 v[4:19], v201, v209, v[4:19]
	s_waitcnt lgkmcnt(10)
	v_mfma_f32_32x32x2_f32 v[4:19], v202, v210, v[4:19]
	s_waitcnt lgkmcnt(8)
	v_mfma_f32_32x32x2_f32 v[4:19], v203, v211, v[4:19]
	s_waitcnt lgkmcnt(6)
	v_mfma_f32_32x32x2_f32 v[4:19], v204, v212, v[4:19]
	s_waitcnt lgkmcnt(4)
	v_mfma_f32_32x32x2_f32 v[4:19], v205, v213, v[4:19]
	s_waitcnt lgkmcnt(2)
	v_mfma_f32_32x32x2_f32 v[4:19], v206, v214, v[4:19]
	s_waitcnt lgkmcnt(0)
	v_mfma_f32_32x32x2_f32 v[4:19], v207, v215, v[4:19]
	s_barrier
	global_load_dwordx4 v[32:35], v[92:93], off offset:1152 sc1
	global_load_dwordx4 v[20:23], v[68:69], off
	s_waitcnt vmcnt(3)
	v_cvt_f32_f16_sdwa v128, v28 dst_sel:DWORD dst_unused:UNUSED_PAD src0_sel:WORD_1
	v_cvt_f32_f16_e32 v28, v28
	v_cvt_f32_f16_e32 v129, v29
	v_cvt_f32_f16_sdwa v130, v30 dst_sel:DWORD dst_unused:UNUSED_PAD src0_sel:WORD_1
	v_cvt_f32_f16_e32 v133, v30
	ds_read_b128 v[36:39], v43 offset:14336
	ds_read_b128 v[116:119], v43 offset:14352
	ds_read_b128 v[120:123], v43 offset:18432
	ds_read_b128 v[124:127], v43 offset:18448
	v_cvt_f32_f16_sdwa v115, v29 dst_sel:DWORD dst_unused:UNUSED_PAD src0_sel:WORD_1
	v_cvt_f32_f16_sdwa v131, v31 dst_sel:DWORD dst_unused:UNUSED_PAD src0_sel:WORD_1
	v_cvt_f32_f16_e32 v132, v31
	v_sub_f32_e32 v28, v28, v0
	v_sub_f32_e32 v29, v128, v1
	v_sub_f32_e32 v30, v129, v2
	v_pk_mul_f32 v[28:29], v[88:89], v[28:29]
	v_sub_f32_e32 v128, v133, v0
	v_sub_f32_e32 v129, v130, v1
	v_sub_f32_e32 v31, v115, v3
	v_sub_f32_e32 v130, v132, v2
	v_sub_f32_e32 v131, v131, v3
	v_pk_mul_f32 v[128:129], v[88:89], v[128:129]
	s_waitcnt lgkmcnt(1)
	v_fma_f32 v28, v36, v28, v120
	v_fma_f32 v29, v37, v29, v121
	v_pk_mul_f32 v[30:31], v[90:91], v[30:31]
	v_pk_mul_f32 v[130:131], v[90:91], v[130:131]
	s_waitcnt lgkmcnt(0)
	v_fma_f32 v36, v116, v128, v124
	ds_write2_b32 v220, v28, v29 offset1:65
	v_fma_f32 v28, v117, v129, v125
	ds_write2_b32 v221, v36, v28 offset1:65
	v_fma_f32 v28, v38, v30, v122
	v_fma_f32 v29, v118, v130, v126
	v_fmac_f32_e32 v123, v39, v31
	v_fmac_f32_e32 v127, v119, v131
	ds_write2_b32 v220, v28, v123 offset0:130 offset1:195
	ds_write2_b32 v221, v29, v127 offset0:130 offset1:195
	s_waitcnt vmcnt(2)
	ds_write_b128 v96, v[24:27] offset:41984
	s_mov_b32 s16, 0
	v_mov_b32_e32 v24, v103
	s_waitcnt lgkmcnt(0)
	s_barrier
	ds_read_b32 v200, v218
	ds_read_b32 v208, v219
	ds_read_b32 v201, v218 offset:520
	ds_read_b32 v209, v219 offset:256
	ds_read_b32 v202, v218 offset:1040
	ds_read_b32 v210, v219 offset:512
	ds_read_b32 v203, v218 offset:1560
	ds_read_b32 v211, v219 offset:768
	ds_read_b32 v204, v218 offset:2080
	ds_read_b32 v212, v219 offset:1024
	ds_read_b32 v205, v218 offset:2600
	ds_read_b32 v213, v219 offset:1280
	ds_read_b32 v206, v218 offset:3120
	ds_read_b32 v214, v219 offset:1536
	s_waitcnt lgkmcnt(12)
	v_mfma_f32_32x32x2_f32 v[4:19], v200, v208, v[4:19]
	ds_read_b32 v207, v218 offset:3640
	ds_read_b32 v215, v219 offset:1792
	s_waitcnt lgkmcnt(12)
	v_mfma_f32_32x32x2_f32 v[4:19], v201, v209, v[4:19]
	s_waitcnt lgkmcnt(10)
	v_mfma_f32_32x32x2_f32 v[4:19], v202, v210, v[4:19]
	s_waitcnt lgkmcnt(8)
	v_mfma_f32_32x32x2_f32 v[4:19], v203, v211, v[4:19]
	s_waitcnt lgkmcnt(6)
	v_mfma_f32_32x32x2_f32 v[4:19], v204, v212, v[4:19]
	s_waitcnt lgkmcnt(4)
	v_mfma_f32_32x32x2_f32 v[4:19], v205, v213, v[4:19]
	s_waitcnt lgkmcnt(2)
	v_mfma_f32_32x32x2_f32 v[4:19], v206, v214, v[4:19]
	s_waitcnt lgkmcnt(0)
	v_mfma_f32_32x32x2_f32 v[4:19], v207, v215, v[4:19]
	s_barrier
	global_load_dwordx4 v[28:31], v[92:93], off offset:1280 sc1
	global_load_dwordx4 v[24:27], v[70:71], off
	s_waitcnt vmcnt(3)
	v_cvt_f32_f16_sdwa v128, v32 dst_sel:DWORD dst_unused:UNUSED_PAD src0_sel:WORD_1
	v_cvt_f32_f16_e32 v32, v32
	v_cvt_f32_f16_e32 v129, v33
	v_cvt_f32_f16_sdwa v130, v34 dst_sel:DWORD dst_unused:UNUSED_PAD src0_sel:WORD_1
	v_cvt_f32_f16_e32 v133, v34
	ds_read_b128 v[36:39], v43 offset:14592
	ds_read_b128 v[116:119], v43 offset:14608
	ds_read_b128 v[120:123], v43 offset:18688
	ds_read_b128 v[124:127], v43 offset:18704
	v_cvt_f32_f16_sdwa v115, v33 dst_sel:DWORD dst_unused:UNUSED_PAD src0_sel:WORD_1
	v_cvt_f32_f16_sdwa v131, v35 dst_sel:DWORD dst_unused:UNUSED_PAD src0_sel:WORD_1
	v_cvt_f32_f16_e32 v132, v35
	v_sub_f32_e32 v32, v32, v0
	v_sub_f32_e32 v33, v128, v1
	v_sub_f32_e32 v34, v129, v2
	v_pk_mul_f32 v[32:33], v[88:89], v[32:33]
	v_sub_f32_e32 v128, v133, v0
	v_sub_f32_e32 v129, v130, v1
	v_sub_f32_e32 v35, v115, v3
	v_sub_f32_e32 v130, v132, v2
	v_sub_f32_e32 v131, v131, v3
	v_pk_mul_f32 v[128:129], v[88:89], v[128:129]
	s_waitcnt lgkmcnt(1)
	v_fma_f32 v32, v36, v32, v120
	v_fma_f32 v33, v37, v33, v121
	v_pk_mul_f32 v[34:35], v[90:91], v[34:35]
	v_pk_mul_f32 v[130:131], v[90:91], v[130:131]
	s_waitcnt lgkmcnt(0)
	v_fma_f32 v36, v116, v128, v124
	ds_write2_b32 v220, v32, v33 offset1:65
	v_fma_f32 v32, v117, v129, v125
	ds_write2_b32 v221, v36, v32 offset1:65
	v_fma_f32 v32, v38, v34, v122
	v_fma_f32 v33, v118, v130, v126
	v_fmac_f32_e32 v123, v39, v35
	v_fmac_f32_e32 v127, v119, v131
	ds_write2_b32 v220, v32, v123 offset0:130 offset1:195
	ds_write2_b32 v221, v33, v127 offset0:130 offset1:195
	s_waitcnt vmcnt(2)
	ds_write_b128 v96, v[20:23] offset:41984
	s_mov_b32 s16, 0
	v_mov_b32_e32 v20, v103
	s_waitcnt lgkmcnt(0)
	s_barrier
	ds_read_b32 v200, v218
	ds_read_b32 v208, v219
	ds_read_b32 v201, v218 offset:520
	ds_read_b32 v209, v219 offset:256
	ds_read_b32 v202, v218 offset:1040
	ds_read_b32 v210, v219 offset:512
	ds_read_b32 v203, v218 offset:1560
	ds_read_b32 v211, v219 offset:768
	ds_read_b32 v204, v218 offset:2080
	ds_read_b32 v212, v219 offset:1024
	ds_read_b32 v205, v218 offset:2600
	ds_read_b32 v213, v219 offset:1280
	ds_read_b32 v206, v218 offset:3120
	ds_read_b32 v214, v219 offset:1536
	s_waitcnt lgkmcnt(12)
	v_mfma_f32_32x32x2_f32 v[4:19], v200, v208, v[4:19]
	ds_read_b32 v207, v218 offset:3640
	ds_read_b32 v215, v219 offset:1792
	s_waitcnt lgkmcnt(12)
	v_mfma_f32_32x32x2_f32 v[4:19], v201, v209, v[4:19]
	s_waitcnt lgkmcnt(10)
	v_mfma_f32_32x32x2_f32 v[4:19], v202, v210, v[4:19]
	s_waitcnt lgkmcnt(8)
	v_mfma_f32_32x32x2_f32 v[4:19], v203, v211, v[4:19]
	s_waitcnt lgkmcnt(6)
	v_mfma_f32_32x32x2_f32 v[4:19], v204, v212, v[4:19]
	s_waitcnt lgkmcnt(4)
	v_mfma_f32_32x32x2_f32 v[4:19], v205, v213, v[4:19]
	s_waitcnt lgkmcnt(2)
	v_mfma_f32_32x32x2_f32 v[4:19], v206, v214, v[4:19]
	s_waitcnt lgkmcnt(0)
	v_mfma_f32_32x32x2_f32 v[4:19], v207, v215, v[4:19]
	s_barrier
	global_load_dwordx4 v[32:35], v[92:93], off offset:1408 sc1
	global_load_dwordx4 v[20:23], v[72:73], off
	s_waitcnt vmcnt(3)
	v_cvt_f32_f16_sdwa v128, v28 dst_sel:DWORD dst_unused:UNUSED_PAD src0_sel:WORD_1
	v_cvt_f32_f16_e32 v28, v28
	v_cvt_f32_f16_e32 v129, v29
	v_cvt_f32_f16_sdwa v130, v30 dst_sel:DWORD dst_unused:UNUSED_PAD src0_sel:WORD_1
	v_cvt_f32_f16_e32 v133, v30
	ds_read_b128 v[36:39], v43 offset:14848
	ds_read_b128 v[116:119], v43 offset:14864
	ds_read_b128 v[120:123], v43 offset:18944
	ds_read_b128 v[124:127], v43 offset:18960
	v_cvt_f32_f16_sdwa v115, v29 dst_sel:DWORD dst_unused:UNUSED_PAD src0_sel:WORD_1
	v_cvt_f32_f16_sdwa v131, v31 dst_sel:DWORD dst_unused:UNUSED_PAD src0_sel:WORD_1
	v_cvt_f32_f16_e32 v132, v31
	v_sub_f32_e32 v28, v28, v0
	v_sub_f32_e32 v29, v128, v1
	v_sub_f32_e32 v30, v129, v2
	v_pk_mul_f32 v[28:29], v[88:89], v[28:29]
	v_sub_f32_e32 v128, v133, v0
	v_sub_f32_e32 v129, v130, v1
	v_sub_f32_e32 v31, v115, v3
	v_sub_f32_e32 v130, v132, v2
	v_sub_f32_e32 v131, v131, v3
	v_pk_mul_f32 v[128:129], v[88:89], v[128:129]
	s_waitcnt lgkmcnt(1)
	v_fma_f32 v28, v36, v28, v120
	v_fma_f32 v29, v37, v29, v121
	v_pk_mul_f32 v[30:31], v[90:91], v[30:31]
	v_pk_mul_f32 v[130:131], v[90:91], v[130:131]
	s_waitcnt lgkmcnt(0)
	v_fma_f32 v36, v116, v128, v124
	ds_write2_b32 v220, v28, v29 offset1:65
	v_fma_f32 v28, v117, v129, v125
	ds_write2_b32 v221, v36, v28 offset1:65
	v_fma_f32 v28, v38, v30, v122
	v_fma_f32 v29, v118, v130, v126
	v_fmac_f32_e32 v123, v39, v31
	v_fmac_f32_e32 v127, v119, v131
	ds_write2_b32 v220, v28, v123 offset0:130 offset1:195
	ds_write2_b32 v221, v29, v127 offset0:130 offset1:195
	s_waitcnt vmcnt(2)
	ds_write_b128 v96, v[24:27] offset:41984
	s_mov_b32 s16, 0
	v_mov_b32_e32 v24, v103
	s_waitcnt lgkmcnt(0)
	s_barrier
	ds_read_b32 v200, v218
	ds_read_b32 v208, v219
	ds_read_b32 v201, v218 offset:520
	ds_read_b32 v209, v219 offset:256
	ds_read_b32 v202, v218 offset:1040
	ds_read_b32 v210, v219 offset:512
	ds_read_b32 v203, v218 offset:1560
	ds_read_b32 v211, v219 offset:768
	ds_read_b32 v204, v218 offset:2080
	ds_read_b32 v212, v219 offset:1024
	ds_read_b32 v205, v218 offset:2600
	ds_read_b32 v213, v219 offset:1280
	ds_read_b32 v206, v218 offset:3120
	ds_read_b32 v214, v219 offset:1536
	s_waitcnt lgkmcnt(12)
	v_mfma_f32_32x32x2_f32 v[4:19], v200, v208, v[4:19]
	ds_read_b32 v207, v218 offset:3640
	ds_read_b32 v215, v219 offset:1792
	s_waitcnt lgkmcnt(12)
	v_mfma_f32_32x32x2_f32 v[4:19], v201, v209, v[4:19]
	s_waitcnt lgkmcnt(10)
	v_mfma_f32_32x32x2_f32 v[4:19], v202, v210, v[4:19]
	s_waitcnt lgkmcnt(8)
	v_mfma_f32_32x32x2_f32 v[4:19], v203, v211, v[4:19]
	s_waitcnt lgkmcnt(6)
	v_mfma_f32_32x32x2_f32 v[4:19], v204, v212, v[4:19]
	s_waitcnt lgkmcnt(4)
	v_mfma_f32_32x32x2_f32 v[4:19], v205, v213, v[4:19]
	s_waitcnt lgkmcnt(2)
	v_mfma_f32_32x32x2_f32 v[4:19], v206, v214, v[4:19]
	s_waitcnt lgkmcnt(0)
	v_mfma_f32_32x32x2_f32 v[4:19], v207, v215, v[4:19]
	s_barrier
	global_load_dwordx4 v[28:31], v[92:93], off offset:1536 sc1
	global_load_dwordx4 v[24:27], v[74:75], off
	s_waitcnt vmcnt(3)
	v_cvt_f32_f16_sdwa v128, v32 dst_sel:DWORD dst_unused:UNUSED_PAD src0_sel:WORD_1
	v_cvt_f32_f16_e32 v32, v32
	v_cvt_f32_f16_e32 v129, v33
	v_cvt_f32_f16_sdwa v130, v34 dst_sel:DWORD dst_unused:UNUSED_PAD src0_sel:WORD_1
	v_cvt_f32_f16_e32 v133, v34
	ds_read_b128 v[36:39], v43 offset:15104
	ds_read_b128 v[116:119], v43 offset:15120
	ds_read_b128 v[120:123], v43 offset:19200
	ds_read_b128 v[124:127], v43 offset:19216
	v_cvt_f32_f16_sdwa v115, v33 dst_sel:DWORD dst_unused:UNUSED_PAD src0_sel:WORD_1
	v_cvt_f32_f16_sdwa v131, v35 dst_sel:DWORD dst_unused:UNUSED_PAD src0_sel:WORD_1
	v_cvt_f32_f16_e32 v132, v35
	v_sub_f32_e32 v32, v32, v0
	v_sub_f32_e32 v33, v128, v1
	v_sub_f32_e32 v34, v129, v2
	v_pk_mul_f32 v[32:33], v[88:89], v[32:33]
	v_sub_f32_e32 v128, v133, v0
	v_sub_f32_e32 v129, v130, v1
	v_sub_f32_e32 v35, v115, v3
	v_sub_f32_e32 v130, v132, v2
	v_sub_f32_e32 v131, v131, v3
	v_pk_mul_f32 v[128:129], v[88:89], v[128:129]
	s_waitcnt lgkmcnt(1)
	v_fma_f32 v32, v36, v32, v120
	v_fma_f32 v33, v37, v33, v121
	v_pk_mul_f32 v[34:35], v[90:91], v[34:35]
	v_pk_mul_f32 v[130:131], v[90:91], v[130:131]
	s_waitcnt lgkmcnt(0)
	v_fma_f32 v36, v116, v128, v124
	ds_write2_b32 v220, v32, v33 offset1:65
	v_fma_f32 v32, v117, v129, v125
	ds_write2_b32 v221, v36, v32 offset1:65
	v_fma_f32 v32, v38, v34, v122
	v_fma_f32 v33, v118, v130, v126
	v_fmac_f32_e32 v123, v39, v35
	v_fmac_f32_e32 v127, v119, v131
	ds_write2_b32 v220, v32, v123 offset0:130 offset1:195
	ds_write2_b32 v221, v33, v127 offset0:130 offset1:195
	s_waitcnt vmcnt(2)
	ds_write_b128 v96, v[20:23] offset:41984
	s_mov_b32 s16, 0
	v_mov_b32_e32 v20, v103
	s_waitcnt lgkmcnt(0)
	s_barrier
	ds_read_b32 v200, v218
	ds_read_b32 v208, v219
	ds_read_b32 v201, v218 offset:520
	ds_read_b32 v209, v219 offset:256
	ds_read_b32 v202, v218 offset:1040
	ds_read_b32 v210, v219 offset:512
	ds_read_b32 v203, v218 offset:1560
	ds_read_b32 v211, v219 offset:768
	ds_read_b32 v204, v218 offset:2080
	ds_read_b32 v212, v219 offset:1024
	ds_read_b32 v205, v218 offset:2600
	ds_read_b32 v213, v219 offset:1280
	ds_read_b32 v206, v218 offset:3120
	ds_read_b32 v214, v219 offset:1536
	s_waitcnt lgkmcnt(12)
	v_mfma_f32_32x32x2_f32 v[4:19], v200, v208, v[4:19]
	ds_read_b32 v207, v218 offset:3640
	ds_read_b32 v215, v219 offset:1792
	s_waitcnt lgkmcnt(12)
	v_mfma_f32_32x32x2_f32 v[4:19], v201, v209, v[4:19]
	s_waitcnt lgkmcnt(10)
	v_mfma_f32_32x32x2_f32 v[4:19], v202, v210, v[4:19]
	s_waitcnt lgkmcnt(8)
	v_mfma_f32_32x32x2_f32 v[4:19], v203, v211, v[4:19]
	s_waitcnt lgkmcnt(6)
	v_mfma_f32_32x32x2_f32 v[4:19], v204, v212, v[4:19]
	s_waitcnt lgkmcnt(4)
	v_mfma_f32_32x32x2_f32 v[4:19], v205, v213, v[4:19]
	s_waitcnt lgkmcnt(2)
	v_mfma_f32_32x32x2_f32 v[4:19], v206, v214, v[4:19]
	s_waitcnt lgkmcnt(0)
	v_mfma_f32_32x32x2_f32 v[4:19], v207, v215, v[4:19]
	s_barrier
	global_load_dwordx4 v[32:35], v[92:93], off offset:1664 sc1
	global_load_dwordx4 v[20:23], v[76:77], off
	s_waitcnt vmcnt(3)
	v_cvt_f32_f16_sdwa v128, v28 dst_sel:DWORD dst_unused:UNUSED_PAD src0_sel:WORD_1
	v_cvt_f32_f16_e32 v28, v28
	v_cvt_f32_f16_e32 v129, v29
	v_cvt_f32_f16_sdwa v130, v30 dst_sel:DWORD dst_unused:UNUSED_PAD src0_sel:WORD_1
	v_cvt_f32_f16_e32 v133, v30
	ds_read_b128 v[36:39], v43 offset:15360
	ds_read_b128 v[116:119], v43 offset:15376
	ds_read_b128 v[120:123], v43 offset:19456
	ds_read_b128 v[124:127], v43 offset:19472
	v_cvt_f32_f16_sdwa v115, v29 dst_sel:DWORD dst_unused:UNUSED_PAD src0_sel:WORD_1
	v_cvt_f32_f16_sdwa v131, v31 dst_sel:DWORD dst_unused:UNUSED_PAD src0_sel:WORD_1
	v_cvt_f32_f16_e32 v132, v31
	v_sub_f32_e32 v28, v28, v0
	v_sub_f32_e32 v29, v128, v1
	v_sub_f32_e32 v30, v129, v2
	v_pk_mul_f32 v[28:29], v[88:89], v[28:29]
	v_sub_f32_e32 v128, v133, v0
	v_sub_f32_e32 v129, v130, v1
	v_sub_f32_e32 v31, v115, v3
	v_sub_f32_e32 v130, v132, v2
	v_sub_f32_e32 v131, v131, v3
	v_pk_mul_f32 v[128:129], v[88:89], v[128:129]
	s_waitcnt lgkmcnt(1)
	v_fma_f32 v28, v36, v28, v120
	v_fma_f32 v29, v37, v29, v121
	v_pk_mul_f32 v[30:31], v[90:91], v[30:31]
	v_pk_mul_f32 v[130:131], v[90:91], v[130:131]
	s_waitcnt lgkmcnt(0)
	v_fma_f32 v36, v116, v128, v124
	ds_write2_b32 v220, v28, v29 offset1:65
	v_fma_f32 v28, v117, v129, v125
	ds_write2_b32 v221, v36, v28 offset1:65
	v_fma_f32 v28, v38, v30, v122
	v_fma_f32 v29, v118, v130, v126
	v_fmac_f32_e32 v123, v39, v31
	v_fmac_f32_e32 v127, v119, v131
	ds_write2_b32 v220, v28, v123 offset0:130 offset1:195
	ds_write2_b32 v221, v29, v127 offset0:130 offset1:195
	s_waitcnt vmcnt(2)
	ds_write_b128 v96, v[24:27] offset:41984
	s_mov_b32 s16, 0
	v_mov_b32_e32 v24, v103
	s_waitcnt lgkmcnt(0)
	s_barrier
	ds_read_b32 v200, v218
	ds_read_b32 v208, v219
	ds_read_b32 v201, v218 offset:520
	ds_read_b32 v209, v219 offset:256
	ds_read_b32 v202, v218 offset:1040
	ds_read_b32 v210, v219 offset:512
	ds_read_b32 v203, v218 offset:1560
	ds_read_b32 v211, v219 offset:768
	ds_read_b32 v204, v218 offset:2080
	ds_read_b32 v212, v219 offset:1024
	ds_read_b32 v205, v218 offset:2600
	ds_read_b32 v213, v219 offset:1280
	ds_read_b32 v206, v218 offset:3120
	ds_read_b32 v214, v219 offset:1536
	s_waitcnt lgkmcnt(12)
	v_mfma_f32_32x32x2_f32 v[4:19], v200, v208, v[4:19]
	ds_read_b32 v207, v218 offset:3640
	ds_read_b32 v215, v219 offset:1792
	s_waitcnt lgkmcnt(12)
	v_mfma_f32_32x32x2_f32 v[4:19], v201, v209, v[4:19]
	s_waitcnt lgkmcnt(10)
	v_mfma_f32_32x32x2_f32 v[4:19], v202, v210, v[4:19]
	s_waitcnt lgkmcnt(8)
	v_mfma_f32_32x32x2_f32 v[4:19], v203, v211, v[4:19]
	s_waitcnt lgkmcnt(6)
	v_mfma_f32_32x32x2_f32 v[4:19], v204, v212, v[4:19]
	s_waitcnt lgkmcnt(4)
	v_mfma_f32_32x32x2_f32 v[4:19], v205, v213, v[4:19]
	s_waitcnt lgkmcnt(2)
	v_mfma_f32_32x32x2_f32 v[4:19], v206, v214, v[4:19]
	s_waitcnt lgkmcnt(0)
	v_mfma_f32_32x32x2_f32 v[4:19], v207, v215, v[4:19]
	s_barrier
	global_load_dwordx4 v[28:31], v[92:93], off offset:1792 sc1
	global_load_dwordx4 v[24:27], v[78:79], off
	s_waitcnt vmcnt(3)
	v_cvt_f32_f16_sdwa v128, v32 dst_sel:DWORD dst_unused:UNUSED_PAD src0_sel:WORD_1
	v_cvt_f32_f16_e32 v32, v32
	v_cvt_f32_f16_e32 v129, v33
	v_cvt_f32_f16_sdwa v130, v34 dst_sel:DWORD dst_unused:UNUSED_PAD src0_sel:WORD_1
	v_cvt_f32_f16_e32 v133, v34
	ds_read_b128 v[36:39], v43 offset:15616
	ds_read_b128 v[116:119], v43 offset:15632
	ds_read_b128 v[120:123], v43 offset:19712
	ds_read_b128 v[124:127], v43 offset:19728
	v_cvt_f32_f16_sdwa v115, v33 dst_sel:DWORD dst_unused:UNUSED_PAD src0_sel:WORD_1
	v_cvt_f32_f16_sdwa v131, v35 dst_sel:DWORD dst_unused:UNUSED_PAD src0_sel:WORD_1
	v_cvt_f32_f16_e32 v132, v35
	v_sub_f32_e32 v32, v32, v0
	v_sub_f32_e32 v33, v128, v1
	v_sub_f32_e32 v34, v129, v2
	v_pk_mul_f32 v[32:33], v[88:89], v[32:33]
	v_sub_f32_e32 v128, v133, v0
	v_sub_f32_e32 v129, v130, v1
	v_sub_f32_e32 v35, v115, v3
	v_sub_f32_e32 v130, v132, v2
	v_sub_f32_e32 v131, v131, v3
	v_pk_mul_f32 v[128:129], v[88:89], v[128:129]
	s_waitcnt lgkmcnt(1)
	v_fma_f32 v32, v36, v32, v120
	v_fma_f32 v33, v37, v33, v121
	v_pk_mul_f32 v[34:35], v[90:91], v[34:35]
	v_pk_mul_f32 v[130:131], v[90:91], v[130:131]
	s_waitcnt lgkmcnt(0)
	v_fma_f32 v36, v116, v128, v124
	ds_write2_b32 v220, v32, v33 offset1:65
	v_fma_f32 v32, v117, v129, v125
	ds_write2_b32 v221, v36, v32 offset1:65
	v_fma_f32 v32, v38, v34, v122
	v_fma_f32 v33, v118, v130, v126
	v_fmac_f32_e32 v123, v39, v35
	v_fmac_f32_e32 v127, v119, v131
	ds_write2_b32 v220, v32, v123 offset0:130 offset1:195
	ds_write2_b32 v221, v33, v127 offset0:130 offset1:195
	s_waitcnt vmcnt(2)
	ds_write_b128 v96, v[20:23] offset:41984
	s_mov_b32 s16, 0
	v_mov_b32_e32 v20, v103
	s_waitcnt lgkmcnt(0)
	s_barrier
	ds_read_b32 v200, v218
	ds_read_b32 v208, v219
	ds_read_b32 v201, v218 offset:520
	ds_read_b32 v209, v219 offset:256
	ds_read_b32 v202, v218 offset:1040
	ds_read_b32 v210, v219 offset:512
	ds_read_b32 v203, v218 offset:1560
	ds_read_b32 v211, v219 offset:768
	ds_read_b32 v204, v218 offset:2080
	ds_read_b32 v212, v219 offset:1024
	ds_read_b32 v205, v218 offset:2600
	ds_read_b32 v213, v219 offset:1280
	ds_read_b32 v206, v218 offset:3120
	ds_read_b32 v214, v219 offset:1536
	s_waitcnt lgkmcnt(12)
	v_mfma_f32_32x32x2_f32 v[4:19], v200, v208, v[4:19]
	ds_read_b32 v207, v218 offset:3640
	ds_read_b32 v215, v219 offset:1792
	s_waitcnt lgkmcnt(12)
	v_mfma_f32_32x32x2_f32 v[4:19], v201, v209, v[4:19]
	s_waitcnt lgkmcnt(10)
	v_mfma_f32_32x32x2_f32 v[4:19], v202, v210, v[4:19]
	s_waitcnt lgkmcnt(8)
	v_mfma_f32_32x32x2_f32 v[4:19], v203, v211, v[4:19]
	s_waitcnt lgkmcnt(6)
	v_mfma_f32_32x32x2_f32 v[4:19], v204, v212, v[4:19]
	s_waitcnt lgkmcnt(4)
	v_mfma_f32_32x32x2_f32 v[4:19], v205, v213, v[4:19]
	s_waitcnt lgkmcnt(2)
	v_mfma_f32_32x32x2_f32 v[4:19], v206, v214, v[4:19]
	s_waitcnt lgkmcnt(0)
	v_mfma_f32_32x32x2_f32 v[4:19], v207, v215, v[4:19]
	s_barrier
	global_load_dwordx4 v[32:35], v[92:93], off offset:1920 sc1
	global_load_dwordx4 v[20:23], v[80:81], off
	s_waitcnt vmcnt(3)
	v_cvt_f32_f16_sdwa v93, v28 dst_sel:DWORD dst_unused:UNUSED_PAD src0_sel:WORD_1
	v_cvt_f32_f16_e32 v28, v28
	v_cvt_f32_f16_sdwa v92, v29 dst_sel:DWORD dst_unused:UNUSED_PAD src0_sel:WORD_1
	v_cvt_f32_f16_sdwa v128, v30 dst_sel:DWORD dst_unused:UNUSED_PAD src0_sel:WORD_1
	v_cvt_f32_f16_e32 v131, v30
	ds_read_b128 v[36:39], v43 offset:15872
	ds_read_b128 v[116:119], v43 offset:15888
	ds_read_b128 v[120:123], v43 offset:19968
	ds_read_b128 v[124:127], v43 offset:19984
	v_cvt_f32_f16_e32 v115, v29
	v_cvt_f32_f16_sdwa v129, v31 dst_sel:DWORD dst_unused:UNUSED_PAD src0_sel:WORD_1
	v_cvt_f32_f16_e32 v130, v31
	v_sub_f32_e32 v28, v28, v0
	v_sub_f32_e32 v29, v93, v1
	v_sub_f32_e32 v31, v92, v3
	v_pk_mul_f32 v[28:29], v[88:89], v[28:29]
	v_sub_f32_e32 v92, v131, v0
	v_sub_f32_e32 v93, v128, v1
	v_sub_f32_e32 v30, v115, v2
	v_sub_f32_e32 v128, v130, v2
	v_sub_f32_e32 v129, v129, v3
	v_pk_mul_f32 v[92:93], v[88:89], v[92:93]
	s_waitcnt lgkmcnt(1)
	v_fma_f32 v28, v36, v28, v120
	v_fma_f32 v29, v37, v29, v121
	v_pk_mul_f32 v[30:31], v[90:91], v[30:31]
	v_pk_mul_f32 v[128:129], v[90:91], v[128:129]
	s_waitcnt lgkmcnt(0)
	v_fma_f32 v36, v116, v92, v124
	ds_write2_b32 v220, v28, v29 offset1:65
	v_fma_f32 v28, v117, v93, v125
	ds_write2_b32 v221, v36, v28 offset1:65
	v_fma_f32 v28, v38, v30, v122
	v_fma_f32 v29, v118, v128, v126
	v_fmac_f32_e32 v123, v39, v31
	v_fmac_f32_e32 v127, v119, v129
	ds_write2_b32 v220, v28, v123 offset0:130 offset1:195
	ds_write2_b32 v221, v29, v127 offset0:130 offset1:195
	s_waitcnt vmcnt(2)
	ds_write_b128 v96, v[24:27] offset:41984
	s_mov_b32 s16, 0
	v_mov_b32_e32 v24, v103
	s_waitcnt lgkmcnt(0)
	s_barrier
	ds_read_b32 v200, v218
	ds_read_b32 v208, v219
	ds_read_b32 v201, v218 offset:520
	ds_read_b32 v209, v219 offset:256
	ds_read_b32 v202, v218 offset:1040
	ds_read_b32 v210, v219 offset:512
	ds_read_b32 v203, v218 offset:1560
	ds_read_b32 v211, v219 offset:768
	ds_read_b32 v204, v218 offset:2080
	ds_read_b32 v212, v219 offset:1024
	ds_read_b32 v205, v218 offset:2600
	ds_read_b32 v213, v219 offset:1280
	ds_read_b32 v206, v218 offset:3120
	ds_read_b32 v214, v219 offset:1536
	s_waitcnt lgkmcnt(12)
	v_mfma_f32_32x32x2_f32 v[4:19], v200, v208, v[4:19]
	ds_read_b32 v207, v218 offset:3640
	ds_read_b32 v215, v219 offset:1792
	s_waitcnt lgkmcnt(12)
	v_mfma_f32_32x32x2_f32 v[4:19], v201, v209, v[4:19]
	s_waitcnt lgkmcnt(10)
	v_mfma_f32_32x32x2_f32 v[4:19], v202, v210, v[4:19]
	s_waitcnt lgkmcnt(8)
	v_mfma_f32_32x32x2_f32 v[4:19], v203, v211, v[4:19]
	s_waitcnt lgkmcnt(6)
	v_mfma_f32_32x32x2_f32 v[4:19], v204, v212, v[4:19]
	s_waitcnt lgkmcnt(4)
	v_mfma_f32_32x32x2_f32 v[4:19], v205, v213, v[4:19]
	s_waitcnt lgkmcnt(2)
	v_mfma_f32_32x32x2_f32 v[4:19], v206, v214, v[4:19]
	s_waitcnt lgkmcnt(0)
	v_mfma_f32_32x32x2_f32 v[4:19], v207, v215, v[4:19]
	s_waitcnt vmcnt(1)
	v_cvt_f32_f16_sdwa v93, v32 dst_sel:DWORD dst_unused:UNUSED_PAD src0_sel:WORD_1
	v_cvt_f32_f16_e32 v32, v32
	v_cvt_f32_f16_sdwa v121, v34 dst_sel:DWORD dst_unused:UNUSED_PAD src0_sel:WORD_1
	v_cvt_f32_f16_e32 v123, v34
	s_barrier
	ds_read_b128 v[24:27], v43 offset:16128
	ds_read_b128 v[28:31], v43 offset:16144
	ds_read_b128 v[36:39], v43 offset:20224
	ds_read_b128 v[116:119], v43 offset:20240
	v_cvt_f32_f16_sdwa v92, v33 dst_sel:DWORD dst_unused:UNUSED_PAD src0_sel:WORD_1
	v_cvt_f32_f16_e32 v115, v33
	v_cvt_f32_f16_sdwa v120, v35 dst_sel:DWORD dst_unused:UNUSED_PAD src0_sel:WORD_1
	v_cvt_f32_f16_e32 v122, v35
	v_sub_f32_e32 v32, v32, v0
	v_sub_f32_e32 v33, v93, v1
	v_sub_f32_e32 v0, v123, v0
	v_sub_f32_e32 v1, v121, v1
	v_sub_f32_e32 v34, v115, v2
	v_sub_f32_e32 v35, v92, v3
	v_pk_mul_f32 v[0:1], v[88:89], v[0:1]
	v_pk_mul_f32 v[34:35], v[90:91], v[34:35]
	v_sub_f32_e32 v2, v122, v2
	v_sub_f32_e32 v3, v120, v3
	s_waitcnt lgkmcnt(0)
	v_fma_f32 v0, v28, v0, v116
	v_fma_f32 v1, v29, v1, v117
	v_pk_mul_f32 v[32:33], v[88:89], v[32:33]
	v_pk_mul_f32 v[2:3], v[90:91], v[2:3]
	ds_write2_b32 v221, v0, v1 offset1:65
	v_fma_f32 v0, v26, v34, v38
	v_fmac_f32_e32 v39, v27, v35
	v_fma_f32 v24, v24, v32, v36
	v_fma_f32 v25, v25, v33, v37
	v_fma_f32 v1, v30, v2, v118
	ds_write2_b32 v220, v0, v39 offset0:130 offset1:195
	v_fmac_f32_e32 v119, v31, v3
	s_mov_b32 s16, 0
	v_mov_b32_e32 v0, v103
	ds_write2_b32 v220, v24, v25 offset1:65
	ds_write2_b32 v221, v1, v119 offset0:130 offset1:195
	s_waitcnt vmcnt(0)
	ds_write_b128 v96, v[20:23] offset:41984
	s_waitcnt lgkmcnt(0)
	s_barrier
	ds_read_b32 v200, v218
	ds_read_b32 v208, v219
	ds_read_b32 v201, v218 offset:520
	ds_read_b32 v209, v219 offset:256
	ds_read_b32 v202, v218 offset:1040
	ds_read_b32 v210, v219 offset:512
	ds_read_b32 v203, v218 offset:1560
	ds_read_b32 v211, v219 offset:768
	ds_read_b32 v204, v218 offset:2080
	ds_read_b32 v212, v219 offset:1024
	ds_read_b32 v205, v218 offset:2600
	ds_read_b32 v213, v219 offset:1280
	ds_read_b32 v206, v218 offset:3120
	ds_read_b32 v214, v219 offset:1536
	s_waitcnt lgkmcnt(12)
	v_mfma_f32_32x32x2_f32 v[4:19], v200, v208, v[4:19]
	ds_read_b32 v207, v218 offset:3640
	ds_read_b32 v215, v219 offset:1792
	s_waitcnt lgkmcnt(12)
	v_mfma_f32_32x32x2_f32 v[4:19], v201, v209, v[4:19]
	s_waitcnt lgkmcnt(10)
	v_mfma_f32_32x32x2_f32 v[4:19], v202, v210, v[4:19]
	s_waitcnt lgkmcnt(8)
	v_mfma_f32_32x32x2_f32 v[4:19], v203, v211, v[4:19]
	s_waitcnt lgkmcnt(6)
	v_mfma_f32_32x32x2_f32 v[4:19], v204, v212, v[4:19]
	s_waitcnt lgkmcnt(4)
	v_mfma_f32_32x32x2_f32 v[4:19], v205, v213, v[4:19]
	s_waitcnt lgkmcnt(2)
	v_mfma_f32_32x32x2_f32 v[4:19], v206, v214, v[4:19]
	s_waitcnt lgkmcnt(0)
	v_mfma_f32_32x32x2_f32 v[4:19], v207, v215, v[4:19]
	s_barrier
	s_nop 15
	s_nop 3
	ds_write_b32 v217, v4 offset:58752
	ds_write_b32 v217, v5 offset:58880
	ds_write_b32 v217, v6 offset:59008
	ds_write_b32 v217, v7 offset:59136
	ds_write_b32 v217, v8 offset:59776
	ds_write_b32 v217, v9 offset:59904
	ds_write_b32 v217, v10 offset:60032
	ds_write_b32 v217, v11 offset:60160
	ds_write_b32 v217, v12 offset:60800
	ds_write_b32 v217, v13 offset:60928
	ds_write_b32 v217, v14 offset:61056
	ds_write_b32 v217, v15 offset:61184
	ds_write_b32 v217, v16 offset:61824
	ds_write_b32 v217, v17 offset:61952
	ds_write_b32 v217, v18 offset:62080
	ds_write_b32 v217, v19 offset:62208
	s_waitcnt lgkmcnt(0)
	s_barrier
	global_load_dwordx4 v[0:3], v[50:51], off offset:384
	ds_read_b128 v[4:7], v98 offset:58752
	ds_read_b128 v[8:11], v99 offset:8192
	ds_read_b128 v[12:15], v99 offset:16384
	ds_read_b128 v[16:19], v99 offset:24576
	v_add_u32_e32 v20, 0xc400, v100
	v_add_u32_e32 v21, 0xc408, v100
	s_waitcnt lgkmcnt(2)
	v_pk_add_f32 v[4:5], v[4:5], v[8:9]
	v_pk_add_f32 v[6:7], v[6:7], v[10:11]
	s_waitcnt lgkmcnt(1)
	v_pk_add_f32 v[4:5], v[12:13], v[4:5]
	v_pk_add_f32 v[6:7], v[14:15], v[6:7]
	s_waitcnt lgkmcnt(0)
	v_pk_add_f32 v[4:5], v[16:17], v[4:5]
	v_pk_add_f32 v[6:7], v[18:19], v[6:7]
	s_waitcnt vmcnt(0)
	v_pk_add_f32 v[0:1], v[0:1], v[4:5]
	v_pk_add_f32 v[2:3], v[6:7], v[2:3]
	ds_write2_b32 v20, v0, v1 offset1:1
	ds_write2_b32 v21, v2, v3 offset1:1
	s_waitcnt lgkmcnt(0)
	s_barrier
	s_and_saveexec_b64 s[36:37], s[6:7]
	s_cbranch_execz .LBB0_3365
	v_add_u32_e32 v0, 0xc400, v108
	v_add_u32_e32 v1, 0xc408, v108
	v_add_u32_e32 v2, 0xc410, v108
	v_add_u32_e32 v3, 0xc418, v108
	ds_read2_b32 v[34:35], v0 offset1:1
	ds_read2_b32 v[28:29], v1 offset1:1
	ds_read2_b32 v[18:19], v2 offset1:1
	ds_read2_b32 v[8:9], v3 offset1:1
	s_mov_b32 s16, 0xff61b1e6
	s_waitcnt lgkmcnt(3)
	v_max_f32_e32 v0, v34, v34
	v_max_f32_e32 v0, 0xff61b1e6, v0
	v_cmp_lt_f32_e32 vcc, s16, v34
	v_cmp_gt_f32_e64 s[16:17], v35, v0
	v_add_u32_e32 v2, 0xc420, v108
	ds_read2_b32 v[20:21], v2 offset1:1
	v_cndmask_b32_e64 v0, v0, v35, s[16:17]
	v_cndmask_b32_e64 v1, 0, 1, s[16:17]
	s_waitcnt lgkmcnt(3)
	v_cmp_gt_f32_e64 s[16:17], v28, v0
	v_add_u32_e32 v2, 0xc428, v108
	v_add_u32_e32 v4, 0xc438, v108
	v_cndmask_b32_e64 v0, v0, v28, s[16:17]
	v_cndmask_b32_e64 v1, v1, 2, s[16:17]
	v_cmp_gt_f32_e64 s[16:17], v29, v0
	v_add_u32_e32 v3, 0xc430, v108
	ds_read2_b32 v[30:31], v2 offset1:1
	ds_read2_b32 v[16:17], v3 offset1:1
	ds_read2_b32 v[4:5], v4 offset1:1
	v_cndmask_b32_e64 v0, v0, v29, s[16:17]
	v_cndmask_b32_e64 v1, v1, 3, s[16:17]
	s_waitcnt lgkmcnt(5)
	v_cmp_gt_f32_e64 s[16:17], v18, v0
	v_add_u32_e32 v2, 0xc440, v108
	ds_read2_b32 v[12:13], v2 offset1:1
	v_cndmask_b32_e64 v0, v0, v18, s[16:17]
	v_cndmask_b32_e64 v1, v1, 4, s[16:17]
	v_cmp_gt_f32_e64 s[16:17], v19, v0
	v_add_u32_e32 v2, 0xc448, v108
	v_add_u32_e32 v6, 0xc458, v108
	v_cndmask_b32_e64 v0, v0, v19, s[16:17]
	v_cndmask_b32_e64 v1, v1, 5, s[16:17]
	s_waitcnt lgkmcnt(5)
	v_cmp_gt_f32_e64 s[16:17], v8, v0
	v_add_u32_e32 v3, 0xc450, v108
	ds_read2_b32 v[26:27], v2 offset1:1
	ds_read2_b32 v[14:15], v3 offset1:1
	ds_read2_b32 v[6:7], v6 offset1:1
	v_cndmask_b32_e64 v0, v0, v8, s[16:17]
	v_cndmask_b32_e64 v1, v1, 6, s[16:17]
	v_cmp_gt_f32_e64 s[16:17], v9, v0
	v_add_u32_e32 v2, 0xc460, v108
	ds_read2_b32 v[22:23], v2 offset1:1
	v_cndmask_b32_e64 v0, v0, v9, s[16:17]
	v_cndmask_b32_e64 v1, v1, 7, s[16:17]
	s_waitcnt lgkmcnt(8)
	v_cmp_gt_f32_e64 s[16:17], v20, v0
	v_add_u32_e32 v2, 0xc468, v108
	v_add_u32_e32 v10, 0xc478, v108
	v_cndmask_b32_e64 v0, v0, v20, s[16:17]
	v_cndmask_b32_e64 v1, v1, 8, s[16:17]
	v_cmp_gt_f32_e64 s[16:17], v21, v0
	v_add_u32_e32 v3, 0xc470, v108
	ds_read2_b32 v[32:33], v2 offset1:1
	ds_read2_b32 v[24:25], v3 offset1:1
	ds_read2_b32 v[10:11], v10 offset1:1
	v_cndmask_b32_e64 v0, v0, v21, s[16:17]
	v_cndmask_b32_e64 v1, v1, 9, s[16:17]
	s_waitcnt lgkmcnt(10)
	v_cmp_gt_f32_e64 s[16:17], v30, v0
	s_nop 1
	v_cndmask_b32_e64 v0, v0, v30, s[16:17]
	v_cndmask_b32_e64 v1, v1, 10, s[16:17]
	v_cmp_gt_f32_e64 s[16:17], v31, v0
	s_nop 1
	v_cndmask_b32_e64 v0, v0, v31, s[16:17]
	v_cndmask_b32_e64 v1, v1, 11, s[16:17]
	s_waitcnt lgkmcnt(9)
	v_cmp_gt_f32_e64 s[16:17], v16, v0
	s_nop 1
	v_cndmask_b32_e64 v0, v0, v16, s[16:17]
	v_cndmask_b32_e64 v1, v1, 12, s[16:17]
	v_cmp_gt_f32_e64 s[16:17], v17, v0
	s_nop 1
	v_cndmask_b32_e64 v0, v0, v17, s[16:17]
	v_cndmask_b32_e64 v1, v1, 13, s[16:17]
	s_waitcnt lgkmcnt(8)
	v_cmp_gt_f32_e64 s[16:17], v4, v0
	s_nop 1
	v_cndmask_b32_e64 v0, v0, v4, s[16:17]
	v_cndmask_b32_e64 v1, v1, 14, s[16:17]
	v_cmp_gt_f32_e64 s[16:17], v5, v0
	s_nop 1
	v_cndmask_b32_e64 v0, v0, v5, s[16:17]
	v_cndmask_b32_e64 v1, v1, 15, s[16:17]
	s_waitcnt lgkmcnt(7)
	v_cmp_gt_f32_e64 s[16:17], v12, v0
	s_nop 1
	v_cndmask_b32_e64 v0, v0, v12, s[16:17]
	v_cndmask_b32_e64 v1, v1, 16, s[16:17]
	v_cmp_gt_f32_e64 s[16:17], v13, v0
	s_nop 1
	v_cndmask_b32_e64 v0, v0, v13, s[16:17]
	v_cndmask_b32_e64 v1, v1, 17, s[16:17]
	s_waitcnt lgkmcnt(6)
	v_cmp_gt_f32_e64 s[16:17], v26, v0
	s_nop 1
	v_cndmask_b32_e64 v0, v0, v26, s[16:17]
	v_cndmask_b32_e64 v1, v1, 18, s[16:17]
	v_cmp_gt_f32_e64 s[16:17], v27, v0
	s_nop 1
	v_cndmask_b32_e64 v0, v0, v27, s[16:17]
	v_cndmask_b32_e64 v1, v1, 19, s[16:17]
	s_waitcnt lgkmcnt(5)
	v_cmp_gt_f32_e64 s[16:17], v14, v0
	s_nop 1
	v_cndmask_b32_e64 v0, v0, v14, s[16:17]
	v_cndmask_b32_e64 v1, v1, 20, s[16:17]
	v_cmp_gt_f32_e64 s[16:17], v15, v0
	s_nop 1
	v_cndmask_b32_e64 v0, v0, v15, s[16:17]
	v_cndmask_b32_e64 v1, v1, 21, s[16:17]
	s_waitcnt lgkmcnt(4)
	v_cmp_gt_f32_e64 s[16:17], v6, v0
	s_nop 1
	v_cndmask_b32_e64 v0, v0, v6, s[16:17]
	v_cndmask_b32_e64 v1, v1, 22, s[16:17]
	v_cmp_gt_f32_e64 s[16:17], v7, v0
	s_nop 1
	v_cndmask_b32_e64 v0, v0, v7, s[16:17]
	v_cndmask_b32_e64 v1, v1, 23, s[16:17]
	s_waitcnt lgkmcnt(3)
	v_cmp_gt_f32_e64 s[16:17], v22, v0
	s_nop 1
	v_cndmask_b32_e64 v0, v0, v22, s[16:17]
	v_cndmask_b32_e64 v1, v1, 24, s[16:17]
	v_cmp_gt_f32_e64 s[16:17], v23, v0
	s_nop 1
	v_cndmask_b32_e64 v0, v0, v23, s[16:17]
	v_cndmask_b32_e64 v1, v1, 25, s[16:17]
	s_waitcnt lgkmcnt(2)
	v_cmp_gt_f32_e64 s[16:17], v32, v0
	s_nop 1
	v_cndmask_b32_e64 v0, v0, v32, s[16:17]
	v_cndmask_b32_e64 v1, v1, 26, s[16:17]
	v_cmp_gt_f32_e64 s[16:17], v33, v0
	s_nop 1
	v_cndmask_b32_e64 v0, v0, v33, s[16:17]
	v_cndmask_b32_e64 v1, v1, 27, s[16:17]
	s_waitcnt lgkmcnt(1)
	v_cmp_gt_f32_e64 s[16:17], v24, v0
	s_nop 1
	v_cndmask_b32_e64 v0, v0, v24, s[16:17]
	v_cndmask_b32_e64 v1, v1, 28, s[16:17]
	v_cmp_gt_f32_e64 s[16:17], v25, v0
	s_nop 1
	v_cndmask_b32_e64 v0, v0, v25, s[16:17]
	v_cndmask_b32_e64 v1, v1, 29, s[16:17]
	s_waitcnt lgkmcnt(0)
	v_cmp_gt_f32_e64 s[16:17], v10, v0
	s_nop 1
	v_cndmask_b32_e64 v0, v0, v10, s[16:17]
	v_cndmask_b32_e64 v1, v1, 30, s[16:17]
	v_cmp_gt_f32_e64 s[16:17], v11, v0
	s_nop 1
	v_cndmask_b32_e64 v36, v0, v11, s[16:17]
	v_cndmask_b32_e64 v0, v1, 31, s[16:17]
	v_cmp_ne_u32_e64 s[16:17], 0, v0
	v_lshlrev_b32_e64 v2, v0, 1
	s_and_b64 s[16:17], s[16:17], vcc
	v_cndmask_b32_e64 v1, v112, v34, s[16:17]
	v_and_b32_e32 v3, 2, v2
	v_cmp_eq_u32_e64 s[16:17], 0, v3
	v_cmp_gt_f32_e64 s[18:19], v35, v1
	s_and_b64 s[16:17], s[16:17], s[18:19]
	v_cndmask_b32_e64 v1, v1, v35, s[16:17]
	v_and_b32_e32 v37, 4, v2
	v_cndmask_b32_e64 v3, 0, 1, s[16:17]
	v_cmp_eq_u32_e64 s[16:17], 0, v37
	v_cmp_gt_f32_e64 s[18:19], v28, v1
	s_and_b64 s[16:17], s[16:17], s[18:19]
	v_cndmask_b32_e64 v1, v1, v28, s[16:17]
	v_and_b32_e32 v37, 8, v2
	v_cndmask_b32_e64 v3, v3, 2, s[16:17]
	v_cmp_eq_u32_e64 s[16:17], 0, v37
	v_cmp_gt_f32_e64 s[18:19], v29, v1
	s_and_b64 s[16:17], s[16:17], s[18:19]
	v_cndmask_b32_e64 v1, v1, v29, s[16:17]
	v_and_b32_e32 v37, 16, v2
	v_cndmask_b32_e64 v3, v3, 3, s[16:17]
	v_cmp_eq_u32_e64 s[16:17], 0, v37
	v_cmp_gt_f32_e64 s[18:19], v18, v1
	s_and_b64 s[16:17], s[16:17], s[18:19]
	v_cndmask_b32_e64 v1, v1, v18, s[16:17]
	v_and_b32_e32 v37, 32, v2
	v_cndmask_b32_e64 v3, v3, 4, s[16:17]
	v_cmp_eq_u32_e64 s[16:17], 0, v37
	v_cmp_gt_f32_e64 s[18:19], v19, v1
	s_and_b64 s[16:17], s[16:17], s[18:19]
	v_cndmask_b32_e64 v1, v1, v19, s[16:17]
	v_and_b32_e32 v37, 64, v2
	v_cndmask_b32_e64 v3, v3, 5, s[16:17]
	v_cmp_eq_u32_e64 s[16:17], 0, v37
	v_cmp_gt_f32_e64 s[18:19], v8, v1
	s_and_b64 s[16:17], s[16:17], s[18:19]
	v_cndmask_b32_e64 v1, v1, v8, s[16:17]
	v_and_b32_e32 v37, 0x80, v2
	v_cndmask_b32_e64 v3, v3, 6, s[16:17]
	v_cmp_eq_u32_e64 s[16:17], 0, v37
	v_cmp_gt_f32_e64 s[18:19], v9, v1
	s_and_b64 s[16:17], s[16:17], s[18:19]
	v_cndmask_b32_e64 v1, v1, v9, s[16:17]
	v_and_b32_e32 v37, 0x100, v2
	v_cndmask_b32_e64 v3, v3, 7, s[16:17]
	v_cmp_eq_u32_e64 s[16:17], 0, v37
	v_cmp_gt_f32_e64 s[18:19], v20, v1
	s_and_b64 s[16:17], s[16:17], s[18:19]
	v_cndmask_b32_e64 v1, v1, v20, s[16:17]
	v_and_b32_e32 v37, 0x200, v2
	v_cndmask_b32_e64 v3, v3, 8, s[16:17]
	v_cmp_eq_u32_e64 s[16:17], 0, v37
	v_cmp_gt_f32_e64 s[18:19], v21, v1
	s_and_b64 s[16:17], s[16:17], s[18:19]
	v_cndmask_b32_e64 v1, v1, v21, s[16:17]
	v_and_b32_e32 v37, 0x400, v2
	v_cndmask_b32_e64 v3, v3, 9, s[16:17]
	v_cmp_eq_u32_e64 s[16:17], 0, v37
	v_cmp_gt_f32_e64 s[18:19], v30, v1
	s_and_b64 s[16:17], s[16:17], s[18:19]
	v_cndmask_b32_e64 v1, v1, v30, s[16:17]
	v_and_b32_e32 v37, 0x800, v2
	v_cndmask_b32_e64 v3, v3, 10, s[16:17]
	v_cmp_eq_u32_e64 s[16:17], 0, v37
	v_cmp_gt_f32_e64 s[18:19], v31, v1
	s_and_b64 s[16:17], s[16:17], s[18:19]
	v_cndmask_b32_e64 v1, v1, v31, s[16:17]
	v_and_b32_e32 v37, 0x1000, v2
	v_cndmask_b32_e64 v3, v3, 11, s[16:17]
	v_cmp_eq_u32_e64 s[16:17], 0, v37
	v_cmp_gt_f32_e64 s[18:19], v16, v1
	s_and_b64 s[16:17], s[16:17], s[18:19]
	v_cndmask_b32_e64 v1, v1, v16, s[16:17]
	v_and_b32_e32 v37, 0x2000, v2
	v_cndmask_b32_e64 v3, v3, 12, s[16:17]
	v_cmp_eq_u32_e64 s[16:17], 0, v37
	v_cmp_gt_f32_e64 s[18:19], v17, v1
	s_and_b64 s[16:17], s[16:17], s[18:19]
	v_cndmask_b32_e64 v1, v1, v17, s[16:17]
	v_and_b32_e32 v37, 0x4000, v2
	v_cndmask_b32_e64 v3, v3, 13, s[16:17]
	v_cmp_eq_u32_e64 s[16:17], 0, v37
	v_cmp_gt_f32_e64 s[18:19], v4, v1
	s_and_b64 s[16:17], s[16:17], s[18:19]
	v_cndmask_b32_e64 v1, v1, v4, s[16:17]
	v_and_b32_e32 v37, 0x8000, v2
	v_cndmask_b32_e64 v3, v3, 14, s[16:17]
	v_cmp_eq_u32_e64 s[16:17], 0, v37
	v_cmp_gt_f32_e64 s[18:19], v5, v1
	s_and_b64 s[16:17], s[16:17], s[18:19]
	v_cndmask_b32_e64 v1, v1, v5, s[16:17]
	v_and_b32_e32 v37, 0x10000, v2
	v_cndmask_b32_e64 v3, v3, 15, s[16:17]
	v_cmp_eq_u32_e64 s[16:17], 0, v37
	v_cmp_gt_f32_e64 s[18:19], v12, v1
	s_and_b64 s[16:17], s[16:17], s[18:19]
	v_cndmask_b32_e64 v1, v1, v12, s[16:17]
	v_and_b32_e32 v37, 0x20000, v2
	v_cndmask_b32_e64 v3, v3, 16, s[16:17]
	v_cmp_eq_u32_e64 s[16:17], 0, v37
	v_cmp_gt_f32_e64 s[18:19], v13, v1
	s_and_b64 s[16:17], s[16:17], s[18:19]
	v_cndmask_b32_e64 v1, v1, v13, s[16:17]
	v_and_b32_e32 v37, 0x40000, v2
	v_cndmask_b32_e64 v3, v3, 17, s[16:17]
	v_cmp_eq_u32_e64 s[16:17], 0, v37
	v_cmp_gt_f32_e64 s[18:19], v26, v1
	s_and_b64 s[16:17], s[16:17], s[18:19]
	v_cndmask_b32_e64 v1, v1, v26, s[16:17]
	v_and_b32_e32 v37, 0x80000, v2
	v_cndmask_b32_e64 v3, v3, 18, s[16:17]
	v_cmp_eq_u32_e64 s[16:17], 0, v37
	v_cmp_gt_f32_e64 s[18:19], v27, v1
	s_and_b64 s[16:17], s[16:17], s[18:19]
	v_cndmask_b32_e64 v1, v1, v27, s[16:17]
	v_and_b32_e32 v37, 0x100000, v2
	v_cndmask_b32_e64 v3, v3, 19, s[16:17]
	v_cmp_eq_u32_e64 s[16:17], 0, v37
	v_cmp_gt_f32_e64 s[18:19], v14, v1
	s_and_b64 s[16:17], s[16:17], s[18:19]
	v_cndmask_b32_e64 v1, v1, v14, s[16:17]
	v_and_b32_e32 v37, 0x200000, v2
	v_cndmask_b32_e64 v3, v3, 20, s[16:17]
	v_cmp_eq_u32_e64 s[16:17], 0, v37
	v_cmp_gt_f32_e64 s[18:19], v15, v1
	s_and_b64 s[16:17], s[16:17], s[18:19]
	v_cndmask_b32_e64 v1, v1, v15, s[16:17]
	v_and_b32_e32 v37, 0x400000, v2
	v_cndmask_b32_e64 v3, v3, 21, s[16:17]
	v_cmp_eq_u32_e64 s[16:17], 0, v37
	v_cmp_gt_f32_e64 s[18:19], v6, v1
	s_and_b64 s[16:17], s[16:17], s[18:19]
	v_cndmask_b32_e64 v1, v1, v6, s[16:17]
	v_and_b32_e32 v37, 0x800000, v2
	v_cndmask_b32_e64 v3, v3, 22, s[16:17]
	v_cmp_eq_u32_e64 s[16:17], 0, v37
	v_cmp_gt_f32_e64 s[18:19], v7, v1
	s_and_b64 s[16:17], s[16:17], s[18:19]
	v_cndmask_b32_e64 v1, v1, v7, s[16:17]
	v_and_b32_e32 v37, 0x1000000, v2
	v_cndmask_b32_e64 v3, v3, 23, s[16:17]
	v_cmp_eq_u32_e64 s[16:17], 0, v37
	v_cmp_gt_f32_e64 s[18:19], v22, v1
	s_and_b64 s[16:17], s[16:17], s[18:19]
	v_cndmask_b32_e64 v1, v1, v22, s[16:17]
	v_and_b32_e32 v37, 0x2000000, v2
	v_cndmask_b32_e64 v3, v3, 24, s[16:17]
	v_cmp_eq_u32_e64 s[16:17], 0, v37
	v_cmp_gt_f32_e64 s[18:19], v23, v1
	s_and_b64 s[16:17], s[16:17], s[18:19]
	v_cndmask_b32_e64 v1, v1, v23, s[16:17]
	v_and_b32_e32 v37, 0x4000000, v2
	v_cndmask_b32_e64 v3, v3, 25, s[16:17]
	v_cmp_eq_u32_e64 s[16:17], 0, v37
	v_cmp_gt_f32_e64 s[18:19], v32, v1
	s_and_b64 s[16:17], s[16:17], s[18:19]
	v_cndmask_b32_e64 v1, v1, v32, s[16:17]
	v_and_b32_e32 v37, 0x8000000, v2
	v_cndmask_b32_e64 v3, v3, 26, s[16:17]
	v_cmp_eq_u32_e64 s[16:17], 0, v37
	v_cmp_gt_f32_e64 s[18:19], v33, v1
	s_and_b64 s[16:17], s[16:17], s[18:19]
	v_cndmask_b32_e64 v1, v1, v33, s[16:17]
	v_and_b32_e32 v37, 0x10000000, v2
	v_cndmask_b32_e64 v3, v3, 27, s[16:17]
	v_cmp_eq_u32_e64 s[16:17], 0, v37
	v_cmp_gt_f32_e64 s[18:19], v24, v1
	s_and_b64 s[16:17], s[16:17], s[18:19]
	v_cndmask_b32_e64 v1, v1, v24, s[16:17]
	v_and_b32_e32 v37, 0x20000000, v2
	v_cndmask_b32_e64 v3, v3, 28, s[16:17]
	v_cmp_eq_u32_e64 s[16:17], 0, v37
	v_cmp_gt_f32_e64 s[18:19], v25, v1
	s_and_b64 s[16:17], s[16:17], s[18:19]
	v_cndmask_b32_e64 v1, v1, v25, s[16:17]
	v_and_b32_e32 v37, 2.0, v2
	v_cndmask_b32_e64 v3, v3, 29, s[16:17]
	v_cmp_eq_u32_e64 s[16:17], 0, v37
	v_cmp_gt_f32_e64 s[18:19], v10, v1
	s_and_b64 s[16:17], s[16:17], s[18:19]
	v_cndmask_b32_e64 v1, v1, v10, s[16:17]
	v_cndmask_b32_e64 v3, v3, 30, s[16:17]
	v_cmp_ne_u32_e64 s[16:17], 31, v0
	v_cmp_gt_f32_e64 s[18:19], v11, v1
	s_and_b64 s[16:17], s[16:17], s[18:19]
	v_cndmask_b32_e64 v37, v1, v11, s[16:17]
	v_cndmask_b32_e64 v1, v3, 31, s[16:17]
	v_lshl_or_b32 v3, 1, v1, v2
	v_and_b32_e32 v2, 1, v3
	v_cmp_eq_u32_e64 s[16:17], 0, v2
	s_and_b64 s[16:17], s[16:17], vcc
	v_and_b32_e32 v38, 2, v3
	v_cndmask_b32_e64 v2, v112, v34, s[16:17]
	v_cmp_eq_u32_e64 s[16:17], 0, v38
	v_cmp_gt_f32_e64 s[18:19], v35, v2
	s_and_b64 s[16:17], s[16:17], s[18:19]
	v_cndmask_b32_e64 v2, v2, v35, s[16:17]
	v_and_b32_e32 v39, 4, v3
	v_cndmask_b32_e64 v38, 0, 1, s[16:17]
	v_cmp_eq_u32_e64 s[16:17], 0, v39
	v_cmp_gt_f32_e64 s[18:19], v28, v2
	s_and_b64 s[16:17], s[16:17], s[18:19]
	v_cndmask_b32_e64 v2, v2, v28, s[16:17]
	v_and_b32_e32 v39, 8, v3
	v_cndmask_b32_e64 v38, v38, 2, s[16:17]
	v_cmp_eq_u32_e64 s[16:17], 0, v39
	v_cmp_gt_f32_e64 s[18:19], v29, v2
	s_and_b64 s[16:17], s[16:17], s[18:19]
	v_cndmask_b32_e64 v2, v2, v29, s[16:17]
	v_and_b32_e32 v39, 16, v3
	v_cndmask_b32_e64 v38, v38, 3, s[16:17]
	v_cmp_eq_u32_e64 s[16:17], 0, v39
	v_cmp_gt_f32_e64 s[18:19], v18, v2
	s_and_b64 s[16:17], s[16:17], s[18:19]
	v_cndmask_b32_e64 v2, v2, v18, s[16:17]
	v_and_b32_e32 v39, 32, v3
	v_cndmask_b32_e64 v38, v38, 4, s[16:17]
	v_cmp_eq_u32_e64 s[16:17], 0, v39
	v_cmp_gt_f32_e64 s[18:19], v19, v2
	s_and_b64 s[16:17], s[16:17], s[18:19]
	v_cndmask_b32_e64 v2, v2, v19, s[16:17]
	v_and_b32_e32 v39, 64, v3
	v_cndmask_b32_e64 v38, v38, 5, s[16:17]
	v_cmp_eq_u32_e64 s[16:17], 0, v39
	v_cmp_gt_f32_e64 s[18:19], v8, v2
	s_and_b64 s[16:17], s[16:17], s[18:19]
	v_cndmask_b32_e64 v2, v2, v8, s[16:17]
	v_and_b32_e32 v39, 0x80, v3
	v_cndmask_b32_e64 v38, v38, 6, s[16:17]
	v_cmp_eq_u32_e64 s[16:17], 0, v39
	v_cmp_gt_f32_e64 s[18:19], v9, v2
	s_and_b64 s[16:17], s[16:17], s[18:19]
	v_cndmask_b32_e64 v2, v2, v9, s[16:17]
	v_and_b32_e32 v39, 0x100, v3
	v_cndmask_b32_e64 v38, v38, 7, s[16:17]
	v_cmp_eq_u32_e64 s[16:17], 0, v39
	v_cmp_gt_f32_e64 s[18:19], v20, v2
	s_and_b64 s[16:17], s[16:17], s[18:19]
	v_cndmask_b32_e64 v2, v2, v20, s[16:17]
	v_and_b32_e32 v39, 0x200, v3
	v_cndmask_b32_e64 v38, v38, 8, s[16:17]
	v_cmp_eq_u32_e64 s[16:17], 0, v39
	v_cmp_gt_f32_e64 s[18:19], v21, v2
	s_and_b64 s[16:17], s[16:17], s[18:19]
	v_cndmask_b32_e64 v2, v2, v21, s[16:17]
	v_and_b32_e32 v39, 0x400, v3
	v_cndmask_b32_e64 v38, v38, 9, s[16:17]
	v_cmp_eq_u32_e64 s[16:17], 0, v39
	v_cmp_gt_f32_e64 s[18:19], v30, v2
	s_and_b64 s[16:17], s[16:17], s[18:19]
	v_cndmask_b32_e64 v2, v2, v30, s[16:17]
	v_and_b32_e32 v39, 0x800, v3
	v_cndmask_b32_e64 v38, v38, 10, s[16:17]
	v_cmp_eq_u32_e64 s[16:17], 0, v39
	v_cmp_gt_f32_e64 s[18:19], v31, v2
	s_and_b64 s[16:17], s[16:17], s[18:19]
	v_cndmask_b32_e64 v2, v2, v31, s[16:17]
	v_and_b32_e32 v39, 0x1000, v3
	v_cndmask_b32_e64 v38, v38, 11, s[16:17]
	v_cmp_eq_u32_e64 s[16:17], 0, v39
	v_cmp_gt_f32_e64 s[18:19], v16, v2
	s_and_b64 s[16:17], s[16:17], s[18:19]
	v_cndmask_b32_e64 v2, v2, v16, s[16:17]
	v_and_b32_e32 v39, 0x2000, v3
	v_cndmask_b32_e64 v38, v38, 12, s[16:17]
	v_cmp_eq_u32_e64 s[16:17], 0, v39
	v_cmp_gt_f32_e64 s[18:19], v17, v2
	s_and_b64 s[16:17], s[16:17], s[18:19]
	v_cndmask_b32_e64 v2, v2, v17, s[16:17]
	v_and_b32_e32 v39, 0x4000, v3
	v_cndmask_b32_e64 v38, v38, 13, s[16:17]
	v_cmp_eq_u32_e64 s[16:17], 0, v39
	v_cmp_gt_f32_e64 s[18:19], v4, v2
	s_and_b64 s[16:17], s[16:17], s[18:19]
	v_cndmask_b32_e64 v2, v2, v4, s[16:17]
	v_and_b32_e32 v39, 0x8000, v3
	v_cndmask_b32_e64 v38, v38, 14, s[16:17]
	v_cmp_eq_u32_e64 s[16:17], 0, v39
	v_cmp_gt_f32_e64 s[18:19], v5, v2
	s_and_b64 s[16:17], s[16:17], s[18:19]
	v_cndmask_b32_e64 v2, v2, v5, s[16:17]
	v_and_b32_e32 v39, 0x10000, v3
	v_cndmask_b32_e64 v38, v38, 15, s[16:17]
	v_cmp_eq_u32_e64 s[16:17], 0, v39
	v_cmp_gt_f32_e64 s[18:19], v12, v2
	s_and_b64 s[16:17], s[16:17], s[18:19]
	v_cndmask_b32_e64 v2, v2, v12, s[16:17]
	v_and_b32_e32 v39, 0x20000, v3
	v_cndmask_b32_e64 v38, v38, 16, s[16:17]
	v_cmp_eq_u32_e64 s[16:17], 0, v39
	v_cmp_gt_f32_e64 s[18:19], v13, v2
	s_and_b64 s[16:17], s[16:17], s[18:19]
	v_cndmask_b32_e64 v2, v2, v13, s[16:17]
	v_and_b32_e32 v39, 0x40000, v3
	v_cndmask_b32_e64 v38, v38, 17, s[16:17]
	v_cmp_eq_u32_e64 s[16:17], 0, v39
	v_cmp_gt_f32_e64 s[18:19], v26, v2
	s_and_b64 s[16:17], s[16:17], s[18:19]
	v_cndmask_b32_e64 v2, v2, v26, s[16:17]
	v_and_b32_e32 v39, 0x80000, v3
	v_cndmask_b32_e64 v38, v38, 18, s[16:17]
	v_cmp_eq_u32_e64 s[16:17], 0, v39
	v_cmp_gt_f32_e64 s[18:19], v27, v2
	s_and_b64 s[16:17], s[16:17], s[18:19]
	v_cndmask_b32_e64 v2, v2, v27, s[16:17]
	v_and_b32_e32 v39, 0x100000, v3
	v_cndmask_b32_e64 v38, v38, 19, s[16:17]
	v_cmp_eq_u32_e64 s[16:17], 0, v39
	v_cmp_gt_f32_e64 s[18:19], v14, v2
	s_and_b64 s[16:17], s[16:17], s[18:19]
	v_cndmask_b32_e64 v2, v2, v14, s[16:17]
	v_and_b32_e32 v39, 0x200000, v3
	v_cndmask_b32_e64 v38, v38, 20, s[16:17]
	v_cmp_eq_u32_e64 s[16:17], 0, v39
	v_cmp_gt_f32_e64 s[18:19], v15, v2
	s_and_b64 s[16:17], s[16:17], s[18:19]
	v_cndmask_b32_e64 v2, v2, v15, s[16:17]
	v_and_b32_e32 v39, 0x400000, v3
	v_cndmask_b32_e64 v38, v38, 21, s[16:17]
	v_cmp_eq_u32_e64 s[16:17], 0, v39
	v_cmp_gt_f32_e64 s[18:19], v6, v2
	s_and_b64 s[16:17], s[16:17], s[18:19]
	v_cndmask_b32_e64 v2, v2, v6, s[16:17]
	v_and_b32_e32 v39, 0x800000, v3
	v_cndmask_b32_e64 v38, v38, 22, s[16:17]
	v_cmp_eq_u32_e64 s[16:17], 0, v39
	v_cmp_gt_f32_e64 s[18:19], v7, v2
	s_and_b64 s[16:17], s[16:17], s[18:19]
	v_cndmask_b32_e64 v2, v2, v7, s[16:17]
	v_and_b32_e32 v39, 0x1000000, v3
	v_cndmask_b32_e64 v38, v38, 23, s[16:17]
	v_cmp_eq_u32_e64 s[16:17], 0, v39
	v_cmp_gt_f32_e64 s[18:19], v22, v2
	s_and_b64 s[16:17], s[16:17], s[18:19]
	v_cndmask_b32_e64 v2, v2, v22, s[16:17]
	v_and_b32_e32 v39, 0x2000000, v3
	v_cndmask_b32_e64 v38, v38, 24, s[16:17]
	v_cmp_eq_u32_e64 s[16:17], 0, v39
	v_cmp_gt_f32_e64 s[18:19], v23, v2
	s_and_b64 s[16:17], s[16:17], s[18:19]
	v_cndmask_b32_e64 v2, v2, v23, s[16:17]
	v_and_b32_e32 v39, 0x4000000, v3
	v_cndmask_b32_e64 v38, v38, 25, s[16:17]
	v_cmp_eq_u32_e64 s[16:17], 0, v39
	v_cmp_gt_f32_e64 s[18:19], v32, v2
	s_and_b64 s[16:17], s[16:17], s[18:19]
	v_cndmask_b32_e64 v2, v2, v32, s[16:17]
	v_and_b32_e32 v39, 0x8000000, v3
	v_cndmask_b32_e64 v38, v38, 26, s[16:17]
	v_cmp_eq_u32_e64 s[16:17], 0, v39
	v_cmp_gt_f32_e64 s[18:19], v33, v2
	s_and_b64 s[16:17], s[16:17], s[18:19]
	v_cndmask_b32_e64 v2, v2, v33, s[16:17]
	v_and_b32_e32 v39, 0x10000000, v3
	v_cndmask_b32_e64 v38, v38, 27, s[16:17]
	v_cmp_eq_u32_e64 s[16:17], 0, v39
	v_cmp_gt_f32_e64 s[18:19], v24, v2
	s_and_b64 s[16:17], s[16:17], s[18:19]
	v_cndmask_b32_e64 v2, v2, v24, s[16:17]
	v_and_b32_e32 v39, 0x20000000, v3
	v_cndmask_b32_e64 v38, v38, 28, s[16:17]
	v_cmp_eq_u32_e64 s[16:17], 0, v39
	v_cmp_gt_f32_e64 s[18:19], v25, v2
	s_and_b64 s[16:17], s[16:17], s[18:19]
	v_cndmask_b32_e64 v2, v2, v25, s[16:17]
	v_and_b32_e32 v39, 2.0, v3
	v_cndmask_b32_e64 v38, v38, 29, s[16:17]
	v_cmp_eq_u32_e64 s[16:17], 0, v39
	v_cmp_gt_f32_e64 s[18:19], v10, v2
	s_and_b64 s[16:17], s[16:17], s[18:19]
	v_cndmask_b32_e64 v2, v2, v10, s[16:17]
	v_cndmask_b32_e64 v38, v38, 30, s[16:17]
	v_cmp_lt_i32_e64 s[16:17], -1, v3
	v_cmp_gt_f32_e64 s[18:19], v11, v2
	s_and_b64 s[16:17], s[16:17], s[18:19]
	v_cndmask_b32_e64 v39, v2, v11, s[16:17]
	v_cndmask_b32_e64 v2, v38, 31, s[16:17]
	v_lshlrev_b32_e64 v38, v2, 1
	v_bitop3_b32 v89, v38, 1, v3 bitop3:0xc8
	v_cmp_eq_u32_e64 s[16:17], 0, v89
	s_and_b64 vcc, s[16:17], vcc
	v_cndmask_b32_e32 v34, v112, v34, vcc
	v_bitop3_b32 v89, v38, 2, v3 bitop3:0xc8
	v_cmp_eq_u32_e32 vcc, 0, v89
	v_cmp_gt_f32_e64 s[16:17], v35, v34
	s_and_b64 vcc, vcc, s[16:17]
	v_cndmask_b32_e32 v34, v34, v35, vcc
	v_bitop3_b32 v89, v38, 4, v3 bitop3:0xc8
	v_cndmask_b32_e64 v35, 0, 1, vcc
	v_cmp_eq_u32_e32 vcc, 0, v89
	v_cmp_gt_f32_e64 s[16:17], v28, v34
	s_and_b64 vcc, vcc, s[16:17]
	v_cndmask_b32_e32 v28, v34, v28, vcc
	v_cndmask_b32_e64 v34, v35, 2, vcc
	v_bitop3_b32 v35, v38, 8, v3 bitop3:0xc8
	v_cmp_eq_u32_e32 vcc, 0, v35
	v_cmp_gt_f32_e64 s[16:17], v29, v28
	s_and_b64 vcc, vcc, s[16:17]
	v_cndmask_b32_e32 v28, v28, v29, vcc
	v_cndmask_b32_e64 v29, v34, 3, vcc
	v_bitop3_b32 v34, v38, 16, v3 bitop3:0xc8
	v_cmp_eq_u32_e32 vcc, 0, v34
	v_cmp_gt_f32_e64 s[16:17], v18, v28
	s_and_b64 vcc, vcc, s[16:17]
	v_cndmask_b32_e32 v18, v28, v18, vcc
	v_cndmask_b32_e64 v28, v29, 4, vcc
	v_bitop3_b32 v29, v38, 32, v3 bitop3:0xc8
	v_cmp_eq_u32_e32 vcc, 0, v29
	v_cmp_gt_f32_e64 s[16:17], v19, v18
	s_and_b64 vcc, vcc, s[16:17]
	v_cndmask_b32_e32 v18, v18, v19, vcc
	v_cndmask_b32_e64 v19, v28, 5, vcc
	v_bitop3_b32 v28, v38, 64, v3 bitop3:0xc8
	v_cmp_eq_u32_e32 vcc, 0, v28
	v_cmp_gt_f32_e64 s[16:17], v8, v18
	s_and_b64 vcc, vcc, s[16:17]
	s_movk_i32 s16, 0x80
	v_cndmask_b32_e32 v8, v18, v8, vcc
	v_cndmask_b32_e64 v18, v19, 6, vcc
	v_bitop3_b32 v19, v38, s16, v3 bitop3:0xc8
	v_cmp_eq_u32_e32 vcc, 0, v19
	v_cmp_gt_f32_e64 s[16:17], v9, v8
	s_and_b64 vcc, vcc, s[16:17]
	s_movk_i32 s16, 0x100
	v_cndmask_b32_e32 v8, v8, v9, vcc
	v_cndmask_b32_e64 v9, v18, 7, vcc
	v_bitop3_b32 v18, v38, s16, v3 bitop3:0xc8
	v_cmp_eq_u32_e32 vcc, 0, v18
	v_cmp_gt_f32_e64 s[16:17], v20, v8
	s_and_b64 vcc, vcc, s[16:17]
	s_movk_i32 s16, 0x200
	v_cndmask_b32_e32 v8, v8, v20, vcc
	v_bitop3_b32 v18, v38, s16, v3 bitop3:0xc8
	v_cndmask_b32_e64 v9, v9, 8, vcc
	v_cmp_eq_u32_e32 vcc, 0, v18
	v_cmp_gt_f32_e64 s[16:17], v21, v8
	s_and_b64 vcc, vcc, s[16:17]
	v_cndmask_b32_e32 v8, v8, v21, vcc
	v_bitop3_b32 v18, v38, s52, v3 bitop3:0xc8
	v_cndmask_b32_e64 v9, v9, 9, vcc
	v_cmp_eq_u32_e32 vcc, 0, v18
	v_cmp_gt_f32_e64 s[16:17], v30, v8
	s_and_b64 vcc, vcc, s[16:17]
	s_movk_i32 s16, 0x800
	v_cndmask_b32_e32 v8, v8, v30, vcc
	v_bitop3_b32 v18, v38, s16, v3 bitop3:0xc8
	v_cndmask_b32_e64 v9, v9, 10, vcc
	v_cmp_eq_u32_e32 vcc, 0, v18
	v_cmp_gt_f32_e64 s[16:17], v31, v8
	s_and_b64 vcc, vcc, s[16:17]
	s_movk_i32 s16, 0x1000
	v_cndmask_b32_e32 v8, v8, v31, vcc
	v_bitop3_b32 v18, v38, s16, v3 bitop3:0xc8
	v_cndmask_b32_e64 v9, v9, 11, vcc
	v_cmp_eq_u32_e32 vcc, 0, v18
	v_cmp_gt_f32_e64 s[16:17], v16, v8
	s_and_b64 vcc, vcc, s[16:17]
	s_movk_i32 s16, 0x2000
	v_cndmask_b32_e32 v8, v8, v16, vcc
	v_bitop3_b32 v16, v38, s16, v3 bitop3:0xc8
	v_cndmask_b32_e64 v9, v9, 12, vcc
	v_cmp_eq_u32_e32 vcc, 0, v16
	v_cmp_gt_f32_e64 s[16:17], v17, v8
	s_and_b64 vcc, vcc, s[16:17]
	s_movk_i32 s16, 0x4000
	v_cndmask_b32_e32 v8, v8, v17, vcc
	v_bitop3_b32 v16, v38, s16, v3 bitop3:0xc8
	v_cndmask_b32_e64 v9, v9, 13, vcc
	v_cmp_eq_u32_e32 vcc, 0, v16
	v_cmp_gt_f32_e64 s[16:17], v4, v8
	s_and_b64 vcc, vcc, s[16:17]
	s_mov_b32 s16, 0x8000
	v_cndmask_b32_e32 v4, v8, v4, vcc
	v_cndmask_b32_e64 v8, v9, 14, vcc
	v_bitop3_b32 v9, v38, s16, v3 bitop3:0xc8
	v_cmp_eq_u32_e32 vcc, 0, v9
	v_cmp_gt_f32_e64 s[16:17], v5, v4
	s_and_b64 vcc, vcc, s[16:17]
	s_mov_b32 s16, 0x10000
	v_cndmask_b32_e32 v4, v4, v5, vcc
	v_cndmask_b32_e64 v5, v8, 15, vcc
	v_bitop3_b32 v8, v38, s16, v3 bitop3:0xc8
	v_cmp_eq_u32_e32 vcc, 0, v8
	v_cmp_gt_f32_e64 s[16:17], v12, v4
	s_and_b64 vcc, vcc, s[16:17]
	s_mov_b32 s16, 0x20000
	v_cndmask_b32_e32 v4, v4, v12, vcc
	v_bitop3_b32 v8, v38, s16, v3 bitop3:0xc8
	v_cndmask_b32_e64 v5, v5, 16, vcc
	v_cmp_eq_u32_e32 vcc, 0, v8
	v_cmp_gt_f32_e64 s[16:17], v13, v4
	s_and_b64 vcc, vcc, s[16:17]
	s_mov_b32 s16, 0x40000
	v_cndmask_b32_e32 v4, v4, v13, vcc
	v_bitop3_b32 v8, v38, s16, v3 bitop3:0xc8
	v_cndmask_b32_e64 v5, v5, 17, vcc
	v_cmp_eq_u32_e32 vcc, 0, v8
	v_cmp_gt_f32_e64 s[16:17], v26, v4
	s_and_b64 vcc, vcc, s[16:17]
	v_cndmask_b32_e32 v4, v4, v26, vcc
	v_bitop3_b32 v8, v38, s61, v3 bitop3:0xc8
	v_cndmask_b32_e64 v5, v5, 18, vcc
	v_cmp_eq_u32_e32 vcc, 0, v8
	v_cmp_gt_f32_e64 s[16:17], v27, v4
	s_and_b64 vcc, vcc, s[16:17]
	v_cndmask_b32_e32 v4, v4, v27, vcc
	v_bitop3_b32 v8, v38, s62, v3 bitop3:0xc8
	v_cndmask_b32_e64 v5, v5, 19, vcc
	v_cmp_eq_u32_e32 vcc, 0, v8
	v_cmp_gt_f32_e64 s[16:17], v14, v4
	s_and_b64 vcc, vcc, s[16:17]
	v_cndmask_b32_e32 v4, v4, v14, vcc
	v_bitop3_b32 v8, v38, s63, v3 bitop3:0xc8
	v_cndmask_b32_e64 v5, v5, 20, vcc
	v_cmp_eq_u32_e32 vcc, 0, v8
	v_cmp_gt_f32_e64 s[16:17], v15, v4
	s_and_b64 vcc, vcc, s[16:17]
	v_cndmask_b32_e32 v4, v4, v15, vcc
	v_bitop3_b32 v8, v38, s64, v3 bitop3:0xc8
	v_cndmask_b32_e64 v5, v5, 21, vcc
	v_cmp_eq_u32_e32 vcc, 0, v8
	v_cmp_gt_f32_e64 s[16:17], v6, v4
	s_and_b64 vcc, vcc, s[16:17]
	v_cndmask_b32_e32 v4, v4, v6, vcc
	v_bitop3_b32 v6, v38, s65, v3 bitop3:0xc8
	v_cndmask_b32_e64 v5, v5, 22, vcc
	v_cmp_eq_u32_e32 vcc, 0, v6
	v_cmp_gt_f32_e64 s[16:17], v7, v4
	s_and_b64 vcc, vcc, s[16:17]
	v_cndmask_b32_e32 v4, v4, v7, vcc
	v_bitop3_b32 v6, v38, s66, v3 bitop3:0xc8
	v_cndmask_b32_e64 v5, v5, 23, vcc
	v_cmp_eq_u32_e32 vcc, 0, v6
	v_cmp_gt_f32_e64 s[16:17], v22, v4
	s_and_b64 vcc, vcc, s[16:17]
	v_cndmask_b32_e32 v4, v4, v22, vcc
	v_bitop3_b32 v6, v38, s67, v3 bitop3:0xc8
	v_cndmask_b32_e64 v5, v5, 24, vcc
	v_cmp_eq_u32_e32 vcc, 0, v6
	v_cmp_gt_f32_e64 s[16:17], v23, v4
	s_and_b64 vcc, vcc, s[16:17]
	v_cndmask_b32_e32 v4, v4, v23, vcc
	v_bitop3_b32 v6, v38, s84, v3 bitop3:0xc8
	v_cndmask_b32_e64 v5, v5, 25, vcc
	v_cmp_eq_u32_e32 vcc, 0, v6
	v_cmp_gt_f32_e64 s[16:17], v32, v4
	s_and_b64 vcc, vcc, s[16:17]
	v_cndmask_b32_e32 v4, v4, v32, vcc
	v_bitop3_b32 v6, v38, s85, v3 bitop3:0xc8
	v_cndmask_b32_e64 v5, v5, 26, vcc
	v_cmp_eq_u32_e32 vcc, 0, v6
	v_cmp_gt_f32_e64 s[16:17], v33, v4
	s_and_b64 vcc, vcc, s[16:17]
	v_cndmask_b32_e32 v4, v4, v33, vcc
	v_bitop3_b32 v6, v38, s86, v3 bitop3:0xc8
	v_cndmask_b32_e64 v5, v5, 27, vcc
	v_cmp_eq_u32_e32 vcc, 0, v6
	v_cmp_gt_f32_e64 s[16:17], v24, v4
	s_and_b64 vcc, vcc, s[16:17]
	v_cndmask_b32_e32 v4, v4, v24, vcc
	v_bitop3_b32 v6, v38, s87, v3 bitop3:0xc8
	v_cndmask_b32_e64 v5, v5, 28, vcc
	v_cmp_eq_u32_e32 vcc, 0, v6
	v_cmp_gt_f32_e64 s[16:17], v25, v4
	s_and_b64 vcc, vcc, s[16:17]
	v_or_b32_e32 v88, v38, v3
	v_cndmask_b32_e32 v4, v4, v25, vcc
	v_bitop3_b32 v3, v38, 2.0, v3 bitop3:0xc8
	v_cndmask_b32_e64 v5, v5, 29, vcc
	v_cmp_eq_u32_e32 vcc, 0, v3
	v_cmp_gt_f32_e64 s[16:17], v10, v4
	s_and_b64 vcc, vcc, s[16:17]
	v_cndmask_b32_e32 v3, v4, v10, vcc
	v_cndmask_b32_e64 v4, v5, 30, vcc
	v_cmp_lt_i32_e32 vcc, -1, v88
	v_cmp_gt_f32_e64 s[16:17], v11, v3
	s_and_b64 vcc, vcc, s[16:17]
	v_cndmask_b32_e32 v5, v3, v11, vcc
	v_cndmask_b32_e64 v3, v4, 31, vcc
	v_sub_f32_e32 v4, v36, v36
	v_mul_f32_e32 v4, 0x3fb8aa3b, v4
	v_exp_f32_e32 v10, v4
	v_sub_f32_e32 v4, v37, v36
	v_mul_f32_e32 v4, 0x3fb8aa3b, v4
	v_exp_f32_e32 v11, v4
	v_sub_f32_e32 v4, v39, v36
	v_mul_f32_e32 v4, 0x3fb8aa3b, v4
	v_exp_f32_e32 v12, v4
	v_sub_f32_e32 v4, v5, v36
	v_mul_f32_e32 v4, 0x3fb8aa3b, v4
	v_exp_f32_e32 v13, v4
	v_add_f32_e32 v4, 0, v10
	v_add_f32_e32 v4, v4, v11
	v_add_f32_e32 v4, v4, v12
	v_add_f32_e32 v14, v4, v13
	v_div_scale_f32 v15, s[16:17], v14, v14, v10
	v_rcp_f32_e32 v16, v15
	v_lshl_add_u32 v4, s91, 8, v94
	v_ashrrev_i32_e32 v5, 31, v4
	v_lshlrev_b64 v[6:7], 2, v[4:5]
	v_fma_f32 v5, -v15, v16, 1.0
	v_fmac_f32_e32 v16, v5, v16
	v_div_scale_f32 v5, vcc, v10, v14, v10
	v_mul_f32_e32 v17, v5, v16
	v_fma_f32 v18, -v15, v17, v5
	v_fmac_f32_e32 v17, v18, v16
	v_fma_f32 v5, -v15, v17, v5
	v_div_fmas_f32 v5, v5, v16, v17
	v_div_fixup_f32 v5, v5, v14, v10
	v_div_scale_f32 v10, s[16:17], v14, v14, v11
	v_rcp_f32_e32 v15, v10
	v_lshl_add_u64 v[8:9], s[20:21], 0, v[6:7]
	v_lshl_add_u64 v[6:7], s[22:23], 0, v[6:7]
	global_store_dword v[6:7], v5, off
	v_or_b32_e32 v6, 1, v4
	v_fma_f32 v4, -v10, v15, 1.0
	v_lshl_add_u32 v5, v0, 2, 0
	v_fmac_f32_e32 v15, v4, v15
	v_div_scale_f32 v4, vcc, v11, v14, v11
	ds_add_u32 v5, v109 offset:58624
	v_mul_f32_e32 v5, v4, v15
	v_fma_f32 v16, -v10, v5, v4
	v_fmac_f32_e32 v5, v16, v15
	v_fma_f32 v4, -v10, v5, v4
	v_div_fmas_f32 v4, v4, v15, v5
	v_div_scale_f32 v5, s[16:17], v14, v14, v12
	v_rcp_f32_e32 v15, v5
	v_ashrrev_i32_e32 v7, 31, v6
	v_div_fixup_f32 v4, v4, v14, v11
	v_lshl_add_u64 v[10:11], v[6:7], 2, s[22:23]
	v_lshl_add_u32 v6, v1, 2, 0
	ds_add_u32 v6, v109 offset:58624
	v_fma_f32 v6, -v5, v15, 1.0
	v_fmac_f32_e32 v15, v6, v15
	v_div_scale_f32 v6, vcc, v12, v14, v12
	v_mul_f32_e32 v7, v6, v15
	v_fma_f32 v16, -v5, v7, v6
	v_fmac_f32_e32 v7, v16, v15
	v_fma_f32 v5, -v5, v7, v6
	v_div_scale_f32 v6, s[16:17], v14, v14, v13
	v_div_fmas_f32 v5, v5, v15, v7
	v_rcp_f32_e32 v7, v6
	v_div_fixup_f32 v5, v5, v14, v12
	v_lshl_add_u32 v12, v2, 2, 0
	ds_add_u32 v12, v109 offset:58624
	global_store_dwordx4 v[8:9], v[0:3], off
	s_nop 1
	v_fma_f32 v0, -v6, v7, 1.0
	v_fmac_f32_e32 v7, v0, v7
	v_div_scale_f32 v0, vcc, v13, v14, v13
	v_mul_f32_e32 v1, v0, v7
	v_fma_f32 v2, -v6, v1, v0
	v_fmac_f32_e32 v1, v2, v7
	v_fma_f32 v0, -v6, v1, v0
	v_div_fmas_f32 v0, v0, v7, v1
	v_div_fixup_f32 v6, v0, v14, v13
	global_store_dwordx3 v[10:11], v[4:6], off
	v_lshl_add_u32 v0, v3, 2, 0
	ds_add_u32 v0, v109 offset:58624
